# s_nop 3 -> s_nop 0 behind every s_setprio 1 in the GEMM K-loops (same bytes); third measurement of the final candidate
# speedup vs baseline: 1.0244x; 1.0244x over previous
; #define PG8_STAGE(bufoff, gbase, voff) do { _Pragma("unroll") for (int _i = 0; _i < 2; ++_i) \
;         __builtin_amdgcn_global_load_lds((const unsigned*)((const char*)(gbase) + (voff)[_i]), (PG8_LAS unsigned*)(lds + (bufoff) + ldsw + _i * 8192), 16, 0, 0); } while (0)
; #define PG8_STAGE_A(bufoff, gbase, h, nx) do { if constexpr (Sched::GATHER) { const unsigned vv_[2] = {(nx) ? vAn[h][0] : vA[h][0], (nx) ? vAn[h][1] : vA[h][1]}; PG8_STAGE(bufoff, gbase, vv_); } \
;         else { PG8_STAGE(bufoff, (gbase) + (h) * hstep, voffA); } } while (0)
; #define PG8_LDA(dst, b, h) do { _Pragma("unroll") for (int m = 0; m < 4; ++m) _Pragma("unroll") for (int k = 0; k < 2; ++k) dst[m][k] = *(const PG8_LAS bf16x8*)(lds + PG8_SA(b, h) + aoff + m * 2048 + k * 1024); } while (0)
; #define PG8_WAIT_V(n) asm volatile("s_waitcnt vmcnt(" #n ")" ::: "memory")
; #define PG8_WAIT_L(n) asm volatile("s_waitcnt lgkmcnt(" #n ")" ::: "memory")
;     ...
;         const bool has_next = S.next(ui + 1, nxt);
;         const char* nA = Sched::GATHER ? cA : (has_next ? (const char*)g.A + (size_t)nxt.pm * tstep : cA);
;         if constexpr (Sched::GATHER) { if (has_next) { PG8_AOFF(vAn, ui + 1); } else { _Pragma("unroll") for (int h_ = 0; h_ < 2; ++h_) _Pragma("unroll") for (int i_ = 0; i_ < 2; ++i_) vAn[h_][i_] = vA[h_][i_]; } } const char* nB = has_next ? (const char*)g.Bt + (size_t)nxt.pb * tstep : cB;
; #pragma nounroll
;         for (int t = 0; t < nt; t += 2) {
;             const bool last = (t == nt - 2);
;             const char* a1 = cA + (size_t)(t + 1) * kstep;
;             const char* a2 = last ? nA : cA + (size_t)(t + 2) * kstep; const char* b2 = last ? nB : cB + (size_t)(t + 2) * kstep;
;             const char* a3 = a2 + kstep; const char* b3 = b2 + kstep;
;             if (last && has_next) S.a_ready(nxt);
;             if constexpr (SP2) {
;             PG8_LDB(B0, 0, 0); PG8_LDB(B1, 0, 1); PG8_SCHED; PG8_LDA(At, 0, 0); PG8_STAGE_A(PG8_SA(1, 1), a1, 1, false);
;             PG8_WAIT_V(8); PG8_WAIT_L(0); PG8_BAR; PG8_MMA(0, 0, At, B0); PG8_MMA(0, 1, At, B1); PG8_BAR; PG8_SCHED;
;             PG8_LDA(At, 0, 1); PG8_STAGE(PG8_SB(0, 0), b2, voffB); PG8_STAGE(PG8_SB(0, 1), b2 + hstepB, voffB); PG8_STAGE_A(PG8_SA(0, 0), a2, 0, last);
;             PG8_WAIT_V(8); PG8_WAIT_L(0); PG8_BAR; PG8_MMA(1, 0, At, B0); PG8_MMA(1, 1, At, B1); PG8_BAR; PG8_SCHED;
.LBB0_152:
	s_ashr_i32 s61, s60, 31
	s_lshl_b64 s[0:1], s[60:61], 18
	v_readlane_b32 s18, v255, 5
	v_readlane_b32 s19, v255, 6
	s_add_u32 s62, s18, s0
	s_addc_u32 s63, s19, s1
	s_and_b64 s[0:1], s[2:3], exec
	s_cselect_b32 s0, s63, s9
	s_cselect_b32 s1, s62, s8
	s_ashr_i32 s73, s72, 31
	s_lshl_b64 s[18:19], s[72:73], 18
	s_add_u32 s64, s14, s18
	s_addc_u32 s65, s15, s19
	s_and_b64 s[18:19], s[2:3], exec
	s_cselect_b32 s5, s65, s11
	s_cselect_b32 s7, s64, s10
	s_add_u32 s8, s8, 0x20080
	s_addc_u32 s9, s9, 0
	s_add_u32 s18, s10, 0x100
	s_addc_u32 s19, s11, 0
	s_mov_b32 s33, -2
	ds_read_b128 v[26:29], v205
	ds_read_b128 v[30:33], v205 offset:1024
	ds_read_b128 v[18:21], v205 offset:2048
	ds_read_b128 v[22:25], v205 offset:3072
	ds_read_b128 v[10:13], v206
	ds_read_b128 v[14:17], v206 offset:1024
	ds_read_b128 v[2:5], v206 offset:2048
	ds_read_b128 v[6:9], v206 offset:3072
	s_add_u32 s10, s8, 0xfffe0080
	s_addc_u32 s11, s9, -1
	s_cmp_eq_u32 s33, 4
	s_cselect_b32 s67, s0, s11
	s_cselect_b32 s66, s1, s10
	s_cselect_b32 s11, s5, s19
	s_cselect_b32 s10, s7, s18
	v_lshl_add_u64 v[162:163], s[8:9], 0, v[176:177]
	s_add_i32 m0, s82, 0xc000
	ds_read_b128 v[184:187], v207
	ds_read_b128 v[188:191], v207 offset:1024
	ds_read_b128 v[192:195], v207 offset:2048
	ds_read_b128 v[196:199], v207 offset:3072
	ds_read_b128 v[214:217], v207 offset:4096
	ds_read_b128 v[218:221], v207 offset:5120
	ds_read_b128 v[222:225], v207 offset:6144
	ds_read_b128 v[226:229], v207 offset:7168
	global_load_lds_dwordx4 v[162:163], off
	v_lshl_add_u64 v[162:163], s[8:9], 0, v[178:179]
	s_add_i32 m0, s82, 0xe000
	s_nop 0
	global_load_lds_dwordx4 v[162:163], off
	s_waitcnt vmcnt(8)
	s_waitcnt lgkmcnt(0)
	s_barrier
	s_setprio 1
	s_nop 0
	s_waitcnt lgkmcnt(0)
	v_mfma_scale_f32_16x16x128_f8f6f4 v[158:161], v[26:33], v[184:191], 0, v208, v209 op_sel_hi:[0,0,0]
	v_mfma_scale_f32_16x16x128_f8f6f4 v[154:157], v[18:25], v[184:191], 0, v208, v209 op_sel_hi:[0,0,0]
	v_mfma_scale_f32_16x16x128_f8f6f4 v[142:145], v[26:33], v[192:199], 0, v208, v209 op_sel_hi:[0,0,0]
	v_mfma_scale_f32_16x16x128_f8f6f4 v[138:141], v[18:25], v[192:199], 0, v208, v209 op_sel_hi:[0,0,0]
	v_mfma_scale_f32_16x16x128_f8f6f4 v[126:129], v[26:33], v[214:221], 0, v208, v209 op_sel_hi:[0,0,0]
	v_mfma_scale_f32_16x16x128_f8f6f4 v[122:125], v[18:25], v[214:221], 0, v208, v209 op_sel_hi:[0,0,0]
	v_mfma_scale_f32_16x16x128_f8f6f4 v[110:113], v[26:33], v[222:229], 0, v208, v209 op_sel_hi:[0,0,0]
	v_mfma_scale_f32_16x16x128_f8f6f4 v[106:109], v[18:25], v[222:229], 0, v208, v209 op_sel_hi:[0,0,0]
	s_setprio 0
	s_setprio 1
	s_nop 0
	v_mfma_scale_f32_16x16x128_f8f6f4 v[150:153], v[10:17], v[184:191], 0, v208, v209 op_sel_hi:[0,0,0]
	v_mfma_scale_f32_16x16x128_f8f6f4 v[146:149], v[2:9], v[184:191], 0, v208, v209 op_sel_hi:[0,0,0]
	v_mfma_scale_f32_16x16x128_f8f6f4 v[134:137], v[10:17], v[192:199], 0, v208, v209 op_sel_hi:[0,0,0]
	v_mfma_scale_f32_16x16x128_f8f6f4 v[130:133], v[2:9], v[192:199], 0, v208, v209 op_sel_hi:[0,0,0]
	v_mfma_scale_f32_16x16x128_f8f6f4 v[118:121], v[10:17], v[214:221], 0, v208, v209 op_sel_hi:[0,0,0]
	v_mfma_scale_f32_16x16x128_f8f6f4 v[114:117], v[2:9], v[214:221], 0, v208, v209 op_sel_hi:[0,0,0]
	v_mfma_scale_f32_16x16x128_f8f6f4 v[102:105], v[10:17], v[222:229], 0, v208, v209 op_sel_hi:[0,0,0]
	v_mfma_scale_f32_16x16x128_f8f6f4 v[98:101], v[2:9], v[222:229], 0, v208, v209 op_sel_hi:[0,0,0]
	s_setprio 0
	s_barrier
	s_add_i32 s59, s96, s77
	v_lshl_add_u64 v[162:163], s[10:11], 0, v[168:169]
	s_mov_b32 m0, s59
	ds_read_b128 v[188:191], v207 offset:16384
	ds_read_b128 v[192:195], v207 offset:17408
	ds_read_b128 v[214:217], v207 offset:18432
	ds_read_b128 v[218:221], v207 offset:19456
	ds_read_b128 v[222:225], v207 offset:20480
	ds_read_b128 v[226:229], v207 offset:21504
	ds_read_b128 v[230:233], v207 offset:22528
	ds_read_b128 v[234:237], v207 offset:23552
	global_load_lds_dwordx4 v[162:163], off
	s_add_i32 m0, s59, 0x2000
	s_add_u32 s68, s10, 0x8000
	v_lshl_add_u64 v[164:165], s[10:11], 0, v[172:173]
	s_addc_u32 s69, s11, 0
	s_add_i32 s59, s97, s77
	global_load_lds_dwordx4 v[164:165], off
	v_lshl_add_u64 v[184:185], s[68:69], 0, v[168:169]
	s_mov_b32 m0, s59
	v_lshl_add_u64 v[186:187], s[66:67], 0, v[170:171]
	global_load_lds_dwordx4 v[184:185], off
	v_lshl_add_u64 v[184:185], s[68:69], 0, v[172:173]
	s_add_i32 m0, s59, 0x2000
	s_nop 0
	global_load_lds_dwordx4 v[184:185], off
	v_lshl_add_u64 v[184:185], s[66:67], 0, v[166:167]
	s_mov_b32 m0, s82
	s_nop 0
	global_load_lds_dwordx4 v[184:185], off
	s_mov_b32 m0, s83
	s_nop 0
	global_load_lds_dwordx4 v[186:187], off
	s_waitcnt vmcnt(8)
	s_waitcnt lgkmcnt(0)
	s_barrier
	s_setprio 1
	s_nop 0
	s_waitcnt lgkmcnt(0)
	v_mfma_scale_f32_16x16x128_f8f6f4 v[94:97], v[26:33], v[188:195], 0, v208, v209 op_sel_hi:[0,0,0]
	v_mfma_scale_f32_16x16x128_f8f6f4 v[90:93], v[18:25], v[188:195], 0, v208, v209 op_sel_hi:[0,0,0]
	v_mfma_scale_f32_16x16x128_f8f6f4 v[78:81], v[26:33], v[214:221], 0, v208, v209 op_sel_hi:[0,0,0]
	v_mfma_scale_f32_16x16x128_f8f6f4 v[74:77], v[18:25], v[214:221], 0, v208, v209 op_sel_hi:[0,0,0]
	v_mfma_scale_f32_16x16x128_f8f6f4 v[62:65], v[26:33], v[222:229], 0, v208, v209 op_sel_hi:[0,0,0]
	v_mfma_scale_f32_16x16x128_f8f6f4 v[58:61], v[18:25], v[222:229], 0, v208, v209 op_sel_hi:[0,0,0]
	v_mfma_scale_f32_16x16x128_f8f6f4 v[46:49], v[26:33], v[230:237], 0, v208, v209 op_sel_hi:[0,0,0]
	v_mfma_scale_f32_16x16x128_f8f6f4 v[42:45], v[18:25], v[230:237], 0, v208, v209 op_sel_hi:[0,0,0]
	s_setprio 0
	s_setprio 1
	s_nop 0
	v_mfma_scale_f32_16x16x128_f8f6f4 v[86:89], v[10:17], v[188:195], 0, v208, v209 op_sel_hi:[0,0,0]
	v_mfma_scale_f32_16x16x128_f8f6f4 v[82:85], v[2:9], v[188:195], 0, v208, v209 op_sel_hi:[0,0,0]
	v_mfma_scale_f32_16x16x128_f8f6f4 v[70:73], v[10:17], v[214:221], 0, v208, v209 op_sel_hi:[0,0,0]
	v_mfma_scale_f32_16x16x128_f8f6f4 v[66:69], v[2:9], v[214:221], 0, v208, v209 op_sel_hi:[0,0,0]
	v_mfma_scale_f32_16x16x128_f8f6f4 v[54:57], v[10:17], v[222:229], 0, v208, v209 op_sel_hi:[0,0,0]
	v_mfma_scale_f32_16x16x128_f8f6f4 v[50:53], v[2:9], v[222:229], 0, v208, v209 op_sel_hi:[0,0,0]
	v_mfma_scale_f32_16x16x128_f8f6f4 v[38:41], v[10:17], v[230:237], 0, v208, v209 op_sel_hi:[0,0,0]
	v_mfma_scale_f32_16x16x128_f8f6f4 v[34:37], v[2:9], v[230:237], 0, v208, v209 op_sel_hi:[0,0,0]
	s_setprio 0
	s_barrier
; #define PG8_STAGE(bufoff, gbase, voff) do { _Pragma("unroll") for (int _i = 0; _i < 2; ++_i) \
;         __builtin_amdgcn_global_load_lds((const unsigned*)((const char*)(gbase) + (voff)[_i]), (PG8_LAS unsigned*)(lds + (bufoff) + ldsw + _i * 8192), 16, 0, 0); } while (0)
; #define PG8_STAGE_A(bufoff, gbase, h, nx) do { if constexpr (Sched::GATHER) { const unsigned vv_[2] = {(nx) ? vAn[h][0] : vA[h][0], (nx) ? vAn[h][1] : vA[h][1]}; PG8_STAGE(bufoff, gbase, vv_); } \
;         else { PG8_STAGE(bufoff, (gbase) + (h) * hstep, voffA); } } while (0)
; #define PG8_LDA(dst, b, h) do { _Pragma("unroll") for (int m = 0; m < 4; ++m) _Pragma("unroll") for (int k = 0; k < 2; ++k) dst[m][k] = *(const PG8_LAS bf16x8*)(lds + PG8_SA(b, h) + aoff + m * 2048 + k * 1024); } while (0)
; #define PG8_LDB(dst, b, h) do { _Pragma("unroll") for (int n = 0; n < 2; ++n) _Pragma("unroll") for (int k = 0; k < 2; ++k) dst[n][k] = *(const PG8_LAS bf16x8*)(lds + PG8_SB(b, h) + boff + n * 2048 + k * 1024); } while (0)
; #define PG8_WAIT_V(n) asm volatile("s_waitcnt vmcnt(" #n ")" ::: "memory")
; #define PG8_WAIT_L(n) asm volatile("s_waitcnt lgkmcnt(" #n ")" ::: "memory")
; #define PG8_BAR __builtin_amdgcn_s_barrier()
; #define PG8_SCHED __builtin_amdgcn_sched_barrier(0)
;     ...
;             PG8_LDB(B0, 1, 0); PG8_LDB(B1, 1, 1); PG8_SCHED; PG8_LDA(At, 1, 0); PG8_STAGE_A(PG8_SA(0, 1), a2, 1, last);
;             PG8_WAIT_V(8); PG8_WAIT_L(0); PG8_BAR; PG8_MMA(0, 0, At, B0); PG8_MMA(0, 1, At, B1); PG8_BAR; PG8_SCHED;
;             PG8_LDA(At, 1, 1); PG8_STAGE(PG8_SB(1, 0), b3, voffB); PG8_STAGE(PG8_SB(1, 1), b3 + hstepB, voffB); PG8_STAGE_A(PG8_SA(1, 0), a3, 0, last);
;             PG8_WAIT_V(8); PG8_WAIT_L(0); PG8_BAR; PG8_MMA(1, 0, At, B0); PG8_MMA(1, 1, At, B1); PG8_BAR; PG8_SCHED;
	s_add_i32 s59, 0, 0x18000
	s_add_i32 s61, 0, 0x1c000
	v_add_u32_e32 v14, s59, v203
	v_add_u32_e32 v30, s61, v203
	ds_read_b128 v[2:5], v14
	ds_read_b128 v[6:9], v14 offset:1024
	ds_read_b128 v[10:13], v14 offset:2048
	ds_read_b128 v[14:17], v14 offset:3072
	ds_read_b128 v[18:21], v30
	ds_read_b128 v[22:25], v30 offset:1024
	ds_read_b128 v[26:29], v30 offset:2048
	ds_read_b128 v[30:33], v30 offset:3072
	s_add_u32 s66, s66, 0x20000
	s_addc_u32 s67, s67, 0
	s_mov_b32 m0, s84
	v_lshl_add_u64 v[196:197], s[66:67], 0, v[166:167]
	ds_read_b128 v[188:191], v207 offset:32768
	ds_read_b128 v[192:195], v207 offset:33792
	ds_read_b128 v[214:217], v207 offset:34816
	ds_read_b128 v[218:221], v207 offset:35840
	ds_read_b128 v[222:225], v207 offset:36864
	ds_read_b128 v[226:229], v207 offset:37888
	ds_read_b128 v[230:233], v207 offset:38912
	ds_read_b128 v[234:237], v207 offset:39936
	global_load_lds_dwordx4 v[196:197], off
	v_lshl_add_u64 v[196:197], s[66:67], 0, v[170:171]
	s_mov_b32 m0, s85
	s_nop 0
	global_load_lds_dwordx4 v[196:197], off
	s_waitcnt vmcnt(8)
	s_waitcnt lgkmcnt(0)
	s_barrier
	s_setprio 1
	s_nop 0
	s_waitcnt lgkmcnt(0)
	v_mfma_scale_f32_16x16x128_f8f6f4 v[158:161], v[2:9], v[188:195], v[158:161], v208, v209 op_sel_hi:[0,0,0]
	v_mfma_scale_f32_16x16x128_f8f6f4 v[154:157], v[10:17], v[188:195], v[154:157], v208, v209 op_sel_hi:[0,0,0]
	v_mfma_scale_f32_16x16x128_f8f6f4 v[142:145], v[2:9], v[214:221], v[142:145], v208, v209 op_sel_hi:[0,0,0]
	v_mfma_scale_f32_16x16x128_f8f6f4 v[138:141], v[10:17], v[214:221], v[138:141], v208, v209 op_sel_hi:[0,0,0]
	v_mfma_scale_f32_16x16x128_f8f6f4 v[126:129], v[2:9], v[222:229], v[126:129], v208, v209 op_sel_hi:[0,0,0]
	v_mfma_scale_f32_16x16x128_f8f6f4 v[122:125], v[10:17], v[222:229], v[122:125], v208, v209 op_sel_hi:[0,0,0]
	v_mfma_scale_f32_16x16x128_f8f6f4 v[110:113], v[2:9], v[230:237], v[110:113], v208, v209 op_sel_hi:[0,0,0]
	v_mfma_scale_f32_16x16x128_f8f6f4 v[106:109], v[10:17], v[230:237], v[106:109], v208, v209 op_sel_hi:[0,0,0]
	s_setprio 0
	s_setprio 1
	s_nop 0
	v_mfma_scale_f32_16x16x128_f8f6f4 v[150:153], v[18:25], v[188:195], v[150:153], v208, v209 op_sel_hi:[0,0,0]
	v_mfma_scale_f32_16x16x128_f8f6f4 v[146:149], v[26:33], v[188:195], v[146:149], v208, v209 op_sel_hi:[0,0,0]
	v_mfma_scale_f32_16x16x128_f8f6f4 v[134:137], v[18:25], v[214:221], v[134:137], v208, v209 op_sel_hi:[0,0,0]
	v_mfma_scale_f32_16x16x128_f8f6f4 v[130:133], v[26:33], v[214:221], v[130:133], v208, v209 op_sel_hi:[0,0,0]
	v_mfma_scale_f32_16x16x128_f8f6f4 v[118:121], v[18:25], v[222:229], v[118:121], v208, v209 op_sel_hi:[0,0,0]
	v_mfma_scale_f32_16x16x128_f8f6f4 v[114:117], v[26:33], v[222:229], v[114:117], v208, v209 op_sel_hi:[0,0,0]
	v_mfma_scale_f32_16x16x128_f8f6f4 v[102:105], v[18:25], v[230:237], v[102:105], v208, v209 op_sel_hi:[0,0,0]
	v_mfma_scale_f32_16x16x128_f8f6f4 v[98:101], v[26:33], v[230:237], v[98:101], v208, v209 op_sel_hi:[0,0,0]
	s_setprio 0
	s_barrier
	s_add_i32 s59, s59, s77
	v_lshl_add_u64 v[162:163], v[162:163], 0, s[40:41]
	s_mov_b32 m0, s59
	ds_read_b128 v[188:191], v207 offset:49152
	ds_read_b128 v[192:195], v207 offset:50176
	ds_read_b128 v[214:217], v207 offset:51200
	ds_read_b128 v[218:221], v207 offset:52224
	ds_read_b128 v[222:225], v207 offset:53248
	ds_read_b128 v[226:229], v207 offset:54272
	ds_read_b128 v[230:233], v207 offset:55296
	ds_read_b128 v[234:237], v207 offset:56320
	global_load_lds_dwordx4 v[162:163], off
	s_add_i32 m0, s59, 0x2000
	s_add_u32 s10, s10, 0x8080
	v_lshl_add_u64 v[162:163], v[164:165], 0, s[40:41]
	s_addc_u32 s11, s11, 0
	s_add_i32 s59, s61, s77
	global_load_lds_dwordx4 v[162:163], off
	v_lshl_add_u64 v[162:163], s[10:11], 0, v[168:169]
	s_mov_b32 m0, s59
	s_nop 0
	global_load_lds_dwordx4 v[162:163], off
	v_lshl_add_u64 v[162:163], s[10:11], 0, v[172:173]
	s_add_i32 m0, s59, 0x2000
	s_nop 0
	global_load_lds_dwordx4 v[162:163], off
	v_lshl_add_u64 v[162:163], v[184:185], 0, s[40:41]
	s_mov_b32 m0, s94
	s_nop 0
	global_load_lds_dwordx4 v[162:163], off
	v_lshl_add_u64 v[162:163], v[186:187], 0, s[40:41]
	s_mov_b32 m0, s95
	s_nop 0
	global_load_lds_dwordx4 v[162:163], off
	s_waitcnt vmcnt(8)
	s_waitcnt lgkmcnt(0)
	s_barrier
	s_setprio 1
	s_nop 0
	s_waitcnt lgkmcnt(0)
	v_mfma_scale_f32_16x16x128_f8f6f4 v[94:97], v[2:9], v[188:195], v[94:97], v208, v209 op_sel_hi:[0,0,0]
	v_mfma_scale_f32_16x16x128_f8f6f4 v[90:93], v[10:17], v[188:195], v[90:93], v208, v209 op_sel_hi:[0,0,0]
	v_mfma_scale_f32_16x16x128_f8f6f4 v[78:81], v[2:9], v[214:221], v[78:81], v208, v209 op_sel_hi:[0,0,0]
	v_mfma_scale_f32_16x16x128_f8f6f4 v[74:77], v[10:17], v[214:221], v[74:77], v208, v209 op_sel_hi:[0,0,0]
	v_mfma_scale_f32_16x16x128_f8f6f4 v[62:65], v[2:9], v[222:229], v[62:65], v208, v209 op_sel_hi:[0,0,0]
	v_mfma_scale_f32_16x16x128_f8f6f4 v[58:61], v[10:17], v[222:229], v[58:61], v208, v209 op_sel_hi:[0,0,0]
	v_mfma_scale_f32_16x16x128_f8f6f4 v[46:49], v[2:9], v[230:237], v[46:49], v208, v209 op_sel_hi:[0,0,0]
	v_mfma_scale_f32_16x16x128_f8f6f4 v[42:45], v[10:17], v[230:237], v[42:45], v208, v209 op_sel_hi:[0,0,0]
	s_setprio 0
	s_setprio 1
	s_nop 0
	v_mfma_scale_f32_16x16x128_f8f6f4 v[86:89], v[18:25], v[188:195], v[86:89], v208, v209 op_sel_hi:[0,0,0]
	v_mfma_scale_f32_16x16x128_f8f6f4 v[82:85], v[26:33], v[188:195], v[82:85], v208, v209 op_sel_hi:[0,0,0]
	v_mfma_scale_f32_16x16x128_f8f6f4 v[70:73], v[18:25], v[214:221], v[70:73], v208, v209 op_sel_hi:[0,0,0]
	v_mfma_scale_f32_16x16x128_f8f6f4 v[66:69], v[26:33], v[214:221], v[66:69], v208, v209 op_sel_hi:[0,0,0]
	v_mfma_scale_f32_16x16x128_f8f6f4 v[54:57], v[18:25], v[222:229], v[54:57], v208, v209 op_sel_hi:[0,0,0]
	v_mfma_scale_f32_16x16x128_f8f6f4 v[50:53], v[26:33], v[222:229], v[50:53], v208, v209 op_sel_hi:[0,0,0]
	v_mfma_scale_f32_16x16x128_f8f6f4 v[38:41], v[18:25], v[230:237], v[38:41], v208, v209 op_sel_hi:[0,0,0]
	v_mfma_scale_f32_16x16x128_f8f6f4 v[34:37], v[26:33], v[230:237], v[34:37], v208, v209 op_sel_hi:[0,0,0]
	s_setprio 0
	s_barrier
	s_add_i32 s33, s33, 2
	s_add_u32 s8, s8, 0x100
	s_addc_u32 s9, s9, 0
	s_add_u32 s18, s18, 0x100
	s_addc_u32 s19, s19, 0
; #define PG8_STAGE(bufoff, gbase, voff) do { _Pragma("unroll") for (int _i = 0; _i < 2; ++_i) \
;         __builtin_amdgcn_global_load_lds((const unsigned*)((const char*)(gbase) + (voff)[_i]), (PG8_LAS unsigned*)(lds + (bufoff) + ldsw + _i * 8192), 16, 0, 0); } while (0)
; #define PG8_STAGE_A(bufoff, gbase, h, nx) do { if constexpr (Sched::GATHER) { const unsigned vv_[2] = {(nx) ? vAn[h][0] : vA[h][0], (nx) ? vAn[h][1] : vA[h][1]}; PG8_STAGE(bufoff, gbase, vv_); } \
;         else { PG8_STAGE(bufoff, (gbase) + (h) * hstep, voffA); } } while (0)
; #define PG8_LDA(dst, b, h) do { _Pragma("unroll") for (int m = 0; m < 4; ++m) _Pragma("unroll") for (int k = 0; k < 2; ++k) dst[m][k] = *(const PG8_LAS bf16x8*)(lds + PG8_SA(b, h) + aoff + m * 2048 + k * 1024); } while (0)
; #define PG8_LDB(dst, b, h) do { _Pragma("unroll") for (int n = 0; n < 2; ++n) _Pragma("unroll") for (int k = 0; k < 2; ++k) dst[n][k] = *(const PG8_LAS bf16x8*)(lds + PG8_SB(b, h) + boff + n * 2048 + k * 1024); } while (0)
; #define PG8_WAIT_V(n) asm volatile("s_waitcnt vmcnt(" #n ")" ::: "memory")
; #define PG8_WAIT_L(n) asm volatile("s_waitcnt lgkmcnt(" #n ")" ::: "memory")
; #define PG8_BAR __builtin_amdgcn_s_barrier()
; #define PG8_SCHED __builtin_amdgcn_sched_barrier(0)
;     ...
;             const bool last = (t == nt - 2);
;             const char* a1 = cA + (size_t)(t + 1) * kstep;
;             const char* a2 = last ? nA : cA + (size_t)(t + 2) * kstep; const char* b2 = last ? nB : cB + (size_t)(t + 2) * kstep;
;             const char* a3 = a2 + kstep; const char* b3 = b2 + kstep;
;             if (last && has_next) S.a_ready(nxt);
;             if constexpr (SP2) {
;             PG8_LDB(B0, 0, 0); PG8_LDB(B1, 0, 1); PG8_SCHED; PG8_LDA(At, 0, 0); PG8_STAGE_A(PG8_SA(1, 1), a1, 1, false);
;             PG8_WAIT_V(8); PG8_WAIT_L(0); PG8_BAR; PG8_MMA(0, 0, At, B0); PG8_MMA(0, 1, At, B1); PG8_BAR; PG8_SCHED;
;             PG8_LDA(At, 0, 1); PG8_STAGE(PG8_SB(0, 0), b2, voffB); PG8_STAGE(PG8_SB(0, 1), b2 + hstepB, voffB); PG8_STAGE_A(PG8_SA(0, 0), a2, 0, last);
;             PG8_WAIT_V(8); PG8_WAIT_L(0); PG8_BAR; PG8_MMA(1, 0, At, B0); PG8_MMA(1, 1, At, B1); PG8_BAR; PG8_SCHED;
.LBB0_153:
	ds_read_b128 v[26:29], v205
	ds_read_b128 v[30:33], v205 offset:1024
	ds_read_b128 v[18:21], v205 offset:2048
	ds_read_b128 v[22:25], v205 offset:3072
	ds_read_b128 v[10:13], v206
	ds_read_b128 v[14:17], v206 offset:1024
	ds_read_b128 v[2:5], v206 offset:2048
	ds_read_b128 v[6:9], v206 offset:3072
	s_add_u32 s10, s8, 0xfffe0080
	s_addc_u32 s11, s9, -1
	s_cmp_eq_u32 s33, 4
	s_cselect_b32 s67, s0, s11
	s_cselect_b32 s66, s1, s10
	s_cselect_b32 s11, s5, s19
	s_cselect_b32 s10, s7, s18
	v_lshl_add_u64 v[162:163], s[8:9], 0, v[176:177]
	s_add_i32 m0, s82, 0xc000
	ds_read_b128 v[184:187], v207
	ds_read_b128 v[188:191], v207 offset:1024
	ds_read_b128 v[192:195], v207 offset:2048
	ds_read_b128 v[196:199], v207 offset:3072
	ds_read_b128 v[214:217], v207 offset:4096
	ds_read_b128 v[218:221], v207 offset:5120
	ds_read_b128 v[222:225], v207 offset:6144
	ds_read_b128 v[226:229], v207 offset:7168
	global_load_lds_dwordx4 v[162:163], off
	v_lshl_add_u64 v[162:163], s[8:9], 0, v[178:179]
	s_add_i32 m0, s82, 0xe000
	s_nop 0
	global_load_lds_dwordx4 v[162:163], off
	s_waitcnt vmcnt(8)
	s_waitcnt lgkmcnt(0)
	s_barrier
	s_setprio 1
	s_nop 0
	s_waitcnt lgkmcnt(0)
	v_mfma_scale_f32_16x16x128_f8f6f4 v[158:161], v[26:33], v[184:191], v[158:161], v208, v209 op_sel_hi:[0,0,0]
	v_mfma_scale_f32_16x16x128_f8f6f4 v[154:157], v[18:25], v[184:191], v[154:157], v208, v209 op_sel_hi:[0,0,0]
	v_mfma_scale_f32_16x16x128_f8f6f4 v[142:145], v[26:33], v[192:199], v[142:145], v208, v209 op_sel_hi:[0,0,0]
	v_mfma_scale_f32_16x16x128_f8f6f4 v[138:141], v[18:25], v[192:199], v[138:141], v208, v209 op_sel_hi:[0,0,0]
	v_mfma_scale_f32_16x16x128_f8f6f4 v[126:129], v[26:33], v[214:221], v[126:129], v208, v209 op_sel_hi:[0,0,0]
	v_mfma_scale_f32_16x16x128_f8f6f4 v[122:125], v[18:25], v[214:221], v[122:125], v208, v209 op_sel_hi:[0,0,0]
	v_mfma_scale_f32_16x16x128_f8f6f4 v[110:113], v[26:33], v[222:229], v[110:113], v208, v209 op_sel_hi:[0,0,0]
	v_mfma_scale_f32_16x16x128_f8f6f4 v[106:109], v[18:25], v[222:229], v[106:109], v208, v209 op_sel_hi:[0,0,0]
	s_setprio 0
	s_setprio 1
	s_nop 0
	v_mfma_scale_f32_16x16x128_f8f6f4 v[150:153], v[10:17], v[184:191], v[150:153], v208, v209 op_sel_hi:[0,0,0]
	v_mfma_scale_f32_16x16x128_f8f6f4 v[146:149], v[2:9], v[184:191], v[146:149], v208, v209 op_sel_hi:[0,0,0]
	v_mfma_scale_f32_16x16x128_f8f6f4 v[134:137], v[10:17], v[192:199], v[134:137], v208, v209 op_sel_hi:[0,0,0]
	v_mfma_scale_f32_16x16x128_f8f6f4 v[130:133], v[2:9], v[192:199], v[130:133], v208, v209 op_sel_hi:[0,0,0]
	v_mfma_scale_f32_16x16x128_f8f6f4 v[118:121], v[10:17], v[214:221], v[118:121], v208, v209 op_sel_hi:[0,0,0]
	v_mfma_scale_f32_16x16x128_f8f6f4 v[114:117], v[2:9], v[214:221], v[114:117], v208, v209 op_sel_hi:[0,0,0]
	v_mfma_scale_f32_16x16x128_f8f6f4 v[102:105], v[10:17], v[222:229], v[102:105], v208, v209 op_sel_hi:[0,0,0]
	v_mfma_scale_f32_16x16x128_f8f6f4 v[98:101], v[2:9], v[222:229], v[98:101], v208, v209 op_sel_hi:[0,0,0]
	s_setprio 0
	s_barrier
	s_add_i32 s59, s96, s77
	v_lshl_add_u64 v[162:163], s[10:11], 0, v[168:169]
	s_mov_b32 m0, s59
	ds_read_b128 v[188:191], v207 offset:16384
	ds_read_b128 v[192:195], v207 offset:17408
	ds_read_b128 v[214:217], v207 offset:18432
	ds_read_b128 v[218:221], v207 offset:19456
	ds_read_b128 v[222:225], v207 offset:20480
	ds_read_b128 v[226:229], v207 offset:21504
	ds_read_b128 v[230:233], v207 offset:22528
	ds_read_b128 v[234:237], v207 offset:23552
	global_load_lds_dwordx4 v[162:163], off
	s_add_i32 m0, s59, 0x2000
	s_add_u32 s68, s10, 0x8000
	v_lshl_add_u64 v[164:165], s[10:11], 0, v[172:173]
	s_addc_u32 s69, s11, 0
	s_add_i32 s59, s97, s77
	global_load_lds_dwordx4 v[164:165], off
	v_lshl_add_u64 v[184:185], s[68:69], 0, v[168:169]
	s_mov_b32 m0, s59
	v_lshl_add_u64 v[186:187], s[66:67], 0, v[170:171]
	global_load_lds_dwordx4 v[184:185], off
	v_lshl_add_u64 v[184:185], s[68:69], 0, v[172:173]
	s_add_i32 m0, s59, 0x2000
	s_nop 0
	global_load_lds_dwordx4 v[184:185], off
	v_lshl_add_u64 v[184:185], s[66:67], 0, v[166:167]
	s_mov_b32 m0, s82
	s_nop 0
	global_load_lds_dwordx4 v[184:185], off
	s_mov_b32 m0, s83
	s_nop 0
	global_load_lds_dwordx4 v[186:187], off
	s_waitcnt vmcnt(8)
	s_waitcnt lgkmcnt(0)
	s_barrier
	s_setprio 1
	s_nop 0
	s_waitcnt lgkmcnt(0)
	v_mfma_scale_f32_16x16x128_f8f6f4 v[94:97], v[26:33], v[188:195], v[94:97], v208, v209 op_sel_hi:[0,0,0]
	v_mfma_scale_f32_16x16x128_f8f6f4 v[90:93], v[18:25], v[188:195], v[90:93], v208, v209 op_sel_hi:[0,0,0]
	v_mfma_scale_f32_16x16x128_f8f6f4 v[78:81], v[26:33], v[214:221], v[78:81], v208, v209 op_sel_hi:[0,0,0]
	v_mfma_scale_f32_16x16x128_f8f6f4 v[74:77], v[18:25], v[214:221], v[74:77], v208, v209 op_sel_hi:[0,0,0]
	v_mfma_scale_f32_16x16x128_f8f6f4 v[62:65], v[26:33], v[222:229], v[62:65], v208, v209 op_sel_hi:[0,0,0]
	v_mfma_scale_f32_16x16x128_f8f6f4 v[58:61], v[18:25], v[222:229], v[58:61], v208, v209 op_sel_hi:[0,0,0]
	v_mfma_scale_f32_16x16x128_f8f6f4 v[46:49], v[26:33], v[230:237], v[46:49], v208, v209 op_sel_hi:[0,0,0]
	v_mfma_scale_f32_16x16x128_f8f6f4 v[42:45], v[18:25], v[230:237], v[42:45], v208, v209 op_sel_hi:[0,0,0]
	s_setprio 0
	s_setprio 1
	s_nop 0
	v_mfma_scale_f32_16x16x128_f8f6f4 v[86:89], v[10:17], v[188:195], v[86:89], v208, v209 op_sel_hi:[0,0,0]
	v_mfma_scale_f32_16x16x128_f8f6f4 v[82:85], v[2:9], v[188:195], v[82:85], v208, v209 op_sel_hi:[0,0,0]
	v_mfma_scale_f32_16x16x128_f8f6f4 v[70:73], v[10:17], v[214:221], v[70:73], v208, v209 op_sel_hi:[0,0,0]
	v_mfma_scale_f32_16x16x128_f8f6f4 v[66:69], v[2:9], v[214:221], v[66:69], v208, v209 op_sel_hi:[0,0,0]
	v_mfma_scale_f32_16x16x128_f8f6f4 v[54:57], v[10:17], v[222:229], v[54:57], v208, v209 op_sel_hi:[0,0,0]
	v_mfma_scale_f32_16x16x128_f8f6f4 v[50:53], v[2:9], v[222:229], v[50:53], v208, v209 op_sel_hi:[0,0,0]
	v_mfma_scale_f32_16x16x128_f8f6f4 v[38:41], v[10:17], v[230:237], v[38:41], v208, v209 op_sel_hi:[0,0,0]
	v_mfma_scale_f32_16x16x128_f8f6f4 v[34:37], v[2:9], v[230:237], v[34:37], v208, v209 op_sel_hi:[0,0,0]
	s_setprio 0
	s_barrier
; #define PG8_STAGE(bufoff, gbase, voff) do { _Pragma("unroll") for (int _i = 0; _i < 2; ++_i) \
;         __builtin_amdgcn_global_load_lds((const unsigned*)((const char*)(gbase) + (voff)[_i]), (PG8_LAS unsigned*)(lds + (bufoff) + ldsw + _i * 8192), 16, 0, 0); } while (0)
; #define PG8_STAGE_A(bufoff, gbase, h, nx) do { if constexpr (Sched::GATHER) { const unsigned vv_[2] = {(nx) ? vAn[h][0] : vA[h][0], (nx) ? vAn[h][1] : vA[h][1]}; PG8_STAGE(bufoff, gbase, vv_); } \
;         else { PG8_STAGE(bufoff, (gbase) + (h) * hstep, voffA); } } while (0)
; #define PG8_LDA(dst, b, h) do { _Pragma("unroll") for (int m = 0; m < 4; ++m) _Pragma("unroll") for (int k = 0; k < 2; ++k) dst[m][k] = *(const PG8_LAS bf16x8*)(lds + PG8_SA(b, h) + aoff + m * 2048 + k * 1024); } while (0)
; #define PG8_LDB(dst, b, h) do { _Pragma("unroll") for (int n = 0; n < 2; ++n) _Pragma("unroll") for (int k = 0; k < 2; ++k) dst[n][k] = *(const PG8_LAS bf16x8*)(lds + PG8_SB(b, h) + boff + n * 2048 + k * 1024); } while (0)
; #define PG8_WAIT_V(n) asm volatile("s_waitcnt vmcnt(" #n ")" ::: "memory")
; #define PG8_WAIT_L(n) asm volatile("s_waitcnt lgkmcnt(" #n ")" ::: "memory")
; #define PG8_BAR __builtin_amdgcn_s_barrier()
; #define PG8_SCHED __builtin_amdgcn_sched_barrier(0)
;     ...
;         for (int t = 0; t < nt; t += 2) {
;     ...
;             PG8_LDB(B0, 1, 0); PG8_LDB(B1, 1, 1); PG8_SCHED; PG8_LDA(At, 1, 0); PG8_STAGE_A(PG8_SA(0, 1), a2, 1, last);
;             PG8_WAIT_V(8); PG8_WAIT_L(0); PG8_BAR; PG8_MMA(0, 0, At, B0); PG8_MMA(0, 1, At, B1); PG8_BAR; PG8_SCHED;
;             PG8_LDA(At, 1, 1); PG8_STAGE(PG8_SB(1, 0), b3, voffB); PG8_STAGE(PG8_SB(1, 1), b3 + hstepB, voffB); PG8_STAGE_A(PG8_SA(1, 0), a3, 0, last);
;             PG8_WAIT_V(8); PG8_WAIT_L(0); PG8_BAR; PG8_MMA(1, 0, At, B0); PG8_MMA(1, 1, At, B1); PG8_BAR; PG8_SCHED;
	s_add_i32 s59, 0, 0x18000
	s_add_i32 s61, 0, 0x1c000
	v_add_u32_e32 v14, s59, v203
	v_add_u32_e32 v30, s61, v203
	ds_read_b128 v[2:5], v14
	ds_read_b128 v[6:9], v14 offset:1024
	ds_read_b128 v[10:13], v14 offset:2048
	ds_read_b128 v[14:17], v14 offset:3072
	ds_read_b128 v[18:21], v30
	ds_read_b128 v[22:25], v30 offset:1024
	ds_read_b128 v[26:29], v30 offset:2048
	ds_read_b128 v[30:33], v30 offset:3072
	s_add_u32 s66, s66, 0x20000
	s_addc_u32 s67, s67, 0
	s_mov_b32 m0, s84
	v_lshl_add_u64 v[196:197], s[66:67], 0, v[166:167]
	ds_read_b128 v[188:191], v207 offset:32768
	ds_read_b128 v[192:195], v207 offset:33792
	ds_read_b128 v[214:217], v207 offset:34816
	ds_read_b128 v[218:221], v207 offset:35840
	ds_read_b128 v[222:225], v207 offset:36864
	ds_read_b128 v[226:229], v207 offset:37888
	ds_read_b128 v[230:233], v207 offset:38912
	ds_read_b128 v[234:237], v207 offset:39936
	global_load_lds_dwordx4 v[196:197], off
	v_lshl_add_u64 v[196:197], s[66:67], 0, v[170:171]
	s_mov_b32 m0, s85
	s_nop 0
	global_load_lds_dwordx4 v[196:197], off
	s_waitcnt vmcnt(8)
	s_waitcnt lgkmcnt(0)
	s_barrier
	s_setprio 1
	s_nop 0
	s_waitcnt lgkmcnt(0)
	v_mfma_scale_f32_16x16x128_f8f6f4 v[158:161], v[2:9], v[188:195], v[158:161], v208, v209 op_sel_hi:[0,0,0]
	v_mfma_scale_f32_16x16x128_f8f6f4 v[154:157], v[10:17], v[188:195], v[154:157], v208, v209 op_sel_hi:[0,0,0]
	v_mfma_scale_f32_16x16x128_f8f6f4 v[142:145], v[2:9], v[214:221], v[142:145], v208, v209 op_sel_hi:[0,0,0]
	v_mfma_scale_f32_16x16x128_f8f6f4 v[138:141], v[10:17], v[214:221], v[138:141], v208, v209 op_sel_hi:[0,0,0]
	v_mfma_scale_f32_16x16x128_f8f6f4 v[126:129], v[2:9], v[222:229], v[126:129], v208, v209 op_sel_hi:[0,0,0]
	v_mfma_scale_f32_16x16x128_f8f6f4 v[122:125], v[10:17], v[222:229], v[122:125], v208, v209 op_sel_hi:[0,0,0]
	v_mfma_scale_f32_16x16x128_f8f6f4 v[110:113], v[2:9], v[230:237], v[110:113], v208, v209 op_sel_hi:[0,0,0]
	v_mfma_scale_f32_16x16x128_f8f6f4 v[106:109], v[10:17], v[230:237], v[106:109], v208, v209 op_sel_hi:[0,0,0]
	s_setprio 0
	s_setprio 1
	s_nop 0
	v_mfma_scale_f32_16x16x128_f8f6f4 v[150:153], v[18:25], v[188:195], v[150:153], v208, v209 op_sel_hi:[0,0,0]
	v_mfma_scale_f32_16x16x128_f8f6f4 v[146:149], v[26:33], v[188:195], v[146:149], v208, v209 op_sel_hi:[0,0,0]
	v_mfma_scale_f32_16x16x128_f8f6f4 v[134:137], v[18:25], v[214:221], v[134:137], v208, v209 op_sel_hi:[0,0,0]
	v_mfma_scale_f32_16x16x128_f8f6f4 v[130:133], v[26:33], v[214:221], v[130:133], v208, v209 op_sel_hi:[0,0,0]
	v_mfma_scale_f32_16x16x128_f8f6f4 v[118:121], v[18:25], v[222:229], v[118:121], v208, v209 op_sel_hi:[0,0,0]
	v_mfma_scale_f32_16x16x128_f8f6f4 v[114:117], v[26:33], v[222:229], v[114:117], v208, v209 op_sel_hi:[0,0,0]
	v_mfma_scale_f32_16x16x128_f8f6f4 v[102:105], v[18:25], v[230:237], v[102:105], v208, v209 op_sel_hi:[0,0,0]
	v_mfma_scale_f32_16x16x128_f8f6f4 v[98:101], v[26:33], v[230:237], v[98:101], v208, v209 op_sel_hi:[0,0,0]
	s_setprio 0
	s_barrier
	s_add_i32 s59, s59, s77
	v_lshl_add_u64 v[162:163], v[162:163], 0, s[40:41]
	s_mov_b32 m0, s59
	ds_read_b128 v[188:191], v207 offset:49152
	ds_read_b128 v[192:195], v207 offset:50176
	ds_read_b128 v[214:217], v207 offset:51200
	ds_read_b128 v[218:221], v207 offset:52224
	ds_read_b128 v[222:225], v207 offset:53248
	ds_read_b128 v[226:229], v207 offset:54272
	ds_read_b128 v[230:233], v207 offset:55296
	ds_read_b128 v[234:237], v207 offset:56320
	global_load_lds_dwordx4 v[162:163], off
	s_add_i32 m0, s59, 0x2000
	s_add_u32 s10, s10, 0x8080
	v_lshl_add_u64 v[162:163], v[164:165], 0, s[40:41]
	s_addc_u32 s11, s11, 0
	s_add_i32 s59, s61, s77
	global_load_lds_dwordx4 v[162:163], off
	v_lshl_add_u64 v[162:163], s[10:11], 0, v[168:169]
	s_mov_b32 m0, s59
	s_nop 0
	global_load_lds_dwordx4 v[162:163], off
	v_lshl_add_u64 v[162:163], s[10:11], 0, v[172:173]
	s_add_i32 m0, s59, 0x2000
	s_nop 0
	global_load_lds_dwordx4 v[162:163], off
	v_lshl_add_u64 v[162:163], v[184:185], 0, s[40:41]
	s_mov_b32 m0, s94
	s_nop 0
	global_load_lds_dwordx4 v[162:163], off
	v_lshl_add_u64 v[162:163], v[186:187], 0, s[40:41]
	s_mov_b32 m0, s95
	s_nop 0
	global_load_lds_dwordx4 v[162:163], off
	s_waitcnt vmcnt(8)
	s_waitcnt lgkmcnt(0)
	s_barrier
	s_setprio 1
	s_nop 0
	s_waitcnt lgkmcnt(0)
	v_mfma_scale_f32_16x16x128_f8f6f4 v[94:97], v[2:9], v[188:195], v[94:97], v208, v209 op_sel_hi:[0,0,0]
	v_mfma_scale_f32_16x16x128_f8f6f4 v[90:93], v[10:17], v[188:195], v[90:93], v208, v209 op_sel_hi:[0,0,0]
	v_mfma_scale_f32_16x16x128_f8f6f4 v[78:81], v[2:9], v[214:221], v[78:81], v208, v209 op_sel_hi:[0,0,0]
	v_mfma_scale_f32_16x16x128_f8f6f4 v[74:77], v[10:17], v[214:221], v[74:77], v208, v209 op_sel_hi:[0,0,0]
	v_mfma_scale_f32_16x16x128_f8f6f4 v[62:65], v[2:9], v[222:229], v[62:65], v208, v209 op_sel_hi:[0,0,0]
	v_mfma_scale_f32_16x16x128_f8f6f4 v[58:61], v[10:17], v[222:229], v[58:61], v208, v209 op_sel_hi:[0,0,0]
	v_mfma_scale_f32_16x16x128_f8f6f4 v[46:49], v[2:9], v[230:237], v[46:49], v208, v209 op_sel_hi:[0,0,0]
	v_mfma_scale_f32_16x16x128_f8f6f4 v[42:45], v[10:17], v[230:237], v[42:45], v208, v209 op_sel_hi:[0,0,0]
	s_setprio 0
	s_setprio 1
	s_nop 0
	v_mfma_scale_f32_16x16x128_f8f6f4 v[86:89], v[18:25], v[188:195], v[86:89], v208, v209 op_sel_hi:[0,0,0]
	v_mfma_scale_f32_16x16x128_f8f6f4 v[82:85], v[26:33], v[188:195], v[82:85], v208, v209 op_sel_hi:[0,0,0]
	v_mfma_scale_f32_16x16x128_f8f6f4 v[70:73], v[18:25], v[214:221], v[70:73], v208, v209 op_sel_hi:[0,0,0]
	v_mfma_scale_f32_16x16x128_f8f6f4 v[66:69], v[26:33], v[214:221], v[66:69], v208, v209 op_sel_hi:[0,0,0]
	v_mfma_scale_f32_16x16x128_f8f6f4 v[54:57], v[18:25], v[222:229], v[54:57], v208, v209 op_sel_hi:[0,0,0]
	v_mfma_scale_f32_16x16x128_f8f6f4 v[50:53], v[26:33], v[222:229], v[50:53], v208, v209 op_sel_hi:[0,0,0]
	v_mfma_scale_f32_16x16x128_f8f6f4 v[38:41], v[18:25], v[230:237], v[38:41], v208, v209 op_sel_hi:[0,0,0]
	v_mfma_scale_f32_16x16x128_f8f6f4 v[34:37], v[26:33], v[230:237], v[34:37], v208, v209 op_sel_hi:[0,0,0]
	s_setprio 0
	s_barrier
	s_add_i32 s33, s33, 2
	s_add_u32 s8, s8, 0x100
	s_addc_u32 s9, s9, 0
	s_add_u32 s18, s18, 0x100
	s_addc_u32 s19, s19, 0
	s_cmp_gt_u32 s33, 5
	s_cbranch_scc0 .LBB0_153
	s_and_b64 vcc, exec, s[42:43]
	s_cbranch_vccz .LBB0_156
	s_barrier

; #define PG8_STAGE(bufoff, gbase, voff) do { _Pragma("unroll") for (int _i = 0; _i < 2; ++_i) \
;         __builtin_amdgcn_global_load_lds((const unsigned*)((const char*)(gbase) + (voff)[_i]), (PG8_LAS unsigned*)(lds + (bufoff) + ldsw + _i * 8192), 16, 0, 0); } while (0)
; #define PG8_STAGE_A(bufoff, gbase, h, nx) do { if constexpr (Sched::GATHER) { const unsigned vv_[2] = {(nx) ? vAn[h][0] : vA[h][0], (nx) ? vAn[h][1] : vA[h][1]}; PG8_STAGE(bufoff, gbase, vv_); } \
;         else { PG8_STAGE(bufoff, (gbase) + (h) * hstep, voffA); } } while (0)
; #define PG8_LDA(dst, b, h) do { _Pragma("unroll") for (int m = 0; m < 4; ++m) _Pragma("unroll") for (int k = 0; k < 2; ++k) dst[m][k] = *(const PG8_LAS bf16x8*)(lds + PG8_SA(b, h) + aoff + m * 2048 + k * 1024); } while (0)
; #define PG8_WAIT_V(n) asm volatile("s_waitcnt vmcnt(" #n ")" ::: "memory")
; #define PG8_WAIT_L(n) asm volatile("s_waitcnt lgkmcnt(" #n ")" ::: "memory")
;     ...
;         const bool has_next = S.next(ui + 1, nxt);
;         const char* nA = Sched::GATHER ? cA : (has_next ? (const char*)g.A + (size_t)nxt.pm * tstep : cA);
;         if constexpr (Sched::GATHER) { if (has_next) { PG8_AOFF(vAn, ui + 1); } else { _Pragma("unroll") for (int h_ = 0; h_ < 2; ++h_) _Pragma("unroll") for (int i_ = 0; i_ < 2; ++i_) vAn[h_][i_] = vA[h_][i_]; } } const char* nB = has_next ? (const char*)g.Bt + (size_t)nxt.pb * tstep : cB;
; #pragma nounroll
;         for (int t = 0; t < nt; t += 2) {
;             const bool last = (t == nt - 2);
;             const char* a1 = cA + (size_t)(t + 1) * kstep;
;             const char* a2 = last ? nA : cA + (size_t)(t + 2) * kstep; const char* b2 = last ? nB : cB + (size_t)(t + 2) * kstep;
;             const char* a3 = a2 + kstep; const char* b3 = b2 + kstep;
;             if (last && has_next) S.a_ready(nxt);
;             if constexpr (SP2) {
;             PG8_LDB(B0, 0, 0); PG8_LDB(B1, 0, 1); PG8_SCHED; PG8_LDA(At, 0, 0); PG8_STAGE_A(PG8_SA(1, 1), a1, 1, false);
;             PG8_WAIT_V(8); PG8_WAIT_L(0); PG8_BAR; PG8_MMA(0, 0, At, B0); PG8_MMA(0, 1, At, B1); PG8_BAR; PG8_SCHED;
;             PG8_LDA(At, 0, 1); PG8_STAGE(PG8_SB(0, 0), b2, voffB); PG8_STAGE(PG8_SB(0, 1), b2 + hstepB, voffB); PG8_STAGE_A(PG8_SA(0, 0), a2, 0, last);
;             PG8_WAIT_V(8); PG8_WAIT_L(0); PG8_BAR; PG8_MMA(1, 0, At, B0); PG8_MMA(1, 1, At, B1); PG8_BAR; PG8_SCHED;
.LBB0_473:
	s_ashr_i32 s15, s14, 31
	s_lshl_b64 s[16:17], s[14:15], 18
	v_readlane_b32 s18, v255, 21
	v_readlane_b32 s19, v255, 22
	s_add_u32 s16, s18, s16
	s_addc_u32 s17, s19, s17
	s_and_b64 s[18:19], s[2:3], exec
	s_cselect_b32 s1, s17, s23
	s_cselect_b32 s15, s16, s22
	s_ashr_i32 s13, s12, 31
	s_lshl_b64 s[18:19], s[12:13], 18
	v_readlane_b32 s26, v254, 53
	v_readlane_b32 s27, v254, 54
	s_add_u32 s18, s26, s18
	s_addc_u32 s19, s27, s19
	s_and_b64 s[26:27], s[2:3], exec
	s_cselect_b32 s13, s19, s25
	s_cselect_b32 s21, s18, s24
	s_add_u32 s22, s22, 0x20080
	s_addc_u32 s23, s23, 0
	s_add_u32 s33, s24, 0x100
	s_addc_u32 s42, s25, 0
	s_mov_b32 s43, -2
	ds_read_b128 v[26:29], v188
	ds_read_b128 v[30:33], v188 offset:1024
	ds_read_b128 v[18:21], v188 offset:2048
	ds_read_b128 v[22:25], v188 offset:3072
	ds_read_b128 v[10:13], v189
	ds_read_b128 v[14:17], v189 offset:1024
	ds_read_b128 v[2:5], v189 offset:2048
	ds_read_b128 v[6:9], v189 offset:3072
	s_add_u32 s24, s22, 0xfffe0080
	s_addc_u32 s25, s23, -1
	s_cmp_eq_u32 s43, 4
	s_cselect_b32 s27, s1, s25
	s_cselect_b32 s26, s15, s24
	s_cselect_b32 s25, s13, s42
	s_cselect_b32 s24, s21, s33
	v_lshl_add_u64 v[218:219], s[22:23], 0, v[170:171]
	s_add_i32 m0, s30, 0xc000
	ds_read_b128 v[178:181], v190
	ds_read_b128 v[182:185], v190 offset:1024
	ds_read_b128 v[194:197], v190 offset:2048
	ds_read_b128 v[198:201], v190 offset:3072
	ds_read_b128 v[202:205], v190 offset:4096
	ds_read_b128 v[206:209], v190 offset:5120
	ds_read_b128 v[210:213], v190 offset:6144
	ds_read_b128 v[214:217], v190 offset:7168
	global_load_lds_dwordx4 v[218:219], off
	v_lshl_add_u64 v[218:219], s[22:23], 0, v[172:173]
	s_add_i32 m0, s30, 0xe000
	s_nop 0
	global_load_lds_dwordx4 v[218:219], off
	s_waitcnt vmcnt(8)
	s_waitcnt lgkmcnt(0)
	s_barrier
	s_setprio 1
	s_nop 0
	s_waitcnt lgkmcnt(0)
	v_mfma_scale_f32_16x16x128_f8f6f4 v[158:161], v[26:33], v[178:185], 0, v191, v192 op_sel_hi:[0,0,0]
	v_mfma_scale_f32_16x16x128_f8f6f4 v[154:157], v[18:25], v[178:185], 0, v191, v192 op_sel_hi:[0,0,0]
	v_mfma_scale_f32_16x16x128_f8f6f4 v[142:145], v[26:33], v[194:201], 0, v191, v192 op_sel_hi:[0,0,0]
	v_mfma_scale_f32_16x16x128_f8f6f4 v[138:141], v[18:25], v[194:201], 0, v191, v192 op_sel_hi:[0,0,0]
	v_mfma_scale_f32_16x16x128_f8f6f4 v[126:129], v[26:33], v[202:209], 0, v191, v192 op_sel_hi:[0,0,0]
	v_mfma_scale_f32_16x16x128_f8f6f4 v[122:125], v[18:25], v[202:209], 0, v191, v192 op_sel_hi:[0,0,0]
	v_mfma_scale_f32_16x16x128_f8f6f4 v[110:113], v[26:33], v[210:217], 0, v191, v192 op_sel_hi:[0,0,0]
	v_mfma_scale_f32_16x16x128_f8f6f4 v[106:109], v[18:25], v[210:217], 0, v191, v192 op_sel_hi:[0,0,0]
	s_setprio 0
	s_setprio 1
	s_nop 0
	v_mfma_scale_f32_16x16x128_f8f6f4 v[150:153], v[10:17], v[178:185], 0, v191, v192 op_sel_hi:[0,0,0]
	v_mfma_scale_f32_16x16x128_f8f6f4 v[146:149], v[2:9], v[178:185], 0, v191, v192 op_sel_hi:[0,0,0]
	v_mfma_scale_f32_16x16x128_f8f6f4 v[134:137], v[10:17], v[194:201], 0, v191, v192 op_sel_hi:[0,0,0]
	v_mfma_scale_f32_16x16x128_f8f6f4 v[130:133], v[2:9], v[194:201], 0, v191, v192 op_sel_hi:[0,0,0]
	v_mfma_scale_f32_16x16x128_f8f6f4 v[118:121], v[10:17], v[202:209], 0, v191, v192 op_sel_hi:[0,0,0]
	v_mfma_scale_f32_16x16x128_f8f6f4 v[114:117], v[2:9], v[202:209], 0, v191, v192 op_sel_hi:[0,0,0]
	v_mfma_scale_f32_16x16x128_f8f6f4 v[102:105], v[10:17], v[210:217], 0, v191, v192 op_sel_hi:[0,0,0]
	v_mfma_scale_f32_16x16x128_f8f6f4 v[98:101], v[2:9], v[210:217], 0, v191, v192 op_sel_hi:[0,0,0]
	s_setprio 0
	s_barrier
	s_add_i32 s44, s40, s28
	v_lshl_add_u64 v[178:179], s[24:25], 0, v[164:165]
	s_mov_b32 m0, s44
	ds_read_b128 v[194:197], v190 offset:16384
	ds_read_b128 v[198:201], v190 offset:17408
	ds_read_b128 v[202:205], v190 offset:18432
	ds_read_b128 v[206:209], v190 offset:19456
	ds_read_b128 v[210:213], v190 offset:20480
	ds_read_b128 v[214:217], v190 offset:21504
	ds_read_b128 v[218:221], v190 offset:22528
	ds_read_b128 v[222:225], v190 offset:23552
	global_load_lds_dwordx4 v[178:179], off
	s_add_i32 m0, s44, 0x2000
	s_add_u32 s44, s24, 0x2000
	v_lshl_add_u64 v[180:181], s[24:25], 0, v[168:169]
	s_addc_u32 s45, s25, 0
	s_add_i32 s46, s41, s28
	global_load_lds_dwordx4 v[180:181], off
	v_lshl_add_u64 v[182:183], s[44:45], 0, v[164:165]
	s_mov_b32 m0, s46
	v_lshl_add_u64 v[184:185], s[26:27], 0, v[166:167]
	global_load_lds_dwordx4 v[182:183], off
	v_lshl_add_u64 v[182:183], s[44:45], 0, v[168:169]
	s_add_i32 m0, s46, 0x2000
	s_nop 0
	global_load_lds_dwordx4 v[182:183], off
	v_lshl_add_u64 v[182:183], s[26:27], 0, v[162:163]
	s_mov_b32 m0, s30
	s_nop 0
	global_load_lds_dwordx4 v[182:183], off
	s_mov_b32 m0, s31
	s_nop 0
	global_load_lds_dwordx4 v[184:185], off
	s_waitcnt vmcnt(8)
	s_waitcnt lgkmcnt(0)
	s_barrier
	s_setprio 1
	s_nop 0
	s_waitcnt lgkmcnt(0)
	v_mfma_scale_f32_16x16x128_f8f6f4 v[94:97], v[26:33], v[194:201], 0, v191, v192 op_sel_hi:[0,0,0]
	v_mfma_scale_f32_16x16x128_f8f6f4 v[90:93], v[18:25], v[194:201], 0, v191, v192 op_sel_hi:[0,0,0]
	v_mfma_scale_f32_16x16x128_f8f6f4 v[78:81], v[26:33], v[202:209], 0, v191, v192 op_sel_hi:[0,0,0]
	v_mfma_scale_f32_16x16x128_f8f6f4 v[74:77], v[18:25], v[202:209], 0, v191, v192 op_sel_hi:[0,0,0]
	v_mfma_scale_f32_16x16x128_f8f6f4 v[62:65], v[26:33], v[210:217], 0, v191, v192 op_sel_hi:[0,0,0]
	v_mfma_scale_f32_16x16x128_f8f6f4 v[58:61], v[18:25], v[210:217], 0, v191, v192 op_sel_hi:[0,0,0]
	v_mfma_scale_f32_16x16x128_f8f6f4 v[46:49], v[26:33], v[218:225], 0, v191, v192 op_sel_hi:[0,0,0]
	v_mfma_scale_f32_16x16x128_f8f6f4 v[42:45], v[18:25], v[218:225], 0, v191, v192 op_sel_hi:[0,0,0]
	s_setprio 0
	s_setprio 1
	s_nop 0
	v_mfma_scale_f32_16x16x128_f8f6f4 v[86:89], v[10:17], v[194:201], 0, v191, v192 op_sel_hi:[0,0,0]
	v_mfma_scale_f32_16x16x128_f8f6f4 v[82:85], v[2:9], v[194:201], 0, v191, v192 op_sel_hi:[0,0,0]
	v_mfma_scale_f32_16x16x128_f8f6f4 v[70:73], v[10:17], v[202:209], 0, v191, v192 op_sel_hi:[0,0,0]
	v_mfma_scale_f32_16x16x128_f8f6f4 v[66:69], v[2:9], v[202:209], 0, v191, v192 op_sel_hi:[0,0,0]
	v_mfma_scale_f32_16x16x128_f8f6f4 v[54:57], v[10:17], v[210:217], 0, v191, v192 op_sel_hi:[0,0,0]
	v_mfma_scale_f32_16x16x128_f8f6f4 v[50:53], v[2:9], v[210:217], 0, v191, v192 op_sel_hi:[0,0,0]
	v_mfma_scale_f32_16x16x128_f8f6f4 v[38:41], v[10:17], v[218:225], 0, v191, v192 op_sel_hi:[0,0,0]
	v_mfma_scale_f32_16x16x128_f8f6f4 v[34:37], v[2:9], v[218:225], 0, v191, v192 op_sel_hi:[0,0,0]
	s_setprio 0
	s_barrier
; #define PG8_STAGE(bufoff, gbase, voff) do { _Pragma("unroll") for (int _i = 0; _i < 2; ++_i) \
;         __builtin_amdgcn_global_load_lds((const unsigned*)((const char*)(gbase) + (voff)[_i]), (PG8_LAS unsigned*)(lds + (bufoff) + ldsw + _i * 8192), 16, 0, 0); } while (0)
; #define PG8_STAGE_A(bufoff, gbase, h, nx) do { if constexpr (Sched::GATHER) { const unsigned vv_[2] = {(nx) ? vAn[h][0] : vA[h][0], (nx) ? vAn[h][1] : vA[h][1]}; PG8_STAGE(bufoff, gbase, vv_); } \
;         else { PG8_STAGE(bufoff, (gbase) + (h) * hstep, voffA); } } while (0)
; #define PG8_LDA(dst, b, h) do { _Pragma("unroll") for (int m = 0; m < 4; ++m) _Pragma("unroll") for (int k = 0; k < 2; ++k) dst[m][k] = *(const PG8_LAS bf16x8*)(lds + PG8_SA(b, h) + aoff + m * 2048 + k * 1024); } while (0)
; #define PG8_LDB(dst, b, h) do { _Pragma("unroll") for (int n = 0; n < 2; ++n) _Pragma("unroll") for (int k = 0; k < 2; ++k) dst[n][k] = *(const PG8_LAS bf16x8*)(lds + PG8_SB(b, h) + boff + n * 2048 + k * 1024); } while (0)
; #define PG8_WAIT_V(n) asm volatile("s_waitcnt vmcnt(" #n ")" ::: "memory")
; #define PG8_WAIT_L(n) asm volatile("s_waitcnt lgkmcnt(" #n ")" ::: "memory")
; #define PG8_BAR __builtin_amdgcn_s_barrier()
; #define PG8_SCHED __builtin_amdgcn_sched_barrier(0)
;     ...
;             PG8_LDB(B0, 1, 0); PG8_LDB(B1, 1, 1); PG8_SCHED; PG8_LDA(At, 1, 0); PG8_STAGE_A(PG8_SA(0, 1), a2, 1, last);
;             PG8_WAIT_V(8); PG8_WAIT_L(0); PG8_BAR; PG8_MMA(0, 0, At, B0); PG8_MMA(0, 1, At, B1); PG8_BAR; PG8_SCHED;
;             PG8_LDA(At, 1, 1); PG8_STAGE(PG8_SB(1, 0), b3, voffB); PG8_STAGE(PG8_SB(1, 1), b3 + hstepB, voffB); PG8_STAGE_A(PG8_SA(1, 0), a3, 0, last);
;             PG8_WAIT_V(8); PG8_WAIT_L(0); PG8_BAR; PG8_MMA(1, 0, At, B0); PG8_MMA(1, 1, At, B1); PG8_BAR; PG8_SCHED;
	s_add_i32 s44, 0, 0x18000
	s_add_i32 s45, 0, 0x1c000
	v_add_u32_e32 v14, s44, v186
	v_add_u32_e32 v30, s45, v186
	ds_read_b128 v[2:5], v14
	ds_read_b128 v[6:9], v14 offset:1024
	ds_read_b128 v[10:13], v14 offset:2048
	ds_read_b128 v[14:17], v14 offset:3072
	ds_read_b128 v[18:21], v30
	ds_read_b128 v[22:25], v30 offset:1024
	ds_read_b128 v[26:29], v30 offset:2048
	ds_read_b128 v[30:33], v30 offset:3072
	s_add_u32 s26, s26, 0x20000
	s_addc_u32 s27, s27, 0
	s_mov_b32 m0, s34
	v_lshl_add_u64 v[226:227], s[26:27], 0, v[162:163]
	ds_read_b128 v[194:197], v190 offset:32768
	ds_read_b128 v[198:201], v190 offset:33792
	ds_read_b128 v[202:205], v190 offset:34816
	ds_read_b128 v[206:209], v190 offset:35840
	ds_read_b128 v[210:213], v190 offset:36864
	ds_read_b128 v[214:217], v190 offset:37888
	ds_read_b128 v[218:221], v190 offset:38912
	ds_read_b128 v[222:225], v190 offset:39936
	global_load_lds_dwordx4 v[226:227], off
	v_lshl_add_u64 v[226:227], s[26:27], 0, v[166:167]
	s_mov_b32 m0, s35
	s_nop 0
	global_load_lds_dwordx4 v[226:227], off
	s_waitcnt vmcnt(8)
	s_waitcnt lgkmcnt(0)
	s_barrier
	s_setprio 1
	s_nop 0
	s_waitcnt lgkmcnt(0)
	v_mfma_scale_f32_16x16x128_f8f6f4 v[158:161], v[2:9], v[194:201], v[158:161], v191, v192 op_sel_hi:[0,0,0]
	v_mfma_scale_f32_16x16x128_f8f6f4 v[154:157], v[10:17], v[194:201], v[154:157], v191, v192 op_sel_hi:[0,0,0]
	v_mfma_scale_f32_16x16x128_f8f6f4 v[142:145], v[2:9], v[202:209], v[142:145], v191, v192 op_sel_hi:[0,0,0]
	v_mfma_scale_f32_16x16x128_f8f6f4 v[138:141], v[10:17], v[202:209], v[138:141], v191, v192 op_sel_hi:[0,0,0]
	v_mfma_scale_f32_16x16x128_f8f6f4 v[126:129], v[2:9], v[210:217], v[126:129], v191, v192 op_sel_hi:[0,0,0]
	v_mfma_scale_f32_16x16x128_f8f6f4 v[122:125], v[10:17], v[210:217], v[122:125], v191, v192 op_sel_hi:[0,0,0]
	v_mfma_scale_f32_16x16x128_f8f6f4 v[110:113], v[2:9], v[218:225], v[110:113], v191, v192 op_sel_hi:[0,0,0]
	v_mfma_scale_f32_16x16x128_f8f6f4 v[106:109], v[10:17], v[218:225], v[106:109], v191, v192 op_sel_hi:[0,0,0]
	s_setprio 0
	s_setprio 1
	s_nop 0
	v_mfma_scale_f32_16x16x128_f8f6f4 v[150:153], v[18:25], v[194:201], v[150:153], v191, v192 op_sel_hi:[0,0,0]
	v_mfma_scale_f32_16x16x128_f8f6f4 v[146:149], v[26:33], v[194:201], v[146:149], v191, v192 op_sel_hi:[0,0,0]
	v_mfma_scale_f32_16x16x128_f8f6f4 v[134:137], v[18:25], v[202:209], v[134:137], v191, v192 op_sel_hi:[0,0,0]
	v_mfma_scale_f32_16x16x128_f8f6f4 v[130:133], v[26:33], v[202:209], v[130:133], v191, v192 op_sel_hi:[0,0,0]
	v_mfma_scale_f32_16x16x128_f8f6f4 v[118:121], v[18:25], v[210:217], v[118:121], v191, v192 op_sel_hi:[0,0,0]
	v_mfma_scale_f32_16x16x128_f8f6f4 v[114:117], v[26:33], v[210:217], v[114:117], v191, v192 op_sel_hi:[0,0,0]
	v_mfma_scale_f32_16x16x128_f8f6f4 v[102:105], v[18:25], v[218:225], v[102:105], v191, v192 op_sel_hi:[0,0,0]
	v_mfma_scale_f32_16x16x128_f8f6f4 v[98:101], v[26:33], v[218:225], v[98:101], v191, v192 op_sel_hi:[0,0,0]
	s_setprio 0
	s_barrier
	s_add_i32 s26, s44, s28
	v_lshl_add_u64 v[178:179], v[178:179], 0, s[8:9]
	s_mov_b32 m0, s26
	ds_read_b128 v[194:197], v190 offset:49152
	ds_read_b128 v[198:201], v190 offset:50176
	ds_read_b128 v[202:205], v190 offset:51200
	ds_read_b128 v[206:209], v190 offset:52224
	ds_read_b128 v[210:213], v190 offset:53248
	ds_read_b128 v[214:217], v190 offset:54272
	ds_read_b128 v[218:221], v190 offset:55296
	ds_read_b128 v[222:225], v190 offset:56320
	global_load_lds_dwordx4 v[178:179], off
	s_add_i32 m0, s26, 0x2000
	s_add_u32 s24, s24, 0x2080
	v_lshl_add_u64 v[178:179], v[180:181], 0, s[8:9]
	s_addc_u32 s25, s25, 0
	s_add_i32 s26, s45, s28
	global_load_lds_dwordx4 v[178:179], off
	v_lshl_add_u64 v[178:179], s[24:25], 0, v[164:165]
	s_mov_b32 m0, s26
	s_nop 0
	global_load_lds_dwordx4 v[178:179], off
	v_lshl_add_u64 v[178:179], s[24:25], 0, v[168:169]
	s_add_i32 m0, s26, 0x2000
	s_nop 0
	global_load_lds_dwordx4 v[178:179], off
	v_lshl_add_u64 v[178:179], v[182:183], 0, s[8:9]
	s_mov_b32 m0, s38
	s_nop 0
	global_load_lds_dwordx4 v[178:179], off
	v_lshl_add_u64 v[178:179], v[184:185], 0, s[8:9]
	s_mov_b32 m0, s39
	s_nop 0
	global_load_lds_dwordx4 v[178:179], off
	s_waitcnt vmcnt(8)
	s_waitcnt lgkmcnt(0)
	s_barrier
	s_setprio 1
	s_nop 0
	s_waitcnt lgkmcnt(0)
	v_mfma_scale_f32_16x16x128_f8f6f4 v[94:97], v[2:9], v[194:201], v[94:97], v191, v192 op_sel_hi:[0,0,0]
	v_mfma_scale_f32_16x16x128_f8f6f4 v[90:93], v[10:17], v[194:201], v[90:93], v191, v192 op_sel_hi:[0,0,0]
	v_mfma_scale_f32_16x16x128_f8f6f4 v[78:81], v[2:9], v[202:209], v[78:81], v191, v192 op_sel_hi:[0,0,0]
	v_mfma_scale_f32_16x16x128_f8f6f4 v[74:77], v[10:17], v[202:209], v[74:77], v191, v192 op_sel_hi:[0,0,0]
	v_mfma_scale_f32_16x16x128_f8f6f4 v[62:65], v[2:9], v[210:217], v[62:65], v191, v192 op_sel_hi:[0,0,0]
	v_mfma_scale_f32_16x16x128_f8f6f4 v[58:61], v[10:17], v[210:217], v[58:61], v191, v192 op_sel_hi:[0,0,0]
	v_mfma_scale_f32_16x16x128_f8f6f4 v[46:49], v[2:9], v[218:225], v[46:49], v191, v192 op_sel_hi:[0,0,0]
	v_mfma_scale_f32_16x16x128_f8f6f4 v[42:45], v[10:17], v[218:225], v[42:45], v191, v192 op_sel_hi:[0,0,0]
	s_setprio 0
	s_setprio 1
	s_nop 0
	v_mfma_scale_f32_16x16x128_f8f6f4 v[86:89], v[18:25], v[194:201], v[86:89], v191, v192 op_sel_hi:[0,0,0]
	v_mfma_scale_f32_16x16x128_f8f6f4 v[82:85], v[26:33], v[194:201], v[82:85], v191, v192 op_sel_hi:[0,0,0]
	v_mfma_scale_f32_16x16x128_f8f6f4 v[70:73], v[18:25], v[202:209], v[70:73], v191, v192 op_sel_hi:[0,0,0]
	v_mfma_scale_f32_16x16x128_f8f6f4 v[66:69], v[26:33], v[202:209], v[66:69], v191, v192 op_sel_hi:[0,0,0]
	v_mfma_scale_f32_16x16x128_f8f6f4 v[54:57], v[18:25], v[210:217], v[54:57], v191, v192 op_sel_hi:[0,0,0]
	v_mfma_scale_f32_16x16x128_f8f6f4 v[50:53], v[26:33], v[210:217], v[50:53], v191, v192 op_sel_hi:[0,0,0]
	v_mfma_scale_f32_16x16x128_f8f6f4 v[38:41], v[18:25], v[218:225], v[38:41], v191, v192 op_sel_hi:[0,0,0]
	v_mfma_scale_f32_16x16x128_f8f6f4 v[34:37], v[26:33], v[218:225], v[34:37], v191, v192 op_sel_hi:[0,0,0]
	s_setprio 0
	s_barrier
	s_add_i32 s43, s43, 2
	s_add_u32 s22, s22, 0x100
	s_addc_u32 s23, s23, 0
	s_add_u32 s33, s33, 0x100
	s_addc_u32 s42, s42, 0
; #define PG8_STAGE(bufoff, gbase, voff) do { _Pragma("unroll") for (int _i = 0; _i < 2; ++_i) \
;         __builtin_amdgcn_global_load_lds((const unsigned*)((const char*)(gbase) + (voff)[_i]), (PG8_LAS unsigned*)(lds + (bufoff) + ldsw + _i * 8192), 16, 0, 0); } while (0)
; #define PG8_STAGE_A(bufoff, gbase, h, nx) do { if constexpr (Sched::GATHER) { const unsigned vv_[2] = {(nx) ? vAn[h][0] : vA[h][0], (nx) ? vAn[h][1] : vA[h][1]}; PG8_STAGE(bufoff, gbase, vv_); } \
;         else { PG8_STAGE(bufoff, (gbase) + (h) * hstep, voffA); } } while (0)
; #define PG8_LDA(dst, b, h) do { _Pragma("unroll") for (int m = 0; m < 4; ++m) _Pragma("unroll") for (int k = 0; k < 2; ++k) dst[m][k] = *(const PG8_LAS bf16x8*)(lds + PG8_SA(b, h) + aoff + m * 2048 + k * 1024); } while (0)
; #define PG8_LDB(dst, b, h) do { _Pragma("unroll") for (int n = 0; n < 2; ++n) _Pragma("unroll") for (int k = 0; k < 2; ++k) dst[n][k] = *(const PG8_LAS bf16x8*)(lds + PG8_SB(b, h) + boff + n * 2048 + k * 1024); } while (0)
; #define PG8_WAIT_V(n) asm volatile("s_waitcnt vmcnt(" #n ")" ::: "memory")
; #define PG8_WAIT_L(n) asm volatile("s_waitcnt lgkmcnt(" #n ")" ::: "memory")
; #define PG8_BAR __builtin_amdgcn_s_barrier()
; #define PG8_SCHED __builtin_amdgcn_sched_barrier(0)
;     ...
;             const bool last = (t == nt - 2);
;             const char* a1 = cA + (size_t)(t + 1) * kstep;
;             const char* a2 = last ? nA : cA + (size_t)(t + 2) * kstep; const char* b2 = last ? nB : cB + (size_t)(t + 2) * kstep;
;             const char* a3 = a2 + kstep; const char* b3 = b2 + kstep;
;             if (last && has_next) S.a_ready(nxt);
;             if constexpr (SP2) {
;             PG8_LDB(B0, 0, 0); PG8_LDB(B1, 0, 1); PG8_SCHED; PG8_LDA(At, 0, 0); PG8_STAGE_A(PG8_SA(1, 1), a1, 1, false);
;             PG8_WAIT_V(8); PG8_WAIT_L(0); PG8_BAR; PG8_MMA(0, 0, At, B0); PG8_MMA(0, 1, At, B1); PG8_BAR; PG8_SCHED;
;             PG8_LDA(At, 0, 1); PG8_STAGE(PG8_SB(0, 0), b2, voffB); PG8_STAGE(PG8_SB(0, 1), b2 + hstepB, voffB); PG8_STAGE_A(PG8_SA(0, 0), a2, 0, last);
;             PG8_WAIT_V(8); PG8_WAIT_L(0); PG8_BAR; PG8_MMA(1, 0, At, B0); PG8_MMA(1, 1, At, B1); PG8_BAR; PG8_SCHED;
.LBB0_474:
	ds_read_b128 v[26:29], v188
	ds_read_b128 v[30:33], v188 offset:1024
	ds_read_b128 v[18:21], v188 offset:2048
	ds_read_b128 v[22:25], v188 offset:3072
	ds_read_b128 v[10:13], v189
	ds_read_b128 v[14:17], v189 offset:1024
	ds_read_b128 v[2:5], v189 offset:2048
	ds_read_b128 v[6:9], v189 offset:3072
	s_add_u32 s24, s22, 0xfffe0080
	s_addc_u32 s25, s23, -1
	s_cmp_eq_u32 s43, 4
	s_cselect_b32 s27, s1, s25
	s_cselect_b32 s26, s15, s24
	s_cselect_b32 s25, s13, s42
	s_cselect_b32 s24, s21, s33
	v_lshl_add_u64 v[218:219], s[22:23], 0, v[170:171]
	s_add_i32 m0, s30, 0xc000
	ds_read_b128 v[178:181], v190
	ds_read_b128 v[182:185], v190 offset:1024
	ds_read_b128 v[194:197], v190 offset:2048
	ds_read_b128 v[198:201], v190 offset:3072
	ds_read_b128 v[202:205], v190 offset:4096
	ds_read_b128 v[206:209], v190 offset:5120
	ds_read_b128 v[210:213], v190 offset:6144
	ds_read_b128 v[214:217], v190 offset:7168
	global_load_lds_dwordx4 v[218:219], off
	v_lshl_add_u64 v[218:219], s[22:23], 0, v[172:173]
	s_add_i32 m0, s30, 0xe000
	s_nop 0
	global_load_lds_dwordx4 v[218:219], off
	s_waitcnt vmcnt(8)
	s_waitcnt lgkmcnt(0)
	s_barrier
	s_setprio 1
	s_nop 0
	s_waitcnt lgkmcnt(0)
	v_mfma_scale_f32_16x16x128_f8f6f4 v[158:161], v[26:33], v[178:185], v[158:161], v191, v192 op_sel_hi:[0,0,0]
	v_mfma_scale_f32_16x16x128_f8f6f4 v[154:157], v[18:25], v[178:185], v[154:157], v191, v192 op_sel_hi:[0,0,0]
	v_mfma_scale_f32_16x16x128_f8f6f4 v[142:145], v[26:33], v[194:201], v[142:145], v191, v192 op_sel_hi:[0,0,0]
	v_mfma_scale_f32_16x16x128_f8f6f4 v[138:141], v[18:25], v[194:201], v[138:141], v191, v192 op_sel_hi:[0,0,0]
	v_mfma_scale_f32_16x16x128_f8f6f4 v[126:129], v[26:33], v[202:209], v[126:129], v191, v192 op_sel_hi:[0,0,0]
	v_mfma_scale_f32_16x16x128_f8f6f4 v[122:125], v[18:25], v[202:209], v[122:125], v191, v192 op_sel_hi:[0,0,0]
	v_mfma_scale_f32_16x16x128_f8f6f4 v[110:113], v[26:33], v[210:217], v[110:113], v191, v192 op_sel_hi:[0,0,0]
	v_mfma_scale_f32_16x16x128_f8f6f4 v[106:109], v[18:25], v[210:217], v[106:109], v191, v192 op_sel_hi:[0,0,0]
	s_setprio 0
	s_setprio 1
	s_nop 0
	v_mfma_scale_f32_16x16x128_f8f6f4 v[150:153], v[10:17], v[178:185], v[150:153], v191, v192 op_sel_hi:[0,0,0]
	v_mfma_scale_f32_16x16x128_f8f6f4 v[146:149], v[2:9], v[178:185], v[146:149], v191, v192 op_sel_hi:[0,0,0]
	v_mfma_scale_f32_16x16x128_f8f6f4 v[134:137], v[10:17], v[194:201], v[134:137], v191, v192 op_sel_hi:[0,0,0]
	v_mfma_scale_f32_16x16x128_f8f6f4 v[130:133], v[2:9], v[194:201], v[130:133], v191, v192 op_sel_hi:[0,0,0]
	v_mfma_scale_f32_16x16x128_f8f6f4 v[118:121], v[10:17], v[202:209], v[118:121], v191, v192 op_sel_hi:[0,0,0]
	v_mfma_scale_f32_16x16x128_f8f6f4 v[114:117], v[2:9], v[202:209], v[114:117], v191, v192 op_sel_hi:[0,0,0]
	v_mfma_scale_f32_16x16x128_f8f6f4 v[102:105], v[10:17], v[210:217], v[102:105], v191, v192 op_sel_hi:[0,0,0]
	v_mfma_scale_f32_16x16x128_f8f6f4 v[98:101], v[2:9], v[210:217], v[98:101], v191, v192 op_sel_hi:[0,0,0]
	s_setprio 0
	s_barrier
	s_add_i32 s44, s40, s28
	v_lshl_add_u64 v[178:179], s[24:25], 0, v[164:165]
	s_mov_b32 m0, s44
	ds_read_b128 v[194:197], v190 offset:16384
	ds_read_b128 v[198:201], v190 offset:17408
	ds_read_b128 v[202:205], v190 offset:18432
	ds_read_b128 v[206:209], v190 offset:19456
	ds_read_b128 v[210:213], v190 offset:20480
	ds_read_b128 v[214:217], v190 offset:21504
	ds_read_b128 v[218:221], v190 offset:22528
	ds_read_b128 v[222:225], v190 offset:23552
	global_load_lds_dwordx4 v[178:179], off
	s_add_i32 m0, s44, 0x2000
	s_add_u32 s44, s24, 0x2000
	v_lshl_add_u64 v[180:181], s[24:25], 0, v[168:169]
	s_addc_u32 s45, s25, 0
	s_add_i32 s46, s41, s28
	global_load_lds_dwordx4 v[180:181], off
	v_lshl_add_u64 v[182:183], s[44:45], 0, v[164:165]
	s_mov_b32 m0, s46
	v_lshl_add_u64 v[184:185], s[26:27], 0, v[166:167]
	global_load_lds_dwordx4 v[182:183], off
	v_lshl_add_u64 v[182:183], s[44:45], 0, v[168:169]
	s_add_i32 m0, s46, 0x2000
	s_nop 0
	global_load_lds_dwordx4 v[182:183], off
	v_lshl_add_u64 v[182:183], s[26:27], 0, v[162:163]
	s_mov_b32 m0, s30
	s_nop 0
	global_load_lds_dwordx4 v[182:183], off
	s_mov_b32 m0, s31
	s_nop 0
	global_load_lds_dwordx4 v[184:185], off
	s_waitcnt vmcnt(8)
	s_waitcnt lgkmcnt(0)
	s_barrier
	s_setprio 1
	s_nop 0
	s_waitcnt lgkmcnt(0)
	v_mfma_scale_f32_16x16x128_f8f6f4 v[94:97], v[26:33], v[194:201], v[94:97], v191, v192 op_sel_hi:[0,0,0]
	v_mfma_scale_f32_16x16x128_f8f6f4 v[90:93], v[18:25], v[194:201], v[90:93], v191, v192 op_sel_hi:[0,0,0]
	v_mfma_scale_f32_16x16x128_f8f6f4 v[78:81], v[26:33], v[202:209], v[78:81], v191, v192 op_sel_hi:[0,0,0]
	v_mfma_scale_f32_16x16x128_f8f6f4 v[74:77], v[18:25], v[202:209], v[74:77], v191, v192 op_sel_hi:[0,0,0]
	v_mfma_scale_f32_16x16x128_f8f6f4 v[62:65], v[26:33], v[210:217], v[62:65], v191, v192 op_sel_hi:[0,0,0]
	v_mfma_scale_f32_16x16x128_f8f6f4 v[58:61], v[18:25], v[210:217], v[58:61], v191, v192 op_sel_hi:[0,0,0]
	v_mfma_scale_f32_16x16x128_f8f6f4 v[46:49], v[26:33], v[218:225], v[46:49], v191, v192 op_sel_hi:[0,0,0]
	v_mfma_scale_f32_16x16x128_f8f6f4 v[42:45], v[18:25], v[218:225], v[42:45], v191, v192 op_sel_hi:[0,0,0]
	s_setprio 0
	s_setprio 1
	s_nop 0
	v_mfma_scale_f32_16x16x128_f8f6f4 v[86:89], v[10:17], v[194:201], v[86:89], v191, v192 op_sel_hi:[0,0,0]
	v_mfma_scale_f32_16x16x128_f8f6f4 v[82:85], v[2:9], v[194:201], v[82:85], v191, v192 op_sel_hi:[0,0,0]
	v_mfma_scale_f32_16x16x128_f8f6f4 v[70:73], v[10:17], v[202:209], v[70:73], v191, v192 op_sel_hi:[0,0,0]
	v_mfma_scale_f32_16x16x128_f8f6f4 v[66:69], v[2:9], v[202:209], v[66:69], v191, v192 op_sel_hi:[0,0,0]
	v_mfma_scale_f32_16x16x128_f8f6f4 v[54:57], v[10:17], v[210:217], v[54:57], v191, v192 op_sel_hi:[0,0,0]
	v_mfma_scale_f32_16x16x128_f8f6f4 v[50:53], v[2:9], v[210:217], v[50:53], v191, v192 op_sel_hi:[0,0,0]
	v_mfma_scale_f32_16x16x128_f8f6f4 v[38:41], v[10:17], v[218:225], v[38:41], v191, v192 op_sel_hi:[0,0,0]
	v_mfma_scale_f32_16x16x128_f8f6f4 v[34:37], v[2:9], v[218:225], v[34:37], v191, v192 op_sel_hi:[0,0,0]
	s_setprio 0
	s_barrier
; #define PG8_STAGE(bufoff, gbase, voff) do { _Pragma("unroll") for (int _i = 0; _i < 2; ++_i) \
;         __builtin_amdgcn_global_load_lds((const unsigned*)((const char*)(gbase) + (voff)[_i]), (PG8_LAS unsigned*)(lds + (bufoff) + ldsw + _i * 8192), 16, 0, 0); } while (0)
; #define PG8_STAGE_A(bufoff, gbase, h, nx) do { if constexpr (Sched::GATHER) { const unsigned vv_[2] = {(nx) ? vAn[h][0] : vA[h][0], (nx) ? vAn[h][1] : vA[h][1]}; PG8_STAGE(bufoff, gbase, vv_); } \
;         else { PG8_STAGE(bufoff, (gbase) + (h) * hstep, voffA); } } while (0)
; #define PG8_LDA(dst, b, h) do { _Pragma("unroll") for (int m = 0; m < 4; ++m) _Pragma("unroll") for (int k = 0; k < 2; ++k) dst[m][k] = *(const PG8_LAS bf16x8*)(lds + PG8_SA(b, h) + aoff + m * 2048 + k * 1024); } while (0)
; #define PG8_LDB(dst, b, h) do { _Pragma("unroll") for (int n = 0; n < 2; ++n) _Pragma("unroll") for (int k = 0; k < 2; ++k) dst[n][k] = *(const PG8_LAS bf16x8*)(lds + PG8_SB(b, h) + boff + n * 2048 + k * 1024); } while (0)
; #define PG8_WAIT_V(n) asm volatile("s_waitcnt vmcnt(" #n ")" ::: "memory")
; #define PG8_WAIT_L(n) asm volatile("s_waitcnt lgkmcnt(" #n ")" ::: "memory")
; #define PG8_BAR __builtin_amdgcn_s_barrier()
; #define PG8_SCHED __builtin_amdgcn_sched_barrier(0)
;     ...
;         for (int t = 0; t < nt; t += 2) {
;     ...
;             PG8_LDB(B0, 1, 0); PG8_LDB(B1, 1, 1); PG8_SCHED; PG8_LDA(At, 1, 0); PG8_STAGE_A(PG8_SA(0, 1), a2, 1, last);
;             PG8_WAIT_V(8); PG8_WAIT_L(0); PG8_BAR; PG8_MMA(0, 0, At, B0); PG8_MMA(0, 1, At, B1); PG8_BAR; PG8_SCHED;
;             PG8_LDA(At, 1, 1); PG8_STAGE(PG8_SB(1, 0), b3, voffB); PG8_STAGE(PG8_SB(1, 1), b3 + hstepB, voffB); PG8_STAGE_A(PG8_SA(1, 0), a3, 0, last);
;             PG8_WAIT_V(8); PG8_WAIT_L(0); PG8_BAR; PG8_MMA(1, 0, At, B0); PG8_MMA(1, 1, At, B1); PG8_BAR; PG8_SCHED;
	s_add_i32 s44, 0, 0x18000
	s_add_i32 s45, 0, 0x1c000
	v_add_u32_e32 v14, s44, v186
	v_add_u32_e32 v30, s45, v186
	ds_read_b128 v[2:5], v14
	ds_read_b128 v[6:9], v14 offset:1024
	ds_read_b128 v[10:13], v14 offset:2048
	ds_read_b128 v[14:17], v14 offset:3072
	ds_read_b128 v[18:21], v30
	ds_read_b128 v[22:25], v30 offset:1024
	ds_read_b128 v[26:29], v30 offset:2048
	ds_read_b128 v[30:33], v30 offset:3072
	s_add_u32 s26, s26, 0x20000
	s_addc_u32 s27, s27, 0
	s_mov_b32 m0, s34
	v_lshl_add_u64 v[226:227], s[26:27], 0, v[162:163]
	ds_read_b128 v[194:197], v190 offset:32768
	ds_read_b128 v[198:201], v190 offset:33792
	ds_read_b128 v[202:205], v190 offset:34816
	ds_read_b128 v[206:209], v190 offset:35840
	ds_read_b128 v[210:213], v190 offset:36864
	ds_read_b128 v[214:217], v190 offset:37888
	ds_read_b128 v[218:221], v190 offset:38912
	ds_read_b128 v[222:225], v190 offset:39936
	global_load_lds_dwordx4 v[226:227], off
	v_lshl_add_u64 v[226:227], s[26:27], 0, v[166:167]
	s_mov_b32 m0, s35
	s_nop 0
	global_load_lds_dwordx4 v[226:227], off
	s_waitcnt vmcnt(8)
	s_waitcnt lgkmcnt(0)
	s_barrier
	s_setprio 1
	s_nop 0
	s_waitcnt lgkmcnt(0)
	v_mfma_scale_f32_16x16x128_f8f6f4 v[158:161], v[2:9], v[194:201], v[158:161], v191, v192 op_sel_hi:[0,0,0]
	v_mfma_scale_f32_16x16x128_f8f6f4 v[154:157], v[10:17], v[194:201], v[154:157], v191, v192 op_sel_hi:[0,0,0]
	v_mfma_scale_f32_16x16x128_f8f6f4 v[142:145], v[2:9], v[202:209], v[142:145], v191, v192 op_sel_hi:[0,0,0]
	v_mfma_scale_f32_16x16x128_f8f6f4 v[138:141], v[10:17], v[202:209], v[138:141], v191, v192 op_sel_hi:[0,0,0]
	v_mfma_scale_f32_16x16x128_f8f6f4 v[126:129], v[2:9], v[210:217], v[126:129], v191, v192 op_sel_hi:[0,0,0]
	v_mfma_scale_f32_16x16x128_f8f6f4 v[122:125], v[10:17], v[210:217], v[122:125], v191, v192 op_sel_hi:[0,0,0]
	v_mfma_scale_f32_16x16x128_f8f6f4 v[110:113], v[2:9], v[218:225], v[110:113], v191, v192 op_sel_hi:[0,0,0]
	v_mfma_scale_f32_16x16x128_f8f6f4 v[106:109], v[10:17], v[218:225], v[106:109], v191, v192 op_sel_hi:[0,0,0]
	s_setprio 0
	s_setprio 1
	s_nop 0
	v_mfma_scale_f32_16x16x128_f8f6f4 v[150:153], v[18:25], v[194:201], v[150:153], v191, v192 op_sel_hi:[0,0,0]
	v_mfma_scale_f32_16x16x128_f8f6f4 v[146:149], v[26:33], v[194:201], v[146:149], v191, v192 op_sel_hi:[0,0,0]
	v_mfma_scale_f32_16x16x128_f8f6f4 v[134:137], v[18:25], v[202:209], v[134:137], v191, v192 op_sel_hi:[0,0,0]
	v_mfma_scale_f32_16x16x128_f8f6f4 v[130:133], v[26:33], v[202:209], v[130:133], v191, v192 op_sel_hi:[0,0,0]
	v_mfma_scale_f32_16x16x128_f8f6f4 v[118:121], v[18:25], v[210:217], v[118:121], v191, v192 op_sel_hi:[0,0,0]
	v_mfma_scale_f32_16x16x128_f8f6f4 v[114:117], v[26:33], v[210:217], v[114:117], v191, v192 op_sel_hi:[0,0,0]
	v_mfma_scale_f32_16x16x128_f8f6f4 v[102:105], v[18:25], v[218:225], v[102:105], v191, v192 op_sel_hi:[0,0,0]
	v_mfma_scale_f32_16x16x128_f8f6f4 v[98:101], v[26:33], v[218:225], v[98:101], v191, v192 op_sel_hi:[0,0,0]
	s_setprio 0
	s_barrier
	s_add_i32 s26, s44, s28
	v_lshl_add_u64 v[178:179], v[178:179], 0, s[8:9]
	s_mov_b32 m0, s26
	ds_read_b128 v[194:197], v190 offset:49152
	ds_read_b128 v[198:201], v190 offset:50176
	ds_read_b128 v[202:205], v190 offset:51200
	ds_read_b128 v[206:209], v190 offset:52224
	ds_read_b128 v[210:213], v190 offset:53248
	ds_read_b128 v[214:217], v190 offset:54272
	ds_read_b128 v[218:221], v190 offset:55296
	ds_read_b128 v[222:225], v190 offset:56320
	global_load_lds_dwordx4 v[178:179], off
	s_add_i32 m0, s26, 0x2000
	s_add_u32 s24, s24, 0x2080
	v_lshl_add_u64 v[178:179], v[180:181], 0, s[8:9]
	s_addc_u32 s25, s25, 0
	s_add_i32 s26, s45, s28
	global_load_lds_dwordx4 v[178:179], off
	v_lshl_add_u64 v[178:179], s[24:25], 0, v[164:165]
	s_mov_b32 m0, s26
	s_nop 0
	global_load_lds_dwordx4 v[178:179], off
	v_lshl_add_u64 v[178:179], s[24:25], 0, v[168:169]
	s_add_i32 m0, s26, 0x2000
	s_nop 0
	global_load_lds_dwordx4 v[178:179], off
	v_lshl_add_u64 v[178:179], v[182:183], 0, s[8:9]
	s_mov_b32 m0, s38
	s_nop 0
	global_load_lds_dwordx4 v[178:179], off
	v_lshl_add_u64 v[178:179], v[184:185], 0, s[8:9]
	s_mov_b32 m0, s39
	s_nop 0
	global_load_lds_dwordx4 v[178:179], off
	s_waitcnt vmcnt(8)
	s_waitcnt lgkmcnt(0)
	s_barrier
	s_setprio 1
	s_nop 0
	s_waitcnt lgkmcnt(0)
	v_mfma_scale_f32_16x16x128_f8f6f4 v[94:97], v[2:9], v[194:201], v[94:97], v191, v192 op_sel_hi:[0,0,0]
	v_mfma_scale_f32_16x16x128_f8f6f4 v[90:93], v[10:17], v[194:201], v[90:93], v191, v192 op_sel_hi:[0,0,0]
	v_mfma_scale_f32_16x16x128_f8f6f4 v[78:81], v[2:9], v[202:209], v[78:81], v191, v192 op_sel_hi:[0,0,0]
	v_mfma_scale_f32_16x16x128_f8f6f4 v[74:77], v[10:17], v[202:209], v[74:77], v191, v192 op_sel_hi:[0,0,0]
	v_mfma_scale_f32_16x16x128_f8f6f4 v[62:65], v[2:9], v[210:217], v[62:65], v191, v192 op_sel_hi:[0,0,0]
	v_mfma_scale_f32_16x16x128_f8f6f4 v[58:61], v[10:17], v[210:217], v[58:61], v191, v192 op_sel_hi:[0,0,0]
	v_mfma_scale_f32_16x16x128_f8f6f4 v[46:49], v[2:9], v[218:225], v[46:49], v191, v192 op_sel_hi:[0,0,0]
	v_mfma_scale_f32_16x16x128_f8f6f4 v[42:45], v[10:17], v[218:225], v[42:45], v191, v192 op_sel_hi:[0,0,0]
	s_setprio 0
	s_setprio 1
	s_nop 0
	v_mfma_scale_f32_16x16x128_f8f6f4 v[86:89], v[18:25], v[194:201], v[86:89], v191, v192 op_sel_hi:[0,0,0]
	v_mfma_scale_f32_16x16x128_f8f6f4 v[82:85], v[26:33], v[194:201], v[82:85], v191, v192 op_sel_hi:[0,0,0]
	v_mfma_scale_f32_16x16x128_f8f6f4 v[70:73], v[18:25], v[202:209], v[70:73], v191, v192 op_sel_hi:[0,0,0]
	v_mfma_scale_f32_16x16x128_f8f6f4 v[66:69], v[26:33], v[202:209], v[66:69], v191, v192 op_sel_hi:[0,0,0]
	v_mfma_scale_f32_16x16x128_f8f6f4 v[54:57], v[18:25], v[210:217], v[54:57], v191, v192 op_sel_hi:[0,0,0]
	v_mfma_scale_f32_16x16x128_f8f6f4 v[50:53], v[26:33], v[210:217], v[50:53], v191, v192 op_sel_hi:[0,0,0]
	v_mfma_scale_f32_16x16x128_f8f6f4 v[38:41], v[18:25], v[218:225], v[38:41], v191, v192 op_sel_hi:[0,0,0]
	v_mfma_scale_f32_16x16x128_f8f6f4 v[34:37], v[26:33], v[218:225], v[34:37], v191, v192 op_sel_hi:[0,0,0]
	s_setprio 0
	s_barrier
	s_add_i32 s43, s43, 2
	s_add_u32 s22, s22, 0x100
	s_addc_u32 s23, s23, 0
	s_add_u32 s33, s33, 0x100
	s_addc_u32 s42, s42, 0
	s_cmp_gt_u32 s43, 5
	s_cbranch_scc0 .LBB0_474
	s_and_b64 vcc, exec, s[10:11]
	s_cbranch_vccz .LBB0_477
	s_barrier

; #define PG8_STAGE(bufoff, gbase, voff) do { _Pragma("unroll") for (int _i = 0; _i < 2; ++_i) \
;         __builtin_amdgcn_global_load_lds((const unsigned*)((const char*)(gbase) + (voff)[_i]), (PG8_LAS unsigned*)(lds + (bufoff) + ldsw + _i * 8192), 16, 0, 0); } while (0)
; #define PG8_STAGE_A(bufoff, gbase, h, nx) do { if constexpr (Sched::GATHER) { const unsigned vv_[2] = {(nx) ? vAn[h][0] : vA[h][0], (nx) ? vAn[h][1] : vA[h][1]}; PG8_STAGE(bufoff, gbase, vv_); } \
;         else { PG8_STAGE(bufoff, (gbase) + (h) * hstep, voffA); } } while (0)
; #define PG8_LDA(dst, b, h) do { _Pragma("unroll") for (int m = 0; m < 4; ++m) _Pragma("unroll") for (int k = 0; k < 2; ++k) dst[m][k] = *(const PG8_LAS bf16x8*)(lds + PG8_SA(b, h) + aoff + m * 2048 + k * 1024); } while (0)
; #define PG8_WAIT_V(n) asm volatile("s_waitcnt vmcnt(" #n ")" ::: "memory")
; #define PG8_WAIT_L(n) asm volatile("s_waitcnt lgkmcnt(" #n ")" ::: "memory")
;     ...
;         const bool has_next = S.next(ui + 1, nxt);
;         const char* nA = Sched::GATHER ? cA : (has_next ? (const char*)g.A + (size_t)nxt.pm * tstep : cA);
;         if constexpr (Sched::GATHER) { if (has_next) { PG8_AOFF(vAn, ui + 1); } else { _Pragma("unroll") for (int h_ = 0; h_ < 2; ++h_) _Pragma("unroll") for (int i_ = 0; i_ < 2; ++i_) vAn[h_][i_] = vA[h_][i_]; } } const char* nB = has_next ? (const char*)g.Bt + (size_t)nxt.pb * tstep : cB;
; #pragma nounroll
;         for (int t = 0; t < nt; t += 2) {
;             const bool last = (t == nt - 2);
;             const char* a1 = cA + (size_t)(t + 1) * kstep;
;             const char* a2 = last ? nA : cA + (size_t)(t + 2) * kstep; const char* b2 = last ? nB : cB + (size_t)(t + 2) * kstep;
;             const char* a3 = a2 + kstep; const char* b3 = b2 + kstep;
;             if (last && has_next) S.a_ready(nxt);
;             if constexpr (SP2) {
;             PG8_LDB(B0, 0, 0); PG8_LDB(B1, 0, 1); PG8_SCHED; PG8_LDA(At, 0, 0); PG8_STAGE_A(PG8_SA(1, 1), a1, 1, false);
;             PG8_WAIT_V(8); PG8_WAIT_L(0); PG8_BAR; PG8_MMA(0, 0, At, B0); PG8_MMA(0, 1, At, B1); PG8_BAR; PG8_SCHED;
;             PG8_LDA(At, 0, 1); PG8_STAGE(PG8_SB(0, 0), b2, voffB); PG8_STAGE(PG8_SB(0, 1), b2 + hstepB, voffB); PG8_STAGE_A(PG8_SA(0, 0), a2, 0, last);
;             PG8_WAIT_V(8); PG8_WAIT_L(0); PG8_BAR; PG8_MMA(1, 0, At, B0); PG8_MMA(1, 1, At, B1); PG8_BAR; PG8_SCHED;
.LBB0_840:
	s_ashr_i32 s17, s16, 31
	s_lshl_b64 s[18:19], s[16:17], 18
	v_readlane_b32 s22, v254, 61
	v_readlane_b32 s23, v254, 62
	s_add_u32 s18, s22, s18
	s_addc_u32 s19, s23, s19
	s_and_b64 s[4:5], s[4:5], exec
	s_cselect_b32 s17, s19, s21
	s_cselect_b32 s48, s18, s20
	v_mov_b32_e32 v175, v167
	v_mov_b32_e32 v177, v167
	s_add_u32 s49, s20, 0x100
	v_readlane_b32 s54, v254, 0
	v_lshl_add_u64 v[178:179], s[12:13], 0, v[176:177]
	v_lshl_add_u64 v[180:181], s[12:13], 0, v[174:175]
	s_addc_u32 s50, s21, 0
	s_mov_b32 s51, -2
	s_mov_b64 s[4:5], 0
	v_readlane_b32 s55, v254, 1
	ds_read_b128 v[26:29], v194
	ds_read_b128 v[30:33], v194 offset:1024
	ds_read_b128 v[18:21], v194 offset:2048
	ds_read_b128 v[22:25], v194 offset:3072
	ds_read_b128 v[10:13], v195
	ds_read_b128 v[14:17], v195 offset:1024
	ds_read_b128 v[2:5], v195 offset:2048
	ds_read_b128 v[6:9], v195 offset:3072
	s_add_u32 s20, s54, s4
	s_addc_u32 s21, s55, s5
	s_add_u32 s22, s20, 0x25400100
	s_addc_u32 s23, s21, 0
	s_add_u32 s52, s49, s4
	s_addc_u32 s53, s50, s5
	s_cmpk_eq_i32 s4, 0x300
	s_cselect_b64 vcc, -1, 0
	s_and_b64 s[20:21], vcc, exec
	s_cselect_b32 s23, s93, s23
	s_cselect_b32 s22, s92, s22
	s_cselect_b32 s21, s17, s53
	s_cselect_b32 s20, s48, s52
	s_mov_b32 m0, s36
	v_lshl_add_u64 v[232:233], v[180:181], 0, s[4:5]
	ds_read_b128 v[182:185], v196
	ds_read_b128 v[186:189], v196 offset:1024
	ds_read_b128 v[208:211], v196 offset:2048
	ds_read_b128 v[212:215], v196 offset:3072
	ds_read_b128 v[216:219], v196 offset:4096
	ds_read_b128 v[220:223], v196 offset:5120
	ds_read_b128 v[224:227], v196 offset:6144
	ds_read_b128 v[228:231], v196 offset:7168
	global_load_lds_dwordx4 v[232:233], off
	v_lshl_add_u64 v[232:233], v[178:179], 0, s[4:5]
	s_mov_b32 m0, s37
	s_nop 0
	global_load_lds_dwordx4 v[232:233], off
	s_waitcnt vmcnt(8)
	s_waitcnt lgkmcnt(0)
	s_barrier
	s_setprio 1
	s_nop 0
	s_waitcnt lgkmcnt(0)
	v_mfma_scale_f32_16x16x128_f8f6f4 v[158:161], v[26:33], v[182:189], 0, v197, v198 op_sel_hi:[0,0,0]
	v_mfma_scale_f32_16x16x128_f8f6f4 v[150:153], v[18:25], v[182:189], 0, v197, v198 op_sel_hi:[0,0,0]
	v_mfma_scale_f32_16x16x128_f8f6f4 v[142:145], v[26:33], v[208:215], 0, v197, v198 op_sel_hi:[0,0,0]
	v_mfma_scale_f32_16x16x128_f8f6f4 v[134:137], v[18:25], v[208:215], 0, v197, v198 op_sel_hi:[0,0,0]
	v_mfma_scale_f32_16x16x128_f8f6f4 v[126:129], v[26:33], v[216:223], 0, v197, v198 op_sel_hi:[0,0,0]
	v_mfma_scale_f32_16x16x128_f8f6f4 v[118:121], v[18:25], v[216:223], 0, v197, v198 op_sel_hi:[0,0,0]
	v_mfma_scale_f32_16x16x128_f8f6f4 v[110:113], v[26:33], v[224:231], 0, v197, v198 op_sel_hi:[0,0,0]
	v_mfma_scale_f32_16x16x128_f8f6f4 v[98:101], v[18:25], v[224:231], 0, v197, v198 op_sel_hi:[0,0,0]
	s_setprio 0
	s_setprio 1
	s_nop 0
	v_mfma_scale_f32_16x16x128_f8f6f4 v[154:157], v[10:17], v[182:189], 0, v197, v198 op_sel_hi:[0,0,0]
	v_mfma_scale_f32_16x16x128_f8f6f4 v[146:149], v[2:9], v[182:189], 0, v197, v198 op_sel_hi:[0,0,0]
	v_mfma_scale_f32_16x16x128_f8f6f4 v[138:141], v[10:17], v[208:215], 0, v197, v198 op_sel_hi:[0,0,0]
	v_mfma_scale_f32_16x16x128_f8f6f4 v[130:133], v[2:9], v[208:215], 0, v197, v198 op_sel_hi:[0,0,0]
	v_mfma_scale_f32_16x16x128_f8f6f4 v[122:125], v[10:17], v[216:223], 0, v197, v198 op_sel_hi:[0,0,0]
	v_mfma_scale_f32_16x16x128_f8f6f4 v[114:117], v[2:9], v[216:223], 0, v197, v198 op_sel_hi:[0,0,0]
	v_mfma_scale_f32_16x16x128_f8f6f4 v[106:109], v[10:17], v[224:231], 0, v197, v198 op_sel_hi:[0,0,0]
	v_mfma_scale_f32_16x16x128_f8f6f4 v[94:97], v[2:9], v[224:231], 0, v197, v198 op_sel_hi:[0,0,0]
	s_setprio 0
	s_barrier
	s_mov_b32 m0, s38
	v_lshl_add_u64 v[182:183], s[20:21], 0, v[164:165]
	s_add_u32 s52, s20, 0x20000
	ds_read_b128 v[208:211], v196 offset:16384
	ds_read_b128 v[212:215], v196 offset:17408
	ds_read_b128 v[216:219], v196 offset:18432
	ds_read_b128 v[220:223], v196 offset:19456
	ds_read_b128 v[224:227], v196 offset:20480
	ds_read_b128 v[228:231], v196 offset:21504
	ds_read_b128 v[232:235], v196 offset:22528
	ds_read_b128 v[236:239], v196 offset:23552
	global_load_lds_dwordx4 v[182:183], off
	v_lshl_add_u64 v[184:185], s[20:21], 0, v[162:163]
	s_mov_b32 m0, s39
	s_addc_u32 s53, s21, 0
	global_load_lds_dwordx4 v[184:185], off
	v_lshl_add_u64 v[186:187], s[52:53], 0, v[164:165]
	s_mov_b32 m0, s40
	v_cndmask_b32_e32 v166, v206, v202, vcc
	global_load_lds_dwordx4 v[186:187], off
	v_lshl_add_u64 v[186:187], s[52:53], 0, v[162:163]
	s_mov_b32 m0, s41
	v_lshl_add_u64 v[188:189], s[22:23], 0, v[166:167]
	global_load_lds_dwordx4 v[186:187], off
	s_mov_b32 m0, s26
	v_cndmask_b32_e32 v186, v172, v203, vcc
	global_load_lds_dwordx4 v166, s[22:23]
	s_mov_b32 m0, s27
	v_mov_b32_e32 v187, v167
	global_load_lds_dwordx4 v186, s[22:23]
	s_waitcnt vmcnt(8)
	s_waitcnt lgkmcnt(0)
	v_lshl_add_u64 v[186:187], s[22:23], 0, v[186:187]
	s_barrier
	s_setprio 1
	s_nop 0
	s_waitcnt lgkmcnt(0)
	v_mfma_scale_f32_16x16x128_f8f6f4 v[82:85], v[26:33], v[208:215], 0, v197, v198 op_sel_hi:[0,0,0]
	v_mfma_scale_f32_16x16x128_f8f6f4 v[70:73], v[18:25], v[208:215], 0, v197, v198 op_sel_hi:[0,0,0]
	v_mfma_scale_f32_16x16x128_f8f6f4 v[78:81], v[26:33], v[216:223], 0, v197, v198 op_sel_hi:[0,0,0]
	v_mfma_scale_f32_16x16x128_f8f6f4 v[66:69], v[18:25], v[216:223], 0, v197, v198 op_sel_hi:[0,0,0]
	v_mfma_scale_f32_16x16x128_f8f6f4 v[58:61], v[26:33], v[224:231], 0, v197, v198 op_sel_hi:[0,0,0]
	v_mfma_scale_f32_16x16x128_f8f6f4 v[50:53], v[18:25], v[224:231], 0, v197, v198 op_sel_hi:[0,0,0]
	v_mfma_scale_f32_16x16x128_f8f6f4 v[42:45], v[26:33], v[232:239], 0, v197, v198 op_sel_hi:[0,0,0]
	v_mfma_scale_f32_16x16x128_f8f6f4 v[34:37], v[18:25], v[232:239], 0, v197, v198 op_sel_hi:[0,0,0]
	s_setprio 0
	s_setprio 1
	s_nop 0
	v_mfma_scale_f32_16x16x128_f8f6f4 v[102:105], v[10:17], v[208:215], 0, v197, v198 op_sel_hi:[0,0,0]
	v_mfma_scale_f32_16x16x128_f8f6f4 v[90:93], v[2:9], v[208:215], 0, v197, v198 op_sel_hi:[0,0,0]
	v_mfma_scale_f32_16x16x128_f8f6f4 v[86:89], v[10:17], v[216:223], 0, v197, v198 op_sel_hi:[0,0,0]
	v_mfma_scale_f32_16x16x128_f8f6f4 v[74:77], v[2:9], v[216:223], 0, v197, v198 op_sel_hi:[0,0,0]
	v_mfma_scale_f32_16x16x128_f8f6f4 v[62:65], v[10:17], v[224:231], 0, v197, v198 op_sel_hi:[0,0,0]
	v_mfma_scale_f32_16x16x128_f8f6f4 v[54:57], v[2:9], v[224:231], 0, v197, v198 op_sel_hi:[0,0,0]
	v_mfma_scale_f32_16x16x128_f8f6f4 v[46:49], v[10:17], v[232:239], 0, v197, v198 op_sel_hi:[0,0,0]
	v_mfma_scale_f32_16x16x128_f8f6f4 v[38:41], v[2:9], v[232:239], 0, v197, v198 op_sel_hi:[0,0,0]
	s_setprio 0
	s_barrier
; #define PG8_STAGE(bufoff, gbase, voff) do { _Pragma("unroll") for (int _i = 0; _i < 2; ++_i) \
;         __builtin_amdgcn_global_load_lds((const unsigned*)((const char*)(gbase) + (voff)[_i]), (PG8_LAS unsigned*)(lds + (bufoff) + ldsw + _i * 8192), 16, 0, 0); } while (0)
; #define PG8_STAGE_A(bufoff, gbase, h, nx) do { if constexpr (Sched::GATHER) { const unsigned vv_[2] = {(nx) ? vAn[h][0] : vA[h][0], (nx) ? vAn[h][1] : vA[h][1]}; PG8_STAGE(bufoff, gbase, vv_); } \
;         else { PG8_STAGE(bufoff, (gbase) + (h) * hstep, voffA); } } while (0)
; #define PG8_LDA(dst, b, h) do { _Pragma("unroll") for (int m = 0; m < 4; ++m) _Pragma("unroll") for (int k = 0; k < 2; ++k) dst[m][k] = *(const PG8_LAS bf16x8*)(lds + PG8_SA(b, h) + aoff + m * 2048 + k * 1024); } while (0)
; #define PG8_LDB(dst, b, h) do { _Pragma("unroll") for (int n = 0; n < 2; ++n) _Pragma("unroll") for (int k = 0; k < 2; ++k) dst[n][k] = *(const PG8_LAS bf16x8*)(lds + PG8_SB(b, h) + boff + n * 2048 + k * 1024); } while (0)
; #define PG8_WAIT_V(n) asm volatile("s_waitcnt vmcnt(" #n ")" ::: "memory")
; #define PG8_WAIT_L(n) asm volatile("s_waitcnt lgkmcnt(" #n ")" ::: "memory")
; #define PG8_BAR __builtin_amdgcn_s_barrier()
; #define PG8_SCHED __builtin_amdgcn_sched_barrier(0)
;     ...
;             PG8_LDB(B0, 1, 0); PG8_LDB(B1, 1, 1); PG8_SCHED; PG8_LDA(At, 1, 0); PG8_STAGE_A(PG8_SA(0, 1), a2, 1, last);
;             PG8_WAIT_V(8); PG8_WAIT_L(0); PG8_BAR; PG8_MMA(0, 0, At, B0); PG8_MMA(0, 1, At, B1); PG8_BAR; PG8_SCHED;
;             PG8_LDA(At, 1, 1); PG8_STAGE(PG8_SB(1, 0), b3, voffB); PG8_STAGE(PG8_SB(1, 1), b3 + hstepB, voffB); PG8_STAGE_A(PG8_SA(1, 0), a3, 0, last);
;             PG8_WAIT_V(8); PG8_WAIT_L(0); PG8_BAR; PG8_MMA(1, 0, At, B0); PG8_MMA(1, 1, At, B1); PG8_BAR; PG8_SCHED;
	ds_read_b128 v[2:5], v199
	ds_read_b128 v[6:9], v199 offset:1024
	ds_read_b128 v[10:13], v199 offset:2048
	ds_read_b128 v[14:17], v199 offset:3072
	ds_read_b128 v[18:21], v200
	ds_read_b128 v[22:25], v200 offset:1024
	ds_read_b128 v[26:29], v200 offset:2048
	ds_read_b128 v[30:33], v200 offset:3072
	s_mov_b32 m0, s28
	v_cndmask_b32_e32 v166, v174, v204, vcc
	ds_read_b128 v[208:211], v196 offset:32768
	ds_read_b128 v[212:215], v196 offset:33792
	ds_read_b128 v[216:219], v196 offset:34816
	ds_read_b128 v[220:223], v196 offset:35840
	ds_read_b128 v[224:227], v196 offset:36864
	ds_read_b128 v[228:231], v196 offset:37888
	ds_read_b128 v[232:235], v196 offset:38912
	ds_read_b128 v[236:239], v196 offset:39936
	v_cndmask_b32_e32 v175, v176, v205, vcc
	global_load_lds_dwordx4 v166, s[22:23]
	s_mov_b32 m0, s29
	s_nop 0
	global_load_lds_dwordx4 v175, s[22:23]
	s_waitcnt vmcnt(8)
	s_waitcnt lgkmcnt(0)
	s_barrier
	s_setprio 1
	s_nop 0
	s_waitcnt lgkmcnt(0)
	v_mfma_scale_f32_16x16x128_f8f6f4 v[158:161], v[2:9], v[208:215], v[158:161], v197, v198 op_sel_hi:[0,0,0]
	v_mfma_scale_f32_16x16x128_f8f6f4 v[150:153], v[10:17], v[208:215], v[150:153], v197, v198 op_sel_hi:[0,0,0]
	v_mfma_scale_f32_16x16x128_f8f6f4 v[142:145], v[2:9], v[216:223], v[142:145], v197, v198 op_sel_hi:[0,0,0]
	v_mfma_scale_f32_16x16x128_f8f6f4 v[134:137], v[10:17], v[216:223], v[134:137], v197, v198 op_sel_hi:[0,0,0]
	v_mfma_scale_f32_16x16x128_f8f6f4 v[126:129], v[2:9], v[224:231], v[126:129], v197, v198 op_sel_hi:[0,0,0]
	v_mfma_scale_f32_16x16x128_f8f6f4 v[118:121], v[10:17], v[224:231], v[118:121], v197, v198 op_sel_hi:[0,0,0]
	v_mfma_scale_f32_16x16x128_f8f6f4 v[110:113], v[2:9], v[232:239], v[110:113], v197, v198 op_sel_hi:[0,0,0]
	v_mfma_scale_f32_16x16x128_f8f6f4 v[98:101], v[10:17], v[232:239], v[98:101], v197, v198 op_sel_hi:[0,0,0]
	s_setprio 0
	s_setprio 1
	s_nop 0
	v_mfma_scale_f32_16x16x128_f8f6f4 v[154:157], v[18:25], v[208:215], v[154:157], v197, v198 op_sel_hi:[0,0,0]
	v_mfma_scale_f32_16x16x128_f8f6f4 v[146:149], v[26:33], v[208:215], v[146:149], v197, v198 op_sel_hi:[0,0,0]
	v_mfma_scale_f32_16x16x128_f8f6f4 v[138:141], v[18:25], v[216:223], v[138:141], v197, v198 op_sel_hi:[0,0,0]
	v_mfma_scale_f32_16x16x128_f8f6f4 v[130:133], v[26:33], v[216:223], v[130:133], v197, v198 op_sel_hi:[0,0,0]
	v_mfma_scale_f32_16x16x128_f8f6f4 v[122:125], v[18:25], v[224:231], v[122:125], v197, v198 op_sel_hi:[0,0,0]
	v_mfma_scale_f32_16x16x128_f8f6f4 v[114:117], v[26:33], v[224:231], v[114:117], v197, v198 op_sel_hi:[0,0,0]
	v_mfma_scale_f32_16x16x128_f8f6f4 v[106:109], v[18:25], v[232:239], v[106:109], v197, v198 op_sel_hi:[0,0,0]
	v_mfma_scale_f32_16x16x128_f8f6f4 v[94:97], v[26:33], v[232:239], v[94:97], v197, v198 op_sel_hi:[0,0,0]
	s_setprio 0
	s_barrier
	s_mov_b32 m0, s42
	v_lshl_add_u64 v[182:183], v[182:183], 0, s[10:11]
	s_add_u32 s20, s20, 0x20080
	ds_read_b128 v[208:211], v196 offset:49152
	ds_read_b128 v[212:215], v196 offset:50176
	ds_read_b128 v[216:219], v196 offset:51200
	ds_read_b128 v[220:223], v196 offset:52224
	ds_read_b128 v[224:227], v196 offset:53248
	ds_read_b128 v[228:231], v196 offset:54272
	ds_read_b128 v[232:235], v196 offset:55296
	ds_read_b128 v[236:239], v196 offset:56320
	global_load_lds_dwordx4 v[182:183], off
	v_lshl_add_u64 v[182:183], v[184:185], 0, s[10:11]
	s_mov_b32 m0, s43
	s_addc_u32 s21, s21, 0
	global_load_lds_dwordx4 v[182:183], off
	v_lshl_add_u64 v[182:183], s[20:21], 0, v[164:165]
	s_mov_b32 m0, s44
	s_nop 0
	global_load_lds_dwordx4 v[182:183], off
	v_lshl_add_u64 v[182:183], s[20:21], 0, v[162:163]
	s_add_i32 m0, s44, 0x2000
	s_nop 0
	global_load_lds_dwordx4 v[182:183], off
	v_lshl_add_u64 v[182:183], v[188:189], 0, s[10:11]
	s_mov_b32 m0, s31
	s_nop 0
	global_load_lds_dwordx4 v[182:183], off
	v_lshl_add_u64 v[182:183], v[186:187], 0, s[10:11]
	s_mov_b32 m0, s34
	s_nop 0
	global_load_lds_dwordx4 v[182:183], off
	s_waitcnt vmcnt(8)
	s_waitcnt lgkmcnt(0)
	s_barrier
	s_setprio 1
	s_nop 0
	s_waitcnt lgkmcnt(0)
	v_mfma_scale_f32_16x16x128_f8f6f4 v[82:85], v[2:9], v[208:215], v[82:85], v197, v198 op_sel_hi:[0,0,0]
	v_mfma_scale_f32_16x16x128_f8f6f4 v[70:73], v[10:17], v[208:215], v[70:73], v197, v198 op_sel_hi:[0,0,0]
	v_mfma_scale_f32_16x16x128_f8f6f4 v[78:81], v[2:9], v[216:223], v[78:81], v197, v198 op_sel_hi:[0,0,0]
	v_mfma_scale_f32_16x16x128_f8f6f4 v[66:69], v[10:17], v[216:223], v[66:69], v197, v198 op_sel_hi:[0,0,0]
	v_mfma_scale_f32_16x16x128_f8f6f4 v[58:61], v[2:9], v[224:231], v[58:61], v197, v198 op_sel_hi:[0,0,0]
	v_mfma_scale_f32_16x16x128_f8f6f4 v[50:53], v[10:17], v[224:231], v[50:53], v197, v198 op_sel_hi:[0,0,0]
	v_mfma_scale_f32_16x16x128_f8f6f4 v[42:45], v[2:9], v[232:239], v[42:45], v197, v198 op_sel_hi:[0,0,0]
	v_mfma_scale_f32_16x16x128_f8f6f4 v[34:37], v[10:17], v[232:239], v[34:37], v197, v198 op_sel_hi:[0,0,0]
	s_setprio 0
	s_setprio 1
	s_nop 0
	v_mfma_scale_f32_16x16x128_f8f6f4 v[102:105], v[18:25], v[208:215], v[102:105], v197, v198 op_sel_hi:[0,0,0]
	v_mfma_scale_f32_16x16x128_f8f6f4 v[90:93], v[26:33], v[208:215], v[90:93], v197, v198 op_sel_hi:[0,0,0]
	v_mfma_scale_f32_16x16x128_f8f6f4 v[86:89], v[18:25], v[216:223], v[86:89], v197, v198 op_sel_hi:[0,0,0]
	v_mfma_scale_f32_16x16x128_f8f6f4 v[74:77], v[26:33], v[216:223], v[74:77], v197, v198 op_sel_hi:[0,0,0]
	v_mfma_scale_f32_16x16x128_f8f6f4 v[62:65], v[18:25], v[224:231], v[62:65], v197, v198 op_sel_hi:[0,0,0]
	v_mfma_scale_f32_16x16x128_f8f6f4 v[54:57], v[26:33], v[224:231], v[54:57], v197, v198 op_sel_hi:[0,0,0]
	v_mfma_scale_f32_16x16x128_f8f6f4 v[46:49], v[18:25], v[232:239], v[46:49], v197, v198 op_sel_hi:[0,0,0]
	v_mfma_scale_f32_16x16x128_f8f6f4 v[38:41], v[26:33], v[232:239], v[38:41], v197, v198 op_sel_hi:[0,0,0]
	s_setprio 0
	s_barrier
	s_add_i32 s51, s51, 2
	s_add_u32 s4, s4, 0x100
	s_addc_u32 s5, s5, 0
; #define PG8_STAGE(bufoff, gbase, voff) do { _Pragma("unroll") for (int _i = 0; _i < 2; ++_i) \
;         __builtin_amdgcn_global_load_lds((const unsigned*)((const char*)(gbase) + (voff)[_i]), (PG8_LAS unsigned*)(lds + (bufoff) + ldsw + _i * 8192), 16, 0, 0); } while (0)
; #define PG8_STAGE_A(bufoff, gbase, h, nx) do { if constexpr (Sched::GATHER) { const unsigned vv_[2] = {(nx) ? vAn[h][0] : vA[h][0], (nx) ? vAn[h][1] : vA[h][1]}; PG8_STAGE(bufoff, gbase, vv_); } \
;         else { PG8_STAGE(bufoff, (gbase) + (h) * hstep, voffA); } } while (0)
; #define PG8_LDA(dst, b, h) do { _Pragma("unroll") for (int m = 0; m < 4; ++m) _Pragma("unroll") for (int k = 0; k < 2; ++k) dst[m][k] = *(const PG8_LAS bf16x8*)(lds + PG8_SA(b, h) + aoff + m * 2048 + k * 1024); } while (0)
; #define PG8_LDB(dst, b, h) do { _Pragma("unroll") for (int n = 0; n < 2; ++n) _Pragma("unroll") for (int k = 0; k < 2; ++k) dst[n][k] = *(const PG8_LAS bf16x8*)(lds + PG8_SB(b, h) + boff + n * 2048 + k * 1024); } while (0)
; #define PG8_WAIT_V(n) asm volatile("s_waitcnt vmcnt(" #n ")" ::: "memory")
; #define PG8_WAIT_L(n) asm volatile("s_waitcnt lgkmcnt(" #n ")" ::: "memory")
; #define PG8_BAR __builtin_amdgcn_s_barrier()
; #define PG8_SCHED __builtin_amdgcn_sched_barrier(0)
;     ...
;             const bool last = (t == nt - 2);
;             const char* a1 = cA + (size_t)(t + 1) * kstep;
;             const char* a2 = last ? nA : cA + (size_t)(t + 2) * kstep; const char* b2 = last ? nB : cB + (size_t)(t + 2) * kstep;
;             const char* a3 = a2 + kstep; const char* b3 = b2 + kstep;
;             if (last && has_next) S.a_ready(nxt);
;             if constexpr (SP2) {
;             PG8_LDB(B0, 0, 0); PG8_LDB(B1, 0, 1); PG8_SCHED; PG8_LDA(At, 0, 0); PG8_STAGE_A(PG8_SA(1, 1), a1, 1, false);
;             PG8_WAIT_V(8); PG8_WAIT_L(0); PG8_BAR; PG8_MMA(0, 0, At, B0); PG8_MMA(0, 1, At, B1); PG8_BAR; PG8_SCHED;
;             PG8_LDA(At, 0, 1); PG8_STAGE(PG8_SB(0, 0), b2, voffB); PG8_STAGE(PG8_SB(0, 1), b2 + hstepB, voffB); PG8_STAGE_A(PG8_SA(0, 0), a2, 0, last);
;             PG8_WAIT_V(8); PG8_WAIT_L(0); PG8_BAR; PG8_MMA(1, 0, At, B0); PG8_MMA(1, 1, At, B1); PG8_BAR; PG8_SCHED;
.LBB0_841:
	ds_read_b128 v[26:29], v194
	ds_read_b128 v[30:33], v194 offset:1024
	ds_read_b128 v[18:21], v194 offset:2048
	ds_read_b128 v[22:25], v194 offset:3072
	ds_read_b128 v[10:13], v195
	ds_read_b128 v[14:17], v195 offset:1024
	ds_read_b128 v[2:5], v195 offset:2048
	ds_read_b128 v[6:9], v195 offset:3072
	s_add_u32 s20, s54, s4
	s_addc_u32 s21, s55, s5
	s_add_u32 s22, s20, 0x25400100
	s_addc_u32 s23, s21, 0
	s_add_u32 s52, s49, s4
	s_addc_u32 s53, s50, s5
	s_cmpk_eq_i32 s4, 0x300
	s_cselect_b64 vcc, -1, 0
	s_and_b64 s[20:21], vcc, exec
	s_cselect_b32 s23, s93, s23
	s_cselect_b32 s22, s92, s22
	s_cselect_b32 s21, s17, s53
	s_cselect_b32 s20, s48, s52
	s_mov_b32 m0, s36
	v_lshl_add_u64 v[232:233], v[180:181], 0, s[4:5]
	ds_read_b128 v[182:185], v196
	ds_read_b128 v[186:189], v196 offset:1024
	ds_read_b128 v[208:211], v196 offset:2048
	ds_read_b128 v[212:215], v196 offset:3072
	ds_read_b128 v[216:219], v196 offset:4096
	ds_read_b128 v[220:223], v196 offset:5120
	ds_read_b128 v[224:227], v196 offset:6144
	ds_read_b128 v[228:231], v196 offset:7168
	global_load_lds_dwordx4 v[232:233], off
	v_lshl_add_u64 v[232:233], v[178:179], 0, s[4:5]
	s_mov_b32 m0, s37
	s_nop 0
	global_load_lds_dwordx4 v[232:233], off
	s_waitcnt vmcnt(8)
	s_waitcnt lgkmcnt(0)
	s_barrier
	s_setprio 1
	s_nop 0
	s_waitcnt lgkmcnt(0)
	v_mfma_scale_f32_16x16x128_f8f6f4 v[158:161], v[26:33], v[182:189], v[158:161], v197, v198 op_sel_hi:[0,0,0]
	v_mfma_scale_f32_16x16x128_f8f6f4 v[150:153], v[18:25], v[182:189], v[150:153], v197, v198 op_sel_hi:[0,0,0]
	v_mfma_scale_f32_16x16x128_f8f6f4 v[142:145], v[26:33], v[208:215], v[142:145], v197, v198 op_sel_hi:[0,0,0]
	v_mfma_scale_f32_16x16x128_f8f6f4 v[134:137], v[18:25], v[208:215], v[134:137], v197, v198 op_sel_hi:[0,0,0]
	v_mfma_scale_f32_16x16x128_f8f6f4 v[126:129], v[26:33], v[216:223], v[126:129], v197, v198 op_sel_hi:[0,0,0]
	v_mfma_scale_f32_16x16x128_f8f6f4 v[118:121], v[18:25], v[216:223], v[118:121], v197, v198 op_sel_hi:[0,0,0]
	v_mfma_scale_f32_16x16x128_f8f6f4 v[110:113], v[26:33], v[224:231], v[110:113], v197, v198 op_sel_hi:[0,0,0]
	v_mfma_scale_f32_16x16x128_f8f6f4 v[98:101], v[18:25], v[224:231], v[98:101], v197, v198 op_sel_hi:[0,0,0]
	s_setprio 0
	s_setprio 1
	s_nop 0
	v_mfma_scale_f32_16x16x128_f8f6f4 v[154:157], v[10:17], v[182:189], v[154:157], v197, v198 op_sel_hi:[0,0,0]
	v_mfma_scale_f32_16x16x128_f8f6f4 v[146:149], v[2:9], v[182:189], v[146:149], v197, v198 op_sel_hi:[0,0,0]
	v_mfma_scale_f32_16x16x128_f8f6f4 v[138:141], v[10:17], v[208:215], v[138:141], v197, v198 op_sel_hi:[0,0,0]
	v_mfma_scale_f32_16x16x128_f8f6f4 v[130:133], v[2:9], v[208:215], v[130:133], v197, v198 op_sel_hi:[0,0,0]
	v_mfma_scale_f32_16x16x128_f8f6f4 v[122:125], v[10:17], v[216:223], v[122:125], v197, v198 op_sel_hi:[0,0,0]
	v_mfma_scale_f32_16x16x128_f8f6f4 v[114:117], v[2:9], v[216:223], v[114:117], v197, v198 op_sel_hi:[0,0,0]
	v_mfma_scale_f32_16x16x128_f8f6f4 v[106:109], v[10:17], v[224:231], v[106:109], v197, v198 op_sel_hi:[0,0,0]
	v_mfma_scale_f32_16x16x128_f8f6f4 v[94:97], v[2:9], v[224:231], v[94:97], v197, v198 op_sel_hi:[0,0,0]
	s_setprio 0
	s_barrier
	s_mov_b32 m0, s38
	v_lshl_add_u64 v[182:183], s[20:21], 0, v[164:165]
	s_add_u32 s52, s20, 0x20000
	ds_read_b128 v[208:211], v196 offset:16384
	ds_read_b128 v[212:215], v196 offset:17408
	ds_read_b128 v[216:219], v196 offset:18432
	ds_read_b128 v[220:223], v196 offset:19456
	ds_read_b128 v[224:227], v196 offset:20480
	ds_read_b128 v[228:231], v196 offset:21504
	ds_read_b128 v[232:235], v196 offset:22528
	ds_read_b128 v[236:239], v196 offset:23552
	global_load_lds_dwordx4 v[182:183], off
	v_lshl_add_u64 v[184:185], s[20:21], 0, v[162:163]
	s_mov_b32 m0, s39
	s_addc_u32 s53, s21, 0
	global_load_lds_dwordx4 v[184:185], off
	v_lshl_add_u64 v[186:187], s[52:53], 0, v[164:165]
	s_mov_b32 m0, s40
	v_cndmask_b32_e32 v166, v206, v202, vcc
	global_load_lds_dwordx4 v[186:187], off
	v_lshl_add_u64 v[186:187], s[52:53], 0, v[162:163]
	s_mov_b32 m0, s41
	v_lshl_add_u64 v[188:189], s[22:23], 0, v[166:167]
	global_load_lds_dwordx4 v[186:187], off
	s_mov_b32 m0, s26
	v_cndmask_b32_e32 v186, v172, v203, vcc
	global_load_lds_dwordx4 v166, s[22:23]
	s_mov_b32 m0, s27
	v_mov_b32_e32 v187, v167
	global_load_lds_dwordx4 v186, s[22:23]
	s_waitcnt vmcnt(8)
	s_waitcnt lgkmcnt(0)
	v_lshl_add_u64 v[186:187], s[22:23], 0, v[186:187]
	s_barrier
	s_setprio 1
	s_nop 0
	s_waitcnt lgkmcnt(0)
	v_mfma_scale_f32_16x16x128_f8f6f4 v[82:85], v[26:33], v[208:215], v[82:85], v197, v198 op_sel_hi:[0,0,0]
	v_mfma_scale_f32_16x16x128_f8f6f4 v[70:73], v[18:25], v[208:215], v[70:73], v197, v198 op_sel_hi:[0,0,0]
	v_mfma_scale_f32_16x16x128_f8f6f4 v[78:81], v[26:33], v[216:223], v[78:81], v197, v198 op_sel_hi:[0,0,0]
	v_mfma_scale_f32_16x16x128_f8f6f4 v[66:69], v[18:25], v[216:223], v[66:69], v197, v198 op_sel_hi:[0,0,0]
	v_mfma_scale_f32_16x16x128_f8f6f4 v[58:61], v[26:33], v[224:231], v[58:61], v197, v198 op_sel_hi:[0,0,0]
	v_mfma_scale_f32_16x16x128_f8f6f4 v[50:53], v[18:25], v[224:231], v[50:53], v197, v198 op_sel_hi:[0,0,0]
	v_mfma_scale_f32_16x16x128_f8f6f4 v[42:45], v[26:33], v[232:239], v[42:45], v197, v198 op_sel_hi:[0,0,0]
	v_mfma_scale_f32_16x16x128_f8f6f4 v[34:37], v[18:25], v[232:239], v[34:37], v197, v198 op_sel_hi:[0,0,0]
	s_setprio 0
	s_setprio 1
	s_nop 0
	v_mfma_scale_f32_16x16x128_f8f6f4 v[102:105], v[10:17], v[208:215], v[102:105], v197, v198 op_sel_hi:[0,0,0]
	v_mfma_scale_f32_16x16x128_f8f6f4 v[90:93], v[2:9], v[208:215], v[90:93], v197, v198 op_sel_hi:[0,0,0]
	v_mfma_scale_f32_16x16x128_f8f6f4 v[86:89], v[10:17], v[216:223], v[86:89], v197, v198 op_sel_hi:[0,0,0]
	v_mfma_scale_f32_16x16x128_f8f6f4 v[74:77], v[2:9], v[216:223], v[74:77], v197, v198 op_sel_hi:[0,0,0]
	v_mfma_scale_f32_16x16x128_f8f6f4 v[62:65], v[10:17], v[224:231], v[62:65], v197, v198 op_sel_hi:[0,0,0]
	v_mfma_scale_f32_16x16x128_f8f6f4 v[54:57], v[2:9], v[224:231], v[54:57], v197, v198 op_sel_hi:[0,0,0]
	v_mfma_scale_f32_16x16x128_f8f6f4 v[46:49], v[10:17], v[232:239], v[46:49], v197, v198 op_sel_hi:[0,0,0]
	v_mfma_scale_f32_16x16x128_f8f6f4 v[38:41], v[2:9], v[232:239], v[38:41], v197, v198 op_sel_hi:[0,0,0]
	s_setprio 0
	s_barrier
; #define PG8_STAGE(bufoff, gbase, voff) do { _Pragma("unroll") for (int _i = 0; _i < 2; ++_i) \
;         __builtin_amdgcn_global_load_lds((const unsigned*)((const char*)(gbase) + (voff)[_i]), (PG8_LAS unsigned*)(lds + (bufoff) + ldsw + _i * 8192), 16, 0, 0); } while (0)
; #define PG8_STAGE_A(bufoff, gbase, h, nx) do { if constexpr (Sched::GATHER) { const unsigned vv_[2] = {(nx) ? vAn[h][0] : vA[h][0], (nx) ? vAn[h][1] : vA[h][1]}; PG8_STAGE(bufoff, gbase, vv_); } \
;         else { PG8_STAGE(bufoff, (gbase) + (h) * hstep, voffA); } } while (0)
; #define PG8_LDA(dst, b, h) do { _Pragma("unroll") for (int m = 0; m < 4; ++m) _Pragma("unroll") for (int k = 0; k < 2; ++k) dst[m][k] = *(const PG8_LAS bf16x8*)(lds + PG8_SA(b, h) + aoff + m * 2048 + k * 1024); } while (0)
; #define PG8_LDB(dst, b, h) do { _Pragma("unroll") for (int n = 0; n < 2; ++n) _Pragma("unroll") for (int k = 0; k < 2; ++k) dst[n][k] = *(const PG8_LAS bf16x8*)(lds + PG8_SB(b, h) + boff + n * 2048 + k * 1024); } while (0)
; #define PG8_WAIT_V(n) asm volatile("s_waitcnt vmcnt(" #n ")" ::: "memory")
; #define PG8_WAIT_L(n) asm volatile("s_waitcnt lgkmcnt(" #n ")" ::: "memory")
; #define PG8_BAR __builtin_amdgcn_s_barrier()
; #define PG8_SCHED __builtin_amdgcn_sched_barrier(0)
;     ...
;         for (int t = 0; t < nt; t += 2) {
;     ...
;             PG8_LDB(B0, 1, 0); PG8_LDB(B1, 1, 1); PG8_SCHED; PG8_LDA(At, 1, 0); PG8_STAGE_A(PG8_SA(0, 1), a2, 1, last);
;             PG8_WAIT_V(8); PG8_WAIT_L(0); PG8_BAR; PG8_MMA(0, 0, At, B0); PG8_MMA(0, 1, At, B1); PG8_BAR; PG8_SCHED;
;             PG8_LDA(At, 1, 1); PG8_STAGE(PG8_SB(1, 0), b3, voffB); PG8_STAGE(PG8_SB(1, 1), b3 + hstepB, voffB); PG8_STAGE_A(PG8_SA(1, 0), a3, 0, last);
;             PG8_WAIT_V(8); PG8_WAIT_L(0); PG8_BAR; PG8_MMA(1, 0, At, B0); PG8_MMA(1, 1, At, B1); PG8_BAR; PG8_SCHED;
	ds_read_b128 v[2:5], v199
	ds_read_b128 v[6:9], v199 offset:1024
	ds_read_b128 v[10:13], v199 offset:2048
	ds_read_b128 v[14:17], v199 offset:3072
	ds_read_b128 v[18:21], v200
	ds_read_b128 v[22:25], v200 offset:1024
	ds_read_b128 v[26:29], v200 offset:2048
	ds_read_b128 v[30:33], v200 offset:3072
	s_mov_b32 m0, s28
	v_cndmask_b32_e32 v166, v174, v204, vcc
	ds_read_b128 v[208:211], v196 offset:32768
	ds_read_b128 v[212:215], v196 offset:33792
	ds_read_b128 v[216:219], v196 offset:34816
	ds_read_b128 v[220:223], v196 offset:35840
	ds_read_b128 v[224:227], v196 offset:36864
	ds_read_b128 v[228:231], v196 offset:37888
	ds_read_b128 v[232:235], v196 offset:38912
	ds_read_b128 v[236:239], v196 offset:39936
	v_cndmask_b32_e32 v175, v176, v205, vcc
	global_load_lds_dwordx4 v166, s[22:23]
	s_mov_b32 m0, s29
	s_nop 0
	global_load_lds_dwordx4 v175, s[22:23]
	s_waitcnt vmcnt(8)
	s_waitcnt lgkmcnt(0)
	s_barrier
	s_setprio 1
	s_nop 0
	s_waitcnt lgkmcnt(0)
	v_mfma_scale_f32_16x16x128_f8f6f4 v[158:161], v[2:9], v[208:215], v[158:161], v197, v198 op_sel_hi:[0,0,0]
	v_mfma_scale_f32_16x16x128_f8f6f4 v[150:153], v[10:17], v[208:215], v[150:153], v197, v198 op_sel_hi:[0,0,0]
	v_mfma_scale_f32_16x16x128_f8f6f4 v[142:145], v[2:9], v[216:223], v[142:145], v197, v198 op_sel_hi:[0,0,0]
	v_mfma_scale_f32_16x16x128_f8f6f4 v[134:137], v[10:17], v[216:223], v[134:137], v197, v198 op_sel_hi:[0,0,0]
	v_mfma_scale_f32_16x16x128_f8f6f4 v[126:129], v[2:9], v[224:231], v[126:129], v197, v198 op_sel_hi:[0,0,0]
	v_mfma_scale_f32_16x16x128_f8f6f4 v[118:121], v[10:17], v[224:231], v[118:121], v197, v198 op_sel_hi:[0,0,0]
	v_mfma_scale_f32_16x16x128_f8f6f4 v[110:113], v[2:9], v[232:239], v[110:113], v197, v198 op_sel_hi:[0,0,0]
	v_mfma_scale_f32_16x16x128_f8f6f4 v[98:101], v[10:17], v[232:239], v[98:101], v197, v198 op_sel_hi:[0,0,0]
	s_setprio 0
	s_setprio 1
	s_nop 0
	v_mfma_scale_f32_16x16x128_f8f6f4 v[154:157], v[18:25], v[208:215], v[154:157], v197, v198 op_sel_hi:[0,0,0]
	v_mfma_scale_f32_16x16x128_f8f6f4 v[146:149], v[26:33], v[208:215], v[146:149], v197, v198 op_sel_hi:[0,0,0]
	v_mfma_scale_f32_16x16x128_f8f6f4 v[138:141], v[18:25], v[216:223], v[138:141], v197, v198 op_sel_hi:[0,0,0]
	v_mfma_scale_f32_16x16x128_f8f6f4 v[130:133], v[26:33], v[216:223], v[130:133], v197, v198 op_sel_hi:[0,0,0]
	v_mfma_scale_f32_16x16x128_f8f6f4 v[122:125], v[18:25], v[224:231], v[122:125], v197, v198 op_sel_hi:[0,0,0]
	v_mfma_scale_f32_16x16x128_f8f6f4 v[114:117], v[26:33], v[224:231], v[114:117], v197, v198 op_sel_hi:[0,0,0]
	v_mfma_scale_f32_16x16x128_f8f6f4 v[106:109], v[18:25], v[232:239], v[106:109], v197, v198 op_sel_hi:[0,0,0]
	v_mfma_scale_f32_16x16x128_f8f6f4 v[94:97], v[26:33], v[232:239], v[94:97], v197, v198 op_sel_hi:[0,0,0]
	s_setprio 0
	s_barrier
	s_mov_b32 m0, s42
	v_lshl_add_u64 v[182:183], v[182:183], 0, s[10:11]
	s_add_u32 s20, s20, 0x20080
	ds_read_b128 v[208:211], v196 offset:49152
	ds_read_b128 v[212:215], v196 offset:50176
	ds_read_b128 v[216:219], v196 offset:51200
	ds_read_b128 v[220:223], v196 offset:52224
	ds_read_b128 v[224:227], v196 offset:53248
	ds_read_b128 v[228:231], v196 offset:54272
	ds_read_b128 v[232:235], v196 offset:55296
	ds_read_b128 v[236:239], v196 offset:56320
	global_load_lds_dwordx4 v[182:183], off
	v_lshl_add_u64 v[182:183], v[184:185], 0, s[10:11]
	s_mov_b32 m0, s43
	s_addc_u32 s21, s21, 0
	global_load_lds_dwordx4 v[182:183], off
	v_lshl_add_u64 v[182:183], s[20:21], 0, v[164:165]
	s_mov_b32 m0, s44
	s_nop 0
	global_load_lds_dwordx4 v[182:183], off
	v_lshl_add_u64 v[182:183], s[20:21], 0, v[162:163]
	s_add_i32 m0, s44, 0x2000
	s_nop 0
	global_load_lds_dwordx4 v[182:183], off
	v_lshl_add_u64 v[182:183], v[188:189], 0, s[10:11]
	s_mov_b32 m0, s31
	s_nop 0
	global_load_lds_dwordx4 v[182:183], off
	v_lshl_add_u64 v[182:183], v[186:187], 0, s[10:11]
	s_mov_b32 m0, s34
	s_nop 0
	global_load_lds_dwordx4 v[182:183], off
	s_waitcnt vmcnt(8)
	s_waitcnt lgkmcnt(0)
	s_barrier
	s_setprio 1
	s_nop 0
	s_waitcnt lgkmcnt(0)
	v_mfma_scale_f32_16x16x128_f8f6f4 v[82:85], v[2:9], v[208:215], v[82:85], v197, v198 op_sel_hi:[0,0,0]
	v_mfma_scale_f32_16x16x128_f8f6f4 v[70:73], v[10:17], v[208:215], v[70:73], v197, v198 op_sel_hi:[0,0,0]
	v_mfma_scale_f32_16x16x128_f8f6f4 v[78:81], v[2:9], v[216:223], v[78:81], v197, v198 op_sel_hi:[0,0,0]
	v_mfma_scale_f32_16x16x128_f8f6f4 v[66:69], v[10:17], v[216:223], v[66:69], v197, v198 op_sel_hi:[0,0,0]
	v_mfma_scale_f32_16x16x128_f8f6f4 v[58:61], v[2:9], v[224:231], v[58:61], v197, v198 op_sel_hi:[0,0,0]
	v_mfma_scale_f32_16x16x128_f8f6f4 v[50:53], v[10:17], v[224:231], v[50:53], v197, v198 op_sel_hi:[0,0,0]
	v_mfma_scale_f32_16x16x128_f8f6f4 v[42:45], v[2:9], v[232:239], v[42:45], v197, v198 op_sel_hi:[0,0,0]
	v_mfma_scale_f32_16x16x128_f8f6f4 v[34:37], v[10:17], v[232:239], v[34:37], v197, v198 op_sel_hi:[0,0,0]
	s_setprio 0
	s_setprio 1
	s_nop 0
	v_mfma_scale_f32_16x16x128_f8f6f4 v[102:105], v[18:25], v[208:215], v[102:105], v197, v198 op_sel_hi:[0,0,0]
	v_mfma_scale_f32_16x16x128_f8f6f4 v[90:93], v[26:33], v[208:215], v[90:93], v197, v198 op_sel_hi:[0,0,0]
	v_mfma_scale_f32_16x16x128_f8f6f4 v[86:89], v[18:25], v[216:223], v[86:89], v197, v198 op_sel_hi:[0,0,0]
	v_mfma_scale_f32_16x16x128_f8f6f4 v[74:77], v[26:33], v[216:223], v[74:77], v197, v198 op_sel_hi:[0,0,0]
	v_mfma_scale_f32_16x16x128_f8f6f4 v[62:65], v[18:25], v[224:231], v[62:65], v197, v198 op_sel_hi:[0,0,0]
	v_mfma_scale_f32_16x16x128_f8f6f4 v[54:57], v[26:33], v[224:231], v[54:57], v197, v198 op_sel_hi:[0,0,0]
	v_mfma_scale_f32_16x16x128_f8f6f4 v[46:49], v[18:25], v[232:239], v[46:49], v197, v198 op_sel_hi:[0,0,0]
	v_mfma_scale_f32_16x16x128_f8f6f4 v[38:41], v[26:33], v[232:239], v[38:41], v197, v198 op_sel_hi:[0,0,0]
	s_setprio 0
	s_barrier
	s_add_i32 s51, s51, 2
	s_add_u32 s4, s4, 0x100
	s_addc_u32 s5, s5, 0
	s_cmp_gt_u32 s51, 5
	s_cbranch_scc0 .LBB0_841
	s_and_b64 vcc, exec, s[14:15]
	s_cbranch_vccz .LBB0_844
	s_barrier

; #define PG8_STAGE(bufoff, gbase, voff) do { _Pragma("unroll") for (int _i = 0; _i < 2; ++_i) \
;         __builtin_amdgcn_global_load_lds((const unsigned*)((const char*)(gbase) + (voff)[_i]), (PG8_LAS unsigned*)(lds + (bufoff) + ldsw + _i * 8192), 16, 0, 0); } while (0)
; #define PG8_STAGE_A(bufoff, gbase, h, nx) do { if constexpr (Sched::GATHER) { const unsigned vv_[2] = {(nx) ? vAn[h][0] : vA[h][0], (nx) ? vAn[h][1] : vA[h][1]}; PG8_STAGE(bufoff, gbase, vv_); } \
;         else { PG8_STAGE(bufoff, (gbase) + (h) * hstep, voffA); } } while (0)
; #define PG8_LDA(dst, b, h) do { _Pragma("unroll") for (int m = 0; m < 4; ++m) _Pragma("unroll") for (int k = 0; k < 2; ++k) dst[m][k] = *(const PG8_LAS bf16x8*)(lds + PG8_SA(b, h) + aoff + m * 2048 + k * 1024); } while (0)
; #define PG8_WAIT_V(n) asm volatile("s_waitcnt vmcnt(" #n ")" ::: "memory")
; #define PG8_WAIT_L(n) asm volatile("s_waitcnt lgkmcnt(" #n ")" ::: "memory")
;     ...
;         const bool has_next = S.next(ui + 1, nxt);
;         const char* nA = Sched::GATHER ? cA : (has_next ? (const char*)g.A + (size_t)nxt.pm * tstep : cA);
;         if constexpr (Sched::GATHER) { if (has_next) { PG8_AOFF(vAn, ui + 1); } else { _Pragma("unroll") for (int h_ = 0; h_ < 2; ++h_) _Pragma("unroll") for (int i_ = 0; i_ < 2; ++i_) vAn[h_][i_] = vA[h_][i_]; } } const char* nB = has_next ? (const char*)g.Bt + (size_t)nxt.pb * tstep : cB;
; #pragma nounroll
;         for (int t = 0; t < nt; t += 2) {
;             const bool last = (t == nt - 2);
;             const char* a1 = cA + (size_t)(t + 1) * kstep;
;             const char* a2 = last ? nA : cA + (size_t)(t + 2) * kstep; const char* b2 = last ? nB : cB + (size_t)(t + 2) * kstep;
;             const char* a3 = a2 + kstep; const char* b3 = b2 + kstep;
;             if (last && has_next) S.a_ready(nxt);
;             if constexpr (SP2) {
;             PG8_LDB(B0, 0, 0); PG8_LDB(B1, 0, 1); PG8_SCHED; PG8_LDA(At, 0, 0); PG8_STAGE_A(PG8_SA(1, 1), a1, 1, false);
;             PG8_WAIT_V(8); PG8_WAIT_L(0); PG8_BAR; PG8_MMA(0, 0, At, B0); PG8_MMA(0, 1, At, B1); PG8_BAR; PG8_SCHED;
;             PG8_LDA(At, 0, 1); PG8_STAGE(PG8_SB(0, 0), b2, voffB); PG8_STAGE(PG8_SB(0, 1), b2 + hstepB, voffB); PG8_STAGE_A(PG8_SA(0, 0), a2, 0, last);
;             PG8_WAIT_V(8); PG8_WAIT_L(0); PG8_BAR; PG8_MMA(1, 0, At, B0); PG8_MMA(1, 1, At, B1); PG8_BAR; PG8_SCHED;
.LBB0_894:
	s_ashr_i32 s13, s12, 31
	s_lshl_b64 s[16:17], s[12:13], 19
	v_readlane_b32 s18, v255, 9
	v_readlane_b32 s19, v255, 10
	s_add_u32 s16, s18, s16
	s_addc_u32 s17, s19, s17
	s_and_b64 s[18:19], s[2:3], exec
	s_cselect_b32 s13, s17, s23
	s_cselect_b32 s21, s16, s22
	s_ashr_i32 s15, s14, 31
	s_lshl_b64 s[18:19], s[14:15], 19
	v_readlane_b32 s26, v254, 63
	v_readlane_b32 s27, v255, 0
	s_add_u32 s18, s26, s18
	s_addc_u32 s19, s27, s19
	s_and_b64 s[26:27], s[2:3], exec
	s_cselect_b32 s15, s19, s25
	s_cselect_b32 s44, s18, s24
	s_add_u32 s22, s22, 0x40080
	s_addc_u32 s23, s23, 0
	s_add_u32 s45, s24, 0x100
	s_addc_u32 s46, s25, 0
	s_mov_b32 s47, -2
	ds_read_b128 v[26:29], v188
	ds_read_b128 v[30:33], v188 offset:1024
	ds_read_b128 v[18:21], v188 offset:2048
	ds_read_b128 v[22:25], v188 offset:3072
	ds_read_b128 v[10:13], v189
	ds_read_b128 v[14:17], v189 offset:1024
	ds_read_b128 v[2:5], v189 offset:2048
	ds_read_b128 v[6:9], v189 offset:3072
	s_add_u32 s24, s22, 0xfffc0080
	s_addc_u32 s25, s23, -1
	s_cmp_eq_u32 s47, 12
	s_cselect_b32 s27, s13, s25
	s_cselect_b32 s26, s21, s24
	s_cselect_b32 s25, s15, s46
	s_cselect_b32 s24, s44, s45
	v_lshl_add_u64 v[218:219], s[22:23], 0, v[170:171]
	s_add_i32 m0, s29, 0xc000
	ds_read_b128 v[178:181], v190
	ds_read_b128 v[182:185], v190 offset:1024
	ds_read_b128 v[194:197], v190 offset:2048
	ds_read_b128 v[198:201], v190 offset:3072
	ds_read_b128 v[202:205], v190 offset:4096
	ds_read_b128 v[206:209], v190 offset:5120
	ds_read_b128 v[210:213], v190 offset:6144
	ds_read_b128 v[214:217], v190 offset:7168
	global_load_lds_dwordx4 v[218:219], off
	v_lshl_add_u64 v[218:219], s[22:23], 0, v[172:173]
	s_add_i32 m0, s29, 0xe000
	s_nop 0
	global_load_lds_dwordx4 v[218:219], off
	s_waitcnt vmcnt(8)
	s_waitcnt lgkmcnt(0)
	s_barrier
	s_setprio 1
	s_nop 0
	s_waitcnt lgkmcnt(0)
	v_mfma_scale_f32_16x16x128_f8f6f4 v[158:161], v[26:33], v[178:185], 0, v191, v192 op_sel_hi:[0,0,0]
	v_mfma_scale_f32_16x16x128_f8f6f4 v[154:157], v[18:25], v[178:185], 0, v191, v192 op_sel_hi:[0,0,0]
	v_mfma_scale_f32_16x16x128_f8f6f4 v[142:145], v[26:33], v[194:201], 0, v191, v192 op_sel_hi:[0,0,0]
	v_mfma_scale_f32_16x16x128_f8f6f4 v[138:141], v[18:25], v[194:201], 0, v191, v192 op_sel_hi:[0,0,0]
	v_mfma_scale_f32_16x16x128_f8f6f4 v[126:129], v[26:33], v[202:209], 0, v191, v192 op_sel_hi:[0,0,0]
	v_mfma_scale_f32_16x16x128_f8f6f4 v[122:125], v[18:25], v[202:209], 0, v191, v192 op_sel_hi:[0,0,0]
	v_mfma_scale_f32_16x16x128_f8f6f4 v[110:113], v[26:33], v[210:217], 0, v191, v192 op_sel_hi:[0,0,0]
	v_mfma_scale_f32_16x16x128_f8f6f4 v[106:109], v[18:25], v[210:217], 0, v191, v192 op_sel_hi:[0,0,0]
	s_setprio 0
	s_setprio 1
	s_nop 0
	v_mfma_scale_f32_16x16x128_f8f6f4 v[150:153], v[10:17], v[178:185], 0, v191, v192 op_sel_hi:[0,0,0]
	v_mfma_scale_f32_16x16x128_f8f6f4 v[146:149], v[2:9], v[178:185], 0, v191, v192 op_sel_hi:[0,0,0]
	v_mfma_scale_f32_16x16x128_f8f6f4 v[134:137], v[10:17], v[194:201], 0, v191, v192 op_sel_hi:[0,0,0]
	v_mfma_scale_f32_16x16x128_f8f6f4 v[130:133], v[2:9], v[194:201], 0, v191, v192 op_sel_hi:[0,0,0]
	v_mfma_scale_f32_16x16x128_f8f6f4 v[118:121], v[10:17], v[202:209], 0, v191, v192 op_sel_hi:[0,0,0]
	v_mfma_scale_f32_16x16x128_f8f6f4 v[114:117], v[2:9], v[202:209], 0, v191, v192 op_sel_hi:[0,0,0]
	v_mfma_scale_f32_16x16x128_f8f6f4 v[102:105], v[10:17], v[210:217], 0, v191, v192 op_sel_hi:[0,0,0]
	v_mfma_scale_f32_16x16x128_f8f6f4 v[98:101], v[2:9], v[210:217], 0, v191, v192 op_sel_hi:[0,0,0]
	s_setprio 0
	s_barrier
	s_add_i32 s48, s40, s28
	v_lshl_add_u64 v[178:179], s[24:25], 0, v[166:167]
	s_mov_b32 m0, s48
	ds_read_b128 v[194:197], v190 offset:16384
	ds_read_b128 v[198:201], v190 offset:17408
	ds_read_b128 v[202:205], v190 offset:18432
	ds_read_b128 v[206:209], v190 offset:19456
	ds_read_b128 v[210:213], v190 offset:20480
	ds_read_b128 v[214:217], v190 offset:21504
	ds_read_b128 v[218:221], v190 offset:22528
	ds_read_b128 v[222:225], v190 offset:23552
	global_load_lds_dwordx4 v[178:179], off
	s_add_i32 m0, s48, 0x2000
	s_add_u32 s48, s24, 0x4000
	v_lshl_add_u64 v[180:181], s[24:25], 0, v[162:163]
	s_addc_u32 s49, s25, 0
	s_add_i32 s50, s41, s28
	global_load_lds_dwordx4 v[180:181], off
	v_lshl_add_u64 v[182:183], s[48:49], 0, v[166:167]
	s_mov_b32 m0, s50
	v_lshl_add_u64 v[184:185], s[26:27], 0, v[164:165]
	global_load_lds_dwordx4 v[182:183], off
	v_lshl_add_u64 v[182:183], s[48:49], 0, v[162:163]
	s_add_i32 m0, s50, 0x2000
	s_nop 0
	global_load_lds_dwordx4 v[182:183], off
	v_lshl_add_u64 v[182:183], s[26:27], 0, v[168:169]
	s_mov_b32 m0, s29
	s_nop 0
	global_load_lds_dwordx4 v[182:183], off
	s_mov_b32 m0, s30
	s_nop 0
	global_load_lds_dwordx4 v[184:185], off
	s_waitcnt vmcnt(8)
	s_waitcnt lgkmcnt(0)
	s_barrier
	s_setprio 1
	s_nop 0
	s_waitcnt lgkmcnt(0)
	v_mfma_scale_f32_16x16x128_f8f6f4 v[94:97], v[26:33], v[194:201], 0, v191, v192 op_sel_hi:[0,0,0]
	v_mfma_scale_f32_16x16x128_f8f6f4 v[90:93], v[18:25], v[194:201], 0, v191, v192 op_sel_hi:[0,0,0]
	v_mfma_scale_f32_16x16x128_f8f6f4 v[78:81], v[26:33], v[202:209], 0, v191, v192 op_sel_hi:[0,0,0]
	v_mfma_scale_f32_16x16x128_f8f6f4 v[74:77], v[18:25], v[202:209], 0, v191, v192 op_sel_hi:[0,0,0]
	v_mfma_scale_f32_16x16x128_f8f6f4 v[62:65], v[26:33], v[210:217], 0, v191, v192 op_sel_hi:[0,0,0]
	v_mfma_scale_f32_16x16x128_f8f6f4 v[58:61], v[18:25], v[210:217], 0, v191, v192 op_sel_hi:[0,0,0]
	v_mfma_scale_f32_16x16x128_f8f6f4 v[46:49], v[26:33], v[218:225], 0, v191, v192 op_sel_hi:[0,0,0]
	v_mfma_scale_f32_16x16x128_f8f6f4 v[42:45], v[18:25], v[218:225], 0, v191, v192 op_sel_hi:[0,0,0]
	s_setprio 0
	s_setprio 1
	s_nop 0
	v_mfma_scale_f32_16x16x128_f8f6f4 v[86:89], v[10:17], v[194:201], 0, v191, v192 op_sel_hi:[0,0,0]
	v_mfma_scale_f32_16x16x128_f8f6f4 v[82:85], v[2:9], v[194:201], 0, v191, v192 op_sel_hi:[0,0,0]
	v_mfma_scale_f32_16x16x128_f8f6f4 v[70:73], v[10:17], v[202:209], 0, v191, v192 op_sel_hi:[0,0,0]
	v_mfma_scale_f32_16x16x128_f8f6f4 v[66:69], v[2:9], v[202:209], 0, v191, v192 op_sel_hi:[0,0,0]
	v_mfma_scale_f32_16x16x128_f8f6f4 v[54:57], v[10:17], v[210:217], 0, v191, v192 op_sel_hi:[0,0,0]
	v_mfma_scale_f32_16x16x128_f8f6f4 v[50:53], v[2:9], v[210:217], 0, v191, v192 op_sel_hi:[0,0,0]
	v_mfma_scale_f32_16x16x128_f8f6f4 v[38:41], v[10:17], v[218:225], 0, v191, v192 op_sel_hi:[0,0,0]
	v_mfma_scale_f32_16x16x128_f8f6f4 v[34:37], v[2:9], v[218:225], 0, v191, v192 op_sel_hi:[0,0,0]
	s_setprio 0
	s_barrier
; #define PG8_STAGE(bufoff, gbase, voff) do { _Pragma("unroll") for (int _i = 0; _i < 2; ++_i) \
;         __builtin_amdgcn_global_load_lds((const unsigned*)((const char*)(gbase) + (voff)[_i]), (PG8_LAS unsigned*)(lds + (bufoff) + ldsw + _i * 8192), 16, 0, 0); } while (0)
; #define PG8_STAGE_A(bufoff, gbase, h, nx) do { if constexpr (Sched::GATHER) { const unsigned vv_[2] = {(nx) ? vAn[h][0] : vA[h][0], (nx) ? vAn[h][1] : vA[h][1]}; PG8_STAGE(bufoff, gbase, vv_); } \
;         else { PG8_STAGE(bufoff, (gbase) + (h) * hstep, voffA); } } while (0)
; #define PG8_LDA(dst, b, h) do { _Pragma("unroll") for (int m = 0; m < 4; ++m) _Pragma("unroll") for (int k = 0; k < 2; ++k) dst[m][k] = *(const PG8_LAS bf16x8*)(lds + PG8_SA(b, h) + aoff + m * 2048 + k * 1024); } while (0)
; #define PG8_LDB(dst, b, h) do { _Pragma("unroll") for (int n = 0; n < 2; ++n) _Pragma("unroll") for (int k = 0; k < 2; ++k) dst[n][k] = *(const PG8_LAS bf16x8*)(lds + PG8_SB(b, h) + boff + n * 2048 + k * 1024); } while (0)
; #define PG8_WAIT_V(n) asm volatile("s_waitcnt vmcnt(" #n ")" ::: "memory")
; #define PG8_WAIT_L(n) asm volatile("s_waitcnt lgkmcnt(" #n ")" ::: "memory")
; #define PG8_BAR __builtin_amdgcn_s_barrier()
; #define PG8_SCHED __builtin_amdgcn_sched_barrier(0)
;     ...
;             PG8_LDB(B0, 1, 0); PG8_LDB(B1, 1, 1); PG8_SCHED; PG8_LDA(At, 1, 0); PG8_STAGE_A(PG8_SA(0, 1), a2, 1, last);
;             PG8_WAIT_V(8); PG8_WAIT_L(0); PG8_BAR; PG8_MMA(0, 0, At, B0); PG8_MMA(0, 1, At, B1); PG8_BAR; PG8_SCHED;
;             PG8_LDA(At, 1, 1); PG8_STAGE(PG8_SB(1, 0), b3, voffB); PG8_STAGE(PG8_SB(1, 1), b3 + hstepB, voffB); PG8_STAGE_A(PG8_SA(1, 0), a3, 0, last);
;             PG8_WAIT_V(8); PG8_WAIT_L(0); PG8_BAR; PG8_MMA(1, 0, At, B0); PG8_MMA(1, 1, At, B1); PG8_BAR; PG8_SCHED;
	s_add_i32 s48, 0, 0x18000
	s_add_i32 s49, 0, 0x1c000
	v_add_u32_e32 v14, s48, v186
	v_add_u32_e32 v30, s49, v186
	ds_read_b128 v[2:5], v14
	ds_read_b128 v[6:9], v14 offset:1024
	ds_read_b128 v[10:13], v14 offset:2048
	ds_read_b128 v[14:17], v14 offset:3072
	ds_read_b128 v[18:21], v30
	ds_read_b128 v[22:25], v30 offset:1024
	ds_read_b128 v[26:29], v30 offset:2048
	ds_read_b128 v[30:33], v30 offset:3072
	s_add_u32 s26, s26, 0x40000
	s_addc_u32 s27, s27, 0
	s_mov_b32 m0, s31
	v_lshl_add_u64 v[226:227], s[26:27], 0, v[168:169]
	ds_read_b128 v[194:197], v190 offset:32768
	ds_read_b128 v[198:201], v190 offset:33792
	ds_read_b128 v[202:205], v190 offset:34816
	ds_read_b128 v[206:209], v190 offset:35840
	ds_read_b128 v[210:213], v190 offset:36864
	ds_read_b128 v[214:217], v190 offset:37888
	ds_read_b128 v[218:221], v190 offset:38912
	ds_read_b128 v[222:225], v190 offset:39936
	global_load_lds_dwordx4 v[226:227], off
	v_lshl_add_u64 v[226:227], s[26:27], 0, v[164:165]
	s_mov_b32 m0, s34
	s_nop 0
	global_load_lds_dwordx4 v[226:227], off
	s_waitcnt vmcnt(8)
	s_waitcnt lgkmcnt(0)
	s_barrier
	s_setprio 1
	s_nop 0
	s_waitcnt lgkmcnt(0)
	v_mfma_scale_f32_16x16x128_f8f6f4 v[158:161], v[2:9], v[194:201], v[158:161], v191, v192 op_sel_hi:[0,0,0]
	v_mfma_scale_f32_16x16x128_f8f6f4 v[154:157], v[10:17], v[194:201], v[154:157], v191, v192 op_sel_hi:[0,0,0]
	v_mfma_scale_f32_16x16x128_f8f6f4 v[142:145], v[2:9], v[202:209], v[142:145], v191, v192 op_sel_hi:[0,0,0]
	v_mfma_scale_f32_16x16x128_f8f6f4 v[138:141], v[10:17], v[202:209], v[138:141], v191, v192 op_sel_hi:[0,0,0]
	v_mfma_scale_f32_16x16x128_f8f6f4 v[126:129], v[2:9], v[210:217], v[126:129], v191, v192 op_sel_hi:[0,0,0]
	v_mfma_scale_f32_16x16x128_f8f6f4 v[122:125], v[10:17], v[210:217], v[122:125], v191, v192 op_sel_hi:[0,0,0]
	v_mfma_scale_f32_16x16x128_f8f6f4 v[110:113], v[2:9], v[218:225], v[110:113], v191, v192 op_sel_hi:[0,0,0]
	v_mfma_scale_f32_16x16x128_f8f6f4 v[106:109], v[10:17], v[218:225], v[106:109], v191, v192 op_sel_hi:[0,0,0]
	s_setprio 0
	s_setprio 1
	s_nop 0
	v_mfma_scale_f32_16x16x128_f8f6f4 v[150:153], v[18:25], v[194:201], v[150:153], v191, v192 op_sel_hi:[0,0,0]
	v_mfma_scale_f32_16x16x128_f8f6f4 v[146:149], v[26:33], v[194:201], v[146:149], v191, v192 op_sel_hi:[0,0,0]
	v_mfma_scale_f32_16x16x128_f8f6f4 v[134:137], v[18:25], v[202:209], v[134:137], v191, v192 op_sel_hi:[0,0,0]
	v_mfma_scale_f32_16x16x128_f8f6f4 v[130:133], v[26:33], v[202:209], v[130:133], v191, v192 op_sel_hi:[0,0,0]
	v_mfma_scale_f32_16x16x128_f8f6f4 v[118:121], v[18:25], v[210:217], v[118:121], v191, v192 op_sel_hi:[0,0,0]
	v_mfma_scale_f32_16x16x128_f8f6f4 v[114:117], v[26:33], v[210:217], v[114:117], v191, v192 op_sel_hi:[0,0,0]
	v_mfma_scale_f32_16x16x128_f8f6f4 v[102:105], v[18:25], v[218:225], v[102:105], v191, v192 op_sel_hi:[0,0,0]
	v_mfma_scale_f32_16x16x128_f8f6f4 v[98:101], v[26:33], v[218:225], v[98:101], v191, v192 op_sel_hi:[0,0,0]
	s_setprio 0
	s_barrier
	s_add_i32 s26, s48, s28
	v_lshl_add_u64 v[178:179], v[178:179], 0, s[8:9]
	s_mov_b32 m0, s26
	ds_read_b128 v[194:197], v190 offset:49152
	ds_read_b128 v[198:201], v190 offset:50176
	ds_read_b128 v[202:205], v190 offset:51200
	ds_read_b128 v[206:209], v190 offset:52224
	ds_read_b128 v[210:213], v190 offset:53248
	ds_read_b128 v[214:217], v190 offset:54272
	ds_read_b128 v[218:221], v190 offset:55296
	ds_read_b128 v[222:225], v190 offset:56320
	global_load_lds_dwordx4 v[178:179], off
	s_add_i32 m0, s26, 0x2000
	s_add_u32 s24, s24, 0x4080
	v_lshl_add_u64 v[178:179], v[180:181], 0, s[8:9]
	s_addc_u32 s25, s25, 0
	s_add_i32 s26, s49, s28
	global_load_lds_dwordx4 v[178:179], off
	v_lshl_add_u64 v[178:179], s[24:25], 0, v[166:167]
	s_mov_b32 m0, s26
	s_nop 0
	global_load_lds_dwordx4 v[178:179], off
	v_lshl_add_u64 v[178:179], s[24:25], 0, v[162:163]
	s_add_i32 m0, s26, 0x2000
	s_nop 0
	global_load_lds_dwordx4 v[178:179], off
	v_lshl_add_u64 v[178:179], v[182:183], 0, s[8:9]
	s_mov_b32 m0, s38
	s_nop 0
	global_load_lds_dwordx4 v[178:179], off
	v_lshl_add_u64 v[178:179], v[184:185], 0, s[8:9]
	s_mov_b32 m0, s39
	s_nop 0
	global_load_lds_dwordx4 v[178:179], off
	s_waitcnt vmcnt(8)
	s_waitcnt lgkmcnt(0)
	s_barrier
	s_setprio 1
	s_nop 0
	s_waitcnt lgkmcnt(0)
	v_mfma_scale_f32_16x16x128_f8f6f4 v[94:97], v[2:9], v[194:201], v[94:97], v191, v192 op_sel_hi:[0,0,0]
	v_mfma_scale_f32_16x16x128_f8f6f4 v[90:93], v[10:17], v[194:201], v[90:93], v191, v192 op_sel_hi:[0,0,0]
	v_mfma_scale_f32_16x16x128_f8f6f4 v[78:81], v[2:9], v[202:209], v[78:81], v191, v192 op_sel_hi:[0,0,0]
	v_mfma_scale_f32_16x16x128_f8f6f4 v[74:77], v[10:17], v[202:209], v[74:77], v191, v192 op_sel_hi:[0,0,0]
	v_mfma_scale_f32_16x16x128_f8f6f4 v[62:65], v[2:9], v[210:217], v[62:65], v191, v192 op_sel_hi:[0,0,0]
	v_mfma_scale_f32_16x16x128_f8f6f4 v[58:61], v[10:17], v[210:217], v[58:61], v191, v192 op_sel_hi:[0,0,0]
	v_mfma_scale_f32_16x16x128_f8f6f4 v[46:49], v[2:9], v[218:225], v[46:49], v191, v192 op_sel_hi:[0,0,0]
	v_mfma_scale_f32_16x16x128_f8f6f4 v[42:45], v[10:17], v[218:225], v[42:45], v191, v192 op_sel_hi:[0,0,0]
	s_setprio 0
	s_setprio 1
	s_nop 0
	v_mfma_scale_f32_16x16x128_f8f6f4 v[86:89], v[18:25], v[194:201], v[86:89], v191, v192 op_sel_hi:[0,0,0]
	v_mfma_scale_f32_16x16x128_f8f6f4 v[82:85], v[26:33], v[194:201], v[82:85], v191, v192 op_sel_hi:[0,0,0]
	v_mfma_scale_f32_16x16x128_f8f6f4 v[70:73], v[18:25], v[202:209], v[70:73], v191, v192 op_sel_hi:[0,0,0]
	v_mfma_scale_f32_16x16x128_f8f6f4 v[66:69], v[26:33], v[202:209], v[66:69], v191, v192 op_sel_hi:[0,0,0]
	v_mfma_scale_f32_16x16x128_f8f6f4 v[54:57], v[18:25], v[210:217], v[54:57], v191, v192 op_sel_hi:[0,0,0]
	v_mfma_scale_f32_16x16x128_f8f6f4 v[50:53], v[26:33], v[210:217], v[50:53], v191, v192 op_sel_hi:[0,0,0]
	v_mfma_scale_f32_16x16x128_f8f6f4 v[38:41], v[18:25], v[218:225], v[38:41], v191, v192 op_sel_hi:[0,0,0]
	v_mfma_scale_f32_16x16x128_f8f6f4 v[34:37], v[26:33], v[218:225], v[34:37], v191, v192 op_sel_hi:[0,0,0]
	s_setprio 0
	s_barrier
	s_add_i32 s47, s47, 2
	s_add_u32 s22, s22, 0x100
	s_addc_u32 s23, s23, 0
	s_add_u32 s45, s45, 0x100
	s_addc_u32 s46, s46, 0
; #define PG8_STAGE(bufoff, gbase, voff) do { _Pragma("unroll") for (int _i = 0; _i < 2; ++_i) \
;         __builtin_amdgcn_global_load_lds((const unsigned*)((const char*)(gbase) + (voff)[_i]), (PG8_LAS unsigned*)(lds + (bufoff) + ldsw + _i * 8192), 16, 0, 0); } while (0)
; #define PG8_STAGE_A(bufoff, gbase, h, nx) do { if constexpr (Sched::GATHER) { const unsigned vv_[2] = {(nx) ? vAn[h][0] : vA[h][0], (nx) ? vAn[h][1] : vA[h][1]}; PG8_STAGE(bufoff, gbase, vv_); } \
;         else { PG8_STAGE(bufoff, (gbase) + (h) * hstep, voffA); } } while (0)
; #define PG8_LDA(dst, b, h) do { _Pragma("unroll") for (int m = 0; m < 4; ++m) _Pragma("unroll") for (int k = 0; k < 2; ++k) dst[m][k] = *(const PG8_LAS bf16x8*)(lds + PG8_SA(b, h) + aoff + m * 2048 + k * 1024); } while (0)
; #define PG8_LDB(dst, b, h) do { _Pragma("unroll") for (int n = 0; n < 2; ++n) _Pragma("unroll") for (int k = 0; k < 2; ++k) dst[n][k] = *(const PG8_LAS bf16x8*)(lds + PG8_SB(b, h) + boff + n * 2048 + k * 1024); } while (0)
; #define PG8_WAIT_V(n) asm volatile("s_waitcnt vmcnt(" #n ")" ::: "memory")
; #define PG8_WAIT_L(n) asm volatile("s_waitcnt lgkmcnt(" #n ")" ::: "memory")
; #define PG8_BAR __builtin_amdgcn_s_barrier()
; #define PG8_SCHED __builtin_amdgcn_sched_barrier(0)
;     ...
;             const bool last = (t == nt - 2);
;             const char* a1 = cA + (size_t)(t + 1) * kstep;
;             const char* a2 = last ? nA : cA + (size_t)(t + 2) * kstep; const char* b2 = last ? nB : cB + (size_t)(t + 2) * kstep;
;             const char* a3 = a2 + kstep; const char* b3 = b2 + kstep;
;             if (last && has_next) S.a_ready(nxt);
;             if constexpr (SP2) {
;             PG8_LDB(B0, 0, 0); PG8_LDB(B1, 0, 1); PG8_SCHED; PG8_LDA(At, 0, 0); PG8_STAGE_A(PG8_SA(1, 1), a1, 1, false);
;             PG8_WAIT_V(8); PG8_WAIT_L(0); PG8_BAR; PG8_MMA(0, 0, At, B0); PG8_MMA(0, 1, At, B1); PG8_BAR; PG8_SCHED;
;             PG8_LDA(At, 0, 1); PG8_STAGE(PG8_SB(0, 0), b2, voffB); PG8_STAGE(PG8_SB(0, 1), b2 + hstepB, voffB); PG8_STAGE_A(PG8_SA(0, 0), a2, 0, last);
;             PG8_WAIT_V(8); PG8_WAIT_L(0); PG8_BAR; PG8_MMA(1, 0, At, B0); PG8_MMA(1, 1, At, B1); PG8_BAR; PG8_SCHED;
.LBB0_895:
	ds_read_b128 v[26:29], v188
	ds_read_b128 v[30:33], v188 offset:1024
	ds_read_b128 v[18:21], v188 offset:2048
	ds_read_b128 v[22:25], v188 offset:3072
	ds_read_b128 v[10:13], v189
	ds_read_b128 v[14:17], v189 offset:1024
	ds_read_b128 v[2:5], v189 offset:2048
	ds_read_b128 v[6:9], v189 offset:3072
	s_add_u32 s24, s22, 0xfffc0080
	s_addc_u32 s25, s23, -1
	s_cmp_eq_u32 s47, 12
	s_cselect_b32 s27, s13, s25
	s_cselect_b32 s26, s21, s24
	s_cselect_b32 s25, s15, s46
	s_cselect_b32 s24, s44, s45
	v_lshl_add_u64 v[218:219], s[22:23], 0, v[170:171]
	s_add_i32 m0, s29, 0xc000
	ds_read_b128 v[178:181], v190
	ds_read_b128 v[182:185], v190 offset:1024
	ds_read_b128 v[194:197], v190 offset:2048
	ds_read_b128 v[198:201], v190 offset:3072
	ds_read_b128 v[202:205], v190 offset:4096
	ds_read_b128 v[206:209], v190 offset:5120
	ds_read_b128 v[210:213], v190 offset:6144
	ds_read_b128 v[214:217], v190 offset:7168
	global_load_lds_dwordx4 v[218:219], off
	v_lshl_add_u64 v[218:219], s[22:23], 0, v[172:173]
	s_add_i32 m0, s29, 0xe000
	s_nop 0
	global_load_lds_dwordx4 v[218:219], off
	s_waitcnt vmcnt(8)
	s_waitcnt lgkmcnt(0)
	s_barrier
	s_setprio 1
	s_nop 0
	s_waitcnt lgkmcnt(0)
	v_mfma_scale_f32_16x16x128_f8f6f4 v[158:161], v[26:33], v[178:185], v[158:161], v191, v192 op_sel_hi:[0,0,0]
	v_mfma_scale_f32_16x16x128_f8f6f4 v[154:157], v[18:25], v[178:185], v[154:157], v191, v192 op_sel_hi:[0,0,0]
	v_mfma_scale_f32_16x16x128_f8f6f4 v[142:145], v[26:33], v[194:201], v[142:145], v191, v192 op_sel_hi:[0,0,0]
	v_mfma_scale_f32_16x16x128_f8f6f4 v[138:141], v[18:25], v[194:201], v[138:141], v191, v192 op_sel_hi:[0,0,0]
	v_mfma_scale_f32_16x16x128_f8f6f4 v[126:129], v[26:33], v[202:209], v[126:129], v191, v192 op_sel_hi:[0,0,0]
	v_mfma_scale_f32_16x16x128_f8f6f4 v[122:125], v[18:25], v[202:209], v[122:125], v191, v192 op_sel_hi:[0,0,0]
	v_mfma_scale_f32_16x16x128_f8f6f4 v[110:113], v[26:33], v[210:217], v[110:113], v191, v192 op_sel_hi:[0,0,0]
	v_mfma_scale_f32_16x16x128_f8f6f4 v[106:109], v[18:25], v[210:217], v[106:109], v191, v192 op_sel_hi:[0,0,0]
	s_setprio 0
	s_setprio 1
	s_nop 0
	v_mfma_scale_f32_16x16x128_f8f6f4 v[150:153], v[10:17], v[178:185], v[150:153], v191, v192 op_sel_hi:[0,0,0]
	v_mfma_scale_f32_16x16x128_f8f6f4 v[146:149], v[2:9], v[178:185], v[146:149], v191, v192 op_sel_hi:[0,0,0]
	v_mfma_scale_f32_16x16x128_f8f6f4 v[134:137], v[10:17], v[194:201], v[134:137], v191, v192 op_sel_hi:[0,0,0]
	v_mfma_scale_f32_16x16x128_f8f6f4 v[130:133], v[2:9], v[194:201], v[130:133], v191, v192 op_sel_hi:[0,0,0]
	v_mfma_scale_f32_16x16x128_f8f6f4 v[118:121], v[10:17], v[202:209], v[118:121], v191, v192 op_sel_hi:[0,0,0]
	v_mfma_scale_f32_16x16x128_f8f6f4 v[114:117], v[2:9], v[202:209], v[114:117], v191, v192 op_sel_hi:[0,0,0]
	v_mfma_scale_f32_16x16x128_f8f6f4 v[102:105], v[10:17], v[210:217], v[102:105], v191, v192 op_sel_hi:[0,0,0]
	v_mfma_scale_f32_16x16x128_f8f6f4 v[98:101], v[2:9], v[210:217], v[98:101], v191, v192 op_sel_hi:[0,0,0]
	s_setprio 0
	s_barrier
	s_add_i32 s48, s40, s28
	v_lshl_add_u64 v[178:179], s[24:25], 0, v[166:167]
	s_mov_b32 m0, s48
	ds_read_b128 v[194:197], v190 offset:16384
	ds_read_b128 v[198:201], v190 offset:17408
	ds_read_b128 v[202:205], v190 offset:18432
	ds_read_b128 v[206:209], v190 offset:19456
	ds_read_b128 v[210:213], v190 offset:20480
	ds_read_b128 v[214:217], v190 offset:21504
	ds_read_b128 v[218:221], v190 offset:22528
	ds_read_b128 v[222:225], v190 offset:23552
	global_load_lds_dwordx4 v[178:179], off
	s_add_i32 m0, s48, 0x2000
	s_add_u32 s48, s24, 0x4000
	v_lshl_add_u64 v[180:181], s[24:25], 0, v[162:163]
	s_addc_u32 s49, s25, 0
	s_add_i32 s50, s41, s28
	global_load_lds_dwordx4 v[180:181], off
	v_lshl_add_u64 v[182:183], s[48:49], 0, v[166:167]
	s_mov_b32 m0, s50
	v_lshl_add_u64 v[184:185], s[26:27], 0, v[164:165]
	global_load_lds_dwordx4 v[182:183], off
	v_lshl_add_u64 v[182:183], s[48:49], 0, v[162:163]
	s_add_i32 m0, s50, 0x2000
	s_nop 0
	global_load_lds_dwordx4 v[182:183], off
	v_lshl_add_u64 v[182:183], s[26:27], 0, v[168:169]
	s_mov_b32 m0, s29
	s_nop 0
	global_load_lds_dwordx4 v[182:183], off
	s_mov_b32 m0, s30
	s_nop 0
	global_load_lds_dwordx4 v[184:185], off
	s_waitcnt vmcnt(8)
	s_waitcnt lgkmcnt(0)
	s_barrier
	s_setprio 1
	s_nop 0
	s_waitcnt lgkmcnt(0)
	v_mfma_scale_f32_16x16x128_f8f6f4 v[94:97], v[26:33], v[194:201], v[94:97], v191, v192 op_sel_hi:[0,0,0]
	v_mfma_scale_f32_16x16x128_f8f6f4 v[90:93], v[18:25], v[194:201], v[90:93], v191, v192 op_sel_hi:[0,0,0]
	v_mfma_scale_f32_16x16x128_f8f6f4 v[78:81], v[26:33], v[202:209], v[78:81], v191, v192 op_sel_hi:[0,0,0]
	v_mfma_scale_f32_16x16x128_f8f6f4 v[74:77], v[18:25], v[202:209], v[74:77], v191, v192 op_sel_hi:[0,0,0]
	v_mfma_scale_f32_16x16x128_f8f6f4 v[62:65], v[26:33], v[210:217], v[62:65], v191, v192 op_sel_hi:[0,0,0]
	v_mfma_scale_f32_16x16x128_f8f6f4 v[58:61], v[18:25], v[210:217], v[58:61], v191, v192 op_sel_hi:[0,0,0]
	v_mfma_scale_f32_16x16x128_f8f6f4 v[46:49], v[26:33], v[218:225], v[46:49], v191, v192 op_sel_hi:[0,0,0]
	v_mfma_scale_f32_16x16x128_f8f6f4 v[42:45], v[18:25], v[218:225], v[42:45], v191, v192 op_sel_hi:[0,0,0]
	s_setprio 0
	s_setprio 1
	s_nop 0
	v_mfma_scale_f32_16x16x128_f8f6f4 v[86:89], v[10:17], v[194:201], v[86:89], v191, v192 op_sel_hi:[0,0,0]
	v_mfma_scale_f32_16x16x128_f8f6f4 v[82:85], v[2:9], v[194:201], v[82:85], v191, v192 op_sel_hi:[0,0,0]
	v_mfma_scale_f32_16x16x128_f8f6f4 v[70:73], v[10:17], v[202:209], v[70:73], v191, v192 op_sel_hi:[0,0,0]
	v_mfma_scale_f32_16x16x128_f8f6f4 v[66:69], v[2:9], v[202:209], v[66:69], v191, v192 op_sel_hi:[0,0,0]
	v_mfma_scale_f32_16x16x128_f8f6f4 v[54:57], v[10:17], v[210:217], v[54:57], v191, v192 op_sel_hi:[0,0,0]
	v_mfma_scale_f32_16x16x128_f8f6f4 v[50:53], v[2:9], v[210:217], v[50:53], v191, v192 op_sel_hi:[0,0,0]
	v_mfma_scale_f32_16x16x128_f8f6f4 v[38:41], v[10:17], v[218:225], v[38:41], v191, v192 op_sel_hi:[0,0,0]
	v_mfma_scale_f32_16x16x128_f8f6f4 v[34:37], v[2:9], v[218:225], v[34:37], v191, v192 op_sel_hi:[0,0,0]
	s_setprio 0
	s_barrier
; #define PG8_STAGE(bufoff, gbase, voff) do { _Pragma("unroll") for (int _i = 0; _i < 2; ++_i) \
;         __builtin_amdgcn_global_load_lds((const unsigned*)((const char*)(gbase) + (voff)[_i]), (PG8_LAS unsigned*)(lds + (bufoff) + ldsw + _i * 8192), 16, 0, 0); } while (0)
; #define PG8_STAGE_A(bufoff, gbase, h, nx) do { if constexpr (Sched::GATHER) { const unsigned vv_[2] = {(nx) ? vAn[h][0] : vA[h][0], (nx) ? vAn[h][1] : vA[h][1]}; PG8_STAGE(bufoff, gbase, vv_); } \
;         else { PG8_STAGE(bufoff, (gbase) + (h) * hstep, voffA); } } while (0)
; #define PG8_LDA(dst, b, h) do { _Pragma("unroll") for (int m = 0; m < 4; ++m) _Pragma("unroll") for (int k = 0; k < 2; ++k) dst[m][k] = *(const PG8_LAS bf16x8*)(lds + PG8_SA(b, h) + aoff + m * 2048 + k * 1024); } while (0)
; #define PG8_LDB(dst, b, h) do { _Pragma("unroll") for (int n = 0; n < 2; ++n) _Pragma("unroll") for (int k = 0; k < 2; ++k) dst[n][k] = *(const PG8_LAS bf16x8*)(lds + PG8_SB(b, h) + boff + n * 2048 + k * 1024); } while (0)
; #define PG8_WAIT_V(n) asm volatile("s_waitcnt vmcnt(" #n ")" ::: "memory")
; #define PG8_WAIT_L(n) asm volatile("s_waitcnt lgkmcnt(" #n ")" ::: "memory")
; #define PG8_BAR __builtin_amdgcn_s_barrier()
; #define PG8_SCHED __builtin_amdgcn_sched_barrier(0)
;     ...
;             PG8_LDB(B0, 1, 0); PG8_LDB(B1, 1, 1); PG8_SCHED; PG8_LDA(At, 1, 0); PG8_STAGE_A(PG8_SA(0, 1), a2, 1, last);
;             PG8_WAIT_V(8); PG8_WAIT_L(0); PG8_BAR; PG8_MMA(0, 0, At, B0); PG8_MMA(0, 1, At, B1); PG8_BAR; PG8_SCHED;
;             PG8_LDA(At, 1, 1); PG8_STAGE(PG8_SB(1, 0), b3, voffB); PG8_STAGE(PG8_SB(1, 1), b3 + hstepB, voffB); PG8_STAGE_A(PG8_SA(1, 0), a3, 0, last);
;             PG8_WAIT_V(8); PG8_WAIT_L(0); PG8_BAR; PG8_MMA(1, 0, At, B0); PG8_MMA(1, 1, At, B1); PG8_BAR; PG8_SCHED;
;     __device__ __forceinline__ void operator()(const f32x4 (&acc)[2][2][4][2], const Unit& u, int wr, int wc, int fr, int fq) const {
;     ...
;             for (int m = 0; m < 4; ++m) { const int row = row0 + ai * HALF + m * 16; const float gt = gate[row] * YSCALE; unsigned char* rowp = O + (size_t)row * ldc + col0;
	s_add_i32 s48, 0, 0x18000
	s_add_i32 s49, 0, 0x1c000
	v_add_u32_e32 v14, s48, v186
	v_add_u32_e32 v30, s49, v186
	ds_read_b128 v[2:5], v14
	ds_read_b128 v[6:9], v14 offset:1024
	ds_read_b128 v[10:13], v14 offset:2048
	ds_read_b128 v[14:17], v14 offset:3072
	ds_read_b128 v[18:21], v30
	ds_read_b128 v[22:25], v30 offset:1024
	ds_read_b128 v[26:29], v30 offset:2048
	ds_read_b128 v[30:33], v30 offset:3072
	s_add_u32 s26, s26, 0x40000
	s_addc_u32 s27, s27, 0
	s_mov_b32 m0, s31
	v_lshl_add_u64 v[226:227], s[26:27], 0, v[168:169]
	ds_read_b128 v[194:197], v190 offset:32768
	ds_read_b128 v[198:201], v190 offset:33792
	ds_read_b128 v[202:205], v190 offset:34816
	ds_read_b128 v[206:209], v190 offset:35840
	ds_read_b128 v[210:213], v190 offset:36864
	ds_read_b128 v[214:217], v190 offset:37888
	ds_read_b128 v[218:221], v190 offset:38912
	ds_read_b128 v[222:225], v190 offset:39936
	global_load_lds_dwordx4 v[226:227], off
	v_lshl_add_u64 v[226:227], s[26:27], 0, v[164:165]
	s_mov_b32 m0, s34
	s_nop 0
	global_load_lds_dwordx4 v[226:227], off
	s_waitcnt vmcnt(8)
	s_waitcnt lgkmcnt(0)
	s_barrier
	s_setprio 1
	s_nop 0
	s_waitcnt lgkmcnt(0)
	v_mfma_scale_f32_16x16x128_f8f6f4 v[158:161], v[2:9], v[194:201], v[158:161], v191, v192 op_sel_hi:[0,0,0]
	v_mfma_scale_f32_16x16x128_f8f6f4 v[154:157], v[10:17], v[194:201], v[154:157], v191, v192 op_sel_hi:[0,0,0]
	v_mfma_scale_f32_16x16x128_f8f6f4 v[142:145], v[2:9], v[202:209], v[142:145], v191, v192 op_sel_hi:[0,0,0]
	v_mfma_scale_f32_16x16x128_f8f6f4 v[138:141], v[10:17], v[202:209], v[138:141], v191, v192 op_sel_hi:[0,0,0]
	v_mfma_scale_f32_16x16x128_f8f6f4 v[126:129], v[2:9], v[210:217], v[126:129], v191, v192 op_sel_hi:[0,0,0]
	v_mfma_scale_f32_16x16x128_f8f6f4 v[122:125], v[10:17], v[210:217], v[122:125], v191, v192 op_sel_hi:[0,0,0]
	v_mfma_scale_f32_16x16x128_f8f6f4 v[110:113], v[2:9], v[218:225], v[110:113], v191, v192 op_sel_hi:[0,0,0]
	v_mfma_scale_f32_16x16x128_f8f6f4 v[106:109], v[10:17], v[218:225], v[106:109], v191, v192 op_sel_hi:[0,0,0]
	s_setprio 0
	s_setprio 1
	s_nop 0
	v_mfma_scale_f32_16x16x128_f8f6f4 v[150:153], v[18:25], v[194:201], v[150:153], v191, v192 op_sel_hi:[0,0,0]
	v_mfma_scale_f32_16x16x128_f8f6f4 v[146:149], v[26:33], v[194:201], v[146:149], v191, v192 op_sel_hi:[0,0,0]
	v_mfma_scale_f32_16x16x128_f8f6f4 v[134:137], v[18:25], v[202:209], v[134:137], v191, v192 op_sel_hi:[0,0,0]
	v_mfma_scale_f32_16x16x128_f8f6f4 v[130:133], v[26:33], v[202:209], v[130:133], v191, v192 op_sel_hi:[0,0,0]
	v_mfma_scale_f32_16x16x128_f8f6f4 v[118:121], v[18:25], v[210:217], v[118:121], v191, v192 op_sel_hi:[0,0,0]
	v_mfma_scale_f32_16x16x128_f8f6f4 v[114:117], v[26:33], v[210:217], v[114:117], v191, v192 op_sel_hi:[0,0,0]
	v_mfma_scale_f32_16x16x128_f8f6f4 v[102:105], v[18:25], v[218:225], v[102:105], v191, v192 op_sel_hi:[0,0,0]
	v_mfma_scale_f32_16x16x128_f8f6f4 v[98:101], v[26:33], v[218:225], v[98:101], v191, v192 op_sel_hi:[0,0,0]
	s_setprio 0
	s_barrier
	s_add_i32 s26, s48, s28
	v_lshl_add_u64 v[178:179], v[178:179], 0, s[8:9]
	s_mov_b32 m0, s26
	ds_read_b128 v[194:197], v190 offset:49152
	ds_read_b128 v[198:201], v190 offset:50176
	ds_read_b128 v[202:205], v190 offset:51200
	ds_read_b128 v[206:209], v190 offset:52224
	ds_read_b128 v[210:213], v190 offset:53248
	ds_read_b128 v[214:217], v190 offset:54272
	ds_read_b128 v[218:221], v190 offset:55296
	ds_read_b128 v[222:225], v190 offset:56320
	global_load_lds_dwordx4 v[178:179], off
	s_add_i32 m0, s26, 0x2000
	s_add_u32 s24, s24, 0x4080
	v_lshl_add_u64 v[178:179], v[180:181], 0, s[8:9]
	s_addc_u32 s25, s25, 0
	s_add_i32 s26, s49, s28
	global_load_lds_dwordx4 v[178:179], off
	v_lshl_add_u64 v[178:179], s[24:25], 0, v[166:167]
	s_mov_b32 m0, s26
	s_nop 0
	global_load_lds_dwordx4 v[178:179], off
	v_lshl_add_u64 v[178:179], s[24:25], 0, v[162:163]
	s_add_i32 m0, s26, 0x2000
	s_nop 0
	global_load_lds_dwordx4 v[178:179], off
	v_lshl_add_u64 v[178:179], v[182:183], 0, s[8:9]
	s_mov_b32 m0, s38
	s_nop 0
	global_load_lds_dwordx4 v[178:179], off
	v_lshl_add_u64 v[178:179], v[184:185], 0, s[8:9]
	s_mov_b32 m0, s39
	s_nop 0
	global_load_lds_dwordx4 v[178:179], off
	s_waitcnt vmcnt(8)
	s_cmp_eq_u32 s47, 12
	s_cbranch_scc0 .Lgate9_skip
	v_lshl_add_u32 v236, s20, 8, v1
	v_ashrrev_i32_e32 v237, 31, v236
	v_lshl_add_u64 v[236:237], v[236:237], 2, s[0:1]
	global_load_dword v228, v[236:237], off
	global_load_dword v229, v[236:237], off offset:64
	global_load_dword v230, v[236:237], off offset:128
	global_load_dword v231, v[236:237], off offset:192
	global_load_dword v232, v[236:237], off offset:512
	global_load_dword v233, v[236:237], off offset:576
	global_load_dword v234, v[236:237], off offset:640
	global_load_dword v235, v[236:237], off offset:704
.Lgate9_skip:
	s_waitcnt lgkmcnt(0)
	s_barrier
	s_setprio 1
	s_nop 0
	s_waitcnt lgkmcnt(0)
	v_mfma_scale_f32_16x16x128_f8f6f4 v[94:97], v[2:9], v[194:201], v[94:97], v191, v192 op_sel_hi:[0,0,0]
	v_mfma_scale_f32_16x16x128_f8f6f4 v[90:93], v[10:17], v[194:201], v[90:93], v191, v192 op_sel_hi:[0,0,0]
	v_mfma_scale_f32_16x16x128_f8f6f4 v[78:81], v[2:9], v[202:209], v[78:81], v191, v192 op_sel_hi:[0,0,0]
	v_mfma_scale_f32_16x16x128_f8f6f4 v[74:77], v[10:17], v[202:209], v[74:77], v191, v192 op_sel_hi:[0,0,0]
	v_mfma_scale_f32_16x16x128_f8f6f4 v[62:65], v[2:9], v[210:217], v[62:65], v191, v192 op_sel_hi:[0,0,0]
	v_mfma_scale_f32_16x16x128_f8f6f4 v[58:61], v[10:17], v[210:217], v[58:61], v191, v192 op_sel_hi:[0,0,0]
	v_mfma_scale_f32_16x16x128_f8f6f4 v[46:49], v[2:9], v[218:225], v[46:49], v191, v192 op_sel_hi:[0,0,0]
	v_mfma_scale_f32_16x16x128_f8f6f4 v[42:45], v[10:17], v[218:225], v[42:45], v191, v192 op_sel_hi:[0,0,0]
	s_setprio 0
	s_setprio 1
	s_nop 0
	v_mfma_scale_f32_16x16x128_f8f6f4 v[86:89], v[18:25], v[194:201], v[86:89], v191, v192 op_sel_hi:[0,0,0]
	v_mfma_scale_f32_16x16x128_f8f6f4 v[82:85], v[26:33], v[194:201], v[82:85], v191, v192 op_sel_hi:[0,0,0]
	v_mfma_scale_f32_16x16x128_f8f6f4 v[70:73], v[18:25], v[202:209], v[70:73], v191, v192 op_sel_hi:[0,0,0]
	v_mfma_scale_f32_16x16x128_f8f6f4 v[66:69], v[26:33], v[202:209], v[66:69], v191, v192 op_sel_hi:[0,0,0]
	v_mfma_scale_f32_16x16x128_f8f6f4 v[54:57], v[18:25], v[210:217], v[54:57], v191, v192 op_sel_hi:[0,0,0]
	v_mfma_scale_f32_16x16x128_f8f6f4 v[50:53], v[26:33], v[210:217], v[50:53], v191, v192 op_sel_hi:[0,0,0]
	v_mfma_scale_f32_16x16x128_f8f6f4 v[38:41], v[18:25], v[218:225], v[38:41], v191, v192 op_sel_hi:[0,0,0]
	v_mfma_scale_f32_16x16x128_f8f6f4 v[34:37], v[26:33], v[218:225], v[34:37], v191, v192 op_sel_hi:[0,0,0]
	s_setprio 0
	s_barrier
	s_add_i32 s47, s47, 2
	s_add_u32 s22, s22, 0x100
	s_addc_u32 s23, s23, 0
	s_add_u32 s45, s45, 0x100
	s_addc_u32 s46, s46, 0
	s_cmp_gt_u32 s47, 13
	s_cbranch_scc0 .LBB0_895
	s_and_b64 vcc, exec, s[10:11]
	s_cbranch_vccz .LBB0_898
	s_barrier

; #define PG8_STAGE(bufoff, gbase, voff) do { _Pragma("unroll") for (int _i = 0; _i < 2; ++_i) \
;         __builtin_amdgcn_global_load_lds((const unsigned*)((const char*)(gbase) + (voff)[_i]), (PG8_LAS unsigned*)(lds + (bufoff) + ldsw + _i * 8192), 16, 0, 0); } while (0)
; #define PG8_STAGE_A(bufoff, gbase, h, nx) do { if constexpr (Sched::GATHER) { const unsigned vv_[2] = {(nx) ? vAn[h][0] : vA[h][0], (nx) ? vAn[h][1] : vA[h][1]}; PG8_STAGE(bufoff, gbase, vv_); } \
;         else { PG8_STAGE(bufoff, (gbase) + (h) * hstep, voffA); } } while (0)
; #define PG8_LDA(dst, b, h) do { _Pragma("unroll") for (int m = 0; m < 4; ++m) _Pragma("unroll") for (int k = 0; k < 2; ++k) dst[m][k] = *(const PG8_LAS bf16x8*)(lds + PG8_SA(b, h) + aoff + m * 2048 + k * 1024); } while (0)
; #define PG8_WAIT_V(n) asm volatile("s_waitcnt vmcnt(" #n ")" ::: "memory")
; #define PG8_WAIT_L(n) asm volatile("s_waitcnt lgkmcnt(" #n ")" ::: "memory")
;     ...
;         const bool has_next = S.next(ui + 1, nxt);
;         const char* nA = Sched::GATHER ? cA : (has_next ? (const char*)g.A + (size_t)nxt.pm * tstep : cA);
;         if constexpr (Sched::GATHER) { if (has_next) { PG8_AOFF(vAn, ui + 1); } else { _Pragma("unroll") for (int h_ = 0; h_ < 2; ++h_) _Pragma("unroll") for (int i_ = 0; i_ < 2; ++i_) vAn[h_][i_] = vA[h_][i_]; } } const char* nB = has_next ? (const char*)g.Bt + (size_t)nxt.pb * tstep : cB;
; #pragma nounroll
;         for (int t = 0; t < nt; t += 2) {
;             const bool last = (t == nt - 2);
;             const char* a1 = cA + (size_t)(t + 1) * kstep;
;             const char* a2 = last ? nA : cA + (size_t)(t + 2) * kstep; const char* b2 = last ? nB : cB + (size_t)(t + 2) * kstep;
;             const char* a3 = a2 + kstep; const char* b3 = b2 + kstep;
;             if (last && has_next) S.a_ready(nxt);
;             if constexpr (SP2) {
;             PG8_LDB(B0, 0, 0); PG8_LDB(B1, 0, 1); PG8_SCHED; PG8_LDA(At, 0, 0); PG8_STAGE_A(PG8_SA(1, 1), a1, 1, false);
;             PG8_WAIT_V(8); PG8_WAIT_L(0); PG8_BAR; PG8_MMA(0, 0, At, B0); PG8_MMA(0, 1, At, B1); PG8_BAR; PG8_SCHED;
;             PG8_LDA(At, 0, 1); PG8_STAGE(PG8_SB(0, 0), b2, voffB); PG8_STAGE(PG8_SB(0, 1), b2 + hstepB, voffB); PG8_STAGE_A(PG8_SA(0, 0), a2, 0, last);
;             PG8_WAIT_V(8); PG8_WAIT_L(0); PG8_BAR; PG8_MMA(1, 0, At, B0); PG8_MMA(1, 1, At, B1); PG8_BAR; PG8_SCHED;
.LBB0_1025:
	s_ashr_i32 s45, s44, 31
	s_lshl_b64 s[46:47], s[44:45], 18
	s_add_u32 s46, s88, s46
	s_addc_u32 s47, s89, s47
	s_and_b64 s[48:49], s[2:3], exec
	s_cselect_b32 s5, s47, s7
	s_cselect_b32 s33, s46, s6
	s_ashr_i32 s43, s42, 31
	s_lshl_b64 s[48:49], s[42:43], 18
	v_readlane_b32 s54, v254, 55
	v_readlane_b32 s55, v254, 56
	s_add_u32 s48, s54, s48
	s_addc_u32 s49, s55, s49
	s_and_b64 s[54:55], s[2:3], exec
	s_cselect_b32 s43, s49, s53
	s_cselect_b32 s45, s48, s52
	s_add_u32 s6, s6, 0x20080
	s_addc_u32 s7, s7, 0
	s_add_u32 s71, s52, 0x100
	s_addc_u32 s72, s53, 0
	s_mov_b32 s73, -2
	ds_read_b128 v[26:29], v188
	ds_read_b128 v[30:33], v188 offset:1024
	ds_read_b128 v[18:21], v188 offset:2048
	ds_read_b128 v[22:25], v188 offset:3072
	ds_read_b128 v[10:13], v189
	ds_read_b128 v[14:17], v189 offset:1024
	ds_read_b128 v[2:5], v189 offset:2048
	ds_read_b128 v[6:9], v189 offset:3072
	s_add_u32 s52, s6, 0xfffe0080
	s_addc_u32 s53, s7, -1
	s_cmp_eq_u32 s73, 4
	s_cselect_b32 s55, s5, s53
	s_cselect_b32 s54, s33, s52
	s_cselect_b32 s53, s43, s72
	s_cselect_b32 s52, s45, s71
	v_lshl_add_u64 v[220:221], s[6:7], 0, v[170:171]
	s_add_i32 m0, s51, 0xc000
	ds_read_b128 v[178:181], v190
	ds_read_b128 v[182:185], v190 offset:1024
	ds_read_b128 v[196:199], v190 offset:2048
	ds_read_b128 v[200:203], v190 offset:3072
	ds_read_b128 v[204:207], v190 offset:4096
	ds_read_b128 v[208:211], v190 offset:5120
	ds_read_b128 v[212:215], v190 offset:6144
	ds_read_b128 v[216:219], v190 offset:7168
	global_load_lds_dwordx4 v[220:221], off
	v_lshl_add_u64 v[220:221], s[6:7], 0, v[172:173]
	s_add_i32 m0, s51, 0xe000
	s_nop 0
	global_load_lds_dwordx4 v[220:221], off
	s_waitcnt vmcnt(8)
	s_waitcnt lgkmcnt(0)
	s_barrier
	s_setprio 1
	s_nop 0
	s_waitcnt lgkmcnt(0)
	v_mfma_scale_f32_16x16x128_f8f6f4 v[158:161], v[26:33], v[178:185], 0, v191, v192 op_sel_hi:[0,0,0]
	v_mfma_scale_f32_16x16x128_f8f6f4 v[154:157], v[18:25], v[178:185], 0, v191, v192 op_sel_hi:[0,0,0]
	v_mfma_scale_f32_16x16x128_f8f6f4 v[142:145], v[26:33], v[196:203], 0, v191, v192 op_sel_hi:[0,0,0]
	v_mfma_scale_f32_16x16x128_f8f6f4 v[138:141], v[18:25], v[196:203], 0, v191, v192 op_sel_hi:[0,0,0]
	v_mfma_scale_f32_16x16x128_f8f6f4 v[126:129], v[26:33], v[204:211], 0, v191, v192 op_sel_hi:[0,0,0]
	v_mfma_scale_f32_16x16x128_f8f6f4 v[122:125], v[18:25], v[204:211], 0, v191, v192 op_sel_hi:[0,0,0]
	v_mfma_scale_f32_16x16x128_f8f6f4 v[110:113], v[26:33], v[212:219], 0, v191, v192 op_sel_hi:[0,0,0]
	v_mfma_scale_f32_16x16x128_f8f6f4 v[106:109], v[18:25], v[212:219], 0, v191, v192 op_sel_hi:[0,0,0]
	s_setprio 0
	s_setprio 1
	s_nop 0
	v_mfma_scale_f32_16x16x128_f8f6f4 v[150:153], v[10:17], v[178:185], 0, v191, v192 op_sel_hi:[0,0,0]
	v_mfma_scale_f32_16x16x128_f8f6f4 v[146:149], v[2:9], v[178:185], 0, v191, v192 op_sel_hi:[0,0,0]
	v_mfma_scale_f32_16x16x128_f8f6f4 v[134:137], v[10:17], v[196:203], 0, v191, v192 op_sel_hi:[0,0,0]
	v_mfma_scale_f32_16x16x128_f8f6f4 v[130:133], v[2:9], v[196:203], 0, v191, v192 op_sel_hi:[0,0,0]
	v_mfma_scale_f32_16x16x128_f8f6f4 v[118:121], v[10:17], v[204:211], 0, v191, v192 op_sel_hi:[0,0,0]
	v_mfma_scale_f32_16x16x128_f8f6f4 v[114:117], v[2:9], v[204:211], 0, v191, v192 op_sel_hi:[0,0,0]
	v_mfma_scale_f32_16x16x128_f8f6f4 v[102:105], v[10:17], v[212:219], 0, v191, v192 op_sel_hi:[0,0,0]
	v_mfma_scale_f32_16x16x128_f8f6f4 v[98:101], v[2:9], v[212:219], 0, v191, v192 op_sel_hi:[0,0,0]
	s_setprio 0
	s_barrier
	s_add_i32 s74, s67, s56
	v_lshl_add_u64 v[178:179], s[52:53], 0, v[164:165]
	s_mov_b32 m0, s74
	ds_read_b128 v[196:199], v190 offset:16384
	ds_read_b128 v[200:203], v190 offset:17408
	ds_read_b128 v[204:207], v190 offset:18432
	ds_read_b128 v[208:211], v190 offset:19456
	ds_read_b128 v[212:215], v190 offset:20480
	ds_read_b128 v[216:219], v190 offset:21504
	ds_read_b128 v[220:223], v190 offset:22528
	ds_read_b128 v[224:227], v190 offset:23552
	global_load_lds_dwordx4 v[178:179], off
	s_add_i32 m0, s74, 0x2000
	s_add_u32 s74, s52, 0x8000
	v_lshl_add_u64 v[180:181], s[52:53], 0, v[168:169]
	s_addc_u32 s75, s53, 0
	s_add_i32 s76, s68, s56
	global_load_lds_dwordx4 v[180:181], off
	v_lshl_add_u64 v[182:183], s[74:75], 0, v[164:165]
	s_mov_b32 m0, s76
	v_lshl_add_u64 v[184:185], s[54:55], 0, v[166:167]
	global_load_lds_dwordx4 v[182:183], off
	v_lshl_add_u64 v[182:183], s[74:75], 0, v[168:169]
	s_add_i32 m0, s76, 0x2000
	s_nop 0
	global_load_lds_dwordx4 v[182:183], off
	v_lshl_add_u64 v[182:183], s[54:55], 0, v[162:163]
	s_mov_b32 m0, s51
	s_nop 0
	global_load_lds_dwordx4 v[182:183], off
	s_mov_b32 m0, s57
	s_nop 0
	global_load_lds_dwordx4 v[184:185], off
	s_waitcnt vmcnt(8)
	s_waitcnt lgkmcnt(0)
	s_barrier
	s_setprio 1
	s_nop 0
	s_waitcnt lgkmcnt(0)
	v_mfma_scale_f32_16x16x128_f8f6f4 v[94:97], v[26:33], v[196:203], 0, v191, v192 op_sel_hi:[0,0,0]
	v_mfma_scale_f32_16x16x128_f8f6f4 v[90:93], v[18:25], v[196:203], 0, v191, v192 op_sel_hi:[0,0,0]
	v_mfma_scale_f32_16x16x128_f8f6f4 v[78:81], v[26:33], v[204:211], 0, v191, v192 op_sel_hi:[0,0,0]
	v_mfma_scale_f32_16x16x128_f8f6f4 v[74:77], v[18:25], v[204:211], 0, v191, v192 op_sel_hi:[0,0,0]
	v_mfma_scale_f32_16x16x128_f8f6f4 v[62:65], v[26:33], v[212:219], 0, v191, v192 op_sel_hi:[0,0,0]
	v_mfma_scale_f32_16x16x128_f8f6f4 v[58:61], v[18:25], v[212:219], 0, v191, v192 op_sel_hi:[0,0,0]
	v_mfma_scale_f32_16x16x128_f8f6f4 v[46:49], v[26:33], v[220:227], 0, v191, v192 op_sel_hi:[0,0,0]
	v_mfma_scale_f32_16x16x128_f8f6f4 v[42:45], v[18:25], v[220:227], 0, v191, v192 op_sel_hi:[0,0,0]
	s_setprio 0
	s_setprio 1
	s_nop 0
	v_mfma_scale_f32_16x16x128_f8f6f4 v[86:89], v[10:17], v[196:203], 0, v191, v192 op_sel_hi:[0,0,0]
	v_mfma_scale_f32_16x16x128_f8f6f4 v[82:85], v[2:9], v[196:203], 0, v191, v192 op_sel_hi:[0,0,0]
	v_mfma_scale_f32_16x16x128_f8f6f4 v[70:73], v[10:17], v[204:211], 0, v191, v192 op_sel_hi:[0,0,0]
	v_mfma_scale_f32_16x16x128_f8f6f4 v[66:69], v[2:9], v[204:211], 0, v191, v192 op_sel_hi:[0,0,0]
	v_mfma_scale_f32_16x16x128_f8f6f4 v[54:57], v[10:17], v[212:219], 0, v191, v192 op_sel_hi:[0,0,0]
	v_mfma_scale_f32_16x16x128_f8f6f4 v[50:53], v[2:9], v[212:219], 0, v191, v192 op_sel_hi:[0,0,0]
	v_mfma_scale_f32_16x16x128_f8f6f4 v[38:41], v[10:17], v[220:227], 0, v191, v192 op_sel_hi:[0,0,0]
	v_mfma_scale_f32_16x16x128_f8f6f4 v[34:37], v[2:9], v[220:227], 0, v191, v192 op_sel_hi:[0,0,0]
	s_setprio 0
	s_barrier
; #define PG8_STAGE(bufoff, gbase, voff) do { _Pragma("unroll") for (int _i = 0; _i < 2; ++_i) \
;         __builtin_amdgcn_global_load_lds((const unsigned*)((const char*)(gbase) + (voff)[_i]), (PG8_LAS unsigned*)(lds + (bufoff) + ldsw + _i * 8192), 16, 0, 0); } while (0)
; #define PG8_STAGE_A(bufoff, gbase, h, nx) do { if constexpr (Sched::GATHER) { const unsigned vv_[2] = {(nx) ? vAn[h][0] : vA[h][0], (nx) ? vAn[h][1] : vA[h][1]}; PG8_STAGE(bufoff, gbase, vv_); } \
;         else { PG8_STAGE(bufoff, (gbase) + (h) * hstep, voffA); } } while (0)
; #define PG8_LDA(dst, b, h) do { _Pragma("unroll") for (int m = 0; m < 4; ++m) _Pragma("unroll") for (int k = 0; k < 2; ++k) dst[m][k] = *(const PG8_LAS bf16x8*)(lds + PG8_SA(b, h) + aoff + m * 2048 + k * 1024); } while (0)
; #define PG8_LDB(dst, b, h) do { _Pragma("unroll") for (int n = 0; n < 2; ++n) _Pragma("unroll") for (int k = 0; k < 2; ++k) dst[n][k] = *(const PG8_LAS bf16x8*)(lds + PG8_SB(b, h) + boff + n * 2048 + k * 1024); } while (0)
; #define PG8_WAIT_V(n) asm volatile("s_waitcnt vmcnt(" #n ")" ::: "memory")
; #define PG8_WAIT_L(n) asm volatile("s_waitcnt lgkmcnt(" #n ")" ::: "memory")
; #define PG8_BAR __builtin_amdgcn_s_barrier()
; #define PG8_SCHED __builtin_amdgcn_sched_barrier(0)
;     ...
;             PG8_LDB(B0, 1, 0); PG8_LDB(B1, 1, 1); PG8_SCHED; PG8_LDA(At, 1, 0); PG8_STAGE_A(PG8_SA(0, 1), a2, 1, last);
;             PG8_WAIT_V(8); PG8_WAIT_L(0); PG8_BAR; PG8_MMA(0, 0, At, B0); PG8_MMA(0, 1, At, B1); PG8_BAR; PG8_SCHED;
;             PG8_LDA(At, 1, 1); PG8_STAGE(PG8_SB(1, 0), b3, voffB); PG8_STAGE(PG8_SB(1, 1), b3 + hstepB, voffB); PG8_STAGE_A(PG8_SA(1, 0), a3, 0, last);
;             PG8_WAIT_V(8); PG8_WAIT_L(0); PG8_BAR; PG8_MMA(1, 0, At, B0); PG8_MMA(1, 1, At, B1); PG8_BAR; PG8_SCHED;
	s_add_i32 s74, 0, 0x18000
	s_add_i32 s75, 0, 0x1c000
	v_add_u32_e32 v14, s74, v187
	v_add_u32_e32 v30, s75, v187
	ds_read_b128 v[2:5], v14
	ds_read_b128 v[6:9], v14 offset:1024
	ds_read_b128 v[10:13], v14 offset:2048
	ds_read_b128 v[14:17], v14 offset:3072
	ds_read_b128 v[18:21], v30
	ds_read_b128 v[22:25], v30 offset:1024
	ds_read_b128 v[26:29], v30 offset:2048
	ds_read_b128 v[30:33], v30 offset:3072
	s_add_u32 s54, s54, 0x20000
	s_addc_u32 s55, s55, 0
	s_mov_b32 m0, s58
	v_lshl_add_u64 v[228:229], s[54:55], 0, v[162:163]
	ds_read_b128 v[196:199], v190 offset:32768
	ds_read_b128 v[200:203], v190 offset:33792
	ds_read_b128 v[204:207], v190 offset:34816
	ds_read_b128 v[208:211], v190 offset:35840
	ds_read_b128 v[212:215], v190 offset:36864
	ds_read_b128 v[216:219], v190 offset:37888
	ds_read_b128 v[220:223], v190 offset:38912
	ds_read_b128 v[224:227], v190 offset:39936
	global_load_lds_dwordx4 v[228:229], off
	v_lshl_add_u64 v[228:229], s[54:55], 0, v[166:167]
	s_mov_b32 m0, s59
	s_nop 0
	global_load_lds_dwordx4 v[228:229], off
	s_waitcnt vmcnt(8)
	s_waitcnt lgkmcnt(0)
	s_barrier
	s_setprio 1
	s_nop 0
	s_waitcnt lgkmcnt(0)
	v_mfma_scale_f32_16x16x128_f8f6f4 v[158:161], v[2:9], v[196:203], v[158:161], v191, v192 op_sel_hi:[0,0,0]
	v_mfma_scale_f32_16x16x128_f8f6f4 v[154:157], v[10:17], v[196:203], v[154:157], v191, v192 op_sel_hi:[0,0,0]
	v_mfma_scale_f32_16x16x128_f8f6f4 v[142:145], v[2:9], v[204:211], v[142:145], v191, v192 op_sel_hi:[0,0,0]
	v_mfma_scale_f32_16x16x128_f8f6f4 v[138:141], v[10:17], v[204:211], v[138:141], v191, v192 op_sel_hi:[0,0,0]
	v_mfma_scale_f32_16x16x128_f8f6f4 v[126:129], v[2:9], v[212:219], v[126:129], v191, v192 op_sel_hi:[0,0,0]
	v_mfma_scale_f32_16x16x128_f8f6f4 v[122:125], v[10:17], v[212:219], v[122:125], v191, v192 op_sel_hi:[0,0,0]
	v_mfma_scale_f32_16x16x128_f8f6f4 v[110:113], v[2:9], v[220:227], v[110:113], v191, v192 op_sel_hi:[0,0,0]
	v_mfma_scale_f32_16x16x128_f8f6f4 v[106:109], v[10:17], v[220:227], v[106:109], v191, v192 op_sel_hi:[0,0,0]
	s_setprio 0
	s_setprio 1
	s_nop 0
	v_mfma_scale_f32_16x16x128_f8f6f4 v[150:153], v[18:25], v[196:203], v[150:153], v191, v192 op_sel_hi:[0,0,0]
	v_mfma_scale_f32_16x16x128_f8f6f4 v[146:149], v[26:33], v[196:203], v[146:149], v191, v192 op_sel_hi:[0,0,0]
	v_mfma_scale_f32_16x16x128_f8f6f4 v[134:137], v[18:25], v[204:211], v[134:137], v191, v192 op_sel_hi:[0,0,0]
	v_mfma_scale_f32_16x16x128_f8f6f4 v[130:133], v[26:33], v[204:211], v[130:133], v191, v192 op_sel_hi:[0,0,0]
	v_mfma_scale_f32_16x16x128_f8f6f4 v[118:121], v[18:25], v[212:219], v[118:121], v191, v192 op_sel_hi:[0,0,0]
	v_mfma_scale_f32_16x16x128_f8f6f4 v[114:117], v[26:33], v[212:219], v[114:117], v191, v192 op_sel_hi:[0,0,0]
	v_mfma_scale_f32_16x16x128_f8f6f4 v[102:105], v[18:25], v[220:227], v[102:105], v191, v192 op_sel_hi:[0,0,0]
	v_mfma_scale_f32_16x16x128_f8f6f4 v[98:101], v[26:33], v[220:227], v[98:101], v191, v192 op_sel_hi:[0,0,0]
	s_setprio 0
	s_barrier
	s_add_i32 s54, s74, s56
	v_lshl_add_u64 v[178:179], v[178:179], 0, s[18:19]
	s_mov_b32 m0, s54
	ds_read_b128 v[196:199], v190 offset:49152
	ds_read_b128 v[200:203], v190 offset:50176
	ds_read_b128 v[204:207], v190 offset:51200
	ds_read_b128 v[208:211], v190 offset:52224
	ds_read_b128 v[212:215], v190 offset:53248
	ds_read_b128 v[216:219], v190 offset:54272
	ds_read_b128 v[220:223], v190 offset:55296
	ds_read_b128 v[224:227], v190 offset:56320
	global_load_lds_dwordx4 v[178:179], off
	s_add_i32 m0, s54, 0x2000
	s_add_u32 s52, s52, 0x8080
	v_lshl_add_u64 v[178:179], v[180:181], 0, s[18:19]
	s_addc_u32 s53, s53, 0
	s_add_i32 s54, s75, s56
	global_load_lds_dwordx4 v[178:179], off
	v_lshl_add_u64 v[178:179], s[52:53], 0, v[164:165]
	s_mov_b32 m0, s54
	s_nop 0
	global_load_lds_dwordx4 v[178:179], off
	v_lshl_add_u64 v[178:179], s[52:53], 0, v[168:169]
	s_add_i32 m0, s54, 0x2000
	s_nop 0
	global_load_lds_dwordx4 v[178:179], off
	v_lshl_add_u64 v[178:179], v[182:183], 0, s[18:19]
	s_mov_b32 m0, s64
	s_nop 0
	global_load_lds_dwordx4 v[178:179], off
	v_lshl_add_u64 v[178:179], v[184:185], 0, s[18:19]
	s_mov_b32 m0, s65
	s_nop 0
	global_load_lds_dwordx4 v[178:179], off
	s_waitcnt vmcnt(8)
	s_waitcnt lgkmcnt(0)
	s_barrier
	s_setprio 1
	s_nop 0
	s_waitcnt lgkmcnt(0)
	v_mfma_scale_f32_16x16x128_f8f6f4 v[94:97], v[2:9], v[196:203], v[94:97], v191, v192 op_sel_hi:[0,0,0]
	v_mfma_scale_f32_16x16x128_f8f6f4 v[90:93], v[10:17], v[196:203], v[90:93], v191, v192 op_sel_hi:[0,0,0]
	v_mfma_scale_f32_16x16x128_f8f6f4 v[78:81], v[2:9], v[204:211], v[78:81], v191, v192 op_sel_hi:[0,0,0]
	v_mfma_scale_f32_16x16x128_f8f6f4 v[74:77], v[10:17], v[204:211], v[74:77], v191, v192 op_sel_hi:[0,0,0]
	v_mfma_scale_f32_16x16x128_f8f6f4 v[62:65], v[2:9], v[212:219], v[62:65], v191, v192 op_sel_hi:[0,0,0]
	v_mfma_scale_f32_16x16x128_f8f6f4 v[58:61], v[10:17], v[212:219], v[58:61], v191, v192 op_sel_hi:[0,0,0]
	v_mfma_scale_f32_16x16x128_f8f6f4 v[46:49], v[2:9], v[220:227], v[46:49], v191, v192 op_sel_hi:[0,0,0]
	v_mfma_scale_f32_16x16x128_f8f6f4 v[42:45], v[10:17], v[220:227], v[42:45], v191, v192 op_sel_hi:[0,0,0]
	s_setprio 0
	s_setprio 1
	s_nop 0
	v_mfma_scale_f32_16x16x128_f8f6f4 v[86:89], v[18:25], v[196:203], v[86:89], v191, v192 op_sel_hi:[0,0,0]
	v_mfma_scale_f32_16x16x128_f8f6f4 v[82:85], v[26:33], v[196:203], v[82:85], v191, v192 op_sel_hi:[0,0,0]
	v_mfma_scale_f32_16x16x128_f8f6f4 v[70:73], v[18:25], v[204:211], v[70:73], v191, v192 op_sel_hi:[0,0,0]
	v_mfma_scale_f32_16x16x128_f8f6f4 v[66:69], v[26:33], v[204:211], v[66:69], v191, v192 op_sel_hi:[0,0,0]
	v_mfma_scale_f32_16x16x128_f8f6f4 v[54:57], v[18:25], v[212:219], v[54:57], v191, v192 op_sel_hi:[0,0,0]
	v_mfma_scale_f32_16x16x128_f8f6f4 v[50:53], v[26:33], v[212:219], v[50:53], v191, v192 op_sel_hi:[0,0,0]
	v_mfma_scale_f32_16x16x128_f8f6f4 v[38:41], v[18:25], v[220:227], v[38:41], v191, v192 op_sel_hi:[0,0,0]
	v_mfma_scale_f32_16x16x128_f8f6f4 v[34:37], v[26:33], v[220:227], v[34:37], v191, v192 op_sel_hi:[0,0,0]
	s_setprio 0
	s_barrier
	s_add_i32 s73, s73, 2
	s_add_u32 s6, s6, 0x100
	s_addc_u32 s7, s7, 0
	s_add_u32 s71, s71, 0x100
	s_addc_u32 s72, s72, 0
; #define PG8_STAGE(bufoff, gbase, voff) do { _Pragma("unroll") for (int _i = 0; _i < 2; ++_i) \
;         __builtin_amdgcn_global_load_lds((const unsigned*)((const char*)(gbase) + (voff)[_i]), (PG8_LAS unsigned*)(lds + (bufoff) + ldsw + _i * 8192), 16, 0, 0); } while (0)
; #define PG8_STAGE_A(bufoff, gbase, h, nx) do { if constexpr (Sched::GATHER) { const unsigned vv_[2] = {(nx) ? vAn[h][0] : vA[h][0], (nx) ? vAn[h][1] : vA[h][1]}; PG8_STAGE(bufoff, gbase, vv_); } \
;         else { PG8_STAGE(bufoff, (gbase) + (h) * hstep, voffA); } } while (0)
; #define PG8_LDA(dst, b, h) do { _Pragma("unroll") for (int m = 0; m < 4; ++m) _Pragma("unroll") for (int k = 0; k < 2; ++k) dst[m][k] = *(const PG8_LAS bf16x8*)(lds + PG8_SA(b, h) + aoff + m * 2048 + k * 1024); } while (0)
; #define PG8_LDB(dst, b, h) do { _Pragma("unroll") for (int n = 0; n < 2; ++n) _Pragma("unroll") for (int k = 0; k < 2; ++k) dst[n][k] = *(const PG8_LAS bf16x8*)(lds + PG8_SB(b, h) + boff + n * 2048 + k * 1024); } while (0)
; #define PG8_WAIT_V(n) asm volatile("s_waitcnt vmcnt(" #n ")" ::: "memory")
; #define PG8_WAIT_L(n) asm volatile("s_waitcnt lgkmcnt(" #n ")" ::: "memory")
; #define PG8_BAR __builtin_amdgcn_s_barrier()
; #define PG8_SCHED __builtin_amdgcn_sched_barrier(0)
;     ...
;             const bool last = (t == nt - 2);
;             const char* a1 = cA + (size_t)(t + 1) * kstep;
;             const char* a2 = last ? nA : cA + (size_t)(t + 2) * kstep; const char* b2 = last ? nB : cB + (size_t)(t + 2) * kstep;
;             const char* a3 = a2 + kstep; const char* b3 = b2 + kstep;
;             if (last && has_next) S.a_ready(nxt);
;             if constexpr (SP2) {
;             PG8_LDB(B0, 0, 0); PG8_LDB(B1, 0, 1); PG8_SCHED; PG8_LDA(At, 0, 0); PG8_STAGE_A(PG8_SA(1, 1), a1, 1, false);
;             PG8_WAIT_V(8); PG8_WAIT_L(0); PG8_BAR; PG8_MMA(0, 0, At, B0); PG8_MMA(0, 1, At, B1); PG8_BAR; PG8_SCHED;
;             PG8_LDA(At, 0, 1); PG8_STAGE(PG8_SB(0, 0), b2, voffB); PG8_STAGE(PG8_SB(0, 1), b2 + hstepB, voffB); PG8_STAGE_A(PG8_SA(0, 0), a2, 0, last);
;             PG8_WAIT_V(8); PG8_WAIT_L(0); PG8_BAR; PG8_MMA(1, 0, At, B0); PG8_MMA(1, 1, At, B1); PG8_BAR; PG8_SCHED;
.LBB0_1026:
	ds_read_b128 v[26:29], v188
	ds_read_b128 v[30:33], v188 offset:1024
	ds_read_b128 v[18:21], v188 offset:2048
	ds_read_b128 v[22:25], v188 offset:3072
	ds_read_b128 v[10:13], v189
	ds_read_b128 v[14:17], v189 offset:1024
	ds_read_b128 v[2:5], v189 offset:2048
	ds_read_b128 v[6:9], v189 offset:3072
	s_add_u32 s52, s6, 0xfffe0080
	s_addc_u32 s53, s7, -1
	s_cmp_eq_u32 s73, 4
	s_cselect_b32 s55, s5, s53
	s_cselect_b32 s54, s33, s52
	s_cselect_b32 s53, s43, s72
	s_cselect_b32 s52, s45, s71
	v_lshl_add_u64 v[220:221], s[6:7], 0, v[170:171]
	s_add_i32 m0, s51, 0xc000
	ds_read_b128 v[178:181], v190
	ds_read_b128 v[182:185], v190 offset:1024
	ds_read_b128 v[196:199], v190 offset:2048
	ds_read_b128 v[200:203], v190 offset:3072
	ds_read_b128 v[204:207], v190 offset:4096
	ds_read_b128 v[208:211], v190 offset:5120
	ds_read_b128 v[212:215], v190 offset:6144
	ds_read_b128 v[216:219], v190 offset:7168
	global_load_lds_dwordx4 v[220:221], off
	v_lshl_add_u64 v[220:221], s[6:7], 0, v[172:173]
	s_add_i32 m0, s51, 0xe000
	s_nop 0
	global_load_lds_dwordx4 v[220:221], off
	s_waitcnt vmcnt(8)
	s_waitcnt lgkmcnt(0)
	s_barrier
	s_setprio 1
	s_nop 0
	s_waitcnt lgkmcnt(0)
	v_mfma_scale_f32_16x16x128_f8f6f4 v[158:161], v[26:33], v[178:185], v[158:161], v191, v192 op_sel_hi:[0,0,0]
	v_mfma_scale_f32_16x16x128_f8f6f4 v[154:157], v[18:25], v[178:185], v[154:157], v191, v192 op_sel_hi:[0,0,0]
	v_mfma_scale_f32_16x16x128_f8f6f4 v[142:145], v[26:33], v[196:203], v[142:145], v191, v192 op_sel_hi:[0,0,0]
	v_mfma_scale_f32_16x16x128_f8f6f4 v[138:141], v[18:25], v[196:203], v[138:141], v191, v192 op_sel_hi:[0,0,0]
	v_mfma_scale_f32_16x16x128_f8f6f4 v[126:129], v[26:33], v[204:211], v[126:129], v191, v192 op_sel_hi:[0,0,0]
	v_mfma_scale_f32_16x16x128_f8f6f4 v[122:125], v[18:25], v[204:211], v[122:125], v191, v192 op_sel_hi:[0,0,0]
	v_mfma_scale_f32_16x16x128_f8f6f4 v[110:113], v[26:33], v[212:219], v[110:113], v191, v192 op_sel_hi:[0,0,0]
	v_mfma_scale_f32_16x16x128_f8f6f4 v[106:109], v[18:25], v[212:219], v[106:109], v191, v192 op_sel_hi:[0,0,0]
	s_setprio 0
	s_setprio 1
	s_nop 0
	v_mfma_scale_f32_16x16x128_f8f6f4 v[150:153], v[10:17], v[178:185], v[150:153], v191, v192 op_sel_hi:[0,0,0]
	v_mfma_scale_f32_16x16x128_f8f6f4 v[146:149], v[2:9], v[178:185], v[146:149], v191, v192 op_sel_hi:[0,0,0]
	v_mfma_scale_f32_16x16x128_f8f6f4 v[134:137], v[10:17], v[196:203], v[134:137], v191, v192 op_sel_hi:[0,0,0]
	v_mfma_scale_f32_16x16x128_f8f6f4 v[130:133], v[2:9], v[196:203], v[130:133], v191, v192 op_sel_hi:[0,0,0]
	v_mfma_scale_f32_16x16x128_f8f6f4 v[118:121], v[10:17], v[204:211], v[118:121], v191, v192 op_sel_hi:[0,0,0]
	v_mfma_scale_f32_16x16x128_f8f6f4 v[114:117], v[2:9], v[204:211], v[114:117], v191, v192 op_sel_hi:[0,0,0]
	v_mfma_scale_f32_16x16x128_f8f6f4 v[102:105], v[10:17], v[212:219], v[102:105], v191, v192 op_sel_hi:[0,0,0]
	v_mfma_scale_f32_16x16x128_f8f6f4 v[98:101], v[2:9], v[212:219], v[98:101], v191, v192 op_sel_hi:[0,0,0]
	s_setprio 0
	s_barrier
	s_add_i32 s74, s67, s56
	v_lshl_add_u64 v[178:179], s[52:53], 0, v[164:165]
	s_mov_b32 m0, s74
	ds_read_b128 v[196:199], v190 offset:16384
	ds_read_b128 v[200:203], v190 offset:17408
	ds_read_b128 v[204:207], v190 offset:18432
	ds_read_b128 v[208:211], v190 offset:19456
	ds_read_b128 v[212:215], v190 offset:20480
	ds_read_b128 v[216:219], v190 offset:21504
	ds_read_b128 v[220:223], v190 offset:22528
	ds_read_b128 v[224:227], v190 offset:23552
	global_load_lds_dwordx4 v[178:179], off
	s_add_i32 m0, s74, 0x2000
	s_add_u32 s74, s52, 0x8000
	v_lshl_add_u64 v[180:181], s[52:53], 0, v[168:169]
	s_addc_u32 s75, s53, 0
	s_add_i32 s76, s68, s56
	global_load_lds_dwordx4 v[180:181], off
	v_lshl_add_u64 v[182:183], s[74:75], 0, v[164:165]
	s_mov_b32 m0, s76
	v_lshl_add_u64 v[184:185], s[54:55], 0, v[166:167]
	global_load_lds_dwordx4 v[182:183], off
	v_lshl_add_u64 v[182:183], s[74:75], 0, v[168:169]
	s_add_i32 m0, s76, 0x2000
	s_nop 0
	global_load_lds_dwordx4 v[182:183], off
	v_lshl_add_u64 v[182:183], s[54:55], 0, v[162:163]
	s_mov_b32 m0, s51
	s_nop 0
	global_load_lds_dwordx4 v[182:183], off
	s_mov_b32 m0, s57
	s_nop 0
	global_load_lds_dwordx4 v[184:185], off
	s_waitcnt vmcnt(8)
	s_waitcnt lgkmcnt(0)
	s_barrier
	s_setprio 1
	s_nop 0
	s_waitcnt lgkmcnt(0)
	v_mfma_scale_f32_16x16x128_f8f6f4 v[94:97], v[26:33], v[196:203], v[94:97], v191, v192 op_sel_hi:[0,0,0]
	v_mfma_scale_f32_16x16x128_f8f6f4 v[90:93], v[18:25], v[196:203], v[90:93], v191, v192 op_sel_hi:[0,0,0]
	v_mfma_scale_f32_16x16x128_f8f6f4 v[78:81], v[26:33], v[204:211], v[78:81], v191, v192 op_sel_hi:[0,0,0]
	v_mfma_scale_f32_16x16x128_f8f6f4 v[74:77], v[18:25], v[204:211], v[74:77], v191, v192 op_sel_hi:[0,0,0]
	v_mfma_scale_f32_16x16x128_f8f6f4 v[62:65], v[26:33], v[212:219], v[62:65], v191, v192 op_sel_hi:[0,0,0]
	v_mfma_scale_f32_16x16x128_f8f6f4 v[58:61], v[18:25], v[212:219], v[58:61], v191, v192 op_sel_hi:[0,0,0]
	v_mfma_scale_f32_16x16x128_f8f6f4 v[46:49], v[26:33], v[220:227], v[46:49], v191, v192 op_sel_hi:[0,0,0]
	v_mfma_scale_f32_16x16x128_f8f6f4 v[42:45], v[18:25], v[220:227], v[42:45], v191, v192 op_sel_hi:[0,0,0]
	s_setprio 0
	s_setprio 1
	s_nop 0
	v_mfma_scale_f32_16x16x128_f8f6f4 v[86:89], v[10:17], v[196:203], v[86:89], v191, v192 op_sel_hi:[0,0,0]
	v_mfma_scale_f32_16x16x128_f8f6f4 v[82:85], v[2:9], v[196:203], v[82:85], v191, v192 op_sel_hi:[0,0,0]
	v_mfma_scale_f32_16x16x128_f8f6f4 v[70:73], v[10:17], v[204:211], v[70:73], v191, v192 op_sel_hi:[0,0,0]
	v_mfma_scale_f32_16x16x128_f8f6f4 v[66:69], v[2:9], v[204:211], v[66:69], v191, v192 op_sel_hi:[0,0,0]
	v_mfma_scale_f32_16x16x128_f8f6f4 v[54:57], v[10:17], v[212:219], v[54:57], v191, v192 op_sel_hi:[0,0,0]
	v_mfma_scale_f32_16x16x128_f8f6f4 v[50:53], v[2:9], v[212:219], v[50:53], v191, v192 op_sel_hi:[0,0,0]
	v_mfma_scale_f32_16x16x128_f8f6f4 v[38:41], v[10:17], v[220:227], v[38:41], v191, v192 op_sel_hi:[0,0,0]
	v_mfma_scale_f32_16x16x128_f8f6f4 v[34:37], v[2:9], v[220:227], v[34:37], v191, v192 op_sel_hi:[0,0,0]
	s_setprio 0
	s_barrier
; #define PG8_STAGE(bufoff, gbase, voff) do { _Pragma("unroll") for (int _i = 0; _i < 2; ++_i) \
;         __builtin_amdgcn_global_load_lds((const unsigned*)((const char*)(gbase) + (voff)[_i]), (PG8_LAS unsigned*)(lds + (bufoff) + ldsw + _i * 8192), 16, 0, 0); } while (0)
; #define PG8_STAGE_A(bufoff, gbase, h, nx) do { if constexpr (Sched::GATHER) { const unsigned vv_[2] = {(nx) ? vAn[h][0] : vA[h][0], (nx) ? vAn[h][1] : vA[h][1]}; PG8_STAGE(bufoff, gbase, vv_); } \
;         else { PG8_STAGE(bufoff, (gbase) + (h) * hstep, voffA); } } while (0)
; #define PG8_LDA(dst, b, h) do { _Pragma("unroll") for (int m = 0; m < 4; ++m) _Pragma("unroll") for (int k = 0; k < 2; ++k) dst[m][k] = *(const PG8_LAS bf16x8*)(lds + PG8_SA(b, h) + aoff + m * 2048 + k * 1024); } while (0)
; #define PG8_LDB(dst, b, h) do { _Pragma("unroll") for (int n = 0; n < 2; ++n) _Pragma("unroll") for (int k = 0; k < 2; ++k) dst[n][k] = *(const PG8_LAS bf16x8*)(lds + PG8_SB(b, h) + boff + n * 2048 + k * 1024); } while (0)
; #define PG8_WAIT_V(n) asm volatile("s_waitcnt vmcnt(" #n ")" ::: "memory")
; #define PG8_WAIT_L(n) asm volatile("s_waitcnt lgkmcnt(" #n ")" ::: "memory")
; #define PG8_BAR __builtin_amdgcn_s_barrier()
; #define PG8_SCHED __builtin_amdgcn_sched_barrier(0)
;     ...
;             PG8_LDB(B0, 1, 0); PG8_LDB(B1, 1, 1); PG8_SCHED; PG8_LDA(At, 1, 0); PG8_STAGE_A(PG8_SA(0, 1), a2, 1, last);
;             PG8_WAIT_V(8); PG8_WAIT_L(0); PG8_BAR; PG8_MMA(0, 0, At, B0); PG8_MMA(0, 1, At, B1); PG8_BAR; PG8_SCHED;
;             PG8_LDA(At, 1, 1); PG8_STAGE(PG8_SB(1, 0), b3, voffB); PG8_STAGE(PG8_SB(1, 1), b3 + hstepB, voffB); PG8_STAGE_A(PG8_SA(1, 0), a3, 0, last);
;             PG8_WAIT_V(8); PG8_WAIT_L(0); PG8_BAR; PG8_MMA(1, 0, At, B0); PG8_MMA(1, 1, At, B1); PG8_BAR; PG8_SCHED;
;     ...
;         }
;         if constexpr (F8) asm volatile("s_nop 15\n\ts_nop 15\n\ts_nop 15" ::: "memory");
;         if constexpr (ALIGN_EPI) { if (wr == 0) PG8_BAR; }
	s_add_i32 s74, 0, 0x18000
	s_add_i32 s75, 0, 0x1c000
	v_add_u32_e32 v14, s74, v187
	v_add_u32_e32 v30, s75, v187
	ds_read_b128 v[2:5], v14
	ds_read_b128 v[6:9], v14 offset:1024
	ds_read_b128 v[10:13], v14 offset:2048
	ds_read_b128 v[14:17], v14 offset:3072
	ds_read_b128 v[18:21], v30
	ds_read_b128 v[22:25], v30 offset:1024
	ds_read_b128 v[26:29], v30 offset:2048
	ds_read_b128 v[30:33], v30 offset:3072
	s_add_u32 s54, s54, 0x20000
	s_addc_u32 s55, s55, 0
	s_mov_b32 m0, s58
	v_lshl_add_u64 v[228:229], s[54:55], 0, v[162:163]
	ds_read_b128 v[196:199], v190 offset:32768
	ds_read_b128 v[200:203], v190 offset:33792
	ds_read_b128 v[204:207], v190 offset:34816
	ds_read_b128 v[208:211], v190 offset:35840
	ds_read_b128 v[212:215], v190 offset:36864
	ds_read_b128 v[216:219], v190 offset:37888
	ds_read_b128 v[220:223], v190 offset:38912
	ds_read_b128 v[224:227], v190 offset:39936
	global_load_lds_dwordx4 v[228:229], off
	v_lshl_add_u64 v[228:229], s[54:55], 0, v[166:167]
	s_mov_b32 m0, s59
	s_nop 0
	global_load_lds_dwordx4 v[228:229], off
	s_waitcnt vmcnt(8)
	s_waitcnt lgkmcnt(0)
	s_barrier
	s_setprio 1
	s_nop 0
	s_waitcnt lgkmcnt(0)
	v_mfma_scale_f32_16x16x128_f8f6f4 v[158:161], v[2:9], v[196:203], v[158:161], v191, v192 op_sel_hi:[0,0,0]
	v_mfma_scale_f32_16x16x128_f8f6f4 v[154:157], v[10:17], v[196:203], v[154:157], v191, v192 op_sel_hi:[0,0,0]
	v_mfma_scale_f32_16x16x128_f8f6f4 v[142:145], v[2:9], v[204:211], v[142:145], v191, v192 op_sel_hi:[0,0,0]
	v_mfma_scale_f32_16x16x128_f8f6f4 v[138:141], v[10:17], v[204:211], v[138:141], v191, v192 op_sel_hi:[0,0,0]
	v_mfma_scale_f32_16x16x128_f8f6f4 v[126:129], v[2:9], v[212:219], v[126:129], v191, v192 op_sel_hi:[0,0,0]
	v_mfma_scale_f32_16x16x128_f8f6f4 v[122:125], v[10:17], v[212:219], v[122:125], v191, v192 op_sel_hi:[0,0,0]
	v_mfma_scale_f32_16x16x128_f8f6f4 v[110:113], v[2:9], v[220:227], v[110:113], v191, v192 op_sel_hi:[0,0,0]
	v_mfma_scale_f32_16x16x128_f8f6f4 v[106:109], v[10:17], v[220:227], v[106:109], v191, v192 op_sel_hi:[0,0,0]
	s_setprio 0
	s_setprio 1
	s_nop 0
	v_mfma_scale_f32_16x16x128_f8f6f4 v[150:153], v[18:25], v[196:203], v[150:153], v191, v192 op_sel_hi:[0,0,0]
	v_mfma_scale_f32_16x16x128_f8f6f4 v[146:149], v[26:33], v[196:203], v[146:149], v191, v192 op_sel_hi:[0,0,0]
	v_mfma_scale_f32_16x16x128_f8f6f4 v[134:137], v[18:25], v[204:211], v[134:137], v191, v192 op_sel_hi:[0,0,0]
	v_mfma_scale_f32_16x16x128_f8f6f4 v[130:133], v[26:33], v[204:211], v[130:133], v191, v192 op_sel_hi:[0,0,0]
	v_mfma_scale_f32_16x16x128_f8f6f4 v[118:121], v[18:25], v[212:219], v[118:121], v191, v192 op_sel_hi:[0,0,0]
	v_mfma_scale_f32_16x16x128_f8f6f4 v[114:117], v[26:33], v[212:219], v[114:117], v191, v192 op_sel_hi:[0,0,0]
	v_mfma_scale_f32_16x16x128_f8f6f4 v[102:105], v[18:25], v[220:227], v[102:105], v191, v192 op_sel_hi:[0,0,0]
	v_mfma_scale_f32_16x16x128_f8f6f4 v[98:101], v[26:33], v[220:227], v[98:101], v191, v192 op_sel_hi:[0,0,0]
	s_setprio 0
	s_barrier
	s_add_i32 s54, s74, s56
	v_lshl_add_u64 v[178:179], v[178:179], 0, s[18:19]
	s_mov_b32 m0, s54
	ds_read_b128 v[196:199], v190 offset:49152
	ds_read_b128 v[200:203], v190 offset:50176
	ds_read_b128 v[204:207], v190 offset:51200
	ds_read_b128 v[208:211], v190 offset:52224
	ds_read_b128 v[212:215], v190 offset:53248
	ds_read_b128 v[216:219], v190 offset:54272
	ds_read_b128 v[220:223], v190 offset:55296
	ds_read_b128 v[224:227], v190 offset:56320
	global_load_lds_dwordx4 v[178:179], off
	s_add_i32 m0, s54, 0x2000
	s_add_u32 s52, s52, 0x8080
	v_lshl_add_u64 v[178:179], v[180:181], 0, s[18:19]
	s_addc_u32 s53, s53, 0
	s_add_i32 s54, s75, s56
	global_load_lds_dwordx4 v[178:179], off
	v_lshl_add_u64 v[178:179], s[52:53], 0, v[164:165]
	s_mov_b32 m0, s54
	s_nop 0
	global_load_lds_dwordx4 v[178:179], off
	v_lshl_add_u64 v[178:179], s[52:53], 0, v[168:169]
	s_add_i32 m0, s54, 0x2000
	s_nop 0
	global_load_lds_dwordx4 v[178:179], off
	v_lshl_add_u64 v[178:179], v[182:183], 0, s[18:19]
	s_mov_b32 m0, s64
	s_nop 0
	global_load_lds_dwordx4 v[178:179], off
	v_lshl_add_u64 v[178:179], v[184:185], 0, s[18:19]
	s_mov_b32 m0, s65
	s_nop 0
	global_load_lds_dwordx4 v[178:179], off
	s_waitcnt vmcnt(8)
	s_waitcnt lgkmcnt(0)
	s_barrier
	s_setprio 1
	s_nop 0
	s_waitcnt lgkmcnt(0)
	v_mfma_scale_f32_16x16x128_f8f6f4 v[94:97], v[2:9], v[196:203], v[94:97], v191, v192 op_sel_hi:[0,0,0]
	v_mfma_scale_f32_16x16x128_f8f6f4 v[90:93], v[10:17], v[196:203], v[90:93], v191, v192 op_sel_hi:[0,0,0]
	v_mfma_scale_f32_16x16x128_f8f6f4 v[78:81], v[2:9], v[204:211], v[78:81], v191, v192 op_sel_hi:[0,0,0]
	v_mfma_scale_f32_16x16x128_f8f6f4 v[74:77], v[10:17], v[204:211], v[74:77], v191, v192 op_sel_hi:[0,0,0]
	v_mfma_scale_f32_16x16x128_f8f6f4 v[62:65], v[2:9], v[212:219], v[62:65], v191, v192 op_sel_hi:[0,0,0]
	v_mfma_scale_f32_16x16x128_f8f6f4 v[58:61], v[10:17], v[212:219], v[58:61], v191, v192 op_sel_hi:[0,0,0]
	v_mfma_scale_f32_16x16x128_f8f6f4 v[46:49], v[2:9], v[220:227], v[46:49], v191, v192 op_sel_hi:[0,0,0]
	v_mfma_scale_f32_16x16x128_f8f6f4 v[42:45], v[10:17], v[220:227], v[42:45], v191, v192 op_sel_hi:[0,0,0]
	s_setprio 0
	s_setprio 1
	s_nop 0
	v_mfma_scale_f32_16x16x128_f8f6f4 v[86:89], v[18:25], v[196:203], v[86:89], v191, v192 op_sel_hi:[0,0,0]
	v_mfma_scale_f32_16x16x128_f8f6f4 v[82:85], v[26:33], v[196:203], v[82:85], v191, v192 op_sel_hi:[0,0,0]
	v_mfma_scale_f32_16x16x128_f8f6f4 v[70:73], v[18:25], v[204:211], v[70:73], v191, v192 op_sel_hi:[0,0,0]
	v_mfma_scale_f32_16x16x128_f8f6f4 v[66:69], v[26:33], v[204:211], v[66:69], v191, v192 op_sel_hi:[0,0,0]
	v_mfma_scale_f32_16x16x128_f8f6f4 v[54:57], v[18:25], v[212:219], v[54:57], v191, v192 op_sel_hi:[0,0,0]
	v_mfma_scale_f32_16x16x128_f8f6f4 v[50:53], v[26:33], v[212:219], v[50:53], v191, v192 op_sel_hi:[0,0,0]
	v_mfma_scale_f32_16x16x128_f8f6f4 v[38:41], v[18:25], v[220:227], v[38:41], v191, v192 op_sel_hi:[0,0,0]
	v_mfma_scale_f32_16x16x128_f8f6f4 v[34:37], v[26:33], v[220:227], v[34:37], v191, v192 op_sel_hi:[0,0,0]
	s_setprio 0
	s_barrier
	s_add_i32 s73, s73, 2
	s_add_u32 s6, s6, 0x100
	s_addc_u32 s7, s7, 0
	s_add_u32 s71, s71, 0x100
	s_addc_u32 s72, s72, 0
	s_cmp_gt_u32 s73, 5
	s_cbranch_scc0 .LBB0_1026
	s_and_b64 vcc, exec, s[20:21]
	s_cbranch_vccz .LBB0_1029
	s_barrier

; #define PG8_STAGE(bufoff, gbase, voff) do { _Pragma("unroll") for (int _i = 0; _i < 2; ++_i) \
;         __builtin_amdgcn_global_load_lds((const unsigned*)((const char*)(gbase) + (voff)[_i]), (PG8_LAS unsigned*)(lds + (bufoff) + ldsw + _i * 8192), 16, 0, 0); } while (0)
; #define PG8_STAGE_A(bufoff, gbase, h, nx) do { if constexpr (Sched::GATHER) { const unsigned vv_[2] = {(nx) ? vAn[h][0] : vA[h][0], (nx) ? vAn[h][1] : vA[h][1]}; PG8_STAGE(bufoff, gbase, vv_); } \
;         else { PG8_STAGE(bufoff, (gbase) + (h) * hstep, voffA); } } while (0)
; #define PG8_LDA(dst, b, h) do { _Pragma("unroll") for (int m = 0; m < 4; ++m) _Pragma("unroll") for (int k = 0; k < 2; ++k) dst[m][k] = *(const PG8_LAS bf16x8*)(lds + PG8_SA(b, h) + aoff + m * 2048 + k * 1024); } while (0)
; #define PG8_WAIT_V(n) asm volatile("s_waitcnt vmcnt(" #n ")" ::: "memory")
; #define PG8_WAIT_L(n) asm volatile("s_waitcnt lgkmcnt(" #n ")" ::: "memory")
;     ...
;         const bool has_next = S.next(ui + 1, nxt);
;         const char* nA = Sched::GATHER ? cA : (has_next ? (const char*)g.A + (size_t)nxt.pm * tstep : cA);
;         if constexpr (Sched::GATHER) { if (has_next) { PG8_AOFF(vAn, ui + 1); } else { _Pragma("unroll") for (int h_ = 0; h_ < 2; ++h_) _Pragma("unroll") for (int i_ = 0; i_ < 2; ++i_) vAn[h_][i_] = vA[h_][i_]; } } const char* nB = has_next ? (const char*)g.Bt + (size_t)nxt.pb * tstep : cB;
; #pragma nounroll
;         for (int t = 0; t < nt; t += 2) {
;             const bool last = (t == nt - 2);
;             const char* a1 = cA + (size_t)(t + 1) * kstep;
;             const char* a2 = last ? nA : cA + (size_t)(t + 2) * kstep; const char* b2 = last ? nB : cB + (size_t)(t + 2) * kstep;
;             const char* a3 = a2 + kstep; const char* b3 = b2 + kstep;
;             if (last && has_next) S.a_ready(nxt);
;             if constexpr (SP2) {
;             PG8_LDB(B0, 0, 0); PG8_LDB(B1, 0, 1); PG8_SCHED; PG8_LDA(At, 0, 0); PG8_STAGE_A(PG8_SA(1, 1), a1, 1, false);
;             PG8_WAIT_V(8); PG8_WAIT_L(0); PG8_BAR; PG8_MMA(0, 0, At, B0); PG8_MMA(0, 1, At, B1); PG8_BAR; PG8_SCHED;
;             PG8_LDA(At, 0, 1); PG8_STAGE(PG8_SB(0, 0), b2, voffB); PG8_STAGE(PG8_SB(0, 1), b2 + hstepB, voffB); PG8_STAGE_A(PG8_SA(0, 0), a2, 0, last);
;             PG8_WAIT_V(8); PG8_WAIT_L(0); PG8_BAR; PG8_MMA(1, 0, At, B0); PG8_MMA(1, 1, At, B1); PG8_BAR; PG8_SCHED;
.LBB0_1204:
	s_ashr_i32 s17, s16, 31
	s_lshl_b64 s[18:19], s[16:17], 18
	v_readlane_b32 s20, v255, 21
	v_readlane_b32 s21, v255, 22
	s_add_u32 s18, s20, s18
	s_addc_u32 s19, s21, s19
	s_and_b64 s[20:21], s[2:3], exec
	s_cselect_b32 s17, s19, s25
	s_cselect_b32 s44, s18, s24
	s_ashr_i32 s15, s14, 31
	s_lshl_b64 s[20:21], s[14:15], 18
	v_readlane_b32 s28, v254, 57
	v_readlane_b32 s29, v254, 58
	s_add_u32 s20, s28, s20
	s_addc_u32 s21, s29, s21
	s_and_b64 s[28:29], s[2:3], exec
	s_cselect_b32 s15, s21, s27
	s_cselect_b32 s45, s20, s26
	s_add_u32 s24, s24, 0x20080
	s_addc_u32 s25, s25, 0
	s_add_u32 s46, s26, 0x100
	s_addc_u32 s47, s27, 0
	s_mov_b32 s48, -2
	ds_read_b128 v[26:29], v188
	ds_read_b128 v[30:33], v188 offset:1024
	ds_read_b128 v[18:21], v188 offset:2048
	ds_read_b128 v[22:25], v188 offset:3072
	ds_read_b128 v[10:13], v189
	ds_read_b128 v[14:17], v189 offset:1024
	ds_read_b128 v[2:5], v189 offset:2048
	ds_read_b128 v[6:9], v189 offset:3072
	s_add_u32 s26, s24, 0xfffe0080
	s_addc_u32 s27, s25, -1
	s_cmp_eq_u32 s48, 4
	s_cselect_b32 s29, s17, s27
	s_cselect_b32 s28, s44, s26
	s_cselect_b32 s27, s15, s47
	s_cselect_b32 s26, s45, s46
	v_lshl_add_u64 v[218:219], s[24:25], 0, v[170:171]
	s_add_i32 m0, s23, 0xc000
	ds_read_b128 v[178:181], v190
	ds_read_b128 v[182:185], v190 offset:1024
	ds_read_b128 v[194:197], v190 offset:2048
	ds_read_b128 v[198:201], v190 offset:3072
	ds_read_b128 v[202:205], v190 offset:4096
	ds_read_b128 v[206:209], v190 offset:5120
	ds_read_b128 v[210:213], v190 offset:6144
	ds_read_b128 v[214:217], v190 offset:7168
	global_load_lds_dwordx4 v[218:219], off
	v_lshl_add_u64 v[218:219], s[24:25], 0, v[172:173]
	s_add_i32 m0, s23, 0xe000
	s_nop 0
	global_load_lds_dwordx4 v[218:219], off
	s_waitcnt vmcnt(8)
	s_waitcnt lgkmcnt(0)
	s_barrier
	s_setprio 1
	s_nop 0
	s_waitcnt lgkmcnt(0)
	v_mfma_scale_f32_16x16x128_f8f6f4 v[158:161], v[26:33], v[178:185], 0, v191, v192 op_sel_hi:[0,0,0]
	v_mfma_scale_f32_16x16x128_f8f6f4 v[154:157], v[18:25], v[178:185], 0, v191, v192 op_sel_hi:[0,0,0]
	v_mfma_scale_f32_16x16x128_f8f6f4 v[142:145], v[26:33], v[194:201], 0, v191, v192 op_sel_hi:[0,0,0]
	v_mfma_scale_f32_16x16x128_f8f6f4 v[138:141], v[18:25], v[194:201], 0, v191, v192 op_sel_hi:[0,0,0]
	v_mfma_scale_f32_16x16x128_f8f6f4 v[126:129], v[26:33], v[202:209], 0, v191, v192 op_sel_hi:[0,0,0]
	v_mfma_scale_f32_16x16x128_f8f6f4 v[122:125], v[18:25], v[202:209], 0, v191, v192 op_sel_hi:[0,0,0]
	v_mfma_scale_f32_16x16x128_f8f6f4 v[110:113], v[26:33], v[210:217], 0, v191, v192 op_sel_hi:[0,0,0]
	v_mfma_scale_f32_16x16x128_f8f6f4 v[106:109], v[18:25], v[210:217], 0, v191, v192 op_sel_hi:[0,0,0]
	s_setprio 0
	s_setprio 1
	s_nop 0
	v_mfma_scale_f32_16x16x128_f8f6f4 v[150:153], v[10:17], v[178:185], 0, v191, v192 op_sel_hi:[0,0,0]
	v_mfma_scale_f32_16x16x128_f8f6f4 v[146:149], v[2:9], v[178:185], 0, v191, v192 op_sel_hi:[0,0,0]
	v_mfma_scale_f32_16x16x128_f8f6f4 v[134:137], v[10:17], v[194:201], 0, v191, v192 op_sel_hi:[0,0,0]
	v_mfma_scale_f32_16x16x128_f8f6f4 v[130:133], v[2:9], v[194:201], 0, v191, v192 op_sel_hi:[0,0,0]
	v_mfma_scale_f32_16x16x128_f8f6f4 v[118:121], v[10:17], v[202:209], 0, v191, v192 op_sel_hi:[0,0,0]
	v_mfma_scale_f32_16x16x128_f8f6f4 v[114:117], v[2:9], v[202:209], 0, v191, v192 op_sel_hi:[0,0,0]
	v_mfma_scale_f32_16x16x128_f8f6f4 v[102:105], v[10:17], v[210:217], 0, v191, v192 op_sel_hi:[0,0,0]
	v_mfma_scale_f32_16x16x128_f8f6f4 v[98:101], v[2:9], v[210:217], 0, v191, v192 op_sel_hi:[0,0,0]
	s_setprio 0
	s_barrier
	s_add_i32 s49, s41, s30
	v_lshl_add_u64 v[178:179], s[26:27], 0, v[164:165]
	s_mov_b32 m0, s49
	ds_read_b128 v[194:197], v190 offset:16384
	ds_read_b128 v[198:201], v190 offset:17408
	ds_read_b128 v[202:205], v190 offset:18432
	ds_read_b128 v[206:209], v190 offset:19456
	ds_read_b128 v[210:213], v190 offset:20480
	ds_read_b128 v[214:217], v190 offset:21504
	ds_read_b128 v[218:221], v190 offset:22528
	ds_read_b128 v[222:225], v190 offset:23552
	global_load_lds_dwordx4 v[178:179], off
	s_add_i32 m0, s49, 0x2000
	s_add_u32 s50, s26, 0x2000
	v_lshl_add_u64 v[180:181], s[26:27], 0, v[168:169]
	s_addc_u32 s51, s27, 0
	s_add_i32 s49, s42, s30
	global_load_lds_dwordx4 v[180:181], off
	v_lshl_add_u64 v[182:183], s[50:51], 0, v[164:165]
	s_mov_b32 m0, s49
	v_lshl_add_u64 v[184:185], s[28:29], 0, v[166:167]
	global_load_lds_dwordx4 v[182:183], off
	v_lshl_add_u64 v[182:183], s[50:51], 0, v[168:169]
	s_add_i32 m0, s49, 0x2000
	s_nop 0
	global_load_lds_dwordx4 v[182:183], off
	v_lshl_add_u64 v[182:183], s[28:29], 0, v[162:163]
	s_mov_b32 m0, s23
	s_nop 0
	global_load_lds_dwordx4 v[182:183], off
	s_mov_b32 m0, s34
	s_nop 0
	global_load_lds_dwordx4 v[184:185], off
	s_waitcnt vmcnt(8)
	s_waitcnt lgkmcnt(0)
	s_barrier
	s_setprio 1
	s_nop 0
	s_waitcnt lgkmcnt(0)
	v_mfma_scale_f32_16x16x128_f8f6f4 v[94:97], v[26:33], v[194:201], 0, v191, v192 op_sel_hi:[0,0,0]
	v_mfma_scale_f32_16x16x128_f8f6f4 v[90:93], v[18:25], v[194:201], 0, v191, v192 op_sel_hi:[0,0,0]
	v_mfma_scale_f32_16x16x128_f8f6f4 v[78:81], v[26:33], v[202:209], 0, v191, v192 op_sel_hi:[0,0,0]
	v_mfma_scale_f32_16x16x128_f8f6f4 v[74:77], v[18:25], v[202:209], 0, v191, v192 op_sel_hi:[0,0,0]
	v_mfma_scale_f32_16x16x128_f8f6f4 v[62:65], v[26:33], v[210:217], 0, v191, v192 op_sel_hi:[0,0,0]
	v_mfma_scale_f32_16x16x128_f8f6f4 v[58:61], v[18:25], v[210:217], 0, v191, v192 op_sel_hi:[0,0,0]
	v_mfma_scale_f32_16x16x128_f8f6f4 v[46:49], v[26:33], v[218:225], 0, v191, v192 op_sel_hi:[0,0,0]
	v_mfma_scale_f32_16x16x128_f8f6f4 v[42:45], v[18:25], v[218:225], 0, v191, v192 op_sel_hi:[0,0,0]
	s_setprio 0
	s_setprio 1
	s_nop 0
	v_mfma_scale_f32_16x16x128_f8f6f4 v[86:89], v[10:17], v[194:201], 0, v191, v192 op_sel_hi:[0,0,0]
	v_mfma_scale_f32_16x16x128_f8f6f4 v[82:85], v[2:9], v[194:201], 0, v191, v192 op_sel_hi:[0,0,0]
	v_mfma_scale_f32_16x16x128_f8f6f4 v[70:73], v[10:17], v[202:209], 0, v191, v192 op_sel_hi:[0,0,0]
	v_mfma_scale_f32_16x16x128_f8f6f4 v[66:69], v[2:9], v[202:209], 0, v191, v192 op_sel_hi:[0,0,0]
	v_mfma_scale_f32_16x16x128_f8f6f4 v[54:57], v[10:17], v[210:217], 0, v191, v192 op_sel_hi:[0,0,0]
	v_mfma_scale_f32_16x16x128_f8f6f4 v[50:53], v[2:9], v[210:217], 0, v191, v192 op_sel_hi:[0,0,0]
	v_mfma_scale_f32_16x16x128_f8f6f4 v[38:41], v[10:17], v[218:225], 0, v191, v192 op_sel_hi:[0,0,0]
	v_mfma_scale_f32_16x16x128_f8f6f4 v[34:37], v[2:9], v[218:225], 0, v191, v192 op_sel_hi:[0,0,0]
	s_setprio 0
	s_barrier
; #define PG8_STAGE(bufoff, gbase, voff) do { _Pragma("unroll") for (int _i = 0; _i < 2; ++_i) \
;         __builtin_amdgcn_global_load_lds((const unsigned*)((const char*)(gbase) + (voff)[_i]), (PG8_LAS unsigned*)(lds + (bufoff) + ldsw + _i * 8192), 16, 0, 0); } while (0)
; #define PG8_STAGE_A(bufoff, gbase, h, nx) do { if constexpr (Sched::GATHER) { const unsigned vv_[2] = {(nx) ? vAn[h][0] : vA[h][0], (nx) ? vAn[h][1] : vA[h][1]}; PG8_STAGE(bufoff, gbase, vv_); } \
;         else { PG8_STAGE(bufoff, (gbase) + (h) * hstep, voffA); } } while (0)
; #define PG8_LDA(dst, b, h) do { _Pragma("unroll") for (int m = 0; m < 4; ++m) _Pragma("unroll") for (int k = 0; k < 2; ++k) dst[m][k] = *(const PG8_LAS bf16x8*)(lds + PG8_SA(b, h) + aoff + m * 2048 + k * 1024); } while (0)
; #define PG8_LDB(dst, b, h) do { _Pragma("unroll") for (int n = 0; n < 2; ++n) _Pragma("unroll") for (int k = 0; k < 2; ++k) dst[n][k] = *(const PG8_LAS bf16x8*)(lds + PG8_SB(b, h) + boff + n * 2048 + k * 1024); } while (0)
; #define PG8_WAIT_V(n) asm volatile("s_waitcnt vmcnt(" #n ")" ::: "memory")
; #define PG8_WAIT_L(n) asm volatile("s_waitcnt lgkmcnt(" #n ")" ::: "memory")
; #define PG8_BAR __builtin_amdgcn_s_barrier()
; #define PG8_SCHED __builtin_amdgcn_sched_barrier(0)
;     ...
;             PG8_LDB(B0, 1, 0); PG8_LDB(B1, 1, 1); PG8_SCHED; PG8_LDA(At, 1, 0); PG8_STAGE_A(PG8_SA(0, 1), a2, 1, last);
;             PG8_WAIT_V(8); PG8_WAIT_L(0); PG8_BAR; PG8_MMA(0, 0, At, B0); PG8_MMA(0, 1, At, B1); PG8_BAR; PG8_SCHED;
;             PG8_LDA(At, 1, 1); PG8_STAGE(PG8_SB(1, 0), b3, voffB); PG8_STAGE(PG8_SB(1, 1), b3 + hstepB, voffB); PG8_STAGE_A(PG8_SA(1, 0), a3, 0, last);
;             PG8_WAIT_V(8); PG8_WAIT_L(0); PG8_BAR; PG8_MMA(1, 0, At, B0); PG8_MMA(1, 1, At, B1); PG8_BAR; PG8_SCHED;
	s_add_i32 s49, 0, 0x18000
	s_add_i32 s50, 0, 0x1c000
	v_add_u32_e32 v14, s49, v186
	v_add_u32_e32 v30, s50, v186
	ds_read_b128 v[2:5], v14
	ds_read_b128 v[6:9], v14 offset:1024
	ds_read_b128 v[10:13], v14 offset:2048
	ds_read_b128 v[14:17], v14 offset:3072
	ds_read_b128 v[18:21], v30
	ds_read_b128 v[22:25], v30 offset:1024
	ds_read_b128 v[26:29], v30 offset:2048
	ds_read_b128 v[30:33], v30 offset:3072
	s_add_u32 s28, s28, 0x20000
	s_addc_u32 s29, s29, 0
	s_mov_b32 m0, s35
	v_lshl_add_u64 v[226:227], s[28:29], 0, v[162:163]
	ds_read_b128 v[194:197], v190 offset:32768
	ds_read_b128 v[198:201], v190 offset:33792
	ds_read_b128 v[202:205], v190 offset:34816
	ds_read_b128 v[206:209], v190 offset:35840
	ds_read_b128 v[210:213], v190 offset:36864
	ds_read_b128 v[214:217], v190 offset:37888
	ds_read_b128 v[218:221], v190 offset:38912
	ds_read_b128 v[222:225], v190 offset:39936
	global_load_lds_dwordx4 v[226:227], off
	v_lshl_add_u64 v[226:227], s[28:29], 0, v[166:167]
	s_mov_b32 m0, s36
	s_nop 0
	global_load_lds_dwordx4 v[226:227], off
	s_waitcnt vmcnt(8)
	s_waitcnt lgkmcnt(0)
	s_barrier
	s_setprio 1
	s_nop 0
	s_waitcnt lgkmcnt(0)
	v_mfma_scale_f32_16x16x128_f8f6f4 v[158:161], v[2:9], v[194:201], v[158:161], v191, v192 op_sel_hi:[0,0,0]
	v_mfma_scale_f32_16x16x128_f8f6f4 v[154:157], v[10:17], v[194:201], v[154:157], v191, v192 op_sel_hi:[0,0,0]
	v_mfma_scale_f32_16x16x128_f8f6f4 v[142:145], v[2:9], v[202:209], v[142:145], v191, v192 op_sel_hi:[0,0,0]
	v_mfma_scale_f32_16x16x128_f8f6f4 v[138:141], v[10:17], v[202:209], v[138:141], v191, v192 op_sel_hi:[0,0,0]
	v_mfma_scale_f32_16x16x128_f8f6f4 v[126:129], v[2:9], v[210:217], v[126:129], v191, v192 op_sel_hi:[0,0,0]
	v_mfma_scale_f32_16x16x128_f8f6f4 v[122:125], v[10:17], v[210:217], v[122:125], v191, v192 op_sel_hi:[0,0,0]
	v_mfma_scale_f32_16x16x128_f8f6f4 v[110:113], v[2:9], v[218:225], v[110:113], v191, v192 op_sel_hi:[0,0,0]
	v_mfma_scale_f32_16x16x128_f8f6f4 v[106:109], v[10:17], v[218:225], v[106:109], v191, v192 op_sel_hi:[0,0,0]
	s_setprio 0
	s_setprio 1
	s_nop 0
	v_mfma_scale_f32_16x16x128_f8f6f4 v[150:153], v[18:25], v[194:201], v[150:153], v191, v192 op_sel_hi:[0,0,0]
	v_mfma_scale_f32_16x16x128_f8f6f4 v[146:149], v[26:33], v[194:201], v[146:149], v191, v192 op_sel_hi:[0,0,0]
	v_mfma_scale_f32_16x16x128_f8f6f4 v[134:137], v[18:25], v[202:209], v[134:137], v191, v192 op_sel_hi:[0,0,0]
	v_mfma_scale_f32_16x16x128_f8f6f4 v[130:133], v[26:33], v[202:209], v[130:133], v191, v192 op_sel_hi:[0,0,0]
	v_mfma_scale_f32_16x16x128_f8f6f4 v[118:121], v[18:25], v[210:217], v[118:121], v191, v192 op_sel_hi:[0,0,0]
	v_mfma_scale_f32_16x16x128_f8f6f4 v[114:117], v[26:33], v[210:217], v[114:117], v191, v192 op_sel_hi:[0,0,0]
	v_mfma_scale_f32_16x16x128_f8f6f4 v[102:105], v[18:25], v[218:225], v[102:105], v191, v192 op_sel_hi:[0,0,0]
	v_mfma_scale_f32_16x16x128_f8f6f4 v[98:101], v[26:33], v[218:225], v[98:101], v191, v192 op_sel_hi:[0,0,0]
	s_setprio 0
	s_barrier
	s_add_i32 s28, s49, s30
	v_lshl_add_u64 v[178:179], v[178:179], 0, s[8:9]
	s_mov_b32 m0, s28
	ds_read_b128 v[194:197], v190 offset:49152
	ds_read_b128 v[198:201], v190 offset:50176
	ds_read_b128 v[202:205], v190 offset:51200
	ds_read_b128 v[206:209], v190 offset:52224
	ds_read_b128 v[210:213], v190 offset:53248
	ds_read_b128 v[214:217], v190 offset:54272
	ds_read_b128 v[218:221], v190 offset:55296
	ds_read_b128 v[222:225], v190 offset:56320
	global_load_lds_dwordx4 v[178:179], off
	s_add_i32 m0, s28, 0x2000
	s_add_u32 s26, s26, 0x2080
	v_lshl_add_u64 v[178:179], v[180:181], 0, s[8:9]
	s_addc_u32 s27, s27, 0
	s_add_i32 s28, s50, s30
	global_load_lds_dwordx4 v[178:179], off
	v_lshl_add_u64 v[178:179], s[26:27], 0, v[164:165]
	s_mov_b32 m0, s28
	s_nop 0
	global_load_lds_dwordx4 v[178:179], off
	v_lshl_add_u64 v[178:179], s[26:27], 0, v[168:169]
	s_add_i32 m0, s28, 0x2000
	s_nop 0
	global_load_lds_dwordx4 v[178:179], off
	v_lshl_add_u64 v[178:179], v[182:183], 0, s[8:9]
	s_mov_b32 m0, s39
	s_nop 0
	global_load_lds_dwordx4 v[178:179], off
	v_lshl_add_u64 v[178:179], v[184:185], 0, s[8:9]
	s_mov_b32 m0, s40
	s_nop 0
	global_load_lds_dwordx4 v[178:179], off
	s_waitcnt vmcnt(8)
	s_waitcnt lgkmcnt(0)
	s_barrier
	s_setprio 1
	s_nop 0
	s_waitcnt lgkmcnt(0)
	v_mfma_scale_f32_16x16x128_f8f6f4 v[94:97], v[2:9], v[194:201], v[94:97], v191, v192 op_sel_hi:[0,0,0]
	v_mfma_scale_f32_16x16x128_f8f6f4 v[90:93], v[10:17], v[194:201], v[90:93], v191, v192 op_sel_hi:[0,0,0]
	v_mfma_scale_f32_16x16x128_f8f6f4 v[78:81], v[2:9], v[202:209], v[78:81], v191, v192 op_sel_hi:[0,0,0]
	v_mfma_scale_f32_16x16x128_f8f6f4 v[74:77], v[10:17], v[202:209], v[74:77], v191, v192 op_sel_hi:[0,0,0]
	v_mfma_scale_f32_16x16x128_f8f6f4 v[62:65], v[2:9], v[210:217], v[62:65], v191, v192 op_sel_hi:[0,0,0]
	v_mfma_scale_f32_16x16x128_f8f6f4 v[58:61], v[10:17], v[210:217], v[58:61], v191, v192 op_sel_hi:[0,0,0]
	v_mfma_scale_f32_16x16x128_f8f6f4 v[46:49], v[2:9], v[218:225], v[46:49], v191, v192 op_sel_hi:[0,0,0]
	v_mfma_scale_f32_16x16x128_f8f6f4 v[42:45], v[10:17], v[218:225], v[42:45], v191, v192 op_sel_hi:[0,0,0]
	s_setprio 0
	s_setprio 1
	s_nop 0
	v_mfma_scale_f32_16x16x128_f8f6f4 v[86:89], v[18:25], v[194:201], v[86:89], v191, v192 op_sel_hi:[0,0,0]
	v_mfma_scale_f32_16x16x128_f8f6f4 v[82:85], v[26:33], v[194:201], v[82:85], v191, v192 op_sel_hi:[0,0,0]
	v_mfma_scale_f32_16x16x128_f8f6f4 v[70:73], v[18:25], v[202:209], v[70:73], v191, v192 op_sel_hi:[0,0,0]
	v_mfma_scale_f32_16x16x128_f8f6f4 v[66:69], v[26:33], v[202:209], v[66:69], v191, v192 op_sel_hi:[0,0,0]
	v_mfma_scale_f32_16x16x128_f8f6f4 v[54:57], v[18:25], v[210:217], v[54:57], v191, v192 op_sel_hi:[0,0,0]
	v_mfma_scale_f32_16x16x128_f8f6f4 v[50:53], v[26:33], v[210:217], v[50:53], v191, v192 op_sel_hi:[0,0,0]
	v_mfma_scale_f32_16x16x128_f8f6f4 v[38:41], v[18:25], v[218:225], v[38:41], v191, v192 op_sel_hi:[0,0,0]
	v_mfma_scale_f32_16x16x128_f8f6f4 v[34:37], v[26:33], v[218:225], v[34:37], v191, v192 op_sel_hi:[0,0,0]
	s_setprio 0
	s_barrier
	s_add_i32 s48, s48, 2
	s_add_u32 s24, s24, 0x100
	s_addc_u32 s25, s25, 0
	s_add_u32 s46, s46, 0x100
	s_addc_u32 s47, s47, 0
; #define PG8_STAGE(bufoff, gbase, voff) do { _Pragma("unroll") for (int _i = 0; _i < 2; ++_i) \
;         __builtin_amdgcn_global_load_lds((const unsigned*)((const char*)(gbase) + (voff)[_i]), (PG8_LAS unsigned*)(lds + (bufoff) + ldsw + _i * 8192), 16, 0, 0); } while (0)
; #define PG8_STAGE_A(bufoff, gbase, h, nx) do { if constexpr (Sched::GATHER) { const unsigned vv_[2] = {(nx) ? vAn[h][0] : vA[h][0], (nx) ? vAn[h][1] : vA[h][1]}; PG8_STAGE(bufoff, gbase, vv_); } \
;         else { PG8_STAGE(bufoff, (gbase) + (h) * hstep, voffA); } } while (0)
; #define PG8_LDA(dst, b, h) do { _Pragma("unroll") for (int m = 0; m < 4; ++m) _Pragma("unroll") for (int k = 0; k < 2; ++k) dst[m][k] = *(const PG8_LAS bf16x8*)(lds + PG8_SA(b, h) + aoff + m * 2048 + k * 1024); } while (0)
; #define PG8_LDB(dst, b, h) do { _Pragma("unroll") for (int n = 0; n < 2; ++n) _Pragma("unroll") for (int k = 0; k < 2; ++k) dst[n][k] = *(const PG8_LAS bf16x8*)(lds + PG8_SB(b, h) + boff + n * 2048 + k * 1024); } while (0)
; #define PG8_WAIT_V(n) asm volatile("s_waitcnt vmcnt(" #n ")" ::: "memory")
; #define PG8_WAIT_L(n) asm volatile("s_waitcnt lgkmcnt(" #n ")" ::: "memory")
; #define PG8_BAR __builtin_amdgcn_s_barrier()
; #define PG8_SCHED __builtin_amdgcn_sched_barrier(0)
;     ...
;             PG8_LDB(B0, 0, 0); PG8_LDB(B1, 0, 1); PG8_SCHED; PG8_LDA(At, 0, 0); PG8_STAGE_A(PG8_SA(1, 1), a1, 1, false);
;             PG8_WAIT_V(8); PG8_WAIT_L(0); PG8_BAR; PG8_MMA(0, 0, At, B0); PG8_MMA(0, 1, At, B1); PG8_BAR; PG8_SCHED;
;             PG8_LDA(At, 0, 1); PG8_STAGE(PG8_SB(0, 0), b2, voffB); PG8_STAGE(PG8_SB(0, 1), b2 + hstepB, voffB); PG8_STAGE_A(PG8_SA(0, 0), a2, 0, last);
;             PG8_WAIT_V(8); PG8_WAIT_L(0); PG8_BAR; PG8_MMA(1, 0, At, B0); PG8_MMA(1, 1, At, B1); PG8_BAR; PG8_SCHED;
.LBB0_1205:
	ds_read_b128 v[26:29], v188
	ds_read_b128 v[30:33], v188 offset:1024
	ds_read_b128 v[18:21], v188 offset:2048
	ds_read_b128 v[22:25], v188 offset:3072
	ds_read_b128 v[10:13], v189
	ds_read_b128 v[14:17], v189 offset:1024
	ds_read_b128 v[2:5], v189 offset:2048
	ds_read_b128 v[6:9], v189 offset:3072
	s_add_u32 s26, s24, 0xfffe0080
	s_addc_u32 s27, s25, -1
	s_cmp_eq_u32 s48, 4
	s_cselect_b32 s29, s17, s27
	s_cselect_b32 s28, s44, s26
	s_cselect_b32 s27, s15, s47
	s_cselect_b32 s26, s45, s46
	v_lshl_add_u64 v[218:219], s[24:25], 0, v[170:171]
	s_add_i32 m0, s23, 0xc000
	ds_read_b128 v[178:181], v190
	ds_read_b128 v[182:185], v190 offset:1024
	ds_read_b128 v[194:197], v190 offset:2048
	ds_read_b128 v[198:201], v190 offset:3072
	ds_read_b128 v[202:205], v190 offset:4096
	ds_read_b128 v[206:209], v190 offset:5120
	ds_read_b128 v[210:213], v190 offset:6144
	ds_read_b128 v[214:217], v190 offset:7168
	global_load_lds_dwordx4 v[218:219], off
	v_lshl_add_u64 v[218:219], s[24:25], 0, v[172:173]
	s_add_i32 m0, s23, 0xe000
	s_nop 0
	global_load_lds_dwordx4 v[218:219], off
	s_waitcnt vmcnt(8)
	s_waitcnt lgkmcnt(0)
	s_barrier
	s_setprio 1
	s_nop 0
	s_waitcnt lgkmcnt(0)
	v_mfma_scale_f32_16x16x128_f8f6f4 v[158:161], v[26:33], v[178:185], v[158:161], v191, v192 op_sel_hi:[0,0,0]
	v_mfma_scale_f32_16x16x128_f8f6f4 v[154:157], v[18:25], v[178:185], v[154:157], v191, v192 op_sel_hi:[0,0,0]
	v_mfma_scale_f32_16x16x128_f8f6f4 v[142:145], v[26:33], v[194:201], v[142:145], v191, v192 op_sel_hi:[0,0,0]
	v_mfma_scale_f32_16x16x128_f8f6f4 v[138:141], v[18:25], v[194:201], v[138:141], v191, v192 op_sel_hi:[0,0,0]
	v_mfma_scale_f32_16x16x128_f8f6f4 v[126:129], v[26:33], v[202:209], v[126:129], v191, v192 op_sel_hi:[0,0,0]
	v_mfma_scale_f32_16x16x128_f8f6f4 v[122:125], v[18:25], v[202:209], v[122:125], v191, v192 op_sel_hi:[0,0,0]
	v_mfma_scale_f32_16x16x128_f8f6f4 v[110:113], v[26:33], v[210:217], v[110:113], v191, v192 op_sel_hi:[0,0,0]
	v_mfma_scale_f32_16x16x128_f8f6f4 v[106:109], v[18:25], v[210:217], v[106:109], v191, v192 op_sel_hi:[0,0,0]
	s_setprio 0
	s_setprio 1
	s_nop 0
	v_mfma_scale_f32_16x16x128_f8f6f4 v[150:153], v[10:17], v[178:185], v[150:153], v191, v192 op_sel_hi:[0,0,0]
	v_mfma_scale_f32_16x16x128_f8f6f4 v[146:149], v[2:9], v[178:185], v[146:149], v191, v192 op_sel_hi:[0,0,0]
	v_mfma_scale_f32_16x16x128_f8f6f4 v[134:137], v[10:17], v[194:201], v[134:137], v191, v192 op_sel_hi:[0,0,0]
	v_mfma_scale_f32_16x16x128_f8f6f4 v[130:133], v[2:9], v[194:201], v[130:133], v191, v192 op_sel_hi:[0,0,0]
	v_mfma_scale_f32_16x16x128_f8f6f4 v[118:121], v[10:17], v[202:209], v[118:121], v191, v192 op_sel_hi:[0,0,0]
	v_mfma_scale_f32_16x16x128_f8f6f4 v[114:117], v[2:9], v[202:209], v[114:117], v191, v192 op_sel_hi:[0,0,0]
	v_mfma_scale_f32_16x16x128_f8f6f4 v[102:105], v[10:17], v[210:217], v[102:105], v191, v192 op_sel_hi:[0,0,0]
	v_mfma_scale_f32_16x16x128_f8f6f4 v[98:101], v[2:9], v[210:217], v[98:101], v191, v192 op_sel_hi:[0,0,0]
	s_setprio 0
	s_barrier
	s_add_i32 s49, s41, s30
	v_lshl_add_u64 v[178:179], s[26:27], 0, v[164:165]
	s_mov_b32 m0, s49
	ds_read_b128 v[194:197], v190 offset:16384
	ds_read_b128 v[198:201], v190 offset:17408
	ds_read_b128 v[202:205], v190 offset:18432
	ds_read_b128 v[206:209], v190 offset:19456
	ds_read_b128 v[210:213], v190 offset:20480
	ds_read_b128 v[214:217], v190 offset:21504
	ds_read_b128 v[218:221], v190 offset:22528
	ds_read_b128 v[222:225], v190 offset:23552
	global_load_lds_dwordx4 v[178:179], off
	s_add_i32 m0, s49, 0x2000
	s_add_u32 s50, s26, 0x2000
	v_lshl_add_u64 v[180:181], s[26:27], 0, v[168:169]
	s_addc_u32 s51, s27, 0
	s_add_i32 s49, s42, s30
	global_load_lds_dwordx4 v[180:181], off
	v_lshl_add_u64 v[182:183], s[50:51], 0, v[164:165]
	s_mov_b32 m0, s49
	v_lshl_add_u64 v[184:185], s[28:29], 0, v[166:167]
	global_load_lds_dwordx4 v[182:183], off
	v_lshl_add_u64 v[182:183], s[50:51], 0, v[168:169]
	s_add_i32 m0, s49, 0x2000
	s_nop 0
	global_load_lds_dwordx4 v[182:183], off
	v_lshl_add_u64 v[182:183], s[28:29], 0, v[162:163]
	s_mov_b32 m0, s23
	s_nop 0
	global_load_lds_dwordx4 v[182:183], off
	s_mov_b32 m0, s34
	s_nop 0
	global_load_lds_dwordx4 v[184:185], off
	s_waitcnt vmcnt(8)
	s_waitcnt lgkmcnt(0)
	s_barrier
	s_setprio 1
	s_nop 0
	s_waitcnt lgkmcnt(0)
	v_mfma_scale_f32_16x16x128_f8f6f4 v[94:97], v[26:33], v[194:201], v[94:97], v191, v192 op_sel_hi:[0,0,0]
	v_mfma_scale_f32_16x16x128_f8f6f4 v[90:93], v[18:25], v[194:201], v[90:93], v191, v192 op_sel_hi:[0,0,0]
	v_mfma_scale_f32_16x16x128_f8f6f4 v[78:81], v[26:33], v[202:209], v[78:81], v191, v192 op_sel_hi:[0,0,0]
	v_mfma_scale_f32_16x16x128_f8f6f4 v[74:77], v[18:25], v[202:209], v[74:77], v191, v192 op_sel_hi:[0,0,0]
	v_mfma_scale_f32_16x16x128_f8f6f4 v[62:65], v[26:33], v[210:217], v[62:65], v191, v192 op_sel_hi:[0,0,0]
	v_mfma_scale_f32_16x16x128_f8f6f4 v[58:61], v[18:25], v[210:217], v[58:61], v191, v192 op_sel_hi:[0,0,0]
	v_mfma_scale_f32_16x16x128_f8f6f4 v[46:49], v[26:33], v[218:225], v[46:49], v191, v192 op_sel_hi:[0,0,0]
	v_mfma_scale_f32_16x16x128_f8f6f4 v[42:45], v[18:25], v[218:225], v[42:45], v191, v192 op_sel_hi:[0,0,0]
	s_setprio 0
	s_setprio 1
	s_nop 0
	v_mfma_scale_f32_16x16x128_f8f6f4 v[86:89], v[10:17], v[194:201], v[86:89], v191, v192 op_sel_hi:[0,0,0]
	v_mfma_scale_f32_16x16x128_f8f6f4 v[82:85], v[2:9], v[194:201], v[82:85], v191, v192 op_sel_hi:[0,0,0]
	v_mfma_scale_f32_16x16x128_f8f6f4 v[70:73], v[10:17], v[202:209], v[70:73], v191, v192 op_sel_hi:[0,0,0]
	v_mfma_scale_f32_16x16x128_f8f6f4 v[66:69], v[2:9], v[202:209], v[66:69], v191, v192 op_sel_hi:[0,0,0]
	v_mfma_scale_f32_16x16x128_f8f6f4 v[54:57], v[10:17], v[210:217], v[54:57], v191, v192 op_sel_hi:[0,0,0]
	v_mfma_scale_f32_16x16x128_f8f6f4 v[50:53], v[2:9], v[210:217], v[50:53], v191, v192 op_sel_hi:[0,0,0]
	v_mfma_scale_f32_16x16x128_f8f6f4 v[38:41], v[10:17], v[218:225], v[38:41], v191, v192 op_sel_hi:[0,0,0]
	v_mfma_scale_f32_16x16x128_f8f6f4 v[34:37], v[2:9], v[218:225], v[34:37], v191, v192 op_sel_hi:[0,0,0]
	s_setprio 0
	s_barrier
; #define PG8_STAGE(bufoff, gbase, voff) do { _Pragma("unroll") for (int _i = 0; _i < 2; ++_i) \
;         __builtin_amdgcn_global_load_lds((const unsigned*)((const char*)(gbase) + (voff)[_i]), (PG8_LAS unsigned*)(lds + (bufoff) + ldsw + _i * 8192), 16, 0, 0); } while (0)
; #define PG8_STAGE_A(bufoff, gbase, h, nx) do { if constexpr (Sched::GATHER) { const unsigned vv_[2] = {(nx) ? vAn[h][0] : vA[h][0], (nx) ? vAn[h][1] : vA[h][1]}; PG8_STAGE(bufoff, gbase, vv_); } \
;         else { PG8_STAGE(bufoff, (gbase) + (h) * hstep, voffA); } } while (0)
; #define PG8_LDA(dst, b, h) do { _Pragma("unroll") for (int m = 0; m < 4; ++m) _Pragma("unroll") for (int k = 0; k < 2; ++k) dst[m][k] = *(const PG8_LAS bf16x8*)(lds + PG8_SA(b, h) + aoff + m * 2048 + k * 1024); } while (0)
; #define PG8_LDB(dst, b, h) do { _Pragma("unroll") for (int n = 0; n < 2; ++n) _Pragma("unroll") for (int k = 0; k < 2; ++k) dst[n][k] = *(const PG8_LAS bf16x8*)(lds + PG8_SB(b, h) + boff + n * 2048 + k * 1024); } while (0)
; #define PG8_WAIT_V(n) asm volatile("s_waitcnt vmcnt(" #n ")" ::: "memory")
; #define PG8_WAIT_L(n) asm volatile("s_waitcnt lgkmcnt(" #n ")" ::: "memory")
; #define PG8_BAR __builtin_amdgcn_s_barrier()
; #define PG8_SCHED __builtin_amdgcn_sched_barrier(0)
;     ...
;             PG8_LDB(B0, 1, 0); PG8_LDB(B1, 1, 1); PG8_SCHED; PG8_LDA(At, 1, 0); PG8_STAGE_A(PG8_SA(0, 1), a2, 1, last);
;             PG8_WAIT_V(8); PG8_WAIT_L(0); PG8_BAR; PG8_MMA(0, 0, At, B0); PG8_MMA(0, 1, At, B1); PG8_BAR; PG8_SCHED;
;             PG8_LDA(At, 1, 1); PG8_STAGE(PG8_SB(1, 0), b3, voffB); PG8_STAGE(PG8_SB(1, 1), b3 + hstepB, voffB); PG8_STAGE_A(PG8_SA(1, 0), a3, 0, last);
;             PG8_WAIT_V(8); PG8_WAIT_L(0); PG8_BAR; PG8_MMA(1, 0, At, B0); PG8_MMA(1, 1, At, B1); PG8_BAR; PG8_SCHED;
	s_add_i32 s49, 0, 0x18000
	s_add_i32 s50, 0, 0x1c000
	v_add_u32_e32 v14, s49, v186
	v_add_u32_e32 v30, s50, v186
	ds_read_b128 v[2:5], v14
	ds_read_b128 v[6:9], v14 offset:1024
	ds_read_b128 v[10:13], v14 offset:2048
	ds_read_b128 v[14:17], v14 offset:3072
	ds_read_b128 v[18:21], v30
	ds_read_b128 v[22:25], v30 offset:1024
	ds_read_b128 v[26:29], v30 offset:2048
	ds_read_b128 v[30:33], v30 offset:3072
	s_add_u32 s28, s28, 0x20000
	s_addc_u32 s29, s29, 0
	s_mov_b32 m0, s35
	v_lshl_add_u64 v[226:227], s[28:29], 0, v[162:163]
	ds_read_b128 v[194:197], v190 offset:32768
	ds_read_b128 v[198:201], v190 offset:33792
	ds_read_b128 v[202:205], v190 offset:34816
	ds_read_b128 v[206:209], v190 offset:35840
	ds_read_b128 v[210:213], v190 offset:36864
	ds_read_b128 v[214:217], v190 offset:37888
	ds_read_b128 v[218:221], v190 offset:38912
	ds_read_b128 v[222:225], v190 offset:39936
	global_load_lds_dwordx4 v[226:227], off
	v_lshl_add_u64 v[226:227], s[28:29], 0, v[166:167]
	s_mov_b32 m0, s36
	s_nop 0
	global_load_lds_dwordx4 v[226:227], off
	s_waitcnt vmcnt(8)
	s_waitcnt lgkmcnt(0)
	s_barrier
	s_setprio 1
	s_nop 0
	s_waitcnt lgkmcnt(0)
	v_mfma_scale_f32_16x16x128_f8f6f4 v[158:161], v[2:9], v[194:201], v[158:161], v191, v192 op_sel_hi:[0,0,0]
	v_mfma_scale_f32_16x16x128_f8f6f4 v[154:157], v[10:17], v[194:201], v[154:157], v191, v192 op_sel_hi:[0,0,0]
	v_mfma_scale_f32_16x16x128_f8f6f4 v[142:145], v[2:9], v[202:209], v[142:145], v191, v192 op_sel_hi:[0,0,0]
	v_mfma_scale_f32_16x16x128_f8f6f4 v[138:141], v[10:17], v[202:209], v[138:141], v191, v192 op_sel_hi:[0,0,0]
	v_mfma_scale_f32_16x16x128_f8f6f4 v[126:129], v[2:9], v[210:217], v[126:129], v191, v192 op_sel_hi:[0,0,0]
	v_mfma_scale_f32_16x16x128_f8f6f4 v[122:125], v[10:17], v[210:217], v[122:125], v191, v192 op_sel_hi:[0,0,0]
	v_mfma_scale_f32_16x16x128_f8f6f4 v[110:113], v[2:9], v[218:225], v[110:113], v191, v192 op_sel_hi:[0,0,0]
	v_mfma_scale_f32_16x16x128_f8f6f4 v[106:109], v[10:17], v[218:225], v[106:109], v191, v192 op_sel_hi:[0,0,0]
	s_setprio 0
	s_setprio 1
	s_nop 0
	v_mfma_scale_f32_16x16x128_f8f6f4 v[150:153], v[18:25], v[194:201], v[150:153], v191, v192 op_sel_hi:[0,0,0]
	v_mfma_scale_f32_16x16x128_f8f6f4 v[146:149], v[26:33], v[194:201], v[146:149], v191, v192 op_sel_hi:[0,0,0]
	v_mfma_scale_f32_16x16x128_f8f6f4 v[134:137], v[18:25], v[202:209], v[134:137], v191, v192 op_sel_hi:[0,0,0]
	v_mfma_scale_f32_16x16x128_f8f6f4 v[130:133], v[26:33], v[202:209], v[130:133], v191, v192 op_sel_hi:[0,0,0]
	v_mfma_scale_f32_16x16x128_f8f6f4 v[118:121], v[18:25], v[210:217], v[118:121], v191, v192 op_sel_hi:[0,0,0]
	v_mfma_scale_f32_16x16x128_f8f6f4 v[114:117], v[26:33], v[210:217], v[114:117], v191, v192 op_sel_hi:[0,0,0]
	v_mfma_scale_f32_16x16x128_f8f6f4 v[102:105], v[18:25], v[218:225], v[102:105], v191, v192 op_sel_hi:[0,0,0]
	v_mfma_scale_f32_16x16x128_f8f6f4 v[98:101], v[26:33], v[218:225], v[98:101], v191, v192 op_sel_hi:[0,0,0]
	s_setprio 0
	s_barrier
	s_add_i32 s28, s49, s30
	v_lshl_add_u64 v[178:179], v[178:179], 0, s[8:9]
	s_mov_b32 m0, s28
	ds_read_b128 v[194:197], v190 offset:49152
	ds_read_b128 v[198:201], v190 offset:50176
	ds_read_b128 v[202:205], v190 offset:51200
	ds_read_b128 v[206:209], v190 offset:52224
	ds_read_b128 v[210:213], v190 offset:53248
	ds_read_b128 v[214:217], v190 offset:54272
	ds_read_b128 v[218:221], v190 offset:55296
	ds_read_b128 v[222:225], v190 offset:56320
	global_load_lds_dwordx4 v[178:179], off
	s_add_i32 m0, s28, 0x2000
	s_add_u32 s26, s26, 0x2080
	v_lshl_add_u64 v[178:179], v[180:181], 0, s[8:9]
	s_addc_u32 s27, s27, 0
	s_add_i32 s28, s50, s30
	global_load_lds_dwordx4 v[178:179], off
	v_lshl_add_u64 v[178:179], s[26:27], 0, v[164:165]
	s_mov_b32 m0, s28
	s_nop 0
	global_load_lds_dwordx4 v[178:179], off
	v_lshl_add_u64 v[178:179], s[26:27], 0, v[168:169]
	s_add_i32 m0, s28, 0x2000
	s_nop 0
	global_load_lds_dwordx4 v[178:179], off
	v_lshl_add_u64 v[178:179], v[182:183], 0, s[8:9]
	s_mov_b32 m0, s39
	s_nop 0
	global_load_lds_dwordx4 v[178:179], off
	v_lshl_add_u64 v[178:179], v[184:185], 0, s[8:9]
	s_mov_b32 m0, s40
	s_nop 0
	global_load_lds_dwordx4 v[178:179], off
	s_waitcnt vmcnt(8)
	s_waitcnt lgkmcnt(0)
	s_barrier
	s_setprio 1
	s_nop 0
	s_waitcnt lgkmcnt(0)
	v_mfma_scale_f32_16x16x128_f8f6f4 v[94:97], v[2:9], v[194:201], v[94:97], v191, v192 op_sel_hi:[0,0,0]
	v_mfma_scale_f32_16x16x128_f8f6f4 v[90:93], v[10:17], v[194:201], v[90:93], v191, v192 op_sel_hi:[0,0,0]
	v_mfma_scale_f32_16x16x128_f8f6f4 v[78:81], v[2:9], v[202:209], v[78:81], v191, v192 op_sel_hi:[0,0,0]
	v_mfma_scale_f32_16x16x128_f8f6f4 v[74:77], v[10:17], v[202:209], v[74:77], v191, v192 op_sel_hi:[0,0,0]
	v_mfma_scale_f32_16x16x128_f8f6f4 v[62:65], v[2:9], v[210:217], v[62:65], v191, v192 op_sel_hi:[0,0,0]
	v_mfma_scale_f32_16x16x128_f8f6f4 v[58:61], v[10:17], v[210:217], v[58:61], v191, v192 op_sel_hi:[0,0,0]
	v_mfma_scale_f32_16x16x128_f8f6f4 v[46:49], v[2:9], v[218:225], v[46:49], v191, v192 op_sel_hi:[0,0,0]
	v_mfma_scale_f32_16x16x128_f8f6f4 v[42:45], v[10:17], v[218:225], v[42:45], v191, v192 op_sel_hi:[0,0,0]
	s_setprio 0
	s_setprio 1
	s_nop 0
	v_mfma_scale_f32_16x16x128_f8f6f4 v[86:89], v[18:25], v[194:201], v[86:89], v191, v192 op_sel_hi:[0,0,0]
	v_mfma_scale_f32_16x16x128_f8f6f4 v[82:85], v[26:33], v[194:201], v[82:85], v191, v192 op_sel_hi:[0,0,0]
	v_mfma_scale_f32_16x16x128_f8f6f4 v[70:73], v[18:25], v[202:209], v[70:73], v191, v192 op_sel_hi:[0,0,0]
	v_mfma_scale_f32_16x16x128_f8f6f4 v[66:69], v[26:33], v[202:209], v[66:69], v191, v192 op_sel_hi:[0,0,0]
	v_mfma_scale_f32_16x16x128_f8f6f4 v[54:57], v[18:25], v[210:217], v[54:57], v191, v192 op_sel_hi:[0,0,0]
	v_mfma_scale_f32_16x16x128_f8f6f4 v[50:53], v[26:33], v[210:217], v[50:53], v191, v192 op_sel_hi:[0,0,0]
	v_mfma_scale_f32_16x16x128_f8f6f4 v[38:41], v[18:25], v[218:225], v[38:41], v191, v192 op_sel_hi:[0,0,0]
	v_mfma_scale_f32_16x16x128_f8f6f4 v[34:37], v[26:33], v[218:225], v[34:37], v191, v192 op_sel_hi:[0,0,0]
	s_setprio 0
	s_barrier
	s_add_i32 s48, s48, 2
	s_add_u32 s24, s24, 0x100
	s_addc_u32 s25, s25, 0
	s_add_u32 s46, s46, 0x100
	s_addc_u32 s47, s47, 0
	s_cmp_gt_u32 s48, 5
	s_cbranch_scc0 .LBB0_1205
	s_and_b64 vcc, exec, s[10:11]
	s_cbranch_vccz .LBB0_1208
	s_barrier

; #define PG8_STAGE(bufoff, gbase, voff) do { _Pragma("unroll") for (int _i = 0; _i < 2; ++_i) \
;         __builtin_amdgcn_global_load_lds((const unsigned*)((const char*)(gbase) + (voff)[_i]), (PG8_LAS unsigned*)(lds + (bufoff) + ldsw + _i * 8192), 16, 0, 0); } while (0)
; #define PG8_STAGE_A(bufoff, gbase, h, nx) do { if constexpr (Sched::GATHER) { const unsigned vv_[2] = {(nx) ? vAn[h][0] : vA[h][0], (nx) ? vAn[h][1] : vA[h][1]}; PG8_STAGE(bufoff, gbase, vv_); } \
;         else { PG8_STAGE(bufoff, (gbase) + (h) * hstep, voffA); } } while (0)
; #define PG8_LDA(dst, b, h) do { _Pragma("unroll") for (int m = 0; m < 4; ++m) _Pragma("unroll") for (int k = 0; k < 2; ++k) dst[m][k] = *(const PG8_LAS bf16x8*)(lds + PG8_SA(b, h) + aoff + m * 2048 + k * 1024); } while (0)
; #define PG8_WAIT_V(n) asm volatile("s_waitcnt vmcnt(" #n ")" ::: "memory")
; #define PG8_WAIT_L(n) asm volatile("s_waitcnt lgkmcnt(" #n ")" ::: "memory")
;     ...
;         const bool has_next = S.next(ui + 1, nxt);
;         const char* nA = Sched::GATHER ? cA : (has_next ? (const char*)g.A + (size_t)nxt.pm * tstep : cA);
;         if constexpr (Sched::GATHER) { if (has_next) { PG8_AOFF(vAn, ui + 1); } else { _Pragma("unroll") for (int h_ = 0; h_ < 2; ++h_) _Pragma("unroll") for (int i_ = 0; i_ < 2; ++i_) vAn[h_][i_] = vA[h_][i_]; } } const char* nB = has_next ? (const char*)g.Bt + (size_t)nxt.pb * tstep : cB;
; #pragma nounroll
;         for (int t = 0; t < nt; t += 2) {
;             const bool last = (t == nt - 2);
;             const char* a1 = cA + (size_t)(t + 1) * kstep;
;             const char* a2 = last ? nA : cA + (size_t)(t + 2) * kstep; const char* b2 = last ? nB : cB + (size_t)(t + 2) * kstep;
;             const char* a3 = a2 + kstep; const char* b3 = b2 + kstep;
;             if (last && has_next) S.a_ready(nxt);
;             if constexpr (SP2) {
;             PG8_LDB(B0, 0, 0); PG8_LDB(B1, 0, 1); PG8_SCHED; PG8_LDA(At, 0, 0); PG8_STAGE_A(PG8_SA(1, 1), a1, 1, false);
;             PG8_WAIT_V(8); PG8_WAIT_L(0); PG8_BAR; PG8_MMA(0, 0, At, B0); PG8_MMA(0, 1, At, B1); PG8_BAR; PG8_SCHED;
;             PG8_LDA(At, 0, 1); PG8_STAGE(PG8_SB(0, 0), b2, voffB); PG8_STAGE(PG8_SB(0, 1), b2 + hstepB, voffB); PG8_STAGE_A(PG8_SA(0, 0), a2, 0, last);
;             PG8_WAIT_V(8); PG8_WAIT_L(0); PG8_BAR; PG8_MMA(1, 0, At, B0); PG8_MMA(1, 1, At, B1); PG8_BAR; PG8_SCHED;
.LBB0_1571:
	s_ashr_i32 s17, s16, 31
	s_lshl_b64 s[18:19], s[16:17], 18
	v_readlane_b32 s22, v255, 1
	v_readlane_b32 s23, v255, 2
	s_add_u32 s18, s22, s18
	s_addc_u32 s19, s23, s19
	s_and_b64 s[4:5], s[4:5], exec
	s_cselect_b32 s17, s19, s21
	s_cselect_b32 s51, s18, s20
	v_mov_b32_e32 v175, v167
	v_mov_b32_e32 v177, v167
	s_add_u32 s52, s20, 0x100
	v_readlane_b32 s58, v254, 0
	v_lshl_add_u64 v[178:179], s[12:13], 0, v[176:177]
	v_lshl_add_u64 v[180:181], s[12:13], 0, v[174:175]
	s_addc_u32 s53, s21, 0
	s_mov_b32 s54, -2
	s_mov_b64 s[4:5], 0
	v_readlane_b32 s59, v254, 1
	ds_read_b128 v[26:29], v194
	ds_read_b128 v[30:33], v194 offset:1024
	ds_read_b128 v[18:21], v194 offset:2048
	ds_read_b128 v[22:25], v194 offset:3072
	ds_read_b128 v[10:13], v195
	ds_read_b128 v[14:17], v195 offset:1024
	ds_read_b128 v[2:5], v195 offset:2048
	ds_read_b128 v[6:9], v195 offset:3072
	s_add_u32 s20, s58, s4
	s_addc_u32 s21, s59, s5
	s_add_u32 s22, s20, 0x25400100
	s_addc_u32 s23, s21, 0
	s_add_u32 s55, s52, s4
	s_addc_u32 s56, s53, s5
	s_cmpk_eq_i32 s4, 0x300
	s_cselect_b64 vcc, -1, 0
	s_and_b64 s[20:21], vcc, exec
	s_cselect_b32 s23, s93, s23
	s_cselect_b32 s22, s92, s22
	s_cselect_b32 s21, s17, s56
	s_cselect_b32 s20, s51, s55
	s_mov_b32 m0, s39
	v_lshl_add_u64 v[232:233], v[180:181], 0, s[4:5]
	ds_read_b128 v[182:185], v196
	ds_read_b128 v[186:189], v196 offset:1024
	ds_read_b128 v[208:211], v196 offset:2048
	ds_read_b128 v[212:215], v196 offset:3072
	ds_read_b128 v[216:219], v196 offset:4096
	ds_read_b128 v[220:223], v196 offset:5120
	ds_read_b128 v[224:227], v196 offset:6144
	ds_read_b128 v[228:231], v196 offset:7168
	global_load_lds_dwordx4 v[232:233], off
	v_lshl_add_u64 v[232:233], v[178:179], 0, s[4:5]
	s_mov_b32 m0, s40
	s_nop 0
	global_load_lds_dwordx4 v[232:233], off
	s_waitcnt vmcnt(8)
	s_waitcnt lgkmcnt(0)
	s_barrier
	s_setprio 1
	s_nop 0
	s_waitcnt lgkmcnt(0)
	v_mfma_scale_f32_16x16x128_f8f6f4 v[158:161], v[26:33], v[182:189], 0, v197, v198 op_sel_hi:[0,0,0]
	v_mfma_scale_f32_16x16x128_f8f6f4 v[150:153], v[18:25], v[182:189], 0, v197, v198 op_sel_hi:[0,0,0]
	v_mfma_scale_f32_16x16x128_f8f6f4 v[142:145], v[26:33], v[208:215], 0, v197, v198 op_sel_hi:[0,0,0]
	v_mfma_scale_f32_16x16x128_f8f6f4 v[134:137], v[18:25], v[208:215], 0, v197, v198 op_sel_hi:[0,0,0]
	v_mfma_scale_f32_16x16x128_f8f6f4 v[126:129], v[26:33], v[216:223], 0, v197, v198 op_sel_hi:[0,0,0]
	v_mfma_scale_f32_16x16x128_f8f6f4 v[118:121], v[18:25], v[216:223], 0, v197, v198 op_sel_hi:[0,0,0]
	v_mfma_scale_f32_16x16x128_f8f6f4 v[110:113], v[26:33], v[224:231], 0, v197, v198 op_sel_hi:[0,0,0]
	v_mfma_scale_f32_16x16x128_f8f6f4 v[98:101], v[18:25], v[224:231], 0, v197, v198 op_sel_hi:[0,0,0]
	s_setprio 0
	s_setprio 1
	s_nop 0
	v_mfma_scale_f32_16x16x128_f8f6f4 v[154:157], v[10:17], v[182:189], 0, v197, v198 op_sel_hi:[0,0,0]
	v_mfma_scale_f32_16x16x128_f8f6f4 v[146:149], v[2:9], v[182:189], 0, v197, v198 op_sel_hi:[0,0,0]
	v_mfma_scale_f32_16x16x128_f8f6f4 v[138:141], v[10:17], v[208:215], 0, v197, v198 op_sel_hi:[0,0,0]
	v_mfma_scale_f32_16x16x128_f8f6f4 v[130:133], v[2:9], v[208:215], 0, v197, v198 op_sel_hi:[0,0,0]
	v_mfma_scale_f32_16x16x128_f8f6f4 v[122:125], v[10:17], v[216:223], 0, v197, v198 op_sel_hi:[0,0,0]
	v_mfma_scale_f32_16x16x128_f8f6f4 v[114:117], v[2:9], v[216:223], 0, v197, v198 op_sel_hi:[0,0,0]
	v_mfma_scale_f32_16x16x128_f8f6f4 v[106:109], v[10:17], v[224:231], 0, v197, v198 op_sel_hi:[0,0,0]
	v_mfma_scale_f32_16x16x128_f8f6f4 v[94:97], v[2:9], v[224:231], 0, v197, v198 op_sel_hi:[0,0,0]
	s_setprio 0
	s_barrier
	s_mov_b32 m0, s41
	v_lshl_add_u64 v[182:183], s[20:21], 0, v[164:165]
	s_add_u32 s56, s20, 0x20000
	ds_read_b128 v[208:211], v196 offset:16384
	ds_read_b128 v[212:215], v196 offset:17408
	ds_read_b128 v[216:219], v196 offset:18432
	ds_read_b128 v[220:223], v196 offset:19456
	ds_read_b128 v[224:227], v196 offset:20480
	ds_read_b128 v[228:231], v196 offset:21504
	ds_read_b128 v[232:235], v196 offset:22528
	ds_read_b128 v[236:239], v196 offset:23552
	global_load_lds_dwordx4 v[182:183], off
	v_lshl_add_u64 v[184:185], s[20:21], 0, v[162:163]
	s_mov_b32 m0, s42
	s_addc_u32 s57, s21, 0
	global_load_lds_dwordx4 v[184:185], off
	v_lshl_add_u64 v[186:187], s[56:57], 0, v[164:165]
	s_mov_b32 m0, s43
	v_cndmask_b32_e32 v166, v206, v202, vcc
	global_load_lds_dwordx4 v[186:187], off
	v_lshl_add_u64 v[186:187], s[56:57], 0, v[162:163]
	s_mov_b32 m0, s44
	v_lshl_add_u64 v[188:189], s[22:23], 0, v[166:167]
	global_load_lds_dwordx4 v[186:187], off
	s_mov_b32 m0, s26
	v_cndmask_b32_e32 v186, v172, v203, vcc
	global_load_lds_dwordx4 v166, s[22:23]
	s_mov_b32 m0, s27
	v_mov_b32_e32 v187, v167
	global_load_lds_dwordx4 v186, s[22:23]
	s_waitcnt vmcnt(8)
	s_waitcnt lgkmcnt(0)
	v_lshl_add_u64 v[186:187], s[22:23], 0, v[186:187]
	s_barrier
	s_setprio 1
	s_nop 0
	s_waitcnt lgkmcnt(0)
	v_mfma_scale_f32_16x16x128_f8f6f4 v[82:85], v[26:33], v[208:215], 0, v197, v198 op_sel_hi:[0,0,0]
	v_mfma_scale_f32_16x16x128_f8f6f4 v[70:73], v[18:25], v[208:215], 0, v197, v198 op_sel_hi:[0,0,0]
	v_mfma_scale_f32_16x16x128_f8f6f4 v[78:81], v[26:33], v[216:223], 0, v197, v198 op_sel_hi:[0,0,0]
	v_mfma_scale_f32_16x16x128_f8f6f4 v[66:69], v[18:25], v[216:223], 0, v197, v198 op_sel_hi:[0,0,0]
	v_mfma_scale_f32_16x16x128_f8f6f4 v[58:61], v[26:33], v[224:231], 0, v197, v198 op_sel_hi:[0,0,0]
	v_mfma_scale_f32_16x16x128_f8f6f4 v[50:53], v[18:25], v[224:231], 0, v197, v198 op_sel_hi:[0,0,0]
	v_mfma_scale_f32_16x16x128_f8f6f4 v[42:45], v[26:33], v[232:239], 0, v197, v198 op_sel_hi:[0,0,0]
	v_mfma_scale_f32_16x16x128_f8f6f4 v[34:37], v[18:25], v[232:239], 0, v197, v198 op_sel_hi:[0,0,0]
	s_setprio 0
	s_setprio 1
	s_nop 0
	v_mfma_scale_f32_16x16x128_f8f6f4 v[102:105], v[10:17], v[208:215], 0, v197, v198 op_sel_hi:[0,0,0]
	v_mfma_scale_f32_16x16x128_f8f6f4 v[90:93], v[2:9], v[208:215], 0, v197, v198 op_sel_hi:[0,0,0]
	v_mfma_scale_f32_16x16x128_f8f6f4 v[86:89], v[10:17], v[216:223], 0, v197, v198 op_sel_hi:[0,0,0]
	v_mfma_scale_f32_16x16x128_f8f6f4 v[74:77], v[2:9], v[216:223], 0, v197, v198 op_sel_hi:[0,0,0]
	v_mfma_scale_f32_16x16x128_f8f6f4 v[62:65], v[10:17], v[224:231], 0, v197, v198 op_sel_hi:[0,0,0]
	v_mfma_scale_f32_16x16x128_f8f6f4 v[54:57], v[2:9], v[224:231], 0, v197, v198 op_sel_hi:[0,0,0]
	v_mfma_scale_f32_16x16x128_f8f6f4 v[46:49], v[10:17], v[232:239], 0, v197, v198 op_sel_hi:[0,0,0]
	v_mfma_scale_f32_16x16x128_f8f6f4 v[38:41], v[2:9], v[232:239], 0, v197, v198 op_sel_hi:[0,0,0]
	s_setprio 0
	s_barrier
; #define PG8_STAGE(bufoff, gbase, voff) do { _Pragma("unroll") for (int _i = 0; _i < 2; ++_i) \
;         __builtin_amdgcn_global_load_lds((const unsigned*)((const char*)(gbase) + (voff)[_i]), (PG8_LAS unsigned*)(lds + (bufoff) + ldsw + _i * 8192), 16, 0, 0); } while (0)
; #define PG8_STAGE_A(bufoff, gbase, h, nx) do { if constexpr (Sched::GATHER) { const unsigned vv_[2] = {(nx) ? vAn[h][0] : vA[h][0], (nx) ? vAn[h][1] : vA[h][1]}; PG8_STAGE(bufoff, gbase, vv_); } \
;         else { PG8_STAGE(bufoff, (gbase) + (h) * hstep, voffA); } } while (0)
; #define PG8_LDA(dst, b, h) do { _Pragma("unroll") for (int m = 0; m < 4; ++m) _Pragma("unroll") for (int k = 0; k < 2; ++k) dst[m][k] = *(const PG8_LAS bf16x8*)(lds + PG8_SA(b, h) + aoff + m * 2048 + k * 1024); } while (0)
; #define PG8_LDB(dst, b, h) do { _Pragma("unroll") for (int n = 0; n < 2; ++n) _Pragma("unroll") for (int k = 0; k < 2; ++k) dst[n][k] = *(const PG8_LAS bf16x8*)(lds + PG8_SB(b, h) + boff + n * 2048 + k * 1024); } while (0)
; #define PG8_WAIT_V(n) asm volatile("s_waitcnt vmcnt(" #n ")" ::: "memory")
; #define PG8_WAIT_L(n) asm volatile("s_waitcnt lgkmcnt(" #n ")" ::: "memory")
; #define PG8_BAR __builtin_amdgcn_s_barrier()
; #define PG8_SCHED __builtin_amdgcn_sched_barrier(0)
;     ...
;             PG8_LDB(B0, 1, 0); PG8_LDB(B1, 1, 1); PG8_SCHED; PG8_LDA(At, 1, 0); PG8_STAGE_A(PG8_SA(0, 1), a2, 1, last);
;             PG8_WAIT_V(8); PG8_WAIT_L(0); PG8_BAR; PG8_MMA(0, 0, At, B0); PG8_MMA(0, 1, At, B1); PG8_BAR; PG8_SCHED;
;             PG8_LDA(At, 1, 1); PG8_STAGE(PG8_SB(1, 0), b3, voffB); PG8_STAGE(PG8_SB(1, 1), b3 + hstepB, voffB); PG8_STAGE_A(PG8_SA(1, 0), a3, 0, last);
;             PG8_WAIT_V(8); PG8_WAIT_L(0); PG8_BAR; PG8_MMA(1, 0, At, B0); PG8_MMA(1, 1, At, B1); PG8_BAR; PG8_SCHED;
	ds_read_b128 v[2:5], v199
	ds_read_b128 v[6:9], v199 offset:1024
	ds_read_b128 v[10:13], v199 offset:2048
	ds_read_b128 v[14:17], v199 offset:3072
	ds_read_b128 v[18:21], v200
	ds_read_b128 v[22:25], v200 offset:1024
	ds_read_b128 v[26:29], v200 offset:2048
	ds_read_b128 v[30:33], v200 offset:3072
	s_mov_b32 m0, s28
	v_cndmask_b32_e32 v166, v174, v204, vcc
	ds_read_b128 v[208:211], v196 offset:32768
	ds_read_b128 v[212:215], v196 offset:33792
	ds_read_b128 v[216:219], v196 offset:34816
	ds_read_b128 v[220:223], v196 offset:35840
	ds_read_b128 v[224:227], v196 offset:36864
	ds_read_b128 v[228:231], v196 offset:37888
	ds_read_b128 v[232:235], v196 offset:38912
	ds_read_b128 v[236:239], v196 offset:39936
	v_cndmask_b32_e32 v175, v176, v205, vcc
	global_load_lds_dwordx4 v166, s[22:23]
	s_mov_b32 m0, s29
	s_nop 0
	global_load_lds_dwordx4 v175, s[22:23]
	s_waitcnt vmcnt(8)
	s_waitcnt lgkmcnt(0)
	s_barrier
	s_setprio 1
	s_nop 0
	s_waitcnt lgkmcnt(0)
	v_mfma_scale_f32_16x16x128_f8f6f4 v[158:161], v[2:9], v[208:215], v[158:161], v197, v198 op_sel_hi:[0,0,0]
	v_mfma_scale_f32_16x16x128_f8f6f4 v[150:153], v[10:17], v[208:215], v[150:153], v197, v198 op_sel_hi:[0,0,0]
	v_mfma_scale_f32_16x16x128_f8f6f4 v[142:145], v[2:9], v[216:223], v[142:145], v197, v198 op_sel_hi:[0,0,0]
	v_mfma_scale_f32_16x16x128_f8f6f4 v[134:137], v[10:17], v[216:223], v[134:137], v197, v198 op_sel_hi:[0,0,0]
	v_mfma_scale_f32_16x16x128_f8f6f4 v[126:129], v[2:9], v[224:231], v[126:129], v197, v198 op_sel_hi:[0,0,0]
	v_mfma_scale_f32_16x16x128_f8f6f4 v[118:121], v[10:17], v[224:231], v[118:121], v197, v198 op_sel_hi:[0,0,0]
	v_mfma_scale_f32_16x16x128_f8f6f4 v[110:113], v[2:9], v[232:239], v[110:113], v197, v198 op_sel_hi:[0,0,0]
	v_mfma_scale_f32_16x16x128_f8f6f4 v[98:101], v[10:17], v[232:239], v[98:101], v197, v198 op_sel_hi:[0,0,0]
	s_setprio 0
	s_setprio 1
	s_nop 0
	v_mfma_scale_f32_16x16x128_f8f6f4 v[154:157], v[18:25], v[208:215], v[154:157], v197, v198 op_sel_hi:[0,0,0]
	v_mfma_scale_f32_16x16x128_f8f6f4 v[146:149], v[26:33], v[208:215], v[146:149], v197, v198 op_sel_hi:[0,0,0]
	v_mfma_scale_f32_16x16x128_f8f6f4 v[138:141], v[18:25], v[216:223], v[138:141], v197, v198 op_sel_hi:[0,0,0]
	v_mfma_scale_f32_16x16x128_f8f6f4 v[130:133], v[26:33], v[216:223], v[130:133], v197, v198 op_sel_hi:[0,0,0]
	v_mfma_scale_f32_16x16x128_f8f6f4 v[122:125], v[18:25], v[224:231], v[122:125], v197, v198 op_sel_hi:[0,0,0]
	v_mfma_scale_f32_16x16x128_f8f6f4 v[114:117], v[26:33], v[224:231], v[114:117], v197, v198 op_sel_hi:[0,0,0]
	v_mfma_scale_f32_16x16x128_f8f6f4 v[106:109], v[18:25], v[232:239], v[106:109], v197, v198 op_sel_hi:[0,0,0]
	v_mfma_scale_f32_16x16x128_f8f6f4 v[94:97], v[26:33], v[232:239], v[94:97], v197, v198 op_sel_hi:[0,0,0]
	s_setprio 0
	s_barrier
	s_mov_b32 m0, s45
	v_lshl_add_u64 v[182:183], v[182:183], 0, s[10:11]
	s_add_u32 s20, s20, 0x20080
	ds_read_b128 v[208:211], v196 offset:49152
	ds_read_b128 v[212:215], v196 offset:50176
	ds_read_b128 v[216:219], v196 offset:51200
	ds_read_b128 v[220:223], v196 offset:52224
	ds_read_b128 v[224:227], v196 offset:53248
	ds_read_b128 v[228:231], v196 offset:54272
	ds_read_b128 v[232:235], v196 offset:55296
	ds_read_b128 v[236:239], v196 offset:56320
	global_load_lds_dwordx4 v[182:183], off
	v_lshl_add_u64 v[182:183], v[184:185], 0, s[10:11]
	s_mov_b32 m0, s46
	s_addc_u32 s21, s21, 0
	global_load_lds_dwordx4 v[182:183], off
	v_lshl_add_u64 v[182:183], s[20:21], 0, v[164:165]
	s_mov_b32 m0, s47
	s_nop 0
	global_load_lds_dwordx4 v[182:183], off
	v_lshl_add_u64 v[182:183], s[20:21], 0, v[162:163]
	s_add_i32 m0, s47, 0x2000
	s_nop 0
	global_load_lds_dwordx4 v[182:183], off
	v_lshl_add_u64 v[182:183], v[188:189], 0, s[10:11]
	s_mov_b32 m0, s31
	s_nop 0
	global_load_lds_dwordx4 v[182:183], off
	v_lshl_add_u64 v[182:183], v[186:187], 0, s[10:11]
	s_mov_b32 m0, s34
	s_nop 0
	global_load_lds_dwordx4 v[182:183], off
	s_waitcnt vmcnt(8)
	s_waitcnt lgkmcnt(0)
	s_barrier
	s_setprio 1
	s_nop 0
	s_waitcnt lgkmcnt(0)
	v_mfma_scale_f32_16x16x128_f8f6f4 v[82:85], v[2:9], v[208:215], v[82:85], v197, v198 op_sel_hi:[0,0,0]
	v_mfma_scale_f32_16x16x128_f8f6f4 v[70:73], v[10:17], v[208:215], v[70:73], v197, v198 op_sel_hi:[0,0,0]
	v_mfma_scale_f32_16x16x128_f8f6f4 v[78:81], v[2:9], v[216:223], v[78:81], v197, v198 op_sel_hi:[0,0,0]
	v_mfma_scale_f32_16x16x128_f8f6f4 v[66:69], v[10:17], v[216:223], v[66:69], v197, v198 op_sel_hi:[0,0,0]
	v_mfma_scale_f32_16x16x128_f8f6f4 v[58:61], v[2:9], v[224:231], v[58:61], v197, v198 op_sel_hi:[0,0,0]
	v_mfma_scale_f32_16x16x128_f8f6f4 v[50:53], v[10:17], v[224:231], v[50:53], v197, v198 op_sel_hi:[0,0,0]
	v_mfma_scale_f32_16x16x128_f8f6f4 v[42:45], v[2:9], v[232:239], v[42:45], v197, v198 op_sel_hi:[0,0,0]
	v_mfma_scale_f32_16x16x128_f8f6f4 v[34:37], v[10:17], v[232:239], v[34:37], v197, v198 op_sel_hi:[0,0,0]
	s_setprio 0
	s_setprio 1
	s_nop 0
	v_mfma_scale_f32_16x16x128_f8f6f4 v[102:105], v[18:25], v[208:215], v[102:105], v197, v198 op_sel_hi:[0,0,0]
	v_mfma_scale_f32_16x16x128_f8f6f4 v[90:93], v[26:33], v[208:215], v[90:93], v197, v198 op_sel_hi:[0,0,0]
	v_mfma_scale_f32_16x16x128_f8f6f4 v[86:89], v[18:25], v[216:223], v[86:89], v197, v198 op_sel_hi:[0,0,0]
	v_mfma_scale_f32_16x16x128_f8f6f4 v[74:77], v[26:33], v[216:223], v[74:77], v197, v198 op_sel_hi:[0,0,0]
	v_mfma_scale_f32_16x16x128_f8f6f4 v[62:65], v[18:25], v[224:231], v[62:65], v197, v198 op_sel_hi:[0,0,0]
	v_mfma_scale_f32_16x16x128_f8f6f4 v[54:57], v[26:33], v[224:231], v[54:57], v197, v198 op_sel_hi:[0,0,0]
	v_mfma_scale_f32_16x16x128_f8f6f4 v[46:49], v[18:25], v[232:239], v[46:49], v197, v198 op_sel_hi:[0,0,0]
	v_mfma_scale_f32_16x16x128_f8f6f4 v[38:41], v[26:33], v[232:239], v[38:41], v197, v198 op_sel_hi:[0,0,0]
	s_setprio 0
	s_barrier
	s_add_i32 s54, s54, 2
	s_add_u32 s4, s4, 0x100
	s_addc_u32 s5, s5, 0
; #define PG8_STAGE(bufoff, gbase, voff) do { _Pragma("unroll") for (int _i = 0; _i < 2; ++_i) \
;         __builtin_amdgcn_global_load_lds((const unsigned*)((const char*)(gbase) + (voff)[_i]), (PG8_LAS unsigned*)(lds + (bufoff) + ldsw + _i * 8192), 16, 0, 0); } while (0)
; #define PG8_STAGE_A(bufoff, gbase, h, nx) do { if constexpr (Sched::GATHER) { const unsigned vv_[2] = {(nx) ? vAn[h][0] : vA[h][0], (nx) ? vAn[h][1] : vA[h][1]}; PG8_STAGE(bufoff, gbase, vv_); } \
;         else { PG8_STAGE(bufoff, (gbase) + (h) * hstep, voffA); } } while (0)
; #define PG8_LDA(dst, b, h) do { _Pragma("unroll") for (int m = 0; m < 4; ++m) _Pragma("unroll") for (int k = 0; k < 2; ++k) dst[m][k] = *(const PG8_LAS bf16x8*)(lds + PG8_SA(b, h) + aoff + m * 2048 + k * 1024); } while (0)
; #define PG8_LDB(dst, b, h) do { _Pragma("unroll") for (int n = 0; n < 2; ++n) _Pragma("unroll") for (int k = 0; k < 2; ++k) dst[n][k] = *(const PG8_LAS bf16x8*)(lds + PG8_SB(b, h) + boff + n * 2048 + k * 1024); } while (0)
; #define PG8_WAIT_V(n) asm volatile("s_waitcnt vmcnt(" #n ")" ::: "memory")
; #define PG8_WAIT_L(n) asm volatile("s_waitcnt lgkmcnt(" #n ")" ::: "memory")
; #define PG8_BAR __builtin_amdgcn_s_barrier()
; #define PG8_SCHED __builtin_amdgcn_sched_barrier(0)
;     ...
;             PG8_LDB(B0, 0, 0); PG8_LDB(B1, 0, 1); PG8_SCHED; PG8_LDA(At, 0, 0); PG8_STAGE_A(PG8_SA(1, 1), a1, 1, false);
;             PG8_WAIT_V(8); PG8_WAIT_L(0); PG8_BAR; PG8_MMA(0, 0, At, B0); PG8_MMA(0, 1, At, B1); PG8_BAR; PG8_SCHED;
;             PG8_LDA(At, 0, 1); PG8_STAGE(PG8_SB(0, 0), b2, voffB); PG8_STAGE(PG8_SB(0, 1), b2 + hstepB, voffB); PG8_STAGE_A(PG8_SA(0, 0), a2, 0, last);
;             PG8_WAIT_V(8); PG8_WAIT_L(0); PG8_BAR; PG8_MMA(1, 0, At, B0); PG8_MMA(1, 1, At, B1); PG8_BAR; PG8_SCHED;
.LBB0_1572:
	ds_read_b128 v[26:29], v194
	ds_read_b128 v[30:33], v194 offset:1024
	ds_read_b128 v[18:21], v194 offset:2048
	ds_read_b128 v[22:25], v194 offset:3072
	ds_read_b128 v[10:13], v195
	ds_read_b128 v[14:17], v195 offset:1024
	ds_read_b128 v[2:5], v195 offset:2048
	ds_read_b128 v[6:9], v195 offset:3072
	s_add_u32 s20, s58, s4
	s_addc_u32 s21, s59, s5
	s_add_u32 s22, s20, 0x25400100
	s_addc_u32 s23, s21, 0
	s_add_u32 s55, s52, s4
	s_addc_u32 s56, s53, s5
	s_cmpk_eq_i32 s4, 0x300
	s_cselect_b64 vcc, -1, 0
	s_and_b64 s[20:21], vcc, exec
	s_cselect_b32 s23, s93, s23
	s_cselect_b32 s22, s92, s22
	s_cselect_b32 s21, s17, s56
	s_cselect_b32 s20, s51, s55
	s_mov_b32 m0, s39
	v_lshl_add_u64 v[232:233], v[180:181], 0, s[4:5]
	ds_read_b128 v[182:185], v196
	ds_read_b128 v[186:189], v196 offset:1024
	ds_read_b128 v[208:211], v196 offset:2048
	ds_read_b128 v[212:215], v196 offset:3072
	ds_read_b128 v[216:219], v196 offset:4096
	ds_read_b128 v[220:223], v196 offset:5120
	ds_read_b128 v[224:227], v196 offset:6144
	ds_read_b128 v[228:231], v196 offset:7168
	global_load_lds_dwordx4 v[232:233], off
	v_lshl_add_u64 v[232:233], v[178:179], 0, s[4:5]
	s_mov_b32 m0, s40
	s_nop 0
	global_load_lds_dwordx4 v[232:233], off
	s_waitcnt vmcnt(8)
	s_waitcnt lgkmcnt(0)
	s_barrier
	s_setprio 1
	s_nop 0
	s_waitcnt lgkmcnt(0)
	v_mfma_scale_f32_16x16x128_f8f6f4 v[158:161], v[26:33], v[182:189], v[158:161], v197, v198 op_sel_hi:[0,0,0]
	v_mfma_scale_f32_16x16x128_f8f6f4 v[150:153], v[18:25], v[182:189], v[150:153], v197, v198 op_sel_hi:[0,0,0]
	v_mfma_scale_f32_16x16x128_f8f6f4 v[142:145], v[26:33], v[208:215], v[142:145], v197, v198 op_sel_hi:[0,0,0]
	v_mfma_scale_f32_16x16x128_f8f6f4 v[134:137], v[18:25], v[208:215], v[134:137], v197, v198 op_sel_hi:[0,0,0]
	v_mfma_scale_f32_16x16x128_f8f6f4 v[126:129], v[26:33], v[216:223], v[126:129], v197, v198 op_sel_hi:[0,0,0]
	v_mfma_scale_f32_16x16x128_f8f6f4 v[118:121], v[18:25], v[216:223], v[118:121], v197, v198 op_sel_hi:[0,0,0]
	v_mfma_scale_f32_16x16x128_f8f6f4 v[110:113], v[26:33], v[224:231], v[110:113], v197, v198 op_sel_hi:[0,0,0]
	v_mfma_scale_f32_16x16x128_f8f6f4 v[98:101], v[18:25], v[224:231], v[98:101], v197, v198 op_sel_hi:[0,0,0]
	s_setprio 0
	s_setprio 1
	s_nop 0
	v_mfma_scale_f32_16x16x128_f8f6f4 v[154:157], v[10:17], v[182:189], v[154:157], v197, v198 op_sel_hi:[0,0,0]
	v_mfma_scale_f32_16x16x128_f8f6f4 v[146:149], v[2:9], v[182:189], v[146:149], v197, v198 op_sel_hi:[0,0,0]
	v_mfma_scale_f32_16x16x128_f8f6f4 v[138:141], v[10:17], v[208:215], v[138:141], v197, v198 op_sel_hi:[0,0,0]
	v_mfma_scale_f32_16x16x128_f8f6f4 v[130:133], v[2:9], v[208:215], v[130:133], v197, v198 op_sel_hi:[0,0,0]
	v_mfma_scale_f32_16x16x128_f8f6f4 v[122:125], v[10:17], v[216:223], v[122:125], v197, v198 op_sel_hi:[0,0,0]
	v_mfma_scale_f32_16x16x128_f8f6f4 v[114:117], v[2:9], v[216:223], v[114:117], v197, v198 op_sel_hi:[0,0,0]
	v_mfma_scale_f32_16x16x128_f8f6f4 v[106:109], v[10:17], v[224:231], v[106:109], v197, v198 op_sel_hi:[0,0,0]
	v_mfma_scale_f32_16x16x128_f8f6f4 v[94:97], v[2:9], v[224:231], v[94:97], v197, v198 op_sel_hi:[0,0,0]
	s_setprio 0
	s_barrier
	s_mov_b32 m0, s41
	v_lshl_add_u64 v[182:183], s[20:21], 0, v[164:165]
	s_add_u32 s56, s20, 0x20000
	ds_read_b128 v[208:211], v196 offset:16384
	ds_read_b128 v[212:215], v196 offset:17408
	ds_read_b128 v[216:219], v196 offset:18432
	ds_read_b128 v[220:223], v196 offset:19456
	ds_read_b128 v[224:227], v196 offset:20480
	ds_read_b128 v[228:231], v196 offset:21504
	ds_read_b128 v[232:235], v196 offset:22528
	ds_read_b128 v[236:239], v196 offset:23552
	global_load_lds_dwordx4 v[182:183], off
	v_lshl_add_u64 v[184:185], s[20:21], 0, v[162:163]
	s_mov_b32 m0, s42
	s_addc_u32 s57, s21, 0
	global_load_lds_dwordx4 v[184:185], off
	v_lshl_add_u64 v[186:187], s[56:57], 0, v[164:165]
	s_mov_b32 m0, s43
	v_cndmask_b32_e32 v166, v206, v202, vcc
	global_load_lds_dwordx4 v[186:187], off
	v_lshl_add_u64 v[186:187], s[56:57], 0, v[162:163]
	s_mov_b32 m0, s44
	v_lshl_add_u64 v[188:189], s[22:23], 0, v[166:167]
	global_load_lds_dwordx4 v[186:187], off
	s_mov_b32 m0, s26
	v_cndmask_b32_e32 v186, v172, v203, vcc
	global_load_lds_dwordx4 v166, s[22:23]
	s_mov_b32 m0, s27
	v_mov_b32_e32 v187, v167
	global_load_lds_dwordx4 v186, s[22:23]
	s_waitcnt vmcnt(8)
	s_waitcnt lgkmcnt(0)
	v_lshl_add_u64 v[186:187], s[22:23], 0, v[186:187]
	s_barrier
	s_setprio 1
	s_nop 0
	s_waitcnt lgkmcnt(0)
	v_mfma_scale_f32_16x16x128_f8f6f4 v[82:85], v[26:33], v[208:215], v[82:85], v197, v198 op_sel_hi:[0,0,0]
	v_mfma_scale_f32_16x16x128_f8f6f4 v[70:73], v[18:25], v[208:215], v[70:73], v197, v198 op_sel_hi:[0,0,0]
	v_mfma_scale_f32_16x16x128_f8f6f4 v[78:81], v[26:33], v[216:223], v[78:81], v197, v198 op_sel_hi:[0,0,0]
	v_mfma_scale_f32_16x16x128_f8f6f4 v[66:69], v[18:25], v[216:223], v[66:69], v197, v198 op_sel_hi:[0,0,0]
	v_mfma_scale_f32_16x16x128_f8f6f4 v[58:61], v[26:33], v[224:231], v[58:61], v197, v198 op_sel_hi:[0,0,0]
	v_mfma_scale_f32_16x16x128_f8f6f4 v[50:53], v[18:25], v[224:231], v[50:53], v197, v198 op_sel_hi:[0,0,0]
	v_mfma_scale_f32_16x16x128_f8f6f4 v[42:45], v[26:33], v[232:239], v[42:45], v197, v198 op_sel_hi:[0,0,0]
	v_mfma_scale_f32_16x16x128_f8f6f4 v[34:37], v[18:25], v[232:239], v[34:37], v197, v198 op_sel_hi:[0,0,0]
	s_setprio 0
	s_setprio 1
	s_nop 0
	v_mfma_scale_f32_16x16x128_f8f6f4 v[102:105], v[10:17], v[208:215], v[102:105], v197, v198 op_sel_hi:[0,0,0]
	v_mfma_scale_f32_16x16x128_f8f6f4 v[90:93], v[2:9], v[208:215], v[90:93], v197, v198 op_sel_hi:[0,0,0]
	v_mfma_scale_f32_16x16x128_f8f6f4 v[86:89], v[10:17], v[216:223], v[86:89], v197, v198 op_sel_hi:[0,0,0]
	v_mfma_scale_f32_16x16x128_f8f6f4 v[74:77], v[2:9], v[216:223], v[74:77], v197, v198 op_sel_hi:[0,0,0]
	v_mfma_scale_f32_16x16x128_f8f6f4 v[62:65], v[10:17], v[224:231], v[62:65], v197, v198 op_sel_hi:[0,0,0]
	v_mfma_scale_f32_16x16x128_f8f6f4 v[54:57], v[2:9], v[224:231], v[54:57], v197, v198 op_sel_hi:[0,0,0]
	v_mfma_scale_f32_16x16x128_f8f6f4 v[46:49], v[10:17], v[232:239], v[46:49], v197, v198 op_sel_hi:[0,0,0]
	v_mfma_scale_f32_16x16x128_f8f6f4 v[38:41], v[2:9], v[232:239], v[38:41], v197, v198 op_sel_hi:[0,0,0]
	s_setprio 0
	s_barrier
; #define PG8_STAGE(bufoff, gbase, voff) do { _Pragma("unroll") for (int _i = 0; _i < 2; ++_i) \
;         __builtin_amdgcn_global_load_lds((const unsigned*)((const char*)(gbase) + (voff)[_i]), (PG8_LAS unsigned*)(lds + (bufoff) + ldsw + _i * 8192), 16, 0, 0); } while (0)
; #define PG8_STAGE_A(bufoff, gbase, h, nx) do { if constexpr (Sched::GATHER) { const unsigned vv_[2] = {(nx) ? vAn[h][0] : vA[h][0], (nx) ? vAn[h][1] : vA[h][1]}; PG8_STAGE(bufoff, gbase, vv_); } \
;         else { PG8_STAGE(bufoff, (gbase) + (h) * hstep, voffA); } } while (0)
; #define PG8_LDA(dst, b, h) do { _Pragma("unroll") for (int m = 0; m < 4; ++m) _Pragma("unroll") for (int k = 0; k < 2; ++k) dst[m][k] = *(const PG8_LAS bf16x8*)(lds + PG8_SA(b, h) + aoff + m * 2048 + k * 1024); } while (0)
; #define PG8_LDB(dst, b, h) do { _Pragma("unroll") for (int n = 0; n < 2; ++n) _Pragma("unroll") for (int k = 0; k < 2; ++k) dst[n][k] = *(const PG8_LAS bf16x8*)(lds + PG8_SB(b, h) + boff + n * 2048 + k * 1024); } while (0)
; #define PG8_WAIT_V(n) asm volatile("s_waitcnt vmcnt(" #n ")" ::: "memory")
; #define PG8_WAIT_L(n) asm volatile("s_waitcnt lgkmcnt(" #n ")" ::: "memory")
; #define PG8_BAR __builtin_amdgcn_s_barrier()
; #define PG8_SCHED __builtin_amdgcn_sched_barrier(0)
;     ...
;             PG8_LDB(B0, 1, 0); PG8_LDB(B1, 1, 1); PG8_SCHED; PG8_LDA(At, 1, 0); PG8_STAGE_A(PG8_SA(0, 1), a2, 1, last);
;             PG8_WAIT_V(8); PG8_WAIT_L(0); PG8_BAR; PG8_MMA(0, 0, At, B0); PG8_MMA(0, 1, At, B1); PG8_BAR; PG8_SCHED;
;             PG8_LDA(At, 1, 1); PG8_STAGE(PG8_SB(1, 0), b3, voffB); PG8_STAGE(PG8_SB(1, 1), b3 + hstepB, voffB); PG8_STAGE_A(PG8_SA(1, 0), a3, 0, last);
;             PG8_WAIT_V(8); PG8_WAIT_L(0); PG8_BAR; PG8_MMA(1, 0, At, B0); PG8_MMA(1, 1, At, B1); PG8_BAR; PG8_SCHED;
	ds_read_b128 v[2:5], v199
	ds_read_b128 v[6:9], v199 offset:1024
	ds_read_b128 v[10:13], v199 offset:2048
	ds_read_b128 v[14:17], v199 offset:3072
	ds_read_b128 v[18:21], v200
	ds_read_b128 v[22:25], v200 offset:1024
	ds_read_b128 v[26:29], v200 offset:2048
	ds_read_b128 v[30:33], v200 offset:3072
	s_mov_b32 m0, s28
	v_cndmask_b32_e32 v166, v174, v204, vcc
	ds_read_b128 v[208:211], v196 offset:32768
	ds_read_b128 v[212:215], v196 offset:33792
	ds_read_b128 v[216:219], v196 offset:34816
	ds_read_b128 v[220:223], v196 offset:35840
	ds_read_b128 v[224:227], v196 offset:36864
	ds_read_b128 v[228:231], v196 offset:37888
	ds_read_b128 v[232:235], v196 offset:38912
	ds_read_b128 v[236:239], v196 offset:39936
	v_cndmask_b32_e32 v175, v176, v205, vcc
	global_load_lds_dwordx4 v166, s[22:23]
	s_mov_b32 m0, s29
	s_nop 0
	global_load_lds_dwordx4 v175, s[22:23]
	s_waitcnt vmcnt(8)
	s_waitcnt lgkmcnt(0)
	s_barrier
	s_setprio 1
	s_nop 0
	s_waitcnt lgkmcnt(0)
	v_mfma_scale_f32_16x16x128_f8f6f4 v[158:161], v[2:9], v[208:215], v[158:161], v197, v198 op_sel_hi:[0,0,0]
	v_mfma_scale_f32_16x16x128_f8f6f4 v[150:153], v[10:17], v[208:215], v[150:153], v197, v198 op_sel_hi:[0,0,0]
	v_mfma_scale_f32_16x16x128_f8f6f4 v[142:145], v[2:9], v[216:223], v[142:145], v197, v198 op_sel_hi:[0,0,0]
	v_mfma_scale_f32_16x16x128_f8f6f4 v[134:137], v[10:17], v[216:223], v[134:137], v197, v198 op_sel_hi:[0,0,0]
	v_mfma_scale_f32_16x16x128_f8f6f4 v[126:129], v[2:9], v[224:231], v[126:129], v197, v198 op_sel_hi:[0,0,0]
	v_mfma_scale_f32_16x16x128_f8f6f4 v[118:121], v[10:17], v[224:231], v[118:121], v197, v198 op_sel_hi:[0,0,0]
	v_mfma_scale_f32_16x16x128_f8f6f4 v[110:113], v[2:9], v[232:239], v[110:113], v197, v198 op_sel_hi:[0,0,0]
	v_mfma_scale_f32_16x16x128_f8f6f4 v[98:101], v[10:17], v[232:239], v[98:101], v197, v198 op_sel_hi:[0,0,0]
	s_setprio 0
	s_setprio 1
	s_nop 0
	v_mfma_scale_f32_16x16x128_f8f6f4 v[154:157], v[18:25], v[208:215], v[154:157], v197, v198 op_sel_hi:[0,0,0]
	v_mfma_scale_f32_16x16x128_f8f6f4 v[146:149], v[26:33], v[208:215], v[146:149], v197, v198 op_sel_hi:[0,0,0]
	v_mfma_scale_f32_16x16x128_f8f6f4 v[138:141], v[18:25], v[216:223], v[138:141], v197, v198 op_sel_hi:[0,0,0]
	v_mfma_scale_f32_16x16x128_f8f6f4 v[130:133], v[26:33], v[216:223], v[130:133], v197, v198 op_sel_hi:[0,0,0]
	v_mfma_scale_f32_16x16x128_f8f6f4 v[122:125], v[18:25], v[224:231], v[122:125], v197, v198 op_sel_hi:[0,0,0]
	v_mfma_scale_f32_16x16x128_f8f6f4 v[114:117], v[26:33], v[224:231], v[114:117], v197, v198 op_sel_hi:[0,0,0]
	v_mfma_scale_f32_16x16x128_f8f6f4 v[106:109], v[18:25], v[232:239], v[106:109], v197, v198 op_sel_hi:[0,0,0]
	v_mfma_scale_f32_16x16x128_f8f6f4 v[94:97], v[26:33], v[232:239], v[94:97], v197, v198 op_sel_hi:[0,0,0]
	s_setprio 0
	s_barrier
	s_mov_b32 m0, s45
	v_lshl_add_u64 v[182:183], v[182:183], 0, s[10:11]
	s_add_u32 s20, s20, 0x20080
	ds_read_b128 v[208:211], v196 offset:49152
	ds_read_b128 v[212:215], v196 offset:50176
	ds_read_b128 v[216:219], v196 offset:51200
	ds_read_b128 v[220:223], v196 offset:52224
	ds_read_b128 v[224:227], v196 offset:53248
	ds_read_b128 v[228:231], v196 offset:54272
	ds_read_b128 v[232:235], v196 offset:55296
	ds_read_b128 v[236:239], v196 offset:56320
	global_load_lds_dwordx4 v[182:183], off
	v_lshl_add_u64 v[182:183], v[184:185], 0, s[10:11]
	s_mov_b32 m0, s46
	s_addc_u32 s21, s21, 0
	global_load_lds_dwordx4 v[182:183], off
	v_lshl_add_u64 v[182:183], s[20:21], 0, v[164:165]
	s_mov_b32 m0, s47
	s_nop 0
	global_load_lds_dwordx4 v[182:183], off
	v_lshl_add_u64 v[182:183], s[20:21], 0, v[162:163]
	s_add_i32 m0, s47, 0x2000
	s_nop 0
	global_load_lds_dwordx4 v[182:183], off
	v_lshl_add_u64 v[182:183], v[188:189], 0, s[10:11]
	s_mov_b32 m0, s31
	s_nop 0
	global_load_lds_dwordx4 v[182:183], off
	v_lshl_add_u64 v[182:183], v[186:187], 0, s[10:11]
	s_mov_b32 m0, s34
	s_nop 0
	global_load_lds_dwordx4 v[182:183], off
	s_waitcnt vmcnt(8)
	s_waitcnt lgkmcnt(0)
	s_barrier
	s_setprio 1
	s_nop 0
	s_waitcnt lgkmcnt(0)
	v_mfma_scale_f32_16x16x128_f8f6f4 v[82:85], v[2:9], v[208:215], v[82:85], v197, v198 op_sel_hi:[0,0,0]
	v_mfma_scale_f32_16x16x128_f8f6f4 v[70:73], v[10:17], v[208:215], v[70:73], v197, v198 op_sel_hi:[0,0,0]
	v_mfma_scale_f32_16x16x128_f8f6f4 v[78:81], v[2:9], v[216:223], v[78:81], v197, v198 op_sel_hi:[0,0,0]
	v_mfma_scale_f32_16x16x128_f8f6f4 v[66:69], v[10:17], v[216:223], v[66:69], v197, v198 op_sel_hi:[0,0,0]
	v_mfma_scale_f32_16x16x128_f8f6f4 v[58:61], v[2:9], v[224:231], v[58:61], v197, v198 op_sel_hi:[0,0,0]
	v_mfma_scale_f32_16x16x128_f8f6f4 v[50:53], v[10:17], v[224:231], v[50:53], v197, v198 op_sel_hi:[0,0,0]
	v_mfma_scale_f32_16x16x128_f8f6f4 v[42:45], v[2:9], v[232:239], v[42:45], v197, v198 op_sel_hi:[0,0,0]
	v_mfma_scale_f32_16x16x128_f8f6f4 v[34:37], v[10:17], v[232:239], v[34:37], v197, v198 op_sel_hi:[0,0,0]
	s_setprio 0
	s_setprio 1
	s_nop 0
	v_mfma_scale_f32_16x16x128_f8f6f4 v[102:105], v[18:25], v[208:215], v[102:105], v197, v198 op_sel_hi:[0,0,0]
	v_mfma_scale_f32_16x16x128_f8f6f4 v[90:93], v[26:33], v[208:215], v[90:93], v197, v198 op_sel_hi:[0,0,0]
	v_mfma_scale_f32_16x16x128_f8f6f4 v[86:89], v[18:25], v[216:223], v[86:89], v197, v198 op_sel_hi:[0,0,0]
	v_mfma_scale_f32_16x16x128_f8f6f4 v[74:77], v[26:33], v[216:223], v[74:77], v197, v198 op_sel_hi:[0,0,0]
	v_mfma_scale_f32_16x16x128_f8f6f4 v[62:65], v[18:25], v[224:231], v[62:65], v197, v198 op_sel_hi:[0,0,0]
	v_mfma_scale_f32_16x16x128_f8f6f4 v[54:57], v[26:33], v[224:231], v[54:57], v197, v198 op_sel_hi:[0,0,0]
	v_mfma_scale_f32_16x16x128_f8f6f4 v[46:49], v[18:25], v[232:239], v[46:49], v197, v198 op_sel_hi:[0,0,0]
	v_mfma_scale_f32_16x16x128_f8f6f4 v[38:41], v[26:33], v[232:239], v[38:41], v197, v198 op_sel_hi:[0,0,0]
	s_setprio 0
	s_barrier
	s_add_i32 s54, s54, 2
	s_add_u32 s4, s4, 0x100
	s_addc_u32 s5, s5, 0
	s_cmp_gt_u32 s54, 5
	s_cbranch_scc0 .LBB0_1572
	s_and_b64 vcc, exec, s[14:15]
	s_cbranch_vccz .LBB0_1575
	s_barrier

; #define PG8_STAGE(bufoff, gbase, voff) do { _Pragma("unroll") for (int _i = 0; _i < 2; ++_i) \
;         __builtin_amdgcn_global_load_lds((const unsigned*)((const char*)(gbase) + (voff)[_i]), (PG8_LAS unsigned*)(lds + (bufoff) + ldsw + _i * 8192), 16, 0, 0); } while (0)
; #define PG8_STAGE_A(bufoff, gbase, h, nx) do { if constexpr (Sched::GATHER) { const unsigned vv_[2] = {(nx) ? vAn[h][0] : vA[h][0], (nx) ? vAn[h][1] : vA[h][1]}; PG8_STAGE(bufoff, gbase, vv_); } \
;         else { PG8_STAGE(bufoff, (gbase) + (h) * hstep, voffA); } } while (0)
; #define PG8_LDA(dst, b, h) do { _Pragma("unroll") for (int m = 0; m < 4; ++m) _Pragma("unroll") for (int k = 0; k < 2; ++k) dst[m][k] = *(const PG8_LAS bf16x8*)(lds + PG8_SA(b, h) + aoff + m * 2048 + k * 1024); } while (0)
; #define PG8_WAIT_V(n) asm volatile("s_waitcnt vmcnt(" #n ")" ::: "memory")
; #define PG8_WAIT_L(n) asm volatile("s_waitcnt lgkmcnt(" #n ")" ::: "memory")
;     ...
;         const bool has_next = S.next(ui + 1, nxt);
;         const char* nA = Sched::GATHER ? cA : (has_next ? (const char*)g.A + (size_t)nxt.pm * tstep : cA);
;         if constexpr (Sched::GATHER) { if (has_next) { PG8_AOFF(vAn, ui + 1); } else { _Pragma("unroll") for (int h_ = 0; h_ < 2; ++h_) _Pragma("unroll") for (int i_ = 0; i_ < 2; ++i_) vAn[h_][i_] = vA[h_][i_]; } } const char* nB = has_next ? (const char*)g.Bt + (size_t)nxt.pb * tstep : cB;
; #pragma nounroll
;         for (int t = 0; t < nt; t += 2) {
;             const bool last = (t == nt - 2);
;             const char* a1 = cA + (size_t)(t + 1) * kstep;
;             const char* a2 = last ? nA : cA + (size_t)(t + 2) * kstep; const char* b2 = last ? nB : cB + (size_t)(t + 2) * kstep;
;             const char* a3 = a2 + kstep; const char* b3 = b2 + kstep;
;             if (last && has_next) S.a_ready(nxt);
;             if constexpr (SP2) {
;             PG8_LDB(B0, 0, 0); PG8_LDB(B1, 0, 1); PG8_SCHED; PG8_LDA(At, 0, 0); PG8_STAGE_A(PG8_SA(1, 1), a1, 1, false);
;             PG8_WAIT_V(8); PG8_WAIT_L(0); PG8_BAR; PG8_MMA(0, 0, At, B0); PG8_MMA(0, 1, At, B1); PG8_BAR; PG8_SCHED;
;             PG8_LDA(At, 0, 1); PG8_STAGE(PG8_SB(0, 0), b2, voffB); PG8_STAGE(PG8_SB(0, 1), b2 + hstepB, voffB); PG8_STAGE_A(PG8_SA(0, 0), a2, 0, last);
;             PG8_WAIT_V(8); PG8_WAIT_L(0); PG8_BAR; PG8_MMA(1, 0, At, B0); PG8_MMA(1, 1, At, B1); PG8_BAR; PG8_SCHED;
.LBB0_1625:
	s_ashr_i32 s13, s12, 31
	s_lshl_b64 s[16:17], s[12:13], 19
	v_readlane_b32 s18, v255, 9
	v_readlane_b32 s19, v255, 10
	s_add_u32 s16, s18, s16
	s_addc_u32 s17, s19, s17
	s_and_b64 s[18:19], s[2:3], exec
	s_cselect_b32 s13, s17, s23
	s_cselect_b32 s46, s16, s22
	s_ashr_i32 s15, s14, 31
	s_lshl_b64 s[18:19], s[14:15], 19
	v_readlane_b32 s26, v255, 3
	v_readlane_b32 s27, v255, 4
	s_add_u32 s18, s26, s18
	s_addc_u32 s19, s27, s19
	s_and_b64 s[26:27], s[2:3], exec
	s_cselect_b32 s15, s19, s25
	s_cselect_b32 s47, s18, s24
	s_add_u32 s22, s22, 0x40080
	s_addc_u32 s23, s23, 0
	s_add_u32 s48, s24, 0x100
	s_addc_u32 s49, s25, 0
	s_mov_b32 s50, -2
	ds_read_b128 v[26:29], v188
	ds_read_b128 v[30:33], v188 offset:1024
	ds_read_b128 v[18:21], v188 offset:2048
	ds_read_b128 v[22:25], v188 offset:3072
	ds_read_b128 v[10:13], v189
	ds_read_b128 v[14:17], v189 offset:1024
	ds_read_b128 v[2:5], v189 offset:2048
	ds_read_b128 v[6:9], v189 offset:3072
	s_add_u32 s24, s22, 0xfffc0080
	s_addc_u32 s25, s23, -1
	s_cmp_eq_u32 s50, 12
	s_cselect_b32 s27, s13, s25
	s_cselect_b32 s26, s46, s24
	s_cselect_b32 s25, s15, s49
	s_cselect_b32 s24, s47, s48
	v_lshl_add_u64 v[218:219], s[22:23], 0, v[170:171]
	s_add_i32 m0, s28, 0xc000
	ds_read_b128 v[178:181], v190
	ds_read_b128 v[182:185], v190 offset:1024
	ds_read_b128 v[194:197], v190 offset:2048
	ds_read_b128 v[198:201], v190 offset:3072
	ds_read_b128 v[202:205], v190 offset:4096
	ds_read_b128 v[206:209], v190 offset:5120
	ds_read_b128 v[210:213], v190 offset:6144
	ds_read_b128 v[214:217], v190 offset:7168
	global_load_lds_dwordx4 v[218:219], off
	v_lshl_add_u64 v[218:219], s[22:23], 0, v[172:173]
	s_add_i32 m0, s28, 0xe000
	s_nop 0
	global_load_lds_dwordx4 v[218:219], off
	s_waitcnt vmcnt(8)
	s_waitcnt lgkmcnt(0)
	s_barrier
	s_setprio 1
	s_nop 0
	s_waitcnt lgkmcnt(0)
	v_mfma_scale_f32_16x16x128_f8f6f4 v[158:161], v[26:33], v[178:185], 0, v191, v192 op_sel_hi:[0,0,0]
	v_mfma_scale_f32_16x16x128_f8f6f4 v[154:157], v[18:25], v[178:185], 0, v191, v192 op_sel_hi:[0,0,0]
	v_mfma_scale_f32_16x16x128_f8f6f4 v[142:145], v[26:33], v[194:201], 0, v191, v192 op_sel_hi:[0,0,0]
	v_mfma_scale_f32_16x16x128_f8f6f4 v[138:141], v[18:25], v[194:201], 0, v191, v192 op_sel_hi:[0,0,0]
	v_mfma_scale_f32_16x16x128_f8f6f4 v[126:129], v[26:33], v[202:209], 0, v191, v192 op_sel_hi:[0,0,0]
	v_mfma_scale_f32_16x16x128_f8f6f4 v[122:125], v[18:25], v[202:209], 0, v191, v192 op_sel_hi:[0,0,0]
	v_mfma_scale_f32_16x16x128_f8f6f4 v[110:113], v[26:33], v[210:217], 0, v191, v192 op_sel_hi:[0,0,0]
	v_mfma_scale_f32_16x16x128_f8f6f4 v[106:109], v[18:25], v[210:217], 0, v191, v192 op_sel_hi:[0,0,0]
	s_setprio 0
	s_setprio 1
	s_nop 0
	v_mfma_scale_f32_16x16x128_f8f6f4 v[150:153], v[10:17], v[178:185], 0, v191, v192 op_sel_hi:[0,0,0]
	v_mfma_scale_f32_16x16x128_f8f6f4 v[146:149], v[2:9], v[178:185], 0, v191, v192 op_sel_hi:[0,0,0]
	v_mfma_scale_f32_16x16x128_f8f6f4 v[134:137], v[10:17], v[194:201], 0, v191, v192 op_sel_hi:[0,0,0]
	v_mfma_scale_f32_16x16x128_f8f6f4 v[130:133], v[2:9], v[194:201], 0, v191, v192 op_sel_hi:[0,0,0]
	v_mfma_scale_f32_16x16x128_f8f6f4 v[118:121], v[10:17], v[202:209], 0, v191, v192 op_sel_hi:[0,0,0]
	v_mfma_scale_f32_16x16x128_f8f6f4 v[114:117], v[2:9], v[202:209], 0, v191, v192 op_sel_hi:[0,0,0]
	v_mfma_scale_f32_16x16x128_f8f6f4 v[102:105], v[10:17], v[210:217], 0, v191, v192 op_sel_hi:[0,0,0]
	v_mfma_scale_f32_16x16x128_f8f6f4 v[98:101], v[2:9], v[210:217], 0, v191, v192 op_sel_hi:[0,0,0]
	s_setprio 0
	s_barrier
	s_add_i32 s51, s39, s21
	v_lshl_add_u64 v[178:179], s[24:25], 0, v[166:167]
	s_mov_b32 m0, s51
	ds_read_b128 v[194:197], v190 offset:16384
	ds_read_b128 v[198:201], v190 offset:17408
	ds_read_b128 v[202:205], v190 offset:18432
	ds_read_b128 v[206:209], v190 offset:19456
	ds_read_b128 v[210:213], v190 offset:20480
	ds_read_b128 v[214:217], v190 offset:21504
	ds_read_b128 v[218:221], v190 offset:22528
	ds_read_b128 v[222:225], v190 offset:23552
	global_load_lds_dwordx4 v[178:179], off
	s_add_i32 m0, s51, 0x2000
	s_add_u32 s52, s24, 0x4000
	v_lshl_add_u64 v[180:181], s[24:25], 0, v[162:163]
	s_addc_u32 s53, s25, 0
	s_add_i32 s51, s40, s21
	global_load_lds_dwordx4 v[180:181], off
	v_lshl_add_u64 v[182:183], s[52:53], 0, v[166:167]
	s_mov_b32 m0, s51
	v_lshl_add_u64 v[184:185], s[26:27], 0, v[164:165]
	global_load_lds_dwordx4 v[182:183], off
	v_lshl_add_u64 v[182:183], s[52:53], 0, v[162:163]
	s_add_i32 m0, s51, 0x2000
	s_nop 0
	global_load_lds_dwordx4 v[182:183], off
	v_lshl_add_u64 v[182:183], s[26:27], 0, v[168:169]
	s_mov_b32 m0, s28
	s_nop 0
	global_load_lds_dwordx4 v[182:183], off
	s_mov_b32 m0, s29
	s_nop 0
	global_load_lds_dwordx4 v[184:185], off
	s_waitcnt vmcnt(8)
	s_waitcnt lgkmcnt(0)
	s_barrier
	s_setprio 1
	s_nop 0
	s_waitcnt lgkmcnt(0)
	v_mfma_scale_f32_16x16x128_f8f6f4 v[94:97], v[26:33], v[194:201], 0, v191, v192 op_sel_hi:[0,0,0]
	v_mfma_scale_f32_16x16x128_f8f6f4 v[90:93], v[18:25], v[194:201], 0, v191, v192 op_sel_hi:[0,0,0]
	v_mfma_scale_f32_16x16x128_f8f6f4 v[78:81], v[26:33], v[202:209], 0, v191, v192 op_sel_hi:[0,0,0]
	v_mfma_scale_f32_16x16x128_f8f6f4 v[74:77], v[18:25], v[202:209], 0, v191, v192 op_sel_hi:[0,0,0]
	v_mfma_scale_f32_16x16x128_f8f6f4 v[62:65], v[26:33], v[210:217], 0, v191, v192 op_sel_hi:[0,0,0]
	v_mfma_scale_f32_16x16x128_f8f6f4 v[58:61], v[18:25], v[210:217], 0, v191, v192 op_sel_hi:[0,0,0]
	v_mfma_scale_f32_16x16x128_f8f6f4 v[46:49], v[26:33], v[218:225], 0, v191, v192 op_sel_hi:[0,0,0]
	v_mfma_scale_f32_16x16x128_f8f6f4 v[42:45], v[18:25], v[218:225], 0, v191, v192 op_sel_hi:[0,0,0]
	s_setprio 0
	s_setprio 1
	s_nop 0
	v_mfma_scale_f32_16x16x128_f8f6f4 v[86:89], v[10:17], v[194:201], 0, v191, v192 op_sel_hi:[0,0,0]
	v_mfma_scale_f32_16x16x128_f8f6f4 v[82:85], v[2:9], v[194:201], 0, v191, v192 op_sel_hi:[0,0,0]
	v_mfma_scale_f32_16x16x128_f8f6f4 v[70:73], v[10:17], v[202:209], 0, v191, v192 op_sel_hi:[0,0,0]
	v_mfma_scale_f32_16x16x128_f8f6f4 v[66:69], v[2:9], v[202:209], 0, v191, v192 op_sel_hi:[0,0,0]
	v_mfma_scale_f32_16x16x128_f8f6f4 v[54:57], v[10:17], v[210:217], 0, v191, v192 op_sel_hi:[0,0,0]
	v_mfma_scale_f32_16x16x128_f8f6f4 v[50:53], v[2:9], v[210:217], 0, v191, v192 op_sel_hi:[0,0,0]
	v_mfma_scale_f32_16x16x128_f8f6f4 v[38:41], v[10:17], v[218:225], 0, v191, v192 op_sel_hi:[0,0,0]
	v_mfma_scale_f32_16x16x128_f8f6f4 v[34:37], v[2:9], v[218:225], 0, v191, v192 op_sel_hi:[0,0,0]
	s_setprio 0
	s_barrier
; #define PG8_STAGE(bufoff, gbase, voff) do { _Pragma("unroll") for (int _i = 0; _i < 2; ++_i) \
;         __builtin_amdgcn_global_load_lds((const unsigned*)((const char*)(gbase) + (voff)[_i]), (PG8_LAS unsigned*)(lds + (bufoff) + ldsw + _i * 8192), 16, 0, 0); } while (0)
; #define PG8_STAGE_A(bufoff, gbase, h, nx) do { if constexpr (Sched::GATHER) { const unsigned vv_[2] = {(nx) ? vAn[h][0] : vA[h][0], (nx) ? vAn[h][1] : vA[h][1]}; PG8_STAGE(bufoff, gbase, vv_); } \
;         else { PG8_STAGE(bufoff, (gbase) + (h) * hstep, voffA); } } while (0)
; #define PG8_LDA(dst, b, h) do { _Pragma("unroll") for (int m = 0; m < 4; ++m) _Pragma("unroll") for (int k = 0; k < 2; ++k) dst[m][k] = *(const PG8_LAS bf16x8*)(lds + PG8_SA(b, h) + aoff + m * 2048 + k * 1024); } while (0)
; #define PG8_LDB(dst, b, h) do { _Pragma("unroll") for (int n = 0; n < 2; ++n) _Pragma("unroll") for (int k = 0; k < 2; ++k) dst[n][k] = *(const PG8_LAS bf16x8*)(lds + PG8_SB(b, h) + boff + n * 2048 + k * 1024); } while (0)
; #define PG8_WAIT_V(n) asm volatile("s_waitcnt vmcnt(" #n ")" ::: "memory")
; #define PG8_WAIT_L(n) asm volatile("s_waitcnt lgkmcnt(" #n ")" ::: "memory")
; #define PG8_BAR __builtin_amdgcn_s_barrier()
; #define PG8_SCHED __builtin_amdgcn_sched_barrier(0)
;     ...
;             PG8_LDB(B0, 1, 0); PG8_LDB(B1, 1, 1); PG8_SCHED; PG8_LDA(At, 1, 0); PG8_STAGE_A(PG8_SA(0, 1), a2, 1, last);
;             PG8_WAIT_V(8); PG8_WAIT_L(0); PG8_BAR; PG8_MMA(0, 0, At, B0); PG8_MMA(0, 1, At, B1); PG8_BAR; PG8_SCHED;
;             PG8_LDA(At, 1, 1); PG8_STAGE(PG8_SB(1, 0), b3, voffB); PG8_STAGE(PG8_SB(1, 1), b3 + hstepB, voffB); PG8_STAGE_A(PG8_SA(1, 0), a3, 0, last);
;             PG8_WAIT_V(8); PG8_WAIT_L(0); PG8_BAR; PG8_MMA(1, 0, At, B0); PG8_MMA(1, 1, At, B1); PG8_BAR; PG8_SCHED;
	s_add_i32 s51, 0, 0x18000
	s_add_i32 s52, 0, 0x1c000
	v_add_u32_e32 v14, s51, v186
	v_add_u32_e32 v30, s52, v186
	ds_read_b128 v[2:5], v14
	ds_read_b128 v[6:9], v14 offset:1024
	ds_read_b128 v[10:13], v14 offset:2048
	ds_read_b128 v[14:17], v14 offset:3072
	ds_read_b128 v[18:21], v30
	ds_read_b128 v[22:25], v30 offset:1024
	ds_read_b128 v[26:29], v30 offset:2048
	ds_read_b128 v[30:33], v30 offset:3072
	s_add_u32 s26, s26, 0x40000
	s_addc_u32 s27, s27, 0
	s_mov_b32 m0, s30
	v_lshl_add_u64 v[226:227], s[26:27], 0, v[168:169]
	ds_read_b128 v[194:197], v190 offset:32768
	ds_read_b128 v[198:201], v190 offset:33792
	ds_read_b128 v[202:205], v190 offset:34816
	ds_read_b128 v[206:209], v190 offset:35840
	ds_read_b128 v[210:213], v190 offset:36864
	ds_read_b128 v[214:217], v190 offset:37888
	ds_read_b128 v[218:221], v190 offset:38912
	ds_read_b128 v[222:225], v190 offset:39936
	global_load_lds_dwordx4 v[226:227], off
	v_lshl_add_u64 v[226:227], s[26:27], 0, v[164:165]
	s_mov_b32 m0, s31
	s_nop 0
	global_load_lds_dwordx4 v[226:227], off
	s_waitcnt vmcnt(8)
	s_waitcnt lgkmcnt(0)
	s_barrier
	s_setprio 1
	s_nop 0
	s_waitcnt lgkmcnt(0)
	v_mfma_scale_f32_16x16x128_f8f6f4 v[158:161], v[2:9], v[194:201], v[158:161], v191, v192 op_sel_hi:[0,0,0]
	v_mfma_scale_f32_16x16x128_f8f6f4 v[154:157], v[10:17], v[194:201], v[154:157], v191, v192 op_sel_hi:[0,0,0]
	v_mfma_scale_f32_16x16x128_f8f6f4 v[142:145], v[2:9], v[202:209], v[142:145], v191, v192 op_sel_hi:[0,0,0]
	v_mfma_scale_f32_16x16x128_f8f6f4 v[138:141], v[10:17], v[202:209], v[138:141], v191, v192 op_sel_hi:[0,0,0]
	v_mfma_scale_f32_16x16x128_f8f6f4 v[126:129], v[2:9], v[210:217], v[126:129], v191, v192 op_sel_hi:[0,0,0]
	v_mfma_scale_f32_16x16x128_f8f6f4 v[122:125], v[10:17], v[210:217], v[122:125], v191, v192 op_sel_hi:[0,0,0]
	v_mfma_scale_f32_16x16x128_f8f6f4 v[110:113], v[2:9], v[218:225], v[110:113], v191, v192 op_sel_hi:[0,0,0]
	v_mfma_scale_f32_16x16x128_f8f6f4 v[106:109], v[10:17], v[218:225], v[106:109], v191, v192 op_sel_hi:[0,0,0]
	s_setprio 0
	s_setprio 1
	s_nop 0
	v_mfma_scale_f32_16x16x128_f8f6f4 v[150:153], v[18:25], v[194:201], v[150:153], v191, v192 op_sel_hi:[0,0,0]
	v_mfma_scale_f32_16x16x128_f8f6f4 v[146:149], v[26:33], v[194:201], v[146:149], v191, v192 op_sel_hi:[0,0,0]
	v_mfma_scale_f32_16x16x128_f8f6f4 v[134:137], v[18:25], v[202:209], v[134:137], v191, v192 op_sel_hi:[0,0,0]
	v_mfma_scale_f32_16x16x128_f8f6f4 v[130:133], v[26:33], v[202:209], v[130:133], v191, v192 op_sel_hi:[0,0,0]
	v_mfma_scale_f32_16x16x128_f8f6f4 v[118:121], v[18:25], v[210:217], v[118:121], v191, v192 op_sel_hi:[0,0,0]
	v_mfma_scale_f32_16x16x128_f8f6f4 v[114:117], v[26:33], v[210:217], v[114:117], v191, v192 op_sel_hi:[0,0,0]
	v_mfma_scale_f32_16x16x128_f8f6f4 v[102:105], v[18:25], v[218:225], v[102:105], v191, v192 op_sel_hi:[0,0,0]
	v_mfma_scale_f32_16x16x128_f8f6f4 v[98:101], v[26:33], v[218:225], v[98:101], v191, v192 op_sel_hi:[0,0,0]
	s_setprio 0
	s_barrier
	s_add_i32 s26, s51, s21
	v_lshl_add_u64 v[178:179], v[178:179], 0, s[8:9]
	s_mov_b32 m0, s26
	ds_read_b128 v[194:197], v190 offset:49152
	ds_read_b128 v[198:201], v190 offset:50176
	ds_read_b128 v[202:205], v190 offset:51200
	ds_read_b128 v[206:209], v190 offset:52224
	ds_read_b128 v[210:213], v190 offset:53248
	ds_read_b128 v[214:217], v190 offset:54272
	ds_read_b128 v[218:221], v190 offset:55296
	ds_read_b128 v[222:225], v190 offset:56320
	global_load_lds_dwordx4 v[178:179], off
	s_add_i32 m0, s26, 0x2000
	s_add_u32 s24, s24, 0x4080
	v_lshl_add_u64 v[178:179], v[180:181], 0, s[8:9]
	s_addc_u32 s25, s25, 0
	s_add_i32 s26, s52, s21
	global_load_lds_dwordx4 v[178:179], off
	v_lshl_add_u64 v[178:179], s[24:25], 0, v[166:167]
	s_mov_b32 m0, s26
	s_nop 0
	global_load_lds_dwordx4 v[178:179], off
	v_lshl_add_u64 v[178:179], s[24:25], 0, v[162:163]
	s_add_i32 m0, s26, 0x2000
	s_nop 0
	global_load_lds_dwordx4 v[178:179], off
	v_lshl_add_u64 v[178:179], v[182:183], 0, s[8:9]
	s_mov_b32 m0, s36
	s_nop 0
	global_load_lds_dwordx4 v[178:179], off
	v_lshl_add_u64 v[178:179], v[184:185], 0, s[8:9]
	s_mov_b32 m0, s37
	s_nop 0
	global_load_lds_dwordx4 v[178:179], off
	s_waitcnt vmcnt(8)
	s_waitcnt lgkmcnt(0)
	s_barrier
	s_setprio 1
	s_nop 0
	s_waitcnt lgkmcnt(0)
	v_mfma_scale_f32_16x16x128_f8f6f4 v[94:97], v[2:9], v[194:201], v[94:97], v191, v192 op_sel_hi:[0,0,0]
	v_mfma_scale_f32_16x16x128_f8f6f4 v[90:93], v[10:17], v[194:201], v[90:93], v191, v192 op_sel_hi:[0,0,0]
	v_mfma_scale_f32_16x16x128_f8f6f4 v[78:81], v[2:9], v[202:209], v[78:81], v191, v192 op_sel_hi:[0,0,0]
	v_mfma_scale_f32_16x16x128_f8f6f4 v[74:77], v[10:17], v[202:209], v[74:77], v191, v192 op_sel_hi:[0,0,0]
	v_mfma_scale_f32_16x16x128_f8f6f4 v[62:65], v[2:9], v[210:217], v[62:65], v191, v192 op_sel_hi:[0,0,0]
	v_mfma_scale_f32_16x16x128_f8f6f4 v[58:61], v[10:17], v[210:217], v[58:61], v191, v192 op_sel_hi:[0,0,0]
	v_mfma_scale_f32_16x16x128_f8f6f4 v[46:49], v[2:9], v[218:225], v[46:49], v191, v192 op_sel_hi:[0,0,0]
	v_mfma_scale_f32_16x16x128_f8f6f4 v[42:45], v[10:17], v[218:225], v[42:45], v191, v192 op_sel_hi:[0,0,0]
	s_setprio 0
	s_setprio 1
	s_nop 0
	v_mfma_scale_f32_16x16x128_f8f6f4 v[86:89], v[18:25], v[194:201], v[86:89], v191, v192 op_sel_hi:[0,0,0]
	v_mfma_scale_f32_16x16x128_f8f6f4 v[82:85], v[26:33], v[194:201], v[82:85], v191, v192 op_sel_hi:[0,0,0]
	v_mfma_scale_f32_16x16x128_f8f6f4 v[70:73], v[18:25], v[202:209], v[70:73], v191, v192 op_sel_hi:[0,0,0]
	v_mfma_scale_f32_16x16x128_f8f6f4 v[66:69], v[26:33], v[202:209], v[66:69], v191, v192 op_sel_hi:[0,0,0]
	v_mfma_scale_f32_16x16x128_f8f6f4 v[54:57], v[18:25], v[210:217], v[54:57], v191, v192 op_sel_hi:[0,0,0]
	v_mfma_scale_f32_16x16x128_f8f6f4 v[50:53], v[26:33], v[210:217], v[50:53], v191, v192 op_sel_hi:[0,0,0]
	v_mfma_scale_f32_16x16x128_f8f6f4 v[38:41], v[18:25], v[218:225], v[38:41], v191, v192 op_sel_hi:[0,0,0]
	v_mfma_scale_f32_16x16x128_f8f6f4 v[34:37], v[26:33], v[218:225], v[34:37], v191, v192 op_sel_hi:[0,0,0]
	s_setprio 0
	s_barrier
	s_add_i32 s50, s50, 2
	s_add_u32 s22, s22, 0x100
	s_addc_u32 s23, s23, 0
	s_add_u32 s48, s48, 0x100
	s_addc_u32 s49, s49, 0
; #define PG8_STAGE(bufoff, gbase, voff) do { _Pragma("unroll") for (int _i = 0; _i < 2; ++_i) \
;         __builtin_amdgcn_global_load_lds((const unsigned*)((const char*)(gbase) + (voff)[_i]), (PG8_LAS unsigned*)(lds + (bufoff) + ldsw + _i * 8192), 16, 0, 0); } while (0)
; #define PG8_STAGE_A(bufoff, gbase, h, nx) do { if constexpr (Sched::GATHER) { const unsigned vv_[2] = {(nx) ? vAn[h][0] : vA[h][0], (nx) ? vAn[h][1] : vA[h][1]}; PG8_STAGE(bufoff, gbase, vv_); } \
;         else { PG8_STAGE(bufoff, (gbase) + (h) * hstep, voffA); } } while (0)
; #define PG8_LDA(dst, b, h) do { _Pragma("unroll") for (int m = 0; m < 4; ++m) _Pragma("unroll") for (int k = 0; k < 2; ++k) dst[m][k] = *(const PG8_LAS bf16x8*)(lds + PG8_SA(b, h) + aoff + m * 2048 + k * 1024); } while (0)
; #define PG8_LDB(dst, b, h) do { _Pragma("unroll") for (int n = 0; n < 2; ++n) _Pragma("unroll") for (int k = 0; k < 2; ++k) dst[n][k] = *(const PG8_LAS bf16x8*)(lds + PG8_SB(b, h) + boff + n * 2048 + k * 1024); } while (0)
; #define PG8_WAIT_V(n) asm volatile("s_waitcnt vmcnt(" #n ")" ::: "memory")
; #define PG8_WAIT_L(n) asm volatile("s_waitcnt lgkmcnt(" #n ")" ::: "memory")
; #define PG8_BAR __builtin_amdgcn_s_barrier()
; #define PG8_SCHED __builtin_amdgcn_sched_barrier(0)
;     ...
;             PG8_LDB(B0, 0, 0); PG8_LDB(B1, 0, 1); PG8_SCHED; PG8_LDA(At, 0, 0); PG8_STAGE_A(PG8_SA(1, 1), a1, 1, false);
;             PG8_WAIT_V(8); PG8_WAIT_L(0); PG8_BAR; PG8_MMA(0, 0, At, B0); PG8_MMA(0, 1, At, B1); PG8_BAR; PG8_SCHED;
;             PG8_LDA(At, 0, 1); PG8_STAGE(PG8_SB(0, 0), b2, voffB); PG8_STAGE(PG8_SB(0, 1), b2 + hstepB, voffB); PG8_STAGE_A(PG8_SA(0, 0), a2, 0, last);
;             PG8_WAIT_V(8); PG8_WAIT_L(0); PG8_BAR; PG8_MMA(1, 0, At, B0); PG8_MMA(1, 1, At, B1); PG8_BAR; PG8_SCHED;
.LBB0_1626:
	ds_read_b128 v[26:29], v188
	ds_read_b128 v[30:33], v188 offset:1024
	ds_read_b128 v[18:21], v188 offset:2048
	ds_read_b128 v[22:25], v188 offset:3072
	ds_read_b128 v[10:13], v189
	ds_read_b128 v[14:17], v189 offset:1024
	ds_read_b128 v[2:5], v189 offset:2048
	ds_read_b128 v[6:9], v189 offset:3072
	s_add_u32 s24, s22, 0xfffc0080
	s_addc_u32 s25, s23, -1
	s_cmp_eq_u32 s50, 12
	s_cselect_b32 s27, s13, s25
	s_cselect_b32 s26, s46, s24
	s_cselect_b32 s25, s15, s49
	s_cselect_b32 s24, s47, s48
	v_lshl_add_u64 v[218:219], s[22:23], 0, v[170:171]
	s_add_i32 m0, s28, 0xc000
	ds_read_b128 v[178:181], v190
	ds_read_b128 v[182:185], v190 offset:1024
	ds_read_b128 v[194:197], v190 offset:2048
	ds_read_b128 v[198:201], v190 offset:3072
	ds_read_b128 v[202:205], v190 offset:4096
	ds_read_b128 v[206:209], v190 offset:5120
	ds_read_b128 v[210:213], v190 offset:6144
	ds_read_b128 v[214:217], v190 offset:7168
	global_load_lds_dwordx4 v[218:219], off
	v_lshl_add_u64 v[218:219], s[22:23], 0, v[172:173]
	s_add_i32 m0, s28, 0xe000
	s_nop 0
	global_load_lds_dwordx4 v[218:219], off
	s_waitcnt vmcnt(8)
	s_waitcnt lgkmcnt(0)
	s_barrier
	s_setprio 1
	s_nop 0
	s_waitcnt lgkmcnt(0)
	v_mfma_scale_f32_16x16x128_f8f6f4 v[158:161], v[26:33], v[178:185], v[158:161], v191, v192 op_sel_hi:[0,0,0]
	v_mfma_scale_f32_16x16x128_f8f6f4 v[154:157], v[18:25], v[178:185], v[154:157], v191, v192 op_sel_hi:[0,0,0]
	v_mfma_scale_f32_16x16x128_f8f6f4 v[142:145], v[26:33], v[194:201], v[142:145], v191, v192 op_sel_hi:[0,0,0]
	v_mfma_scale_f32_16x16x128_f8f6f4 v[138:141], v[18:25], v[194:201], v[138:141], v191, v192 op_sel_hi:[0,0,0]
	v_mfma_scale_f32_16x16x128_f8f6f4 v[126:129], v[26:33], v[202:209], v[126:129], v191, v192 op_sel_hi:[0,0,0]
	v_mfma_scale_f32_16x16x128_f8f6f4 v[122:125], v[18:25], v[202:209], v[122:125], v191, v192 op_sel_hi:[0,0,0]
	v_mfma_scale_f32_16x16x128_f8f6f4 v[110:113], v[26:33], v[210:217], v[110:113], v191, v192 op_sel_hi:[0,0,0]
	v_mfma_scale_f32_16x16x128_f8f6f4 v[106:109], v[18:25], v[210:217], v[106:109], v191, v192 op_sel_hi:[0,0,0]
	s_setprio 0
	s_setprio 1
	s_nop 0
	v_mfma_scale_f32_16x16x128_f8f6f4 v[150:153], v[10:17], v[178:185], v[150:153], v191, v192 op_sel_hi:[0,0,0]
	v_mfma_scale_f32_16x16x128_f8f6f4 v[146:149], v[2:9], v[178:185], v[146:149], v191, v192 op_sel_hi:[0,0,0]
	v_mfma_scale_f32_16x16x128_f8f6f4 v[134:137], v[10:17], v[194:201], v[134:137], v191, v192 op_sel_hi:[0,0,0]
	v_mfma_scale_f32_16x16x128_f8f6f4 v[130:133], v[2:9], v[194:201], v[130:133], v191, v192 op_sel_hi:[0,0,0]
	v_mfma_scale_f32_16x16x128_f8f6f4 v[118:121], v[10:17], v[202:209], v[118:121], v191, v192 op_sel_hi:[0,0,0]
	v_mfma_scale_f32_16x16x128_f8f6f4 v[114:117], v[2:9], v[202:209], v[114:117], v191, v192 op_sel_hi:[0,0,0]
	v_mfma_scale_f32_16x16x128_f8f6f4 v[102:105], v[10:17], v[210:217], v[102:105], v191, v192 op_sel_hi:[0,0,0]
	v_mfma_scale_f32_16x16x128_f8f6f4 v[98:101], v[2:9], v[210:217], v[98:101], v191, v192 op_sel_hi:[0,0,0]
	s_setprio 0
	s_barrier
	s_add_i32 s51, s39, s21
	v_lshl_add_u64 v[178:179], s[24:25], 0, v[166:167]
	s_mov_b32 m0, s51
	ds_read_b128 v[194:197], v190 offset:16384
	ds_read_b128 v[198:201], v190 offset:17408
	ds_read_b128 v[202:205], v190 offset:18432
	ds_read_b128 v[206:209], v190 offset:19456
	ds_read_b128 v[210:213], v190 offset:20480
	ds_read_b128 v[214:217], v190 offset:21504
	ds_read_b128 v[218:221], v190 offset:22528
	ds_read_b128 v[222:225], v190 offset:23552
	global_load_lds_dwordx4 v[178:179], off
	s_add_i32 m0, s51, 0x2000
	s_add_u32 s52, s24, 0x4000
	v_lshl_add_u64 v[180:181], s[24:25], 0, v[162:163]
	s_addc_u32 s53, s25, 0
	s_add_i32 s51, s40, s21
	global_load_lds_dwordx4 v[180:181], off
	v_lshl_add_u64 v[182:183], s[52:53], 0, v[166:167]
	s_mov_b32 m0, s51
	v_lshl_add_u64 v[184:185], s[26:27], 0, v[164:165]
	global_load_lds_dwordx4 v[182:183], off
	v_lshl_add_u64 v[182:183], s[52:53], 0, v[162:163]
	s_add_i32 m0, s51, 0x2000
	s_nop 0
	global_load_lds_dwordx4 v[182:183], off
	v_lshl_add_u64 v[182:183], s[26:27], 0, v[168:169]
	s_mov_b32 m0, s28
	s_nop 0
	global_load_lds_dwordx4 v[182:183], off
	s_mov_b32 m0, s29
	s_nop 0
	global_load_lds_dwordx4 v[184:185], off
	s_waitcnt vmcnt(8)
	s_waitcnt lgkmcnt(0)
	s_barrier
	s_setprio 1
	s_nop 0
	s_waitcnt lgkmcnt(0)
	v_mfma_scale_f32_16x16x128_f8f6f4 v[94:97], v[26:33], v[194:201], v[94:97], v191, v192 op_sel_hi:[0,0,0]
	v_mfma_scale_f32_16x16x128_f8f6f4 v[90:93], v[18:25], v[194:201], v[90:93], v191, v192 op_sel_hi:[0,0,0]
	v_mfma_scale_f32_16x16x128_f8f6f4 v[78:81], v[26:33], v[202:209], v[78:81], v191, v192 op_sel_hi:[0,0,0]
	v_mfma_scale_f32_16x16x128_f8f6f4 v[74:77], v[18:25], v[202:209], v[74:77], v191, v192 op_sel_hi:[0,0,0]
	v_mfma_scale_f32_16x16x128_f8f6f4 v[62:65], v[26:33], v[210:217], v[62:65], v191, v192 op_sel_hi:[0,0,0]
	v_mfma_scale_f32_16x16x128_f8f6f4 v[58:61], v[18:25], v[210:217], v[58:61], v191, v192 op_sel_hi:[0,0,0]
	v_mfma_scale_f32_16x16x128_f8f6f4 v[46:49], v[26:33], v[218:225], v[46:49], v191, v192 op_sel_hi:[0,0,0]
	v_mfma_scale_f32_16x16x128_f8f6f4 v[42:45], v[18:25], v[218:225], v[42:45], v191, v192 op_sel_hi:[0,0,0]
	s_setprio 0
	s_setprio 1
	s_nop 0
	v_mfma_scale_f32_16x16x128_f8f6f4 v[86:89], v[10:17], v[194:201], v[86:89], v191, v192 op_sel_hi:[0,0,0]
	v_mfma_scale_f32_16x16x128_f8f6f4 v[82:85], v[2:9], v[194:201], v[82:85], v191, v192 op_sel_hi:[0,0,0]
	v_mfma_scale_f32_16x16x128_f8f6f4 v[70:73], v[10:17], v[202:209], v[70:73], v191, v192 op_sel_hi:[0,0,0]
	v_mfma_scale_f32_16x16x128_f8f6f4 v[66:69], v[2:9], v[202:209], v[66:69], v191, v192 op_sel_hi:[0,0,0]
	v_mfma_scale_f32_16x16x128_f8f6f4 v[54:57], v[10:17], v[210:217], v[54:57], v191, v192 op_sel_hi:[0,0,0]
	v_mfma_scale_f32_16x16x128_f8f6f4 v[50:53], v[2:9], v[210:217], v[50:53], v191, v192 op_sel_hi:[0,0,0]
	v_mfma_scale_f32_16x16x128_f8f6f4 v[38:41], v[10:17], v[218:225], v[38:41], v191, v192 op_sel_hi:[0,0,0]
	v_mfma_scale_f32_16x16x128_f8f6f4 v[34:37], v[2:9], v[218:225], v[34:37], v191, v192 op_sel_hi:[0,0,0]
	s_setprio 0
	s_barrier
; #define PG8_STAGE(bufoff, gbase, voff) do { _Pragma("unroll") for (int _i = 0; _i < 2; ++_i) \
;         __builtin_amdgcn_global_load_lds((const unsigned*)((const char*)(gbase) + (voff)[_i]), (PG8_LAS unsigned*)(lds + (bufoff) + ldsw + _i * 8192), 16, 0, 0); } while (0)
; #define PG8_STAGE_A(bufoff, gbase, h, nx) do { if constexpr (Sched::GATHER) { const unsigned vv_[2] = {(nx) ? vAn[h][0] : vA[h][0], (nx) ? vAn[h][1] : vA[h][1]}; PG8_STAGE(bufoff, gbase, vv_); } \
;         else { PG8_STAGE(bufoff, (gbase) + (h) * hstep, voffA); } } while (0)
; #define PG8_LDA(dst, b, h) do { _Pragma("unroll") for (int m = 0; m < 4; ++m) _Pragma("unroll") for (int k = 0; k < 2; ++k) dst[m][k] = *(const PG8_LAS bf16x8*)(lds + PG8_SA(b, h) + aoff + m * 2048 + k * 1024); } while (0)
; #define PG8_LDB(dst, b, h) do { _Pragma("unroll") for (int n = 0; n < 2; ++n) _Pragma("unroll") for (int k = 0; k < 2; ++k) dst[n][k] = *(const PG8_LAS bf16x8*)(lds + PG8_SB(b, h) + boff + n * 2048 + k * 1024); } while (0)
; #define PG8_WAIT_V(n) asm volatile("s_waitcnt vmcnt(" #n ")" ::: "memory")
; #define PG8_WAIT_L(n) asm volatile("s_waitcnt lgkmcnt(" #n ")" ::: "memory")
; #define PG8_BAR __builtin_amdgcn_s_barrier()
; #define PG8_SCHED __builtin_amdgcn_sched_barrier(0)
;     ...
;             PG8_LDB(B0, 1, 0); PG8_LDB(B1, 1, 1); PG8_SCHED; PG8_LDA(At, 1, 0); PG8_STAGE_A(PG8_SA(0, 1), a2, 1, last);
;             PG8_WAIT_V(8); PG8_WAIT_L(0); PG8_BAR; PG8_MMA(0, 0, At, B0); PG8_MMA(0, 1, At, B1); PG8_BAR; PG8_SCHED;
;             PG8_LDA(At, 1, 1); PG8_STAGE(PG8_SB(1, 0), b3, voffB); PG8_STAGE(PG8_SB(1, 1), b3 + hstepB, voffB); PG8_STAGE_A(PG8_SA(1, 0), a3, 0, last);
;             PG8_WAIT_V(8); PG8_WAIT_L(0); PG8_BAR; PG8_MMA(1, 0, At, B0); PG8_MMA(1, 1, At, B1); PG8_BAR; PG8_SCHED;
;     __device__ __forceinline__ void operator()(const f32x4 (&acc)[2][2][4][2], const Unit& u, int wr, int wc, int fr, int fq) const {
;     ...
;             for (int m = 0; m < 4; ++m) { const int row = row0 + ai * HALF + m * 16; const float gt = gate[row] * YSCALE; unsigned char* rowp = O + (size_t)row * ldc + col0;
	s_add_i32 s51, 0, 0x18000
	s_add_i32 s52, 0, 0x1c000
	v_add_u32_e32 v14, s51, v186
	v_add_u32_e32 v30, s52, v186
	ds_read_b128 v[2:5], v14
	ds_read_b128 v[6:9], v14 offset:1024
	ds_read_b128 v[10:13], v14 offset:2048
	ds_read_b128 v[14:17], v14 offset:3072
	ds_read_b128 v[18:21], v30
	ds_read_b128 v[22:25], v30 offset:1024
	ds_read_b128 v[26:29], v30 offset:2048
	ds_read_b128 v[30:33], v30 offset:3072
	s_add_u32 s26, s26, 0x40000
	s_addc_u32 s27, s27, 0
	s_mov_b32 m0, s30
	v_lshl_add_u64 v[226:227], s[26:27], 0, v[168:169]
	ds_read_b128 v[194:197], v190 offset:32768
	ds_read_b128 v[198:201], v190 offset:33792
	ds_read_b128 v[202:205], v190 offset:34816
	ds_read_b128 v[206:209], v190 offset:35840
	ds_read_b128 v[210:213], v190 offset:36864
	ds_read_b128 v[214:217], v190 offset:37888
	ds_read_b128 v[218:221], v190 offset:38912
	ds_read_b128 v[222:225], v190 offset:39936
	global_load_lds_dwordx4 v[226:227], off
	v_lshl_add_u64 v[226:227], s[26:27], 0, v[164:165]
	s_mov_b32 m0, s31
	s_nop 0
	global_load_lds_dwordx4 v[226:227], off
	s_waitcnt vmcnt(8)
	s_waitcnt lgkmcnt(0)
	s_barrier
	s_setprio 1
	s_nop 0
	s_waitcnt lgkmcnt(0)
	v_mfma_scale_f32_16x16x128_f8f6f4 v[158:161], v[2:9], v[194:201], v[158:161], v191, v192 op_sel_hi:[0,0,0]
	v_mfma_scale_f32_16x16x128_f8f6f4 v[154:157], v[10:17], v[194:201], v[154:157], v191, v192 op_sel_hi:[0,0,0]
	v_mfma_scale_f32_16x16x128_f8f6f4 v[142:145], v[2:9], v[202:209], v[142:145], v191, v192 op_sel_hi:[0,0,0]
	v_mfma_scale_f32_16x16x128_f8f6f4 v[138:141], v[10:17], v[202:209], v[138:141], v191, v192 op_sel_hi:[0,0,0]
	v_mfma_scale_f32_16x16x128_f8f6f4 v[126:129], v[2:9], v[210:217], v[126:129], v191, v192 op_sel_hi:[0,0,0]
	v_mfma_scale_f32_16x16x128_f8f6f4 v[122:125], v[10:17], v[210:217], v[122:125], v191, v192 op_sel_hi:[0,0,0]
	v_mfma_scale_f32_16x16x128_f8f6f4 v[110:113], v[2:9], v[218:225], v[110:113], v191, v192 op_sel_hi:[0,0,0]
	v_mfma_scale_f32_16x16x128_f8f6f4 v[106:109], v[10:17], v[218:225], v[106:109], v191, v192 op_sel_hi:[0,0,0]
	s_setprio 0
	s_setprio 1
	s_nop 0
	v_mfma_scale_f32_16x16x128_f8f6f4 v[150:153], v[18:25], v[194:201], v[150:153], v191, v192 op_sel_hi:[0,0,0]
	v_mfma_scale_f32_16x16x128_f8f6f4 v[146:149], v[26:33], v[194:201], v[146:149], v191, v192 op_sel_hi:[0,0,0]
	v_mfma_scale_f32_16x16x128_f8f6f4 v[134:137], v[18:25], v[202:209], v[134:137], v191, v192 op_sel_hi:[0,0,0]
	v_mfma_scale_f32_16x16x128_f8f6f4 v[130:133], v[26:33], v[202:209], v[130:133], v191, v192 op_sel_hi:[0,0,0]
	v_mfma_scale_f32_16x16x128_f8f6f4 v[118:121], v[18:25], v[210:217], v[118:121], v191, v192 op_sel_hi:[0,0,0]
	v_mfma_scale_f32_16x16x128_f8f6f4 v[114:117], v[26:33], v[210:217], v[114:117], v191, v192 op_sel_hi:[0,0,0]
	v_mfma_scale_f32_16x16x128_f8f6f4 v[102:105], v[18:25], v[218:225], v[102:105], v191, v192 op_sel_hi:[0,0,0]
	v_mfma_scale_f32_16x16x128_f8f6f4 v[98:101], v[26:33], v[218:225], v[98:101], v191, v192 op_sel_hi:[0,0,0]
	s_setprio 0
	s_barrier
	s_add_i32 s26, s51, s21
	v_lshl_add_u64 v[178:179], v[178:179], 0, s[8:9]
	s_mov_b32 m0, s26
	ds_read_b128 v[194:197], v190 offset:49152
	ds_read_b128 v[198:201], v190 offset:50176
	ds_read_b128 v[202:205], v190 offset:51200
	ds_read_b128 v[206:209], v190 offset:52224
	ds_read_b128 v[210:213], v190 offset:53248
	ds_read_b128 v[214:217], v190 offset:54272
	ds_read_b128 v[218:221], v190 offset:55296
	ds_read_b128 v[222:225], v190 offset:56320
	global_load_lds_dwordx4 v[178:179], off
	s_add_i32 m0, s26, 0x2000
	s_add_u32 s24, s24, 0x4080
	v_lshl_add_u64 v[178:179], v[180:181], 0, s[8:9]
	s_addc_u32 s25, s25, 0
	s_add_i32 s26, s52, s21
	global_load_lds_dwordx4 v[178:179], off
	v_lshl_add_u64 v[178:179], s[24:25], 0, v[166:167]
	s_mov_b32 m0, s26
	s_nop 0
	global_load_lds_dwordx4 v[178:179], off
	v_lshl_add_u64 v[178:179], s[24:25], 0, v[162:163]
	s_add_i32 m0, s26, 0x2000
	s_nop 0
	global_load_lds_dwordx4 v[178:179], off
	v_lshl_add_u64 v[178:179], v[182:183], 0, s[8:9]
	s_mov_b32 m0, s36
	s_nop 0
	global_load_lds_dwordx4 v[178:179], off
	v_lshl_add_u64 v[178:179], v[184:185], 0, s[8:9]
	s_mov_b32 m0, s37
	s_nop 0
	global_load_lds_dwordx4 v[178:179], off
	s_waitcnt vmcnt(8)
	s_cmp_eq_u32 s50, 12
	s_cbranch_scc0 .Lgate19_skip
	v_lshl_add_u32 v236, s20, 8, v1
	v_ashrrev_i32_e32 v237, 31, v236
	v_lshl_add_u64 v[236:237], v[236:237], 2, s[0:1]
	global_load_dword v228, v[236:237], off
	global_load_dword v229, v[236:237], off offset:64
	global_load_dword v230, v[236:237], off offset:128
	global_load_dword v231, v[236:237], off offset:192
	global_load_dword v232, v[236:237], off offset:512
	global_load_dword v233, v[236:237], off offset:576
	global_load_dword v234, v[236:237], off offset:640
	global_load_dword v235, v[236:237], off offset:704
.Lgate19_skip:
	s_waitcnt lgkmcnt(0)
	s_barrier
	s_setprio 1
	s_nop 0
	s_waitcnt lgkmcnt(0)
	v_mfma_scale_f32_16x16x128_f8f6f4 v[94:97], v[2:9], v[194:201], v[94:97], v191, v192 op_sel_hi:[0,0,0]
	v_mfma_scale_f32_16x16x128_f8f6f4 v[90:93], v[10:17], v[194:201], v[90:93], v191, v192 op_sel_hi:[0,0,0]
	v_mfma_scale_f32_16x16x128_f8f6f4 v[78:81], v[2:9], v[202:209], v[78:81], v191, v192 op_sel_hi:[0,0,0]
	v_mfma_scale_f32_16x16x128_f8f6f4 v[74:77], v[10:17], v[202:209], v[74:77], v191, v192 op_sel_hi:[0,0,0]
	v_mfma_scale_f32_16x16x128_f8f6f4 v[62:65], v[2:9], v[210:217], v[62:65], v191, v192 op_sel_hi:[0,0,0]
	v_mfma_scale_f32_16x16x128_f8f6f4 v[58:61], v[10:17], v[210:217], v[58:61], v191, v192 op_sel_hi:[0,0,0]
	v_mfma_scale_f32_16x16x128_f8f6f4 v[46:49], v[2:9], v[218:225], v[46:49], v191, v192 op_sel_hi:[0,0,0]
	v_mfma_scale_f32_16x16x128_f8f6f4 v[42:45], v[10:17], v[218:225], v[42:45], v191, v192 op_sel_hi:[0,0,0]
	s_setprio 0
	s_setprio 1
	s_nop 0
	v_mfma_scale_f32_16x16x128_f8f6f4 v[86:89], v[18:25], v[194:201], v[86:89], v191, v192 op_sel_hi:[0,0,0]
	v_mfma_scale_f32_16x16x128_f8f6f4 v[82:85], v[26:33], v[194:201], v[82:85], v191, v192 op_sel_hi:[0,0,0]
	v_mfma_scale_f32_16x16x128_f8f6f4 v[70:73], v[18:25], v[202:209], v[70:73], v191, v192 op_sel_hi:[0,0,0]
	v_mfma_scale_f32_16x16x128_f8f6f4 v[66:69], v[26:33], v[202:209], v[66:69], v191, v192 op_sel_hi:[0,0,0]
	v_mfma_scale_f32_16x16x128_f8f6f4 v[54:57], v[18:25], v[210:217], v[54:57], v191, v192 op_sel_hi:[0,0,0]
	v_mfma_scale_f32_16x16x128_f8f6f4 v[50:53], v[26:33], v[210:217], v[50:53], v191, v192 op_sel_hi:[0,0,0]
	v_mfma_scale_f32_16x16x128_f8f6f4 v[38:41], v[18:25], v[218:225], v[38:41], v191, v192 op_sel_hi:[0,0,0]
	v_mfma_scale_f32_16x16x128_f8f6f4 v[34:37], v[26:33], v[218:225], v[34:37], v191, v192 op_sel_hi:[0,0,0]
	s_setprio 0
	s_barrier
	s_add_i32 s50, s50, 2
	s_add_u32 s22, s22, 0x100
	s_addc_u32 s23, s23, 0
	s_add_u32 s48, s48, 0x100
	s_addc_u32 s49, s49, 0
	s_cmp_gt_u32 s50, 13
	s_cbranch_scc0 .LBB0_1626
	s_and_b64 vcc, exec, s[10:11]
	s_cbranch_vccz .LBB0_1629
	s_barrier
